# GEMM K-loops: pad and redundant lgkmcnt(0) behind the barrier that opens each MFMA segment removed (8 bytes per site)
# speedup vs baseline: 1.0250x; 1.0005x over previous
; #define PG8_STAGE(bufoff, gbase, voff) do { _Pragma("unroll") for (int _i = 0; _i < 2; ++_i) \
;         __builtin_amdgcn_global_load_lds((const unsigned*)((const char*)(gbase) + (voff)[_i]), (PG8_LAS unsigned*)(lds + (bufoff) + ldsw + _i * 8192), 16, 0, 0); } while (0)
; #define PG8_STAGE_A(bufoff, gbase, h, nx) do { if constexpr (Sched::GATHER) { const unsigned vv_[2] = {(nx) ? vAn[h][0] : vA[h][0], (nx) ? vAn[h][1] : vA[h][1]}; PG8_STAGE(bufoff, gbase, vv_); } \
;         else { PG8_STAGE(bufoff, (gbase) + (h) * hstep, voffA); } } while (0)
; #define PG8_LDA(dst, b, h) do { _Pragma("unroll") for (int m = 0; m < 4; ++m) _Pragma("unroll") for (int k = 0; k < 2; ++k) dst[m][k] = *(const PG8_LAS bf16x8*)(lds + PG8_SA(b, h) + aoff + m * 2048 + k * 1024); } while (0)
; #define PG8_WAIT_V(n) asm volatile("s_waitcnt vmcnt(" #n ")" ::: "memory")
; #define PG8_WAIT_L(n) asm volatile("s_waitcnt lgkmcnt(" #n ")" ::: "memory")
;     ...
;         const bool has_next = S.next(ui + 1, nxt);
;         const char* nA = Sched::GATHER ? cA : (has_next ? (const char*)g.A + (size_t)nxt.pm * tstep : cA);
;         if constexpr (Sched::GATHER) { if (has_next) { PG8_AOFF(vAn, ui + 1); } else { _Pragma("unroll") for (int h_ = 0; h_ < 2; ++h_) _Pragma("unroll") for (int i_ = 0; i_ < 2; ++i_) vAn[h_][i_] = vA[h_][i_]; } } const char* nB = has_next ? (const char*)g.Bt + (size_t)nxt.pb * tstep : cB;
; #pragma nounroll
;         for (int t = 0; t < nt; t += 2) {
;             const bool last = (t == nt - 2);
;             const char* a1 = cA + (size_t)(t + 1) * kstep;
;             const char* a2 = last ? nA : cA + (size_t)(t + 2) * kstep; const char* b2 = last ? nB : cB + (size_t)(t + 2) * kstep;
;             const char* a3 = a2 + kstep; const char* b3 = b2 + kstep;
;             if (last && has_next) S.a_ready(nxt);
;             if constexpr (SP2) {
;             PG8_LDB(B0, 0, 0); PG8_LDB(B1, 0, 1); PG8_SCHED; PG8_LDA(At, 0, 0); PG8_STAGE_A(PG8_SA(1, 1), a1, 1, false);
;             PG8_WAIT_V(8); PG8_WAIT_L(0); PG8_BAR; PG8_MMA(0, 0, At, B0); PG8_MMA(0, 1, At, B1); PG8_BAR; PG8_SCHED;
;             PG8_LDA(At, 0, 1); PG8_STAGE(PG8_SB(0, 0), b2, voffB); PG8_STAGE(PG8_SB(0, 1), b2 + hstepB, voffB); PG8_STAGE_A(PG8_SA(0, 0), a2, 0, last);
;             PG8_WAIT_V(8); PG8_WAIT_L(0); PG8_BAR; PG8_MMA(1, 0, At, B0); PG8_MMA(1, 1, At, B1); PG8_BAR; PG8_SCHED;
.LBB0_152:
	s_ashr_i32 s61, s60, 31
	s_lshl_b64 s[0:1], s[60:61], 18
	v_readlane_b32 s18, v255, 5
	v_readlane_b32 s19, v255, 6
	s_add_u32 s62, s18, s0
	s_addc_u32 s63, s19, s1
	s_and_b64 s[0:1], s[2:3], exec
	s_cselect_b32 s0, s63, s9
	s_cselect_b32 s1, s62, s8
	s_ashr_i32 s73, s72, 31
	s_lshl_b64 s[18:19], s[72:73], 18
	s_add_u32 s64, s14, s18
	s_addc_u32 s65, s15, s19
	s_and_b64 s[18:19], s[2:3], exec
	s_cselect_b32 s5, s65, s11
	s_cselect_b32 s7, s64, s10
	s_add_u32 s8, s8, 0x20080
	s_addc_u32 s9, s9, 0
	s_add_u32 s18, s10, 0x100
	s_addc_u32 s19, s11, 0
	s_mov_b32 s33, -2
	ds_read_b128 v[26:29], v205
	ds_read_b128 v[30:33], v205 offset:1024
	ds_read_b128 v[18:21], v205 offset:2048
	ds_read_b128 v[22:25], v205 offset:3072
	ds_read_b128 v[10:13], v206
	ds_read_b128 v[14:17], v206 offset:1024
	ds_read_b128 v[2:5], v206 offset:2048
	ds_read_b128 v[6:9], v206 offset:3072
	s_add_u32 s10, s8, 0xfffe0080
	s_addc_u32 s11, s9, -1
	s_cmp_eq_u32 s33, 4
	s_cselect_b32 s67, s0, s11
	s_cselect_b32 s66, s1, s10
	s_cselect_b32 s11, s5, s19
	s_cselect_b32 s10, s7, s18
	v_lshl_add_u64 v[162:163], s[8:9], 0, v[176:177]
	s_add_i32 m0, s82, 0xc000
	ds_read_b128 v[184:187], v207
	ds_read_b128 v[188:191], v207 offset:1024
	ds_read_b128 v[192:195], v207 offset:2048
	ds_read_b128 v[196:199], v207 offset:3072
	ds_read_b128 v[214:217], v207 offset:4096
	ds_read_b128 v[218:221], v207 offset:5120
	ds_read_b128 v[222:225], v207 offset:6144
	ds_read_b128 v[226:229], v207 offset:7168
	global_load_lds_dwordx4 v[162:163], off
	v_lshl_add_u64 v[162:163], s[8:9], 0, v[178:179]
	s_add_i32 m0, s82, 0xe000
	s_nop 0
	global_load_lds_dwordx4 v[162:163], off
	s_waitcnt vmcnt(8)
	s_waitcnt lgkmcnt(0)
	s_barrier
	s_setprio 1
	v_mfma_scale_f32_16x16x128_f8f6f4 v[158:161], v[26:33], v[184:191], 0, v208, v209 op_sel_hi:[0,0,0]
	v_mfma_scale_f32_16x16x128_f8f6f4 v[154:157], v[18:25], v[184:191], 0, v208, v209 op_sel_hi:[0,0,0]
	v_mfma_scale_f32_16x16x128_f8f6f4 v[142:145], v[26:33], v[192:199], 0, v208, v209 op_sel_hi:[0,0,0]
	v_mfma_scale_f32_16x16x128_f8f6f4 v[138:141], v[18:25], v[192:199], 0, v208, v209 op_sel_hi:[0,0,0]
	v_mfma_scale_f32_16x16x128_f8f6f4 v[126:129], v[26:33], v[214:221], 0, v208, v209 op_sel_hi:[0,0,0]
	v_mfma_scale_f32_16x16x128_f8f6f4 v[122:125], v[18:25], v[214:221], 0, v208, v209 op_sel_hi:[0,0,0]
	v_mfma_scale_f32_16x16x128_f8f6f4 v[110:113], v[26:33], v[222:229], 0, v208, v209 op_sel_hi:[0,0,0]
	v_mfma_scale_f32_16x16x128_f8f6f4 v[106:109], v[18:25], v[222:229], 0, v208, v209 op_sel_hi:[0,0,0]
	s_setprio 0
	s_setprio 1
	s_nop 0
	v_mfma_scale_f32_16x16x128_f8f6f4 v[150:153], v[10:17], v[184:191], 0, v208, v209 op_sel_hi:[0,0,0]
	v_mfma_scale_f32_16x16x128_f8f6f4 v[146:149], v[2:9], v[184:191], 0, v208, v209 op_sel_hi:[0,0,0]
	v_mfma_scale_f32_16x16x128_f8f6f4 v[134:137], v[10:17], v[192:199], 0, v208, v209 op_sel_hi:[0,0,0]
	v_mfma_scale_f32_16x16x128_f8f6f4 v[130:133], v[2:9], v[192:199], 0, v208, v209 op_sel_hi:[0,0,0]
	v_mfma_scale_f32_16x16x128_f8f6f4 v[118:121], v[10:17], v[214:221], 0, v208, v209 op_sel_hi:[0,0,0]
	v_mfma_scale_f32_16x16x128_f8f6f4 v[114:117], v[2:9], v[214:221], 0, v208, v209 op_sel_hi:[0,0,0]
	v_mfma_scale_f32_16x16x128_f8f6f4 v[102:105], v[10:17], v[222:229], 0, v208, v209 op_sel_hi:[0,0,0]
	v_mfma_scale_f32_16x16x128_f8f6f4 v[98:101], v[2:9], v[222:229], 0, v208, v209 op_sel_hi:[0,0,0]
	s_setprio 0
	s_barrier
	s_add_i32 s59, s96, s77
	v_lshl_add_u64 v[162:163], s[10:11], 0, v[168:169]
	s_mov_b32 m0, s59
	ds_read_b128 v[188:191], v207 offset:16384
	ds_read_b128 v[192:195], v207 offset:17408
	ds_read_b128 v[214:217], v207 offset:18432
	ds_read_b128 v[218:221], v207 offset:19456
	ds_read_b128 v[222:225], v207 offset:20480
	ds_read_b128 v[226:229], v207 offset:21504
	ds_read_b128 v[230:233], v207 offset:22528
	ds_read_b128 v[234:237], v207 offset:23552
	global_load_lds_dwordx4 v[162:163], off
	s_add_i32 m0, s59, 0x2000
	s_add_u32 s68, s10, 0x8000
	v_lshl_add_u64 v[164:165], s[10:11], 0, v[172:173]
	s_addc_u32 s69, s11, 0
	s_add_i32 s59, s97, s77
	global_load_lds_dwordx4 v[164:165], off
	v_lshl_add_u64 v[184:185], s[68:69], 0, v[168:169]
	s_mov_b32 m0, s59
	v_lshl_add_u64 v[186:187], s[66:67], 0, v[170:171]
	global_load_lds_dwordx4 v[184:185], off
	v_lshl_add_u64 v[184:185], s[68:69], 0, v[172:173]
	s_add_i32 m0, s59, 0x2000
	s_nop 0
	global_load_lds_dwordx4 v[184:185], off
	v_lshl_add_u64 v[184:185], s[66:67], 0, v[166:167]
	s_mov_b32 m0, s82
	s_nop 0
	global_load_lds_dwordx4 v[184:185], off
	s_mov_b32 m0, s83
	s_nop 0
	global_load_lds_dwordx4 v[186:187], off
	s_waitcnt vmcnt(8)
	s_waitcnt lgkmcnt(0)
	s_barrier
	s_setprio 1
	v_mfma_scale_f32_16x16x128_f8f6f4 v[94:97], v[26:33], v[188:195], 0, v208, v209 op_sel_hi:[0,0,0]
	v_mfma_scale_f32_16x16x128_f8f6f4 v[90:93], v[18:25], v[188:195], 0, v208, v209 op_sel_hi:[0,0,0]
	v_mfma_scale_f32_16x16x128_f8f6f4 v[78:81], v[26:33], v[214:221], 0, v208, v209 op_sel_hi:[0,0,0]
	v_mfma_scale_f32_16x16x128_f8f6f4 v[74:77], v[18:25], v[214:221], 0, v208, v209 op_sel_hi:[0,0,0]
	v_mfma_scale_f32_16x16x128_f8f6f4 v[62:65], v[26:33], v[222:229], 0, v208, v209 op_sel_hi:[0,0,0]
	v_mfma_scale_f32_16x16x128_f8f6f4 v[58:61], v[18:25], v[222:229], 0, v208, v209 op_sel_hi:[0,0,0]
	v_mfma_scale_f32_16x16x128_f8f6f4 v[46:49], v[26:33], v[230:237], 0, v208, v209 op_sel_hi:[0,0,0]
	v_mfma_scale_f32_16x16x128_f8f6f4 v[42:45], v[18:25], v[230:237], 0, v208, v209 op_sel_hi:[0,0,0]
	s_setprio 0
	s_setprio 1
	s_nop 0
	v_mfma_scale_f32_16x16x128_f8f6f4 v[86:89], v[10:17], v[188:195], 0, v208, v209 op_sel_hi:[0,0,0]
	v_mfma_scale_f32_16x16x128_f8f6f4 v[82:85], v[2:9], v[188:195], 0, v208, v209 op_sel_hi:[0,0,0]
	v_mfma_scale_f32_16x16x128_f8f6f4 v[70:73], v[10:17], v[214:221], 0, v208, v209 op_sel_hi:[0,0,0]
	v_mfma_scale_f32_16x16x128_f8f6f4 v[66:69], v[2:9], v[214:221], 0, v208, v209 op_sel_hi:[0,0,0]
	v_mfma_scale_f32_16x16x128_f8f6f4 v[54:57], v[10:17], v[222:229], 0, v208, v209 op_sel_hi:[0,0,0]
	v_mfma_scale_f32_16x16x128_f8f6f4 v[50:53], v[2:9], v[222:229], 0, v208, v209 op_sel_hi:[0,0,0]
	v_mfma_scale_f32_16x16x128_f8f6f4 v[38:41], v[10:17], v[230:237], 0, v208, v209 op_sel_hi:[0,0,0]
	v_mfma_scale_f32_16x16x128_f8f6f4 v[34:37], v[2:9], v[230:237], 0, v208, v209 op_sel_hi:[0,0,0]
	s_setprio 0
	s_barrier
; #define PG8_STAGE(bufoff, gbase, voff) do { _Pragma("unroll") for (int _i = 0; _i < 2; ++_i) \
;         __builtin_amdgcn_global_load_lds((const unsigned*)((const char*)(gbase) + (voff)[_i]), (PG8_LAS unsigned*)(lds + (bufoff) + ldsw + _i * 8192), 16, 0, 0); } while (0)
; #define PG8_STAGE_A(bufoff, gbase, h, nx) do { if constexpr (Sched::GATHER) { const unsigned vv_[2] = {(nx) ? vAn[h][0] : vA[h][0], (nx) ? vAn[h][1] : vA[h][1]}; PG8_STAGE(bufoff, gbase, vv_); } \
;         else { PG8_STAGE(bufoff, (gbase) + (h) * hstep, voffA); } } while (0)
; #define PG8_LDA(dst, b, h) do { _Pragma("unroll") for (int m = 0; m < 4; ++m) _Pragma("unroll") for (int k = 0; k < 2; ++k) dst[m][k] = *(const PG8_LAS bf16x8*)(lds + PG8_SA(b, h) + aoff + m * 2048 + k * 1024); } while (0)
; #define PG8_LDB(dst, b, h) do { _Pragma("unroll") for (int n = 0; n < 2; ++n) _Pragma("unroll") for (int k = 0; k < 2; ++k) dst[n][k] = *(const PG8_LAS bf16x8*)(lds + PG8_SB(b, h) + boff + n * 2048 + k * 1024); } while (0)
; #define PG8_WAIT_V(n) asm volatile("s_waitcnt vmcnt(" #n ")" ::: "memory")
; #define PG8_WAIT_L(n) asm volatile("s_waitcnt lgkmcnt(" #n ")" ::: "memory")
; #define PG8_BAR __builtin_amdgcn_s_barrier()
; #define PG8_SCHED __builtin_amdgcn_sched_barrier(0)
;     ...
;             PG8_LDB(B0, 1, 0); PG8_LDB(B1, 1, 1); PG8_SCHED; PG8_LDA(At, 1, 0); PG8_STAGE_A(PG8_SA(0, 1), a2, 1, last);
;             PG8_WAIT_V(8); PG8_WAIT_L(0); PG8_BAR; PG8_MMA(0, 0, At, B0); PG8_MMA(0, 1, At, B1); PG8_BAR; PG8_SCHED;
;             PG8_LDA(At, 1, 1); PG8_STAGE(PG8_SB(1, 0), b3, voffB); PG8_STAGE(PG8_SB(1, 1), b3 + hstepB, voffB); PG8_STAGE_A(PG8_SA(1, 0), a3, 0, last);
;             PG8_WAIT_V(8); PG8_WAIT_L(0); PG8_BAR; PG8_MMA(1, 0, At, B0); PG8_MMA(1, 1, At, B1); PG8_BAR; PG8_SCHED;
	s_add_i32 s59, 0, 0x18000
	s_add_i32 s61, 0, 0x1c000
	v_add_u32_e32 v14, s59, v203
	v_add_u32_e32 v30, s61, v203
	ds_read_b128 v[2:5], v14
	ds_read_b128 v[6:9], v14 offset:1024
	ds_read_b128 v[10:13], v14 offset:2048
	ds_read_b128 v[14:17], v14 offset:3072
	ds_read_b128 v[18:21], v30
	ds_read_b128 v[22:25], v30 offset:1024
	ds_read_b128 v[26:29], v30 offset:2048
	ds_read_b128 v[30:33], v30 offset:3072
	s_add_u32 s66, s66, 0x20000
	s_addc_u32 s67, s67, 0
	s_mov_b32 m0, s84
	v_lshl_add_u64 v[196:197], s[66:67], 0, v[166:167]
	ds_read_b128 v[188:191], v207 offset:32768
	ds_read_b128 v[192:195], v207 offset:33792
	ds_read_b128 v[214:217], v207 offset:34816
	ds_read_b128 v[218:221], v207 offset:35840
	ds_read_b128 v[222:225], v207 offset:36864
	ds_read_b128 v[226:229], v207 offset:37888
	ds_read_b128 v[230:233], v207 offset:38912
	ds_read_b128 v[234:237], v207 offset:39936
	global_load_lds_dwordx4 v[196:197], off
	v_lshl_add_u64 v[196:197], s[66:67], 0, v[170:171]
	s_mov_b32 m0, s85
	s_nop 0
	global_load_lds_dwordx4 v[196:197], off
	s_waitcnt vmcnt(8)
	s_waitcnt lgkmcnt(0)
	s_barrier
	s_setprio 1
	v_mfma_scale_f32_16x16x128_f8f6f4 v[158:161], v[2:9], v[188:195], v[158:161], v208, v209 op_sel_hi:[0,0,0]
	v_mfma_scale_f32_16x16x128_f8f6f4 v[154:157], v[10:17], v[188:195], v[154:157], v208, v209 op_sel_hi:[0,0,0]
	v_mfma_scale_f32_16x16x128_f8f6f4 v[142:145], v[2:9], v[214:221], v[142:145], v208, v209 op_sel_hi:[0,0,0]
	v_mfma_scale_f32_16x16x128_f8f6f4 v[138:141], v[10:17], v[214:221], v[138:141], v208, v209 op_sel_hi:[0,0,0]
	v_mfma_scale_f32_16x16x128_f8f6f4 v[126:129], v[2:9], v[222:229], v[126:129], v208, v209 op_sel_hi:[0,0,0]
	v_mfma_scale_f32_16x16x128_f8f6f4 v[122:125], v[10:17], v[222:229], v[122:125], v208, v209 op_sel_hi:[0,0,0]
	v_mfma_scale_f32_16x16x128_f8f6f4 v[110:113], v[2:9], v[230:237], v[110:113], v208, v209 op_sel_hi:[0,0,0]
	v_mfma_scale_f32_16x16x128_f8f6f4 v[106:109], v[10:17], v[230:237], v[106:109], v208, v209 op_sel_hi:[0,0,0]
	s_setprio 0
	s_setprio 1
	s_nop 0
	v_mfma_scale_f32_16x16x128_f8f6f4 v[150:153], v[18:25], v[188:195], v[150:153], v208, v209 op_sel_hi:[0,0,0]
	v_mfma_scale_f32_16x16x128_f8f6f4 v[146:149], v[26:33], v[188:195], v[146:149], v208, v209 op_sel_hi:[0,0,0]
	v_mfma_scale_f32_16x16x128_f8f6f4 v[134:137], v[18:25], v[214:221], v[134:137], v208, v209 op_sel_hi:[0,0,0]
	v_mfma_scale_f32_16x16x128_f8f6f4 v[130:133], v[26:33], v[214:221], v[130:133], v208, v209 op_sel_hi:[0,0,0]
	v_mfma_scale_f32_16x16x128_f8f6f4 v[118:121], v[18:25], v[222:229], v[118:121], v208, v209 op_sel_hi:[0,0,0]
	v_mfma_scale_f32_16x16x128_f8f6f4 v[114:117], v[26:33], v[222:229], v[114:117], v208, v209 op_sel_hi:[0,0,0]
	v_mfma_scale_f32_16x16x128_f8f6f4 v[102:105], v[18:25], v[230:237], v[102:105], v208, v209 op_sel_hi:[0,0,0]
	v_mfma_scale_f32_16x16x128_f8f6f4 v[98:101], v[26:33], v[230:237], v[98:101], v208, v209 op_sel_hi:[0,0,0]
	s_setprio 0
	s_barrier
	s_add_i32 s59, s59, s77
	v_lshl_add_u64 v[162:163], v[162:163], 0, s[40:41]
	s_mov_b32 m0, s59
	ds_read_b128 v[188:191], v207 offset:49152
	ds_read_b128 v[192:195], v207 offset:50176
	ds_read_b128 v[214:217], v207 offset:51200
	ds_read_b128 v[218:221], v207 offset:52224
	ds_read_b128 v[222:225], v207 offset:53248
	ds_read_b128 v[226:229], v207 offset:54272
	ds_read_b128 v[230:233], v207 offset:55296
	ds_read_b128 v[234:237], v207 offset:56320
	global_load_lds_dwordx4 v[162:163], off
	s_add_i32 m0, s59, 0x2000
	s_add_u32 s10, s10, 0x8080
	v_lshl_add_u64 v[162:163], v[164:165], 0, s[40:41]
	s_addc_u32 s11, s11, 0
	s_add_i32 s59, s61, s77
	global_load_lds_dwordx4 v[162:163], off
	v_lshl_add_u64 v[162:163], s[10:11], 0, v[168:169]
	s_mov_b32 m0, s59
	s_nop 0
	global_load_lds_dwordx4 v[162:163], off
	v_lshl_add_u64 v[162:163], s[10:11], 0, v[172:173]
	s_add_i32 m0, s59, 0x2000
	s_nop 0
	global_load_lds_dwordx4 v[162:163], off
	v_lshl_add_u64 v[162:163], v[184:185], 0, s[40:41]
	s_mov_b32 m0, s94
	s_nop 0
	global_load_lds_dwordx4 v[162:163], off
	v_lshl_add_u64 v[162:163], v[186:187], 0, s[40:41]
	s_mov_b32 m0, s95
	s_nop 0
	global_load_lds_dwordx4 v[162:163], off
	s_waitcnt vmcnt(8)
	s_waitcnt lgkmcnt(0)
	s_barrier
	s_setprio 1
	v_mfma_scale_f32_16x16x128_f8f6f4 v[94:97], v[2:9], v[188:195], v[94:97], v208, v209 op_sel_hi:[0,0,0]
	v_mfma_scale_f32_16x16x128_f8f6f4 v[90:93], v[10:17], v[188:195], v[90:93], v208, v209 op_sel_hi:[0,0,0]
	v_mfma_scale_f32_16x16x128_f8f6f4 v[78:81], v[2:9], v[214:221], v[78:81], v208, v209 op_sel_hi:[0,0,0]
	v_mfma_scale_f32_16x16x128_f8f6f4 v[74:77], v[10:17], v[214:221], v[74:77], v208, v209 op_sel_hi:[0,0,0]
	v_mfma_scale_f32_16x16x128_f8f6f4 v[62:65], v[2:9], v[222:229], v[62:65], v208, v209 op_sel_hi:[0,0,0]
	v_mfma_scale_f32_16x16x128_f8f6f4 v[58:61], v[10:17], v[222:229], v[58:61], v208, v209 op_sel_hi:[0,0,0]
	v_mfma_scale_f32_16x16x128_f8f6f4 v[46:49], v[2:9], v[230:237], v[46:49], v208, v209 op_sel_hi:[0,0,0]
	v_mfma_scale_f32_16x16x128_f8f6f4 v[42:45], v[10:17], v[230:237], v[42:45], v208, v209 op_sel_hi:[0,0,0]
	s_setprio 0
	s_setprio 1
	s_nop 0
	v_mfma_scale_f32_16x16x128_f8f6f4 v[86:89], v[18:25], v[188:195], v[86:89], v208, v209 op_sel_hi:[0,0,0]
	v_mfma_scale_f32_16x16x128_f8f6f4 v[82:85], v[26:33], v[188:195], v[82:85], v208, v209 op_sel_hi:[0,0,0]
	v_mfma_scale_f32_16x16x128_f8f6f4 v[70:73], v[18:25], v[214:221], v[70:73], v208, v209 op_sel_hi:[0,0,0]
	v_mfma_scale_f32_16x16x128_f8f6f4 v[66:69], v[26:33], v[214:221], v[66:69], v208, v209 op_sel_hi:[0,0,0]
	v_mfma_scale_f32_16x16x128_f8f6f4 v[54:57], v[18:25], v[222:229], v[54:57], v208, v209 op_sel_hi:[0,0,0]
	v_mfma_scale_f32_16x16x128_f8f6f4 v[50:53], v[26:33], v[222:229], v[50:53], v208, v209 op_sel_hi:[0,0,0]
	v_mfma_scale_f32_16x16x128_f8f6f4 v[38:41], v[18:25], v[230:237], v[38:41], v208, v209 op_sel_hi:[0,0,0]
	v_mfma_scale_f32_16x16x128_f8f6f4 v[34:37], v[26:33], v[230:237], v[34:37], v208, v209 op_sel_hi:[0,0,0]
	s_setprio 0
	s_barrier
	s_add_i32 s33, s33, 2
	s_add_u32 s8, s8, 0x100
	s_addc_u32 s9, s9, 0
	s_add_u32 s18, s18, 0x100
	s_addc_u32 s19, s19, 0
; #define PG8_STAGE(bufoff, gbase, voff) do { _Pragma("unroll") for (int _i = 0; _i < 2; ++_i) \
;         __builtin_amdgcn_global_load_lds((const unsigned*)((const char*)(gbase) + (voff)[_i]), (PG8_LAS unsigned*)(lds + (bufoff) + ldsw + _i * 8192), 16, 0, 0); } while (0)
; #define PG8_STAGE_A(bufoff, gbase, h, nx) do { if constexpr (Sched::GATHER) { const unsigned vv_[2] = {(nx) ? vAn[h][0] : vA[h][0], (nx) ? vAn[h][1] : vA[h][1]}; PG8_STAGE(bufoff, gbase, vv_); } \
;         else { PG8_STAGE(bufoff, (gbase) + (h) * hstep, voffA); } } while (0)
; #define PG8_LDA(dst, b, h) do { _Pragma("unroll") for (int m = 0; m < 4; ++m) _Pragma("unroll") for (int k = 0; k < 2; ++k) dst[m][k] = *(const PG8_LAS bf16x8*)(lds + PG8_SA(b, h) + aoff + m * 2048 + k * 1024); } while (0)
; #define PG8_LDB(dst, b, h) do { _Pragma("unroll") for (int n = 0; n < 2; ++n) _Pragma("unroll") for (int k = 0; k < 2; ++k) dst[n][k] = *(const PG8_LAS bf16x8*)(lds + PG8_SB(b, h) + boff + n * 2048 + k * 1024); } while (0)
; #define PG8_WAIT_V(n) asm volatile("s_waitcnt vmcnt(" #n ")" ::: "memory")
; #define PG8_WAIT_L(n) asm volatile("s_waitcnt lgkmcnt(" #n ")" ::: "memory")
; #define PG8_BAR __builtin_amdgcn_s_barrier()
; #define PG8_SCHED __builtin_amdgcn_sched_barrier(0)
;     ...
;             PG8_LDB(B0, 0, 0); PG8_LDB(B1, 0, 1); PG8_SCHED; PG8_LDA(At, 0, 0); PG8_STAGE_A(PG8_SA(1, 1), a1, 1, false);
;             PG8_WAIT_V(8); PG8_WAIT_L(0); PG8_BAR; PG8_MMA(0, 0, At, B0); PG8_MMA(0, 1, At, B1); PG8_BAR; PG8_SCHED;
;             PG8_LDA(At, 0, 1); PG8_STAGE(PG8_SB(0, 0), b2, voffB); PG8_STAGE(PG8_SB(0, 1), b2 + hstepB, voffB); PG8_STAGE_A(PG8_SA(0, 0), a2, 0, last);
;             PG8_WAIT_V(8); PG8_WAIT_L(0); PG8_BAR; PG8_MMA(1, 0, At, B0); PG8_MMA(1, 1, At, B1); PG8_BAR; PG8_SCHED;
.LBB0_153:
	ds_read_b128 v[26:29], v205
	ds_read_b128 v[30:33], v205 offset:1024
	ds_read_b128 v[18:21], v205 offset:2048
	ds_read_b128 v[22:25], v205 offset:3072
	ds_read_b128 v[10:13], v206
	ds_read_b128 v[14:17], v206 offset:1024
	ds_read_b128 v[2:5], v206 offset:2048
	ds_read_b128 v[6:9], v206 offset:3072
	s_add_u32 s10, s8, 0xfffe0080
	s_addc_u32 s11, s9, -1
	s_cmp_eq_u32 s33, 4
	s_cselect_b32 s67, s0, s11
	s_cselect_b32 s66, s1, s10
	s_cselect_b32 s11, s5, s19
	s_cselect_b32 s10, s7, s18
	v_lshl_add_u64 v[162:163], s[8:9], 0, v[176:177]
	s_add_i32 m0, s82, 0xc000
	ds_read_b128 v[184:187], v207
	ds_read_b128 v[188:191], v207 offset:1024
	ds_read_b128 v[192:195], v207 offset:2048
	ds_read_b128 v[196:199], v207 offset:3072
	ds_read_b128 v[214:217], v207 offset:4096
	ds_read_b128 v[218:221], v207 offset:5120
	ds_read_b128 v[222:225], v207 offset:6144
	ds_read_b128 v[226:229], v207 offset:7168
	global_load_lds_dwordx4 v[162:163], off
	v_lshl_add_u64 v[162:163], s[8:9], 0, v[178:179]
	s_add_i32 m0, s82, 0xe000
	s_nop 0
	global_load_lds_dwordx4 v[162:163], off
	s_waitcnt vmcnt(8)
	s_waitcnt lgkmcnt(0)
	s_barrier
	s_setprio 1
	v_mfma_scale_f32_16x16x128_f8f6f4 v[158:161], v[26:33], v[184:191], v[158:161], v208, v209 op_sel_hi:[0,0,0]
	v_mfma_scale_f32_16x16x128_f8f6f4 v[154:157], v[18:25], v[184:191], v[154:157], v208, v209 op_sel_hi:[0,0,0]
	v_mfma_scale_f32_16x16x128_f8f6f4 v[142:145], v[26:33], v[192:199], v[142:145], v208, v209 op_sel_hi:[0,0,0]
	v_mfma_scale_f32_16x16x128_f8f6f4 v[138:141], v[18:25], v[192:199], v[138:141], v208, v209 op_sel_hi:[0,0,0]
	v_mfma_scale_f32_16x16x128_f8f6f4 v[126:129], v[26:33], v[214:221], v[126:129], v208, v209 op_sel_hi:[0,0,0]
	v_mfma_scale_f32_16x16x128_f8f6f4 v[122:125], v[18:25], v[214:221], v[122:125], v208, v209 op_sel_hi:[0,0,0]
	v_mfma_scale_f32_16x16x128_f8f6f4 v[110:113], v[26:33], v[222:229], v[110:113], v208, v209 op_sel_hi:[0,0,0]
	v_mfma_scale_f32_16x16x128_f8f6f4 v[106:109], v[18:25], v[222:229], v[106:109], v208, v209 op_sel_hi:[0,0,0]
	s_setprio 0
	s_setprio 1
	s_nop 0
	v_mfma_scale_f32_16x16x128_f8f6f4 v[150:153], v[10:17], v[184:191], v[150:153], v208, v209 op_sel_hi:[0,0,0]
	v_mfma_scale_f32_16x16x128_f8f6f4 v[146:149], v[2:9], v[184:191], v[146:149], v208, v209 op_sel_hi:[0,0,0]
	v_mfma_scale_f32_16x16x128_f8f6f4 v[134:137], v[10:17], v[192:199], v[134:137], v208, v209 op_sel_hi:[0,0,0]
	v_mfma_scale_f32_16x16x128_f8f6f4 v[130:133], v[2:9], v[192:199], v[130:133], v208, v209 op_sel_hi:[0,0,0]
	v_mfma_scale_f32_16x16x128_f8f6f4 v[118:121], v[10:17], v[214:221], v[118:121], v208, v209 op_sel_hi:[0,0,0]
	v_mfma_scale_f32_16x16x128_f8f6f4 v[114:117], v[2:9], v[214:221], v[114:117], v208, v209 op_sel_hi:[0,0,0]
	v_mfma_scale_f32_16x16x128_f8f6f4 v[102:105], v[10:17], v[222:229], v[102:105], v208, v209 op_sel_hi:[0,0,0]
	v_mfma_scale_f32_16x16x128_f8f6f4 v[98:101], v[2:9], v[222:229], v[98:101], v208, v209 op_sel_hi:[0,0,0]
	s_setprio 0
	s_barrier
	s_add_i32 s59, s96, s77
	v_lshl_add_u64 v[162:163], s[10:11], 0, v[168:169]
	s_mov_b32 m0, s59
	ds_read_b128 v[188:191], v207 offset:16384
	ds_read_b128 v[192:195], v207 offset:17408
	ds_read_b128 v[214:217], v207 offset:18432
	ds_read_b128 v[218:221], v207 offset:19456
	ds_read_b128 v[222:225], v207 offset:20480
	ds_read_b128 v[226:229], v207 offset:21504
	ds_read_b128 v[230:233], v207 offset:22528
	ds_read_b128 v[234:237], v207 offset:23552
	global_load_lds_dwordx4 v[162:163], off
	s_add_i32 m0, s59, 0x2000
	s_add_u32 s68, s10, 0x8000
	v_lshl_add_u64 v[164:165], s[10:11], 0, v[172:173]
	s_addc_u32 s69, s11, 0
	s_add_i32 s59, s97, s77
	global_load_lds_dwordx4 v[164:165], off
	v_lshl_add_u64 v[184:185], s[68:69], 0, v[168:169]
	s_mov_b32 m0, s59
	v_lshl_add_u64 v[186:187], s[66:67], 0, v[170:171]
	global_load_lds_dwordx4 v[184:185], off
	v_lshl_add_u64 v[184:185], s[68:69], 0, v[172:173]
	s_add_i32 m0, s59, 0x2000
	s_nop 0
	global_load_lds_dwordx4 v[184:185], off
	v_lshl_add_u64 v[184:185], s[66:67], 0, v[166:167]
	s_mov_b32 m0, s82
	s_nop 0
	global_load_lds_dwordx4 v[184:185], off
	s_mov_b32 m0, s83
	s_nop 0
	global_load_lds_dwordx4 v[186:187], off
	s_waitcnt vmcnt(8)
	s_waitcnt lgkmcnt(0)
	s_barrier
	s_setprio 1
	v_mfma_scale_f32_16x16x128_f8f6f4 v[94:97], v[26:33], v[188:195], v[94:97], v208, v209 op_sel_hi:[0,0,0]
	v_mfma_scale_f32_16x16x128_f8f6f4 v[90:93], v[18:25], v[188:195], v[90:93], v208, v209 op_sel_hi:[0,0,0]
	v_mfma_scale_f32_16x16x128_f8f6f4 v[78:81], v[26:33], v[214:221], v[78:81], v208, v209 op_sel_hi:[0,0,0]
	v_mfma_scale_f32_16x16x128_f8f6f4 v[74:77], v[18:25], v[214:221], v[74:77], v208, v209 op_sel_hi:[0,0,0]
	v_mfma_scale_f32_16x16x128_f8f6f4 v[62:65], v[26:33], v[222:229], v[62:65], v208, v209 op_sel_hi:[0,0,0]
	v_mfma_scale_f32_16x16x128_f8f6f4 v[58:61], v[18:25], v[222:229], v[58:61], v208, v209 op_sel_hi:[0,0,0]
	v_mfma_scale_f32_16x16x128_f8f6f4 v[46:49], v[26:33], v[230:237], v[46:49], v208, v209 op_sel_hi:[0,0,0]
	v_mfma_scale_f32_16x16x128_f8f6f4 v[42:45], v[18:25], v[230:237], v[42:45], v208, v209 op_sel_hi:[0,0,0]
	s_setprio 0
	s_setprio 1
	s_nop 0
	v_mfma_scale_f32_16x16x128_f8f6f4 v[86:89], v[10:17], v[188:195], v[86:89], v208, v209 op_sel_hi:[0,0,0]
	v_mfma_scale_f32_16x16x128_f8f6f4 v[82:85], v[2:9], v[188:195], v[82:85], v208, v209 op_sel_hi:[0,0,0]
	v_mfma_scale_f32_16x16x128_f8f6f4 v[70:73], v[10:17], v[214:221], v[70:73], v208, v209 op_sel_hi:[0,0,0]
	v_mfma_scale_f32_16x16x128_f8f6f4 v[66:69], v[2:9], v[214:221], v[66:69], v208, v209 op_sel_hi:[0,0,0]
	v_mfma_scale_f32_16x16x128_f8f6f4 v[54:57], v[10:17], v[222:229], v[54:57], v208, v209 op_sel_hi:[0,0,0]
	v_mfma_scale_f32_16x16x128_f8f6f4 v[50:53], v[2:9], v[222:229], v[50:53], v208, v209 op_sel_hi:[0,0,0]
	v_mfma_scale_f32_16x16x128_f8f6f4 v[38:41], v[10:17], v[230:237], v[38:41], v208, v209 op_sel_hi:[0,0,0]
	v_mfma_scale_f32_16x16x128_f8f6f4 v[34:37], v[2:9], v[230:237], v[34:37], v208, v209 op_sel_hi:[0,0,0]
	s_setprio 0
	s_barrier
; #define PG8_STAGE(bufoff, gbase, voff) do { _Pragma("unroll") for (int _i = 0; _i < 2; ++_i) \
;         __builtin_amdgcn_global_load_lds((const unsigned*)((const char*)(gbase) + (voff)[_i]), (PG8_LAS unsigned*)(lds + (bufoff) + ldsw + _i * 8192), 16, 0, 0); } while (0)
; #define PG8_STAGE_A(bufoff, gbase, h, nx) do { if constexpr (Sched::GATHER) { const unsigned vv_[2] = {(nx) ? vAn[h][0] : vA[h][0], (nx) ? vAn[h][1] : vA[h][1]}; PG8_STAGE(bufoff, gbase, vv_); } \
;         else { PG8_STAGE(bufoff, (gbase) + (h) * hstep, voffA); } } while (0)
; #define PG8_LDA(dst, b, h) do { _Pragma("unroll") for (int m = 0; m < 4; ++m) _Pragma("unroll") for (int k = 0; k < 2; ++k) dst[m][k] = *(const PG8_LAS bf16x8*)(lds + PG8_SA(b, h) + aoff + m * 2048 + k * 1024); } while (0)
; #define PG8_LDB(dst, b, h) do { _Pragma("unroll") for (int n = 0; n < 2; ++n) _Pragma("unroll") for (int k = 0; k < 2; ++k) dst[n][k] = *(const PG8_LAS bf16x8*)(lds + PG8_SB(b, h) + boff + n * 2048 + k * 1024); } while (0)
; #define PG8_WAIT_V(n) asm volatile("s_waitcnt vmcnt(" #n ")" ::: "memory")
; #define PG8_WAIT_L(n) asm volatile("s_waitcnt lgkmcnt(" #n ")" ::: "memory")
; #define PG8_BAR __builtin_amdgcn_s_barrier()
; #define PG8_SCHED __builtin_amdgcn_sched_barrier(0)
;     ...
;             PG8_LDB(B0, 1, 0); PG8_LDB(B1, 1, 1); PG8_SCHED; PG8_LDA(At, 1, 0); PG8_STAGE_A(PG8_SA(0, 1), a2, 1, last);
;             PG8_WAIT_V(8); PG8_WAIT_L(0); PG8_BAR; PG8_MMA(0, 0, At, B0); PG8_MMA(0, 1, At, B1); PG8_BAR; PG8_SCHED;
;             PG8_LDA(At, 1, 1); PG8_STAGE(PG8_SB(1, 0), b3, voffB); PG8_STAGE(PG8_SB(1, 1), b3 + hstepB, voffB); PG8_STAGE_A(PG8_SA(1, 0), a3, 0, last);
;             PG8_WAIT_V(8); PG8_WAIT_L(0); PG8_BAR; PG8_MMA(1, 0, At, B0); PG8_MMA(1, 1, At, B1); PG8_BAR; PG8_SCHED;
;     ...
;         }
;         if constexpr (F8) asm volatile("s_nop 15\n\ts_nop 15\n\ts_nop 15" ::: "memory");
;         if constexpr (ALIGN_EPI) { if (wr == 0) PG8_BAR; }
	s_add_i32 s59, 0, 0x18000
	s_add_i32 s61, 0, 0x1c000
	v_add_u32_e32 v14, s59, v203
	v_add_u32_e32 v30, s61, v203
	ds_read_b128 v[2:5], v14
	ds_read_b128 v[6:9], v14 offset:1024
	ds_read_b128 v[10:13], v14 offset:2048
	ds_read_b128 v[14:17], v14 offset:3072
	ds_read_b128 v[18:21], v30
	ds_read_b128 v[22:25], v30 offset:1024
	ds_read_b128 v[26:29], v30 offset:2048
	ds_read_b128 v[30:33], v30 offset:3072
	s_add_u32 s66, s66, 0x20000
	s_addc_u32 s67, s67, 0
	s_mov_b32 m0, s84
	v_lshl_add_u64 v[196:197], s[66:67], 0, v[166:167]
	ds_read_b128 v[188:191], v207 offset:32768
	ds_read_b128 v[192:195], v207 offset:33792
	ds_read_b128 v[214:217], v207 offset:34816
	ds_read_b128 v[218:221], v207 offset:35840
	ds_read_b128 v[222:225], v207 offset:36864
	ds_read_b128 v[226:229], v207 offset:37888
	ds_read_b128 v[230:233], v207 offset:38912
	ds_read_b128 v[234:237], v207 offset:39936
	global_load_lds_dwordx4 v[196:197], off
	v_lshl_add_u64 v[196:197], s[66:67], 0, v[170:171]
	s_mov_b32 m0, s85
	s_nop 0
	global_load_lds_dwordx4 v[196:197], off
	s_waitcnt vmcnt(8)
	s_waitcnt lgkmcnt(0)
	s_barrier
	s_setprio 1
	v_mfma_scale_f32_16x16x128_f8f6f4 v[158:161], v[2:9], v[188:195], v[158:161], v208, v209 op_sel_hi:[0,0,0]
	v_mfma_scale_f32_16x16x128_f8f6f4 v[154:157], v[10:17], v[188:195], v[154:157], v208, v209 op_sel_hi:[0,0,0]
	v_mfma_scale_f32_16x16x128_f8f6f4 v[142:145], v[2:9], v[214:221], v[142:145], v208, v209 op_sel_hi:[0,0,0]
	v_mfma_scale_f32_16x16x128_f8f6f4 v[138:141], v[10:17], v[214:221], v[138:141], v208, v209 op_sel_hi:[0,0,0]
	v_mfma_scale_f32_16x16x128_f8f6f4 v[126:129], v[2:9], v[222:229], v[126:129], v208, v209 op_sel_hi:[0,0,0]
	v_mfma_scale_f32_16x16x128_f8f6f4 v[122:125], v[10:17], v[222:229], v[122:125], v208, v209 op_sel_hi:[0,0,0]
	v_mfma_scale_f32_16x16x128_f8f6f4 v[110:113], v[2:9], v[230:237], v[110:113], v208, v209 op_sel_hi:[0,0,0]
	v_mfma_scale_f32_16x16x128_f8f6f4 v[106:109], v[10:17], v[230:237], v[106:109], v208, v209 op_sel_hi:[0,0,0]
	s_setprio 0
	s_setprio 1
	s_nop 0
	v_mfma_scale_f32_16x16x128_f8f6f4 v[150:153], v[18:25], v[188:195], v[150:153], v208, v209 op_sel_hi:[0,0,0]
	v_mfma_scale_f32_16x16x128_f8f6f4 v[146:149], v[26:33], v[188:195], v[146:149], v208, v209 op_sel_hi:[0,0,0]
	v_mfma_scale_f32_16x16x128_f8f6f4 v[134:137], v[18:25], v[214:221], v[134:137], v208, v209 op_sel_hi:[0,0,0]
	v_mfma_scale_f32_16x16x128_f8f6f4 v[130:133], v[26:33], v[214:221], v[130:133], v208, v209 op_sel_hi:[0,0,0]
	v_mfma_scale_f32_16x16x128_f8f6f4 v[118:121], v[18:25], v[222:229], v[118:121], v208, v209 op_sel_hi:[0,0,0]
	v_mfma_scale_f32_16x16x128_f8f6f4 v[114:117], v[26:33], v[222:229], v[114:117], v208, v209 op_sel_hi:[0,0,0]
	v_mfma_scale_f32_16x16x128_f8f6f4 v[102:105], v[18:25], v[230:237], v[102:105], v208, v209 op_sel_hi:[0,0,0]
	v_mfma_scale_f32_16x16x128_f8f6f4 v[98:101], v[26:33], v[230:237], v[98:101], v208, v209 op_sel_hi:[0,0,0]
	s_setprio 0
	s_barrier
	s_add_i32 s59, s59, s77
	v_lshl_add_u64 v[162:163], v[162:163], 0, s[40:41]
	s_mov_b32 m0, s59
	ds_read_b128 v[188:191], v207 offset:49152
	ds_read_b128 v[192:195], v207 offset:50176
	ds_read_b128 v[214:217], v207 offset:51200
	ds_read_b128 v[218:221], v207 offset:52224
	ds_read_b128 v[222:225], v207 offset:53248
	ds_read_b128 v[226:229], v207 offset:54272
	ds_read_b128 v[230:233], v207 offset:55296
	ds_read_b128 v[234:237], v207 offset:56320
	global_load_lds_dwordx4 v[162:163], off
	s_add_i32 m0, s59, 0x2000
	s_add_u32 s10, s10, 0x8080
	v_lshl_add_u64 v[162:163], v[164:165], 0, s[40:41]
	s_addc_u32 s11, s11, 0
	s_add_i32 s59, s61, s77
	global_load_lds_dwordx4 v[162:163], off
	v_lshl_add_u64 v[162:163], s[10:11], 0, v[168:169]
	s_mov_b32 m0, s59
	s_nop 0
	global_load_lds_dwordx4 v[162:163], off
	v_lshl_add_u64 v[162:163], s[10:11], 0, v[172:173]
	s_add_i32 m0, s59, 0x2000
	s_nop 0
	global_load_lds_dwordx4 v[162:163], off
	v_lshl_add_u64 v[162:163], v[184:185], 0, s[40:41]
	s_mov_b32 m0, s94
	s_nop 0
	global_load_lds_dwordx4 v[162:163], off
	v_lshl_add_u64 v[162:163], v[186:187], 0, s[40:41]
	s_mov_b32 m0, s95
	s_nop 0
	global_load_lds_dwordx4 v[162:163], off
	s_waitcnt vmcnt(8)
	s_waitcnt lgkmcnt(0)
	s_barrier
	s_setprio 1
	v_mfma_scale_f32_16x16x128_f8f6f4 v[94:97], v[2:9], v[188:195], v[94:97], v208, v209 op_sel_hi:[0,0,0]
	v_mfma_scale_f32_16x16x128_f8f6f4 v[90:93], v[10:17], v[188:195], v[90:93], v208, v209 op_sel_hi:[0,0,0]
	v_mfma_scale_f32_16x16x128_f8f6f4 v[78:81], v[2:9], v[214:221], v[78:81], v208, v209 op_sel_hi:[0,0,0]
	v_mfma_scale_f32_16x16x128_f8f6f4 v[74:77], v[10:17], v[214:221], v[74:77], v208, v209 op_sel_hi:[0,0,0]
	v_mfma_scale_f32_16x16x128_f8f6f4 v[62:65], v[2:9], v[222:229], v[62:65], v208, v209 op_sel_hi:[0,0,0]
	v_mfma_scale_f32_16x16x128_f8f6f4 v[58:61], v[10:17], v[222:229], v[58:61], v208, v209 op_sel_hi:[0,0,0]
	v_mfma_scale_f32_16x16x128_f8f6f4 v[46:49], v[2:9], v[230:237], v[46:49], v208, v209 op_sel_hi:[0,0,0]
	v_mfma_scale_f32_16x16x128_f8f6f4 v[42:45], v[10:17], v[230:237], v[42:45], v208, v209 op_sel_hi:[0,0,0]
	s_setprio 0
	s_setprio 1
	s_nop 0
	v_mfma_scale_f32_16x16x128_f8f6f4 v[86:89], v[18:25], v[188:195], v[86:89], v208, v209 op_sel_hi:[0,0,0]
	v_mfma_scale_f32_16x16x128_f8f6f4 v[82:85], v[26:33], v[188:195], v[82:85], v208, v209 op_sel_hi:[0,0,0]
	v_mfma_scale_f32_16x16x128_f8f6f4 v[70:73], v[18:25], v[214:221], v[70:73], v208, v209 op_sel_hi:[0,0,0]
	v_mfma_scale_f32_16x16x128_f8f6f4 v[66:69], v[26:33], v[214:221], v[66:69], v208, v209 op_sel_hi:[0,0,0]
	v_mfma_scale_f32_16x16x128_f8f6f4 v[54:57], v[18:25], v[222:229], v[54:57], v208, v209 op_sel_hi:[0,0,0]
	v_mfma_scale_f32_16x16x128_f8f6f4 v[50:53], v[26:33], v[222:229], v[50:53], v208, v209 op_sel_hi:[0,0,0]
	v_mfma_scale_f32_16x16x128_f8f6f4 v[38:41], v[18:25], v[230:237], v[38:41], v208, v209 op_sel_hi:[0,0,0]
	v_mfma_scale_f32_16x16x128_f8f6f4 v[34:37], v[26:33], v[230:237], v[34:37], v208, v209 op_sel_hi:[0,0,0]
	s_setprio 0
	s_barrier
	s_add_i32 s33, s33, 2
	s_add_u32 s8, s8, 0x100
	s_addc_u32 s9, s9, 0
	s_add_u32 s18, s18, 0x100
	s_addc_u32 s19, s19, 0
	s_cmp_gt_u32 s33, 5
	s_cbranch_scc0 .LBB0_153
	s_and_b64 vcc, exec, s[42:43]
	s_cbranch_vccz .LBB0_156
	s_barrier

; #define PG8_STAGE(bufoff, gbase, voff) do { _Pragma("unroll") for (int _i = 0; _i < 2; ++_i) \
;         __builtin_amdgcn_global_load_lds((const unsigned*)((const char*)(gbase) + (voff)[_i]), (PG8_LAS unsigned*)(lds + (bufoff) + ldsw + _i * 8192), 16, 0, 0); } while (0)
; #define PG8_STAGE_A(bufoff, gbase, h, nx) do { if constexpr (Sched::GATHER) { const unsigned vv_[2] = {(nx) ? vAn[h][0] : vA[h][0], (nx) ? vAn[h][1] : vA[h][1]}; PG8_STAGE(bufoff, gbase, vv_); } \
;         else { PG8_STAGE(bufoff, (gbase) + (h) * hstep, voffA); } } while (0)
; #define PG8_LDA(dst, b, h) do { _Pragma("unroll") for (int m = 0; m < 4; ++m) _Pragma("unroll") for (int k = 0; k < 2; ++k) dst[m][k] = *(const PG8_LAS bf16x8*)(lds + PG8_SA(b, h) + aoff + m * 2048 + k * 1024); } while (0)
; #define PG8_WAIT_V(n) asm volatile("s_waitcnt vmcnt(" #n ")" ::: "memory")
; #define PG8_WAIT_L(n) asm volatile("s_waitcnt lgkmcnt(" #n ")" ::: "memory")
;     ...
;         const bool has_next = S.next(ui + 1, nxt);
;         const char* nA = Sched::GATHER ? cA : (has_next ? (const char*)g.A + (size_t)nxt.pm * tstep : cA);
;         if constexpr (Sched::GATHER) { if (has_next) { PG8_AOFF(vAn, ui + 1); } else { _Pragma("unroll") for (int h_ = 0; h_ < 2; ++h_) _Pragma("unroll") for (int i_ = 0; i_ < 2; ++i_) vAn[h_][i_] = vA[h_][i_]; } } const char* nB = has_next ? (const char*)g.Bt + (size_t)nxt.pb * tstep : cB;
; #pragma nounroll
;         for (int t = 0; t < nt; t += 2) {
;             const bool last = (t == nt - 2);
;             const char* a1 = cA + (size_t)(t + 1) * kstep;
;             const char* a2 = last ? nA : cA + (size_t)(t + 2) * kstep; const char* b2 = last ? nB : cB + (size_t)(t + 2) * kstep;
;             const char* a3 = a2 + kstep; const char* b3 = b2 + kstep;
;             if (last && has_next) S.a_ready(nxt);
;             if constexpr (SP2) {
;             PG8_LDB(B0, 0, 0); PG8_LDB(B1, 0, 1); PG8_SCHED; PG8_LDA(At, 0, 0); PG8_STAGE_A(PG8_SA(1, 1), a1, 1, false);
;             PG8_WAIT_V(8); PG8_WAIT_L(0); PG8_BAR; PG8_MMA(0, 0, At, B0); PG8_MMA(0, 1, At, B1); PG8_BAR; PG8_SCHED;
;             PG8_LDA(At, 0, 1); PG8_STAGE(PG8_SB(0, 0), b2, voffB); PG8_STAGE(PG8_SB(0, 1), b2 + hstepB, voffB); PG8_STAGE_A(PG8_SA(0, 0), a2, 0, last);
;             PG8_WAIT_V(8); PG8_WAIT_L(0); PG8_BAR; PG8_MMA(1, 0, At, B0); PG8_MMA(1, 1, At, B1); PG8_BAR; PG8_SCHED;
.LBB0_473:
	s_ashr_i32 s15, s14, 31
	s_lshl_b64 s[16:17], s[14:15], 18
	v_readlane_b32 s18, v255, 21
	v_readlane_b32 s19, v255, 22
	s_add_u32 s16, s18, s16
	s_addc_u32 s17, s19, s17
	s_and_b64 s[18:19], s[2:3], exec
	s_cselect_b32 s1, s17, s23
	s_cselect_b32 s15, s16, s22
	s_ashr_i32 s13, s12, 31
	s_lshl_b64 s[18:19], s[12:13], 18
	v_readlane_b32 s26, v254, 53
	v_readlane_b32 s27, v254, 54
	s_add_u32 s18, s26, s18
	s_addc_u32 s19, s27, s19
	s_and_b64 s[26:27], s[2:3], exec
	s_cselect_b32 s13, s19, s25
	s_cselect_b32 s21, s18, s24
	s_add_u32 s22, s22, 0x20080
	s_addc_u32 s23, s23, 0
	s_add_u32 s33, s24, 0x100
	s_addc_u32 s42, s25, 0
	s_mov_b32 s43, -2
	ds_read_b128 v[26:29], v188
	ds_read_b128 v[30:33], v188 offset:1024
	ds_read_b128 v[18:21], v188 offset:2048
	ds_read_b128 v[22:25], v188 offset:3072
	ds_read_b128 v[10:13], v189
	ds_read_b128 v[14:17], v189 offset:1024
	ds_read_b128 v[2:5], v189 offset:2048
	ds_read_b128 v[6:9], v189 offset:3072
	s_add_u32 s24, s22, 0xfffe0080
	s_addc_u32 s25, s23, -1
	s_cmp_eq_u32 s43, 4
	s_cselect_b32 s27, s1, s25
	s_cselect_b32 s26, s15, s24
	s_cselect_b32 s25, s13, s42
	s_cselect_b32 s24, s21, s33
	v_lshl_add_u64 v[218:219], s[22:23], 0, v[170:171]
	s_add_i32 m0, s30, 0xc000
	ds_read_b128 v[178:181], v190
	ds_read_b128 v[182:185], v190 offset:1024
	ds_read_b128 v[194:197], v190 offset:2048
	ds_read_b128 v[198:201], v190 offset:3072
	ds_read_b128 v[202:205], v190 offset:4096
	ds_read_b128 v[206:209], v190 offset:5120
	ds_read_b128 v[210:213], v190 offset:6144
	ds_read_b128 v[214:217], v190 offset:7168
	global_load_lds_dwordx4 v[218:219], off
	v_lshl_add_u64 v[218:219], s[22:23], 0, v[172:173]
	s_add_i32 m0, s30, 0xe000
	s_nop 0
	global_load_lds_dwordx4 v[218:219], off
	s_waitcnt vmcnt(8)
	s_waitcnt lgkmcnt(0)
	s_barrier
	s_setprio 1
	v_mfma_scale_f32_16x16x128_f8f6f4 v[158:161], v[26:33], v[178:185], 0, v191, v192 op_sel_hi:[0,0,0]
	v_mfma_scale_f32_16x16x128_f8f6f4 v[154:157], v[18:25], v[178:185], 0, v191, v192 op_sel_hi:[0,0,0]
	v_mfma_scale_f32_16x16x128_f8f6f4 v[142:145], v[26:33], v[194:201], 0, v191, v192 op_sel_hi:[0,0,0]
	v_mfma_scale_f32_16x16x128_f8f6f4 v[138:141], v[18:25], v[194:201], 0, v191, v192 op_sel_hi:[0,0,0]
	v_mfma_scale_f32_16x16x128_f8f6f4 v[126:129], v[26:33], v[202:209], 0, v191, v192 op_sel_hi:[0,0,0]
	v_mfma_scale_f32_16x16x128_f8f6f4 v[122:125], v[18:25], v[202:209], 0, v191, v192 op_sel_hi:[0,0,0]
	v_mfma_scale_f32_16x16x128_f8f6f4 v[110:113], v[26:33], v[210:217], 0, v191, v192 op_sel_hi:[0,0,0]
	v_mfma_scale_f32_16x16x128_f8f6f4 v[106:109], v[18:25], v[210:217], 0, v191, v192 op_sel_hi:[0,0,0]
	s_setprio 0
	s_setprio 1
	s_nop 0
	v_mfma_scale_f32_16x16x128_f8f6f4 v[150:153], v[10:17], v[178:185], 0, v191, v192 op_sel_hi:[0,0,0]
	v_mfma_scale_f32_16x16x128_f8f6f4 v[146:149], v[2:9], v[178:185], 0, v191, v192 op_sel_hi:[0,0,0]
	v_mfma_scale_f32_16x16x128_f8f6f4 v[134:137], v[10:17], v[194:201], 0, v191, v192 op_sel_hi:[0,0,0]
	v_mfma_scale_f32_16x16x128_f8f6f4 v[130:133], v[2:9], v[194:201], 0, v191, v192 op_sel_hi:[0,0,0]
	v_mfma_scale_f32_16x16x128_f8f6f4 v[118:121], v[10:17], v[202:209], 0, v191, v192 op_sel_hi:[0,0,0]
	v_mfma_scale_f32_16x16x128_f8f6f4 v[114:117], v[2:9], v[202:209], 0, v191, v192 op_sel_hi:[0,0,0]
	v_mfma_scale_f32_16x16x128_f8f6f4 v[102:105], v[10:17], v[210:217], 0, v191, v192 op_sel_hi:[0,0,0]
	v_mfma_scale_f32_16x16x128_f8f6f4 v[98:101], v[2:9], v[210:217], 0, v191, v192 op_sel_hi:[0,0,0]
	s_setprio 0
	s_barrier
	s_add_i32 s44, s40, s28
	v_lshl_add_u64 v[178:179], s[24:25], 0, v[164:165]
	s_mov_b32 m0, s44
	ds_read_b128 v[194:197], v190 offset:16384
	ds_read_b128 v[198:201], v190 offset:17408
	ds_read_b128 v[202:205], v190 offset:18432
	ds_read_b128 v[206:209], v190 offset:19456
	ds_read_b128 v[210:213], v190 offset:20480
	ds_read_b128 v[214:217], v190 offset:21504
	ds_read_b128 v[218:221], v190 offset:22528
	ds_read_b128 v[222:225], v190 offset:23552
	global_load_lds_dwordx4 v[178:179], off
	s_add_i32 m0, s44, 0x2000
	s_add_u32 s44, s24, 0x2000
	v_lshl_add_u64 v[180:181], s[24:25], 0, v[168:169]
	s_addc_u32 s45, s25, 0
	s_add_i32 s46, s41, s28
	global_load_lds_dwordx4 v[180:181], off
	v_lshl_add_u64 v[182:183], s[44:45], 0, v[164:165]
	s_mov_b32 m0, s46
	v_lshl_add_u64 v[184:185], s[26:27], 0, v[166:167]
	global_load_lds_dwordx4 v[182:183], off
	v_lshl_add_u64 v[182:183], s[44:45], 0, v[168:169]
	s_add_i32 m0, s46, 0x2000
	s_nop 0
	global_load_lds_dwordx4 v[182:183], off
	v_lshl_add_u64 v[182:183], s[26:27], 0, v[162:163]
	s_mov_b32 m0, s30
	s_nop 0
	global_load_lds_dwordx4 v[182:183], off
	s_mov_b32 m0, s31
	s_nop 0
	global_load_lds_dwordx4 v[184:185], off
	s_waitcnt vmcnt(8)
	s_waitcnt lgkmcnt(0)
	s_barrier
	s_setprio 1
	v_mfma_scale_f32_16x16x128_f8f6f4 v[94:97], v[26:33], v[194:201], 0, v191, v192 op_sel_hi:[0,0,0]
	v_mfma_scale_f32_16x16x128_f8f6f4 v[90:93], v[18:25], v[194:201], 0, v191, v192 op_sel_hi:[0,0,0]
	v_mfma_scale_f32_16x16x128_f8f6f4 v[78:81], v[26:33], v[202:209], 0, v191, v192 op_sel_hi:[0,0,0]
	v_mfma_scale_f32_16x16x128_f8f6f4 v[74:77], v[18:25], v[202:209], 0, v191, v192 op_sel_hi:[0,0,0]
	v_mfma_scale_f32_16x16x128_f8f6f4 v[62:65], v[26:33], v[210:217], 0, v191, v192 op_sel_hi:[0,0,0]
	v_mfma_scale_f32_16x16x128_f8f6f4 v[58:61], v[18:25], v[210:217], 0, v191, v192 op_sel_hi:[0,0,0]
	v_mfma_scale_f32_16x16x128_f8f6f4 v[46:49], v[26:33], v[218:225], 0, v191, v192 op_sel_hi:[0,0,0]
	v_mfma_scale_f32_16x16x128_f8f6f4 v[42:45], v[18:25], v[218:225], 0, v191, v192 op_sel_hi:[0,0,0]
	s_setprio 0
	s_setprio 1
	s_nop 0
	v_mfma_scale_f32_16x16x128_f8f6f4 v[86:89], v[10:17], v[194:201], 0, v191, v192 op_sel_hi:[0,0,0]
	v_mfma_scale_f32_16x16x128_f8f6f4 v[82:85], v[2:9], v[194:201], 0, v191, v192 op_sel_hi:[0,0,0]
	v_mfma_scale_f32_16x16x128_f8f6f4 v[70:73], v[10:17], v[202:209], 0, v191, v192 op_sel_hi:[0,0,0]
	v_mfma_scale_f32_16x16x128_f8f6f4 v[66:69], v[2:9], v[202:209], 0, v191, v192 op_sel_hi:[0,0,0]
	v_mfma_scale_f32_16x16x128_f8f6f4 v[54:57], v[10:17], v[210:217], 0, v191, v192 op_sel_hi:[0,0,0]
	v_mfma_scale_f32_16x16x128_f8f6f4 v[50:53], v[2:9], v[210:217], 0, v191, v192 op_sel_hi:[0,0,0]
	v_mfma_scale_f32_16x16x128_f8f6f4 v[38:41], v[10:17], v[218:225], 0, v191, v192 op_sel_hi:[0,0,0]
	v_mfma_scale_f32_16x16x128_f8f6f4 v[34:37], v[2:9], v[218:225], 0, v191, v192 op_sel_hi:[0,0,0]
	s_setprio 0
	s_barrier
; #define PG8_STAGE(bufoff, gbase, voff) do { _Pragma("unroll") for (int _i = 0; _i < 2; ++_i) \
;         __builtin_amdgcn_global_load_lds((const unsigned*)((const char*)(gbase) + (voff)[_i]), (PG8_LAS unsigned*)(lds + (bufoff) + ldsw + _i * 8192), 16, 0, 0); } while (0)
; #define PG8_STAGE_A(bufoff, gbase, h, nx) do { if constexpr (Sched::GATHER) { const unsigned vv_[2] = {(nx) ? vAn[h][0] : vA[h][0], (nx) ? vAn[h][1] : vA[h][1]}; PG8_STAGE(bufoff, gbase, vv_); } \
;         else { PG8_STAGE(bufoff, (gbase) + (h) * hstep, voffA); } } while (0)
; #define PG8_LDA(dst, b, h) do { _Pragma("unroll") for (int m = 0; m < 4; ++m) _Pragma("unroll") for (int k = 0; k < 2; ++k) dst[m][k] = *(const PG8_LAS bf16x8*)(lds + PG8_SA(b, h) + aoff + m * 2048 + k * 1024); } while (0)
; #define PG8_LDB(dst, b, h) do { _Pragma("unroll") for (int n = 0; n < 2; ++n) _Pragma("unroll") for (int k = 0; k < 2; ++k) dst[n][k] = *(const PG8_LAS bf16x8*)(lds + PG8_SB(b, h) + boff + n * 2048 + k * 1024); } while (0)
; #define PG8_WAIT_V(n) asm volatile("s_waitcnt vmcnt(" #n ")" ::: "memory")
; #define PG8_WAIT_L(n) asm volatile("s_waitcnt lgkmcnt(" #n ")" ::: "memory")
; #define PG8_BAR __builtin_amdgcn_s_barrier()
; #define PG8_SCHED __builtin_amdgcn_sched_barrier(0)
;     ...
;             PG8_LDB(B0, 1, 0); PG8_LDB(B1, 1, 1); PG8_SCHED; PG8_LDA(At, 1, 0); PG8_STAGE_A(PG8_SA(0, 1), a2, 1, last);
;             PG8_WAIT_V(8); PG8_WAIT_L(0); PG8_BAR; PG8_MMA(0, 0, At, B0); PG8_MMA(0, 1, At, B1); PG8_BAR; PG8_SCHED;
;             PG8_LDA(At, 1, 1); PG8_STAGE(PG8_SB(1, 0), b3, voffB); PG8_STAGE(PG8_SB(1, 1), b3 + hstepB, voffB); PG8_STAGE_A(PG8_SA(1, 0), a3, 0, last);
;             PG8_WAIT_V(8); PG8_WAIT_L(0); PG8_BAR; PG8_MMA(1, 0, At, B0); PG8_MMA(1, 1, At, B1); PG8_BAR; PG8_SCHED;
	s_add_i32 s44, 0, 0x18000
	s_add_i32 s45, 0, 0x1c000
	v_add_u32_e32 v14, s44, v186
	v_add_u32_e32 v30, s45, v186
	ds_read_b128 v[2:5], v14
	ds_read_b128 v[6:9], v14 offset:1024
	ds_read_b128 v[10:13], v14 offset:2048
	ds_read_b128 v[14:17], v14 offset:3072
	ds_read_b128 v[18:21], v30
	ds_read_b128 v[22:25], v30 offset:1024
	ds_read_b128 v[26:29], v30 offset:2048
	ds_read_b128 v[30:33], v30 offset:3072
	s_add_u32 s26, s26, 0x20000
	s_addc_u32 s27, s27, 0
	s_mov_b32 m0, s34
	v_lshl_add_u64 v[226:227], s[26:27], 0, v[162:163]
	ds_read_b128 v[194:197], v190 offset:32768
	ds_read_b128 v[198:201], v190 offset:33792
	ds_read_b128 v[202:205], v190 offset:34816
	ds_read_b128 v[206:209], v190 offset:35840
	ds_read_b128 v[210:213], v190 offset:36864
	ds_read_b128 v[214:217], v190 offset:37888
	ds_read_b128 v[218:221], v190 offset:38912
	ds_read_b128 v[222:225], v190 offset:39936
	global_load_lds_dwordx4 v[226:227], off
	v_lshl_add_u64 v[226:227], s[26:27], 0, v[166:167]
	s_mov_b32 m0, s35
	s_nop 0
	global_load_lds_dwordx4 v[226:227], off
	s_waitcnt vmcnt(8)
	s_waitcnt lgkmcnt(0)
	s_barrier
	s_setprio 1
	v_mfma_scale_f32_16x16x128_f8f6f4 v[158:161], v[2:9], v[194:201], v[158:161], v191, v192 op_sel_hi:[0,0,0]
	v_mfma_scale_f32_16x16x128_f8f6f4 v[154:157], v[10:17], v[194:201], v[154:157], v191, v192 op_sel_hi:[0,0,0]
	v_mfma_scale_f32_16x16x128_f8f6f4 v[142:145], v[2:9], v[202:209], v[142:145], v191, v192 op_sel_hi:[0,0,0]
	v_mfma_scale_f32_16x16x128_f8f6f4 v[138:141], v[10:17], v[202:209], v[138:141], v191, v192 op_sel_hi:[0,0,0]
	v_mfma_scale_f32_16x16x128_f8f6f4 v[126:129], v[2:9], v[210:217], v[126:129], v191, v192 op_sel_hi:[0,0,0]
	v_mfma_scale_f32_16x16x128_f8f6f4 v[122:125], v[10:17], v[210:217], v[122:125], v191, v192 op_sel_hi:[0,0,0]
	v_mfma_scale_f32_16x16x128_f8f6f4 v[110:113], v[2:9], v[218:225], v[110:113], v191, v192 op_sel_hi:[0,0,0]
	v_mfma_scale_f32_16x16x128_f8f6f4 v[106:109], v[10:17], v[218:225], v[106:109], v191, v192 op_sel_hi:[0,0,0]
	s_setprio 0
	s_setprio 1
	s_nop 0
	v_mfma_scale_f32_16x16x128_f8f6f4 v[150:153], v[18:25], v[194:201], v[150:153], v191, v192 op_sel_hi:[0,0,0]
	v_mfma_scale_f32_16x16x128_f8f6f4 v[146:149], v[26:33], v[194:201], v[146:149], v191, v192 op_sel_hi:[0,0,0]
	v_mfma_scale_f32_16x16x128_f8f6f4 v[134:137], v[18:25], v[202:209], v[134:137], v191, v192 op_sel_hi:[0,0,0]
	v_mfma_scale_f32_16x16x128_f8f6f4 v[130:133], v[26:33], v[202:209], v[130:133], v191, v192 op_sel_hi:[0,0,0]
	v_mfma_scale_f32_16x16x128_f8f6f4 v[118:121], v[18:25], v[210:217], v[118:121], v191, v192 op_sel_hi:[0,0,0]
	v_mfma_scale_f32_16x16x128_f8f6f4 v[114:117], v[26:33], v[210:217], v[114:117], v191, v192 op_sel_hi:[0,0,0]
	v_mfma_scale_f32_16x16x128_f8f6f4 v[102:105], v[18:25], v[218:225], v[102:105], v191, v192 op_sel_hi:[0,0,0]
	v_mfma_scale_f32_16x16x128_f8f6f4 v[98:101], v[26:33], v[218:225], v[98:101], v191, v192 op_sel_hi:[0,0,0]
	s_setprio 0
	s_barrier
	s_add_i32 s26, s44, s28
	v_lshl_add_u64 v[178:179], v[178:179], 0, s[8:9]
	s_mov_b32 m0, s26
	ds_read_b128 v[194:197], v190 offset:49152
	ds_read_b128 v[198:201], v190 offset:50176
	ds_read_b128 v[202:205], v190 offset:51200
	ds_read_b128 v[206:209], v190 offset:52224
	ds_read_b128 v[210:213], v190 offset:53248
	ds_read_b128 v[214:217], v190 offset:54272
	ds_read_b128 v[218:221], v190 offset:55296
	ds_read_b128 v[222:225], v190 offset:56320
	global_load_lds_dwordx4 v[178:179], off
	s_add_i32 m0, s26, 0x2000
	s_add_u32 s24, s24, 0x2080
	v_lshl_add_u64 v[178:179], v[180:181], 0, s[8:9]
	s_addc_u32 s25, s25, 0
	s_add_i32 s26, s45, s28
	global_load_lds_dwordx4 v[178:179], off
	v_lshl_add_u64 v[178:179], s[24:25], 0, v[164:165]
	s_mov_b32 m0, s26
	s_nop 0
	global_load_lds_dwordx4 v[178:179], off
	v_lshl_add_u64 v[178:179], s[24:25], 0, v[168:169]
	s_add_i32 m0, s26, 0x2000
	s_nop 0
	global_load_lds_dwordx4 v[178:179], off
	v_lshl_add_u64 v[178:179], v[182:183], 0, s[8:9]
	s_mov_b32 m0, s38
	s_nop 0
	global_load_lds_dwordx4 v[178:179], off
	v_lshl_add_u64 v[178:179], v[184:185], 0, s[8:9]
	s_mov_b32 m0, s39
	s_nop 0
	global_load_lds_dwordx4 v[178:179], off
	s_waitcnt vmcnt(8)
	s_waitcnt lgkmcnt(0)
	s_barrier
	s_setprio 1
	v_mfma_scale_f32_16x16x128_f8f6f4 v[94:97], v[2:9], v[194:201], v[94:97], v191, v192 op_sel_hi:[0,0,0]
	v_mfma_scale_f32_16x16x128_f8f6f4 v[90:93], v[10:17], v[194:201], v[90:93], v191, v192 op_sel_hi:[0,0,0]
	v_mfma_scale_f32_16x16x128_f8f6f4 v[78:81], v[2:9], v[202:209], v[78:81], v191, v192 op_sel_hi:[0,0,0]
	v_mfma_scale_f32_16x16x128_f8f6f4 v[74:77], v[10:17], v[202:209], v[74:77], v191, v192 op_sel_hi:[0,0,0]
	v_mfma_scale_f32_16x16x128_f8f6f4 v[62:65], v[2:9], v[210:217], v[62:65], v191, v192 op_sel_hi:[0,0,0]
	v_mfma_scale_f32_16x16x128_f8f6f4 v[58:61], v[10:17], v[210:217], v[58:61], v191, v192 op_sel_hi:[0,0,0]
	v_mfma_scale_f32_16x16x128_f8f6f4 v[46:49], v[2:9], v[218:225], v[46:49], v191, v192 op_sel_hi:[0,0,0]
	v_mfma_scale_f32_16x16x128_f8f6f4 v[42:45], v[10:17], v[218:225], v[42:45], v191, v192 op_sel_hi:[0,0,0]
	s_setprio 0
	s_setprio 1
	s_nop 0
	v_mfma_scale_f32_16x16x128_f8f6f4 v[86:89], v[18:25], v[194:201], v[86:89], v191, v192 op_sel_hi:[0,0,0]
	v_mfma_scale_f32_16x16x128_f8f6f4 v[82:85], v[26:33], v[194:201], v[82:85], v191, v192 op_sel_hi:[0,0,0]
	v_mfma_scale_f32_16x16x128_f8f6f4 v[70:73], v[18:25], v[202:209], v[70:73], v191, v192 op_sel_hi:[0,0,0]
	v_mfma_scale_f32_16x16x128_f8f6f4 v[66:69], v[26:33], v[202:209], v[66:69], v191, v192 op_sel_hi:[0,0,0]
	v_mfma_scale_f32_16x16x128_f8f6f4 v[54:57], v[18:25], v[210:217], v[54:57], v191, v192 op_sel_hi:[0,0,0]
	v_mfma_scale_f32_16x16x128_f8f6f4 v[50:53], v[26:33], v[210:217], v[50:53], v191, v192 op_sel_hi:[0,0,0]
	v_mfma_scale_f32_16x16x128_f8f6f4 v[38:41], v[18:25], v[218:225], v[38:41], v191, v192 op_sel_hi:[0,0,0]
	v_mfma_scale_f32_16x16x128_f8f6f4 v[34:37], v[26:33], v[218:225], v[34:37], v191, v192 op_sel_hi:[0,0,0]
	s_setprio 0
	s_barrier
	s_add_i32 s43, s43, 2
	s_add_u32 s22, s22, 0x100
	s_addc_u32 s23, s23, 0
	s_add_u32 s33, s33, 0x100
	s_addc_u32 s42, s42, 0
; #define PG8_STAGE(bufoff, gbase, voff) do { _Pragma("unroll") for (int _i = 0; _i < 2; ++_i) \
;         __builtin_amdgcn_global_load_lds((const unsigned*)((const char*)(gbase) + (voff)[_i]), (PG8_LAS unsigned*)(lds + (bufoff) + ldsw + _i * 8192), 16, 0, 0); } while (0)
; #define PG8_STAGE_A(bufoff, gbase, h, nx) do { if constexpr (Sched::GATHER) { const unsigned vv_[2] = {(nx) ? vAn[h][0] : vA[h][0], (nx) ? vAn[h][1] : vA[h][1]}; PG8_STAGE(bufoff, gbase, vv_); } \
;         else { PG8_STAGE(bufoff, (gbase) + (h) * hstep, voffA); } } while (0)
; #define PG8_LDA(dst, b, h) do { _Pragma("unroll") for (int m = 0; m < 4; ++m) _Pragma("unroll") for (int k = 0; k < 2; ++k) dst[m][k] = *(const PG8_LAS bf16x8*)(lds + PG8_SA(b, h) + aoff + m * 2048 + k * 1024); } while (0)
; #define PG8_LDB(dst, b, h) do { _Pragma("unroll") for (int n = 0; n < 2; ++n) _Pragma("unroll") for (int k = 0; k < 2; ++k) dst[n][k] = *(const PG8_LAS bf16x8*)(lds + PG8_SB(b, h) + boff + n * 2048 + k * 1024); } while (0)
; #define PG8_WAIT_V(n) asm volatile("s_waitcnt vmcnt(" #n ")" ::: "memory")
; #define PG8_WAIT_L(n) asm volatile("s_waitcnt lgkmcnt(" #n ")" ::: "memory")
; #define PG8_BAR __builtin_amdgcn_s_barrier()
; #define PG8_SCHED __builtin_amdgcn_sched_barrier(0)
;     ...
;             PG8_LDB(B0, 0, 0); PG8_LDB(B1, 0, 1); PG8_SCHED; PG8_LDA(At, 0, 0); PG8_STAGE_A(PG8_SA(1, 1), a1, 1, false);
;             PG8_WAIT_V(8); PG8_WAIT_L(0); PG8_BAR; PG8_MMA(0, 0, At, B0); PG8_MMA(0, 1, At, B1); PG8_BAR; PG8_SCHED;
;             PG8_LDA(At, 0, 1); PG8_STAGE(PG8_SB(0, 0), b2, voffB); PG8_STAGE(PG8_SB(0, 1), b2 + hstepB, voffB); PG8_STAGE_A(PG8_SA(0, 0), a2, 0, last);
;             PG8_WAIT_V(8); PG8_WAIT_L(0); PG8_BAR; PG8_MMA(1, 0, At, B0); PG8_MMA(1, 1, At, B1); PG8_BAR; PG8_SCHED;
.LBB0_474:
	ds_read_b128 v[26:29], v188
	ds_read_b128 v[30:33], v188 offset:1024
	ds_read_b128 v[18:21], v188 offset:2048
	ds_read_b128 v[22:25], v188 offset:3072
	ds_read_b128 v[10:13], v189
	ds_read_b128 v[14:17], v189 offset:1024
	ds_read_b128 v[2:5], v189 offset:2048
	ds_read_b128 v[6:9], v189 offset:3072
	s_add_u32 s24, s22, 0xfffe0080
	s_addc_u32 s25, s23, -1
	s_cmp_eq_u32 s43, 4
	s_cselect_b32 s27, s1, s25
	s_cselect_b32 s26, s15, s24
	s_cselect_b32 s25, s13, s42
	s_cselect_b32 s24, s21, s33
	v_lshl_add_u64 v[218:219], s[22:23], 0, v[170:171]
	s_add_i32 m0, s30, 0xc000
	ds_read_b128 v[178:181], v190
	ds_read_b128 v[182:185], v190 offset:1024
	ds_read_b128 v[194:197], v190 offset:2048
	ds_read_b128 v[198:201], v190 offset:3072
	ds_read_b128 v[202:205], v190 offset:4096
	ds_read_b128 v[206:209], v190 offset:5120
	ds_read_b128 v[210:213], v190 offset:6144
	ds_read_b128 v[214:217], v190 offset:7168
	global_load_lds_dwordx4 v[218:219], off
	v_lshl_add_u64 v[218:219], s[22:23], 0, v[172:173]
	s_add_i32 m0, s30, 0xe000
	s_nop 0
	global_load_lds_dwordx4 v[218:219], off
	s_waitcnt vmcnt(8)
	s_waitcnt lgkmcnt(0)
	s_barrier
	s_setprio 1
	v_mfma_scale_f32_16x16x128_f8f6f4 v[158:161], v[26:33], v[178:185], v[158:161], v191, v192 op_sel_hi:[0,0,0]
	v_mfma_scale_f32_16x16x128_f8f6f4 v[154:157], v[18:25], v[178:185], v[154:157], v191, v192 op_sel_hi:[0,0,0]
	v_mfma_scale_f32_16x16x128_f8f6f4 v[142:145], v[26:33], v[194:201], v[142:145], v191, v192 op_sel_hi:[0,0,0]
	v_mfma_scale_f32_16x16x128_f8f6f4 v[138:141], v[18:25], v[194:201], v[138:141], v191, v192 op_sel_hi:[0,0,0]
	v_mfma_scale_f32_16x16x128_f8f6f4 v[126:129], v[26:33], v[202:209], v[126:129], v191, v192 op_sel_hi:[0,0,0]
	v_mfma_scale_f32_16x16x128_f8f6f4 v[122:125], v[18:25], v[202:209], v[122:125], v191, v192 op_sel_hi:[0,0,0]
	v_mfma_scale_f32_16x16x128_f8f6f4 v[110:113], v[26:33], v[210:217], v[110:113], v191, v192 op_sel_hi:[0,0,0]
	v_mfma_scale_f32_16x16x128_f8f6f4 v[106:109], v[18:25], v[210:217], v[106:109], v191, v192 op_sel_hi:[0,0,0]
	s_setprio 0
	s_setprio 1
	s_nop 0
	v_mfma_scale_f32_16x16x128_f8f6f4 v[150:153], v[10:17], v[178:185], v[150:153], v191, v192 op_sel_hi:[0,0,0]
	v_mfma_scale_f32_16x16x128_f8f6f4 v[146:149], v[2:9], v[178:185], v[146:149], v191, v192 op_sel_hi:[0,0,0]
	v_mfma_scale_f32_16x16x128_f8f6f4 v[134:137], v[10:17], v[194:201], v[134:137], v191, v192 op_sel_hi:[0,0,0]
	v_mfma_scale_f32_16x16x128_f8f6f4 v[130:133], v[2:9], v[194:201], v[130:133], v191, v192 op_sel_hi:[0,0,0]
	v_mfma_scale_f32_16x16x128_f8f6f4 v[118:121], v[10:17], v[202:209], v[118:121], v191, v192 op_sel_hi:[0,0,0]
	v_mfma_scale_f32_16x16x128_f8f6f4 v[114:117], v[2:9], v[202:209], v[114:117], v191, v192 op_sel_hi:[0,0,0]
	v_mfma_scale_f32_16x16x128_f8f6f4 v[102:105], v[10:17], v[210:217], v[102:105], v191, v192 op_sel_hi:[0,0,0]
	v_mfma_scale_f32_16x16x128_f8f6f4 v[98:101], v[2:9], v[210:217], v[98:101], v191, v192 op_sel_hi:[0,0,0]
	s_setprio 0
	s_barrier
	s_add_i32 s44, s40, s28
	v_lshl_add_u64 v[178:179], s[24:25], 0, v[164:165]
	s_mov_b32 m0, s44
	ds_read_b128 v[194:197], v190 offset:16384
	ds_read_b128 v[198:201], v190 offset:17408
	ds_read_b128 v[202:205], v190 offset:18432
	ds_read_b128 v[206:209], v190 offset:19456
	ds_read_b128 v[210:213], v190 offset:20480
	ds_read_b128 v[214:217], v190 offset:21504
	ds_read_b128 v[218:221], v190 offset:22528
	ds_read_b128 v[222:225], v190 offset:23552
	global_load_lds_dwordx4 v[178:179], off
	s_add_i32 m0, s44, 0x2000
	s_add_u32 s44, s24, 0x2000
	v_lshl_add_u64 v[180:181], s[24:25], 0, v[168:169]
	s_addc_u32 s45, s25, 0
	s_add_i32 s46, s41, s28
	global_load_lds_dwordx4 v[180:181], off
	v_lshl_add_u64 v[182:183], s[44:45], 0, v[164:165]
	s_mov_b32 m0, s46
	v_lshl_add_u64 v[184:185], s[26:27], 0, v[166:167]
	global_load_lds_dwordx4 v[182:183], off
	v_lshl_add_u64 v[182:183], s[44:45], 0, v[168:169]
	s_add_i32 m0, s46, 0x2000
	s_nop 0
	global_load_lds_dwordx4 v[182:183], off
	v_lshl_add_u64 v[182:183], s[26:27], 0, v[162:163]
	s_mov_b32 m0, s30
	s_nop 0
	global_load_lds_dwordx4 v[182:183], off
	s_mov_b32 m0, s31
	s_nop 0
	global_load_lds_dwordx4 v[184:185], off
	s_waitcnt vmcnt(8)
	s_waitcnt lgkmcnt(0)
	s_barrier
	s_setprio 1
	v_mfma_scale_f32_16x16x128_f8f6f4 v[94:97], v[26:33], v[194:201], v[94:97], v191, v192 op_sel_hi:[0,0,0]
	v_mfma_scale_f32_16x16x128_f8f6f4 v[90:93], v[18:25], v[194:201], v[90:93], v191, v192 op_sel_hi:[0,0,0]
	v_mfma_scale_f32_16x16x128_f8f6f4 v[78:81], v[26:33], v[202:209], v[78:81], v191, v192 op_sel_hi:[0,0,0]
	v_mfma_scale_f32_16x16x128_f8f6f4 v[74:77], v[18:25], v[202:209], v[74:77], v191, v192 op_sel_hi:[0,0,0]
	v_mfma_scale_f32_16x16x128_f8f6f4 v[62:65], v[26:33], v[210:217], v[62:65], v191, v192 op_sel_hi:[0,0,0]
	v_mfma_scale_f32_16x16x128_f8f6f4 v[58:61], v[18:25], v[210:217], v[58:61], v191, v192 op_sel_hi:[0,0,0]
	v_mfma_scale_f32_16x16x128_f8f6f4 v[46:49], v[26:33], v[218:225], v[46:49], v191, v192 op_sel_hi:[0,0,0]
	v_mfma_scale_f32_16x16x128_f8f6f4 v[42:45], v[18:25], v[218:225], v[42:45], v191, v192 op_sel_hi:[0,0,0]
	s_setprio 0
	s_setprio 1
	s_nop 0
	v_mfma_scale_f32_16x16x128_f8f6f4 v[86:89], v[10:17], v[194:201], v[86:89], v191, v192 op_sel_hi:[0,0,0]
	v_mfma_scale_f32_16x16x128_f8f6f4 v[82:85], v[2:9], v[194:201], v[82:85], v191, v192 op_sel_hi:[0,0,0]
	v_mfma_scale_f32_16x16x128_f8f6f4 v[70:73], v[10:17], v[202:209], v[70:73], v191, v192 op_sel_hi:[0,0,0]
	v_mfma_scale_f32_16x16x128_f8f6f4 v[66:69], v[2:9], v[202:209], v[66:69], v191, v192 op_sel_hi:[0,0,0]
	v_mfma_scale_f32_16x16x128_f8f6f4 v[54:57], v[10:17], v[210:217], v[54:57], v191, v192 op_sel_hi:[0,0,0]
	v_mfma_scale_f32_16x16x128_f8f6f4 v[50:53], v[2:9], v[210:217], v[50:53], v191, v192 op_sel_hi:[0,0,0]
	v_mfma_scale_f32_16x16x128_f8f6f4 v[38:41], v[10:17], v[218:225], v[38:41], v191, v192 op_sel_hi:[0,0,0]
	v_mfma_scale_f32_16x16x128_f8f6f4 v[34:37], v[2:9], v[218:225], v[34:37], v191, v192 op_sel_hi:[0,0,0]
	s_setprio 0
	s_barrier
; #define PG8_STAGE(bufoff, gbase, voff) do { _Pragma("unroll") for (int _i = 0; _i < 2; ++_i) \
;         __builtin_amdgcn_global_load_lds((const unsigned*)((const char*)(gbase) + (voff)[_i]), (PG8_LAS unsigned*)(lds + (bufoff) + ldsw + _i * 8192), 16, 0, 0); } while (0)
; #define PG8_STAGE_A(bufoff, gbase, h, nx) do { if constexpr (Sched::GATHER) { const unsigned vv_[2] = {(nx) ? vAn[h][0] : vA[h][0], (nx) ? vAn[h][1] : vA[h][1]}; PG8_STAGE(bufoff, gbase, vv_); } \
;         else { PG8_STAGE(bufoff, (gbase) + (h) * hstep, voffA); } } while (0)
; #define PG8_LDA(dst, b, h) do { _Pragma("unroll") for (int m = 0; m < 4; ++m) _Pragma("unroll") for (int k = 0; k < 2; ++k) dst[m][k] = *(const PG8_LAS bf16x8*)(lds + PG8_SA(b, h) + aoff + m * 2048 + k * 1024); } while (0)
; #define PG8_LDB(dst, b, h) do { _Pragma("unroll") for (int n = 0; n < 2; ++n) _Pragma("unroll") for (int k = 0; k < 2; ++k) dst[n][k] = *(const PG8_LAS bf16x8*)(lds + PG8_SB(b, h) + boff + n * 2048 + k * 1024); } while (0)
; #define PG8_WAIT_V(n) asm volatile("s_waitcnt vmcnt(" #n ")" ::: "memory")
; #define PG8_WAIT_L(n) asm volatile("s_waitcnt lgkmcnt(" #n ")" ::: "memory")
; #define PG8_BAR __builtin_amdgcn_s_barrier()
; #define PG8_SCHED __builtin_amdgcn_sched_barrier(0)
;     ...
;             PG8_LDB(B0, 1, 0); PG8_LDB(B1, 1, 1); PG8_SCHED; PG8_LDA(At, 1, 0); PG8_STAGE_A(PG8_SA(0, 1), a2, 1, last);
;             PG8_WAIT_V(8); PG8_WAIT_L(0); PG8_BAR; PG8_MMA(0, 0, At, B0); PG8_MMA(0, 1, At, B1); PG8_BAR; PG8_SCHED;
;             PG8_LDA(At, 1, 1); PG8_STAGE(PG8_SB(1, 0), b3, voffB); PG8_STAGE(PG8_SB(1, 1), b3 + hstepB, voffB); PG8_STAGE_A(PG8_SA(1, 0), a3, 0, last);
;             PG8_WAIT_V(8); PG8_WAIT_L(0); PG8_BAR; PG8_MMA(1, 0, At, B0); PG8_MMA(1, 1, At, B1); PG8_BAR; PG8_SCHED;
;     ...
;         }
;         if constexpr (F8) asm volatile("s_nop 15\n\ts_nop 15\n\ts_nop 15" ::: "memory");
;         if constexpr (ALIGN_EPI) { if (wr == 0) PG8_BAR; }
	s_add_i32 s44, 0, 0x18000
	s_add_i32 s45, 0, 0x1c000
	v_add_u32_e32 v14, s44, v186
	v_add_u32_e32 v30, s45, v186
	ds_read_b128 v[2:5], v14
	ds_read_b128 v[6:9], v14 offset:1024
	ds_read_b128 v[10:13], v14 offset:2048
	ds_read_b128 v[14:17], v14 offset:3072
	ds_read_b128 v[18:21], v30
	ds_read_b128 v[22:25], v30 offset:1024
	ds_read_b128 v[26:29], v30 offset:2048
	ds_read_b128 v[30:33], v30 offset:3072
	s_add_u32 s26, s26, 0x20000
	s_addc_u32 s27, s27, 0
	s_mov_b32 m0, s34
	v_lshl_add_u64 v[226:227], s[26:27], 0, v[162:163]
	ds_read_b128 v[194:197], v190 offset:32768
	ds_read_b128 v[198:201], v190 offset:33792
	ds_read_b128 v[202:205], v190 offset:34816
	ds_read_b128 v[206:209], v190 offset:35840
	ds_read_b128 v[210:213], v190 offset:36864
	ds_read_b128 v[214:217], v190 offset:37888
	ds_read_b128 v[218:221], v190 offset:38912
	ds_read_b128 v[222:225], v190 offset:39936
	global_load_lds_dwordx4 v[226:227], off
	v_lshl_add_u64 v[226:227], s[26:27], 0, v[166:167]
	s_mov_b32 m0, s35
	s_nop 0
	global_load_lds_dwordx4 v[226:227], off
	s_waitcnt vmcnt(8)
	s_waitcnt lgkmcnt(0)
	s_barrier
	s_setprio 1
	v_mfma_scale_f32_16x16x128_f8f6f4 v[158:161], v[2:9], v[194:201], v[158:161], v191, v192 op_sel_hi:[0,0,0]
	v_mfma_scale_f32_16x16x128_f8f6f4 v[154:157], v[10:17], v[194:201], v[154:157], v191, v192 op_sel_hi:[0,0,0]
	v_mfma_scale_f32_16x16x128_f8f6f4 v[142:145], v[2:9], v[202:209], v[142:145], v191, v192 op_sel_hi:[0,0,0]
	v_mfma_scale_f32_16x16x128_f8f6f4 v[138:141], v[10:17], v[202:209], v[138:141], v191, v192 op_sel_hi:[0,0,0]
	v_mfma_scale_f32_16x16x128_f8f6f4 v[126:129], v[2:9], v[210:217], v[126:129], v191, v192 op_sel_hi:[0,0,0]
	v_mfma_scale_f32_16x16x128_f8f6f4 v[122:125], v[10:17], v[210:217], v[122:125], v191, v192 op_sel_hi:[0,0,0]
	v_mfma_scale_f32_16x16x128_f8f6f4 v[110:113], v[2:9], v[218:225], v[110:113], v191, v192 op_sel_hi:[0,0,0]
	v_mfma_scale_f32_16x16x128_f8f6f4 v[106:109], v[10:17], v[218:225], v[106:109], v191, v192 op_sel_hi:[0,0,0]
	s_setprio 0
	s_setprio 1
	s_nop 0
	v_mfma_scale_f32_16x16x128_f8f6f4 v[150:153], v[18:25], v[194:201], v[150:153], v191, v192 op_sel_hi:[0,0,0]
	v_mfma_scale_f32_16x16x128_f8f6f4 v[146:149], v[26:33], v[194:201], v[146:149], v191, v192 op_sel_hi:[0,0,0]
	v_mfma_scale_f32_16x16x128_f8f6f4 v[134:137], v[18:25], v[202:209], v[134:137], v191, v192 op_sel_hi:[0,0,0]
	v_mfma_scale_f32_16x16x128_f8f6f4 v[130:133], v[26:33], v[202:209], v[130:133], v191, v192 op_sel_hi:[0,0,0]
	v_mfma_scale_f32_16x16x128_f8f6f4 v[118:121], v[18:25], v[210:217], v[118:121], v191, v192 op_sel_hi:[0,0,0]
	v_mfma_scale_f32_16x16x128_f8f6f4 v[114:117], v[26:33], v[210:217], v[114:117], v191, v192 op_sel_hi:[0,0,0]
	v_mfma_scale_f32_16x16x128_f8f6f4 v[102:105], v[18:25], v[218:225], v[102:105], v191, v192 op_sel_hi:[0,0,0]
	v_mfma_scale_f32_16x16x128_f8f6f4 v[98:101], v[26:33], v[218:225], v[98:101], v191, v192 op_sel_hi:[0,0,0]
	s_setprio 0
	s_barrier
	s_add_i32 s26, s44, s28
	v_lshl_add_u64 v[178:179], v[178:179], 0, s[8:9]
	s_mov_b32 m0, s26
	ds_read_b128 v[194:197], v190 offset:49152
	ds_read_b128 v[198:201], v190 offset:50176
	ds_read_b128 v[202:205], v190 offset:51200
	ds_read_b128 v[206:209], v190 offset:52224
	ds_read_b128 v[210:213], v190 offset:53248
	ds_read_b128 v[214:217], v190 offset:54272
	ds_read_b128 v[218:221], v190 offset:55296
	ds_read_b128 v[222:225], v190 offset:56320
	global_load_lds_dwordx4 v[178:179], off
	s_add_i32 m0, s26, 0x2000
	s_add_u32 s24, s24, 0x2080
	v_lshl_add_u64 v[178:179], v[180:181], 0, s[8:9]
	s_addc_u32 s25, s25, 0
	s_add_i32 s26, s45, s28
	global_load_lds_dwordx4 v[178:179], off
	v_lshl_add_u64 v[178:179], s[24:25], 0, v[164:165]
	s_mov_b32 m0, s26
	s_nop 0
	global_load_lds_dwordx4 v[178:179], off
	v_lshl_add_u64 v[178:179], s[24:25], 0, v[168:169]
	s_add_i32 m0, s26, 0x2000
	s_nop 0
	global_load_lds_dwordx4 v[178:179], off
	v_lshl_add_u64 v[178:179], v[182:183], 0, s[8:9]
	s_mov_b32 m0, s38
	s_nop 0
	global_load_lds_dwordx4 v[178:179], off
	v_lshl_add_u64 v[178:179], v[184:185], 0, s[8:9]
	s_mov_b32 m0, s39
	s_nop 0
	global_load_lds_dwordx4 v[178:179], off
	s_waitcnt vmcnt(8)
	s_waitcnt lgkmcnt(0)
	s_barrier
	s_setprio 1
	v_mfma_scale_f32_16x16x128_f8f6f4 v[94:97], v[2:9], v[194:201], v[94:97], v191, v192 op_sel_hi:[0,0,0]
	v_mfma_scale_f32_16x16x128_f8f6f4 v[90:93], v[10:17], v[194:201], v[90:93], v191, v192 op_sel_hi:[0,0,0]
	v_mfma_scale_f32_16x16x128_f8f6f4 v[78:81], v[2:9], v[202:209], v[78:81], v191, v192 op_sel_hi:[0,0,0]
	v_mfma_scale_f32_16x16x128_f8f6f4 v[74:77], v[10:17], v[202:209], v[74:77], v191, v192 op_sel_hi:[0,0,0]
	v_mfma_scale_f32_16x16x128_f8f6f4 v[62:65], v[2:9], v[210:217], v[62:65], v191, v192 op_sel_hi:[0,0,0]
	v_mfma_scale_f32_16x16x128_f8f6f4 v[58:61], v[10:17], v[210:217], v[58:61], v191, v192 op_sel_hi:[0,0,0]
	v_mfma_scale_f32_16x16x128_f8f6f4 v[46:49], v[2:9], v[218:225], v[46:49], v191, v192 op_sel_hi:[0,0,0]
	v_mfma_scale_f32_16x16x128_f8f6f4 v[42:45], v[10:17], v[218:225], v[42:45], v191, v192 op_sel_hi:[0,0,0]
	s_setprio 0
	s_setprio 1
	s_nop 0
	v_mfma_scale_f32_16x16x128_f8f6f4 v[86:89], v[18:25], v[194:201], v[86:89], v191, v192 op_sel_hi:[0,0,0]
	v_mfma_scale_f32_16x16x128_f8f6f4 v[82:85], v[26:33], v[194:201], v[82:85], v191, v192 op_sel_hi:[0,0,0]
	v_mfma_scale_f32_16x16x128_f8f6f4 v[70:73], v[18:25], v[202:209], v[70:73], v191, v192 op_sel_hi:[0,0,0]
	v_mfma_scale_f32_16x16x128_f8f6f4 v[66:69], v[26:33], v[202:209], v[66:69], v191, v192 op_sel_hi:[0,0,0]
	v_mfma_scale_f32_16x16x128_f8f6f4 v[54:57], v[18:25], v[210:217], v[54:57], v191, v192 op_sel_hi:[0,0,0]
	v_mfma_scale_f32_16x16x128_f8f6f4 v[50:53], v[26:33], v[210:217], v[50:53], v191, v192 op_sel_hi:[0,0,0]
	v_mfma_scale_f32_16x16x128_f8f6f4 v[38:41], v[18:25], v[218:225], v[38:41], v191, v192 op_sel_hi:[0,0,0]
	v_mfma_scale_f32_16x16x128_f8f6f4 v[34:37], v[26:33], v[218:225], v[34:37], v191, v192 op_sel_hi:[0,0,0]
	s_setprio 0
	s_barrier
	s_add_i32 s43, s43, 2
	s_add_u32 s22, s22, 0x100
	s_addc_u32 s23, s23, 0
	s_add_u32 s33, s33, 0x100
	s_addc_u32 s42, s42, 0
	s_cmp_gt_u32 s43, 5
	s_cbranch_scc0 .LBB0_474
	s_and_b64 vcc, exec, s[10:11]
	s_cbranch_vccz .LBB0_477
	s_barrier

; #define PG8_STAGE(bufoff, gbase, voff) do { _Pragma("unroll") for (int _i = 0; _i < 2; ++_i) \
;         __builtin_amdgcn_global_load_lds((const unsigned*)((const char*)(gbase) + (voff)[_i]), (PG8_LAS unsigned*)(lds + (bufoff) + ldsw + _i * 8192), 16, 0, 0); } while (0)
; #define PG8_STAGE_A(bufoff, gbase, h, nx) do { if constexpr (Sched::GATHER) { const unsigned vv_[2] = {(nx) ? vAn[h][0] : vA[h][0], (nx) ? vAn[h][1] : vA[h][1]}; PG8_STAGE(bufoff, gbase, vv_); } \
;         else { PG8_STAGE(bufoff, (gbase) + (h) * hstep, voffA); } } while (0)
; #define PG8_LDA(dst, b, h) do { _Pragma("unroll") for (int m = 0; m < 4; ++m) _Pragma("unroll") for (int k = 0; k < 2; ++k) dst[m][k] = *(const PG8_LAS bf16x8*)(lds + PG8_SA(b, h) + aoff + m * 2048 + k * 1024); } while (0)
; #define PG8_WAIT_V(n) asm volatile("s_waitcnt vmcnt(" #n ")" ::: "memory")
; #define PG8_WAIT_L(n) asm volatile("s_waitcnt lgkmcnt(" #n ")" ::: "memory")
;     ...
;         const bool has_next = S.next(ui + 1, nxt);
;         const char* nA = Sched::GATHER ? cA : (has_next ? (const char*)g.A + (size_t)nxt.pm * tstep : cA);
;         if constexpr (Sched::GATHER) { if (has_next) { PG8_AOFF(vAn, ui + 1); } else { _Pragma("unroll") for (int h_ = 0; h_ < 2; ++h_) _Pragma("unroll") for (int i_ = 0; i_ < 2; ++i_) vAn[h_][i_] = vA[h_][i_]; } } const char* nB = has_next ? (const char*)g.Bt + (size_t)nxt.pb * tstep : cB;
; #pragma nounroll
;         for (int t = 0; t < nt; t += 2) {
;             const bool last = (t == nt - 2);
;             const char* a1 = cA + (size_t)(t + 1) * kstep;
;             const char* a2 = last ? nA : cA + (size_t)(t + 2) * kstep; const char* b2 = last ? nB : cB + (size_t)(t + 2) * kstep;
;             const char* a3 = a2 + kstep; const char* b3 = b2 + kstep;
;             if (last && has_next) S.a_ready(nxt);
;             if constexpr (SP2) {
;             PG8_LDB(B0, 0, 0); PG8_LDB(B1, 0, 1); PG8_SCHED; PG8_LDA(At, 0, 0); PG8_STAGE_A(PG8_SA(1, 1), a1, 1, false);
;             PG8_WAIT_V(8); PG8_WAIT_L(0); PG8_BAR; PG8_MMA(0, 0, At, B0); PG8_MMA(0, 1, At, B1); PG8_BAR; PG8_SCHED;
;             PG8_LDA(At, 0, 1); PG8_STAGE(PG8_SB(0, 0), b2, voffB); PG8_STAGE(PG8_SB(0, 1), b2 + hstepB, voffB); PG8_STAGE_A(PG8_SA(0, 0), a2, 0, last);
;             PG8_WAIT_V(8); PG8_WAIT_L(0); PG8_BAR; PG8_MMA(1, 0, At, B0); PG8_MMA(1, 1, At, B1); PG8_BAR; PG8_SCHED;
.LBB0_840:
	s_ashr_i32 s17, s16, 31
	s_lshl_b64 s[18:19], s[16:17], 18
	v_readlane_b32 s22, v254, 61
	v_readlane_b32 s23, v254, 62
	s_add_u32 s18, s22, s18
	s_addc_u32 s19, s23, s19
	s_and_b64 s[4:5], s[4:5], exec
	s_cselect_b32 s17, s19, s21
	s_cselect_b32 s48, s18, s20
	v_mov_b32_e32 v175, v167
	v_mov_b32_e32 v177, v167
	s_add_u32 s49, s20, 0x100
	v_readlane_b32 s54, v254, 0
	v_lshl_add_u64 v[178:179], s[12:13], 0, v[176:177]
	v_lshl_add_u64 v[180:181], s[12:13], 0, v[174:175]
	s_addc_u32 s50, s21, 0
	s_mov_b32 s51, -2
	s_mov_b64 s[4:5], 0
	v_readlane_b32 s55, v254, 1
	ds_read_b128 v[26:29], v194
	ds_read_b128 v[30:33], v194 offset:1024
	ds_read_b128 v[18:21], v194 offset:2048
	ds_read_b128 v[22:25], v194 offset:3072
	ds_read_b128 v[10:13], v195
	ds_read_b128 v[14:17], v195 offset:1024
	ds_read_b128 v[2:5], v195 offset:2048
	ds_read_b128 v[6:9], v195 offset:3072
	s_add_u32 s20, s54, s4
	s_addc_u32 s21, s55, s5
	s_add_u32 s22, s20, 0x25400100
	s_addc_u32 s23, s21, 0
	s_add_u32 s52, s49, s4
	s_addc_u32 s53, s50, s5
	s_cmpk_eq_i32 s4, 0x300
	s_cselect_b64 vcc, -1, 0
	s_and_b64 s[20:21], vcc, exec
	s_cselect_b32 s23, s93, s23
	s_cselect_b32 s22, s92, s22
	s_cselect_b32 s21, s17, s53
	s_cselect_b32 s20, s48, s52
	s_mov_b32 m0, s36
	v_lshl_add_u64 v[232:233], v[180:181], 0, s[4:5]
	ds_read_b128 v[182:185], v196
	ds_read_b128 v[186:189], v196 offset:1024
	ds_read_b128 v[208:211], v196 offset:2048
	ds_read_b128 v[212:215], v196 offset:3072
	ds_read_b128 v[216:219], v196 offset:4096
	ds_read_b128 v[220:223], v196 offset:5120
	ds_read_b128 v[224:227], v196 offset:6144
	ds_read_b128 v[228:231], v196 offset:7168
	global_load_lds_dwordx4 v[232:233], off
	v_lshl_add_u64 v[232:233], v[178:179], 0, s[4:5]
	s_mov_b32 m0, s37
	s_nop 0
	global_load_lds_dwordx4 v[232:233], off
	s_waitcnt vmcnt(8)
	s_waitcnt lgkmcnt(0)
	s_barrier
	s_setprio 1
	v_mfma_scale_f32_16x16x128_f8f6f4 v[158:161], v[26:33], v[182:189], 0, v197, v198 op_sel_hi:[0,0,0]
	v_mfma_scale_f32_16x16x128_f8f6f4 v[150:153], v[18:25], v[182:189], 0, v197, v198 op_sel_hi:[0,0,0]
	v_mfma_scale_f32_16x16x128_f8f6f4 v[142:145], v[26:33], v[208:215], 0, v197, v198 op_sel_hi:[0,0,0]
	v_mfma_scale_f32_16x16x128_f8f6f4 v[134:137], v[18:25], v[208:215], 0, v197, v198 op_sel_hi:[0,0,0]
	v_mfma_scale_f32_16x16x128_f8f6f4 v[126:129], v[26:33], v[216:223], 0, v197, v198 op_sel_hi:[0,0,0]
	v_mfma_scale_f32_16x16x128_f8f6f4 v[118:121], v[18:25], v[216:223], 0, v197, v198 op_sel_hi:[0,0,0]
	v_mfma_scale_f32_16x16x128_f8f6f4 v[110:113], v[26:33], v[224:231], 0, v197, v198 op_sel_hi:[0,0,0]
	v_mfma_scale_f32_16x16x128_f8f6f4 v[98:101], v[18:25], v[224:231], 0, v197, v198 op_sel_hi:[0,0,0]
	s_setprio 0
	s_setprio 1
	s_nop 0
	v_mfma_scale_f32_16x16x128_f8f6f4 v[154:157], v[10:17], v[182:189], 0, v197, v198 op_sel_hi:[0,0,0]
	v_mfma_scale_f32_16x16x128_f8f6f4 v[146:149], v[2:9], v[182:189], 0, v197, v198 op_sel_hi:[0,0,0]
	v_mfma_scale_f32_16x16x128_f8f6f4 v[138:141], v[10:17], v[208:215], 0, v197, v198 op_sel_hi:[0,0,0]
	v_mfma_scale_f32_16x16x128_f8f6f4 v[130:133], v[2:9], v[208:215], 0, v197, v198 op_sel_hi:[0,0,0]
	v_mfma_scale_f32_16x16x128_f8f6f4 v[122:125], v[10:17], v[216:223], 0, v197, v198 op_sel_hi:[0,0,0]
	v_mfma_scale_f32_16x16x128_f8f6f4 v[114:117], v[2:9], v[216:223], 0, v197, v198 op_sel_hi:[0,0,0]
	v_mfma_scale_f32_16x16x128_f8f6f4 v[106:109], v[10:17], v[224:231], 0, v197, v198 op_sel_hi:[0,0,0]
	v_mfma_scale_f32_16x16x128_f8f6f4 v[94:97], v[2:9], v[224:231], 0, v197, v198 op_sel_hi:[0,0,0]
	s_setprio 0
	s_barrier
	s_mov_b32 m0, s38
	v_lshl_add_u64 v[182:183], s[20:21], 0, v[164:165]
	s_add_u32 s52, s20, 0x20000
	ds_read_b128 v[208:211], v196 offset:16384
	ds_read_b128 v[212:215], v196 offset:17408
	ds_read_b128 v[216:219], v196 offset:18432
	ds_read_b128 v[220:223], v196 offset:19456
	ds_read_b128 v[224:227], v196 offset:20480
	ds_read_b128 v[228:231], v196 offset:21504
	ds_read_b128 v[232:235], v196 offset:22528
	ds_read_b128 v[236:239], v196 offset:23552
	global_load_lds_dwordx4 v[182:183], off
	v_lshl_add_u64 v[184:185], s[20:21], 0, v[162:163]
	s_mov_b32 m0, s39
	s_addc_u32 s53, s21, 0
	global_load_lds_dwordx4 v[184:185], off
	v_lshl_add_u64 v[186:187], s[52:53], 0, v[164:165]
	s_mov_b32 m0, s40
	v_cndmask_b32_e32 v166, v206, v202, vcc
	global_load_lds_dwordx4 v[186:187], off
	v_lshl_add_u64 v[186:187], s[52:53], 0, v[162:163]
	s_mov_b32 m0, s41
	v_lshl_add_u64 v[188:189], s[22:23], 0, v[166:167]
	global_load_lds_dwordx4 v[186:187], off
	s_mov_b32 m0, s26
	v_cndmask_b32_e32 v186, v172, v203, vcc
	global_load_lds_dwordx4 v166, s[22:23]
	s_mov_b32 m0, s27
	v_mov_b32_e32 v187, v167
	global_load_lds_dwordx4 v186, s[22:23]
	s_waitcnt vmcnt(8)
	s_waitcnt lgkmcnt(0)
	v_lshl_add_u64 v[186:187], s[22:23], 0, v[186:187]
	s_barrier
	s_setprio 1
	s_nop 0
	s_waitcnt lgkmcnt(0)
	v_mfma_scale_f32_16x16x128_f8f6f4 v[82:85], v[26:33], v[208:215], 0, v197, v198 op_sel_hi:[0,0,0]
	v_mfma_scale_f32_16x16x128_f8f6f4 v[70:73], v[18:25], v[208:215], 0, v197, v198 op_sel_hi:[0,0,0]
	v_mfma_scale_f32_16x16x128_f8f6f4 v[78:81], v[26:33], v[216:223], 0, v197, v198 op_sel_hi:[0,0,0]
	v_mfma_scale_f32_16x16x128_f8f6f4 v[66:69], v[18:25], v[216:223], 0, v197, v198 op_sel_hi:[0,0,0]
	v_mfma_scale_f32_16x16x128_f8f6f4 v[58:61], v[26:33], v[224:231], 0, v197, v198 op_sel_hi:[0,0,0]
	v_mfma_scale_f32_16x16x128_f8f6f4 v[50:53], v[18:25], v[224:231], 0, v197, v198 op_sel_hi:[0,0,0]
	v_mfma_scale_f32_16x16x128_f8f6f4 v[42:45], v[26:33], v[232:239], 0, v197, v198 op_sel_hi:[0,0,0]
	v_mfma_scale_f32_16x16x128_f8f6f4 v[34:37], v[18:25], v[232:239], 0, v197, v198 op_sel_hi:[0,0,0]
	s_setprio 0
	s_setprio 1
	s_nop 0
	v_mfma_scale_f32_16x16x128_f8f6f4 v[102:105], v[10:17], v[208:215], 0, v197, v198 op_sel_hi:[0,0,0]
	v_mfma_scale_f32_16x16x128_f8f6f4 v[90:93], v[2:9], v[208:215], 0, v197, v198 op_sel_hi:[0,0,0]
	v_mfma_scale_f32_16x16x128_f8f6f4 v[86:89], v[10:17], v[216:223], 0, v197, v198 op_sel_hi:[0,0,0]
	v_mfma_scale_f32_16x16x128_f8f6f4 v[74:77], v[2:9], v[216:223], 0, v197, v198 op_sel_hi:[0,0,0]
	v_mfma_scale_f32_16x16x128_f8f6f4 v[62:65], v[10:17], v[224:231], 0, v197, v198 op_sel_hi:[0,0,0]
	v_mfma_scale_f32_16x16x128_f8f6f4 v[54:57], v[2:9], v[224:231], 0, v197, v198 op_sel_hi:[0,0,0]
	v_mfma_scale_f32_16x16x128_f8f6f4 v[46:49], v[10:17], v[232:239], 0, v197, v198 op_sel_hi:[0,0,0]
	v_mfma_scale_f32_16x16x128_f8f6f4 v[38:41], v[2:9], v[232:239], 0, v197, v198 op_sel_hi:[0,0,0]
	s_setprio 0
	s_barrier
; #define PG8_STAGE(bufoff, gbase, voff) do { _Pragma("unroll") for (int _i = 0; _i < 2; ++_i) \
;         __builtin_amdgcn_global_load_lds((const unsigned*)((const char*)(gbase) + (voff)[_i]), (PG8_LAS unsigned*)(lds + (bufoff) + ldsw + _i * 8192), 16, 0, 0); } while (0)
; #define PG8_STAGE_A(bufoff, gbase, h, nx) do { if constexpr (Sched::GATHER) { const unsigned vv_[2] = {(nx) ? vAn[h][0] : vA[h][0], (nx) ? vAn[h][1] : vA[h][1]}; PG8_STAGE(bufoff, gbase, vv_); } \
;         else { PG8_STAGE(bufoff, (gbase) + (h) * hstep, voffA); } } while (0)
; #define PG8_LDA(dst, b, h) do { _Pragma("unroll") for (int m = 0; m < 4; ++m) _Pragma("unroll") for (int k = 0; k < 2; ++k) dst[m][k] = *(const PG8_LAS bf16x8*)(lds + PG8_SA(b, h) + aoff + m * 2048 + k * 1024); } while (0)
; #define PG8_LDB(dst, b, h) do { _Pragma("unroll") for (int n = 0; n < 2; ++n) _Pragma("unroll") for (int k = 0; k < 2; ++k) dst[n][k] = *(const PG8_LAS bf16x8*)(lds + PG8_SB(b, h) + boff + n * 2048 + k * 1024); } while (0)
; #define PG8_WAIT_V(n) asm volatile("s_waitcnt vmcnt(" #n ")" ::: "memory")
; #define PG8_WAIT_L(n) asm volatile("s_waitcnt lgkmcnt(" #n ")" ::: "memory")
; #define PG8_BAR __builtin_amdgcn_s_barrier()
; #define PG8_SCHED __builtin_amdgcn_sched_barrier(0)
;     ...
;             PG8_LDB(B0, 1, 0); PG8_LDB(B1, 1, 1); PG8_SCHED; PG8_LDA(At, 1, 0); PG8_STAGE_A(PG8_SA(0, 1), a2, 1, last);
;             PG8_WAIT_V(8); PG8_WAIT_L(0); PG8_BAR; PG8_MMA(0, 0, At, B0); PG8_MMA(0, 1, At, B1); PG8_BAR; PG8_SCHED;
;             PG8_LDA(At, 1, 1); PG8_STAGE(PG8_SB(1, 0), b3, voffB); PG8_STAGE(PG8_SB(1, 1), b3 + hstepB, voffB); PG8_STAGE_A(PG8_SA(1, 0), a3, 0, last);
;             PG8_WAIT_V(8); PG8_WAIT_L(0); PG8_BAR; PG8_MMA(1, 0, At, B0); PG8_MMA(1, 1, At, B1); PG8_BAR; PG8_SCHED;
	ds_read_b128 v[2:5], v199
	ds_read_b128 v[6:9], v199 offset:1024
	ds_read_b128 v[10:13], v199 offset:2048
	ds_read_b128 v[14:17], v199 offset:3072
	ds_read_b128 v[18:21], v200
	ds_read_b128 v[22:25], v200 offset:1024
	ds_read_b128 v[26:29], v200 offset:2048
	ds_read_b128 v[30:33], v200 offset:3072
	s_mov_b32 m0, s28
	v_cndmask_b32_e32 v166, v174, v204, vcc
	ds_read_b128 v[208:211], v196 offset:32768
	ds_read_b128 v[212:215], v196 offset:33792
	ds_read_b128 v[216:219], v196 offset:34816
	ds_read_b128 v[220:223], v196 offset:35840
	ds_read_b128 v[224:227], v196 offset:36864
	ds_read_b128 v[228:231], v196 offset:37888
	ds_read_b128 v[232:235], v196 offset:38912
	ds_read_b128 v[236:239], v196 offset:39936
	v_cndmask_b32_e32 v175, v176, v205, vcc
	global_load_lds_dwordx4 v166, s[22:23]
	s_mov_b32 m0, s29
	s_nop 0
	global_load_lds_dwordx4 v175, s[22:23]
	s_waitcnt vmcnt(8)
	s_waitcnt lgkmcnt(0)
	s_barrier
	s_setprio 1
	v_mfma_scale_f32_16x16x128_f8f6f4 v[158:161], v[2:9], v[208:215], v[158:161], v197, v198 op_sel_hi:[0,0,0]
	v_mfma_scale_f32_16x16x128_f8f6f4 v[150:153], v[10:17], v[208:215], v[150:153], v197, v198 op_sel_hi:[0,0,0]
	v_mfma_scale_f32_16x16x128_f8f6f4 v[142:145], v[2:9], v[216:223], v[142:145], v197, v198 op_sel_hi:[0,0,0]
	v_mfma_scale_f32_16x16x128_f8f6f4 v[134:137], v[10:17], v[216:223], v[134:137], v197, v198 op_sel_hi:[0,0,0]
	v_mfma_scale_f32_16x16x128_f8f6f4 v[126:129], v[2:9], v[224:231], v[126:129], v197, v198 op_sel_hi:[0,0,0]
	v_mfma_scale_f32_16x16x128_f8f6f4 v[118:121], v[10:17], v[224:231], v[118:121], v197, v198 op_sel_hi:[0,0,0]
	v_mfma_scale_f32_16x16x128_f8f6f4 v[110:113], v[2:9], v[232:239], v[110:113], v197, v198 op_sel_hi:[0,0,0]
	v_mfma_scale_f32_16x16x128_f8f6f4 v[98:101], v[10:17], v[232:239], v[98:101], v197, v198 op_sel_hi:[0,0,0]
	s_setprio 0
	s_setprio 1
	s_nop 0
	v_mfma_scale_f32_16x16x128_f8f6f4 v[154:157], v[18:25], v[208:215], v[154:157], v197, v198 op_sel_hi:[0,0,0]
	v_mfma_scale_f32_16x16x128_f8f6f4 v[146:149], v[26:33], v[208:215], v[146:149], v197, v198 op_sel_hi:[0,0,0]
	v_mfma_scale_f32_16x16x128_f8f6f4 v[138:141], v[18:25], v[216:223], v[138:141], v197, v198 op_sel_hi:[0,0,0]
	v_mfma_scale_f32_16x16x128_f8f6f4 v[130:133], v[26:33], v[216:223], v[130:133], v197, v198 op_sel_hi:[0,0,0]
	v_mfma_scale_f32_16x16x128_f8f6f4 v[122:125], v[18:25], v[224:231], v[122:125], v197, v198 op_sel_hi:[0,0,0]
	v_mfma_scale_f32_16x16x128_f8f6f4 v[114:117], v[26:33], v[224:231], v[114:117], v197, v198 op_sel_hi:[0,0,0]
	v_mfma_scale_f32_16x16x128_f8f6f4 v[106:109], v[18:25], v[232:239], v[106:109], v197, v198 op_sel_hi:[0,0,0]
	v_mfma_scale_f32_16x16x128_f8f6f4 v[94:97], v[26:33], v[232:239], v[94:97], v197, v198 op_sel_hi:[0,0,0]
	s_setprio 0
	s_barrier
	s_mov_b32 m0, s42
	v_lshl_add_u64 v[182:183], v[182:183], 0, s[10:11]
	s_add_u32 s20, s20, 0x20080
	ds_read_b128 v[208:211], v196 offset:49152
	ds_read_b128 v[212:215], v196 offset:50176
	ds_read_b128 v[216:219], v196 offset:51200
	ds_read_b128 v[220:223], v196 offset:52224
	ds_read_b128 v[224:227], v196 offset:53248
	ds_read_b128 v[228:231], v196 offset:54272
	ds_read_b128 v[232:235], v196 offset:55296
	ds_read_b128 v[236:239], v196 offset:56320
	global_load_lds_dwordx4 v[182:183], off
	v_lshl_add_u64 v[182:183], v[184:185], 0, s[10:11]
	s_mov_b32 m0, s43
	s_addc_u32 s21, s21, 0
	global_load_lds_dwordx4 v[182:183], off
	v_lshl_add_u64 v[182:183], s[20:21], 0, v[164:165]
	s_mov_b32 m0, s44
	s_nop 0
	global_load_lds_dwordx4 v[182:183], off
	v_lshl_add_u64 v[182:183], s[20:21], 0, v[162:163]
	s_add_i32 m0, s44, 0x2000
	s_nop 0
	global_load_lds_dwordx4 v[182:183], off
	v_lshl_add_u64 v[182:183], v[188:189], 0, s[10:11]
	s_mov_b32 m0, s31
	s_nop 0
	global_load_lds_dwordx4 v[182:183], off
	v_lshl_add_u64 v[182:183], v[186:187], 0, s[10:11]
	s_mov_b32 m0, s34
	s_nop 0
	global_load_lds_dwordx4 v[182:183], off
	s_waitcnt vmcnt(8)
	s_waitcnt lgkmcnt(0)
	s_barrier
	s_setprio 1
	v_mfma_scale_f32_16x16x128_f8f6f4 v[82:85], v[2:9], v[208:215], v[82:85], v197, v198 op_sel_hi:[0,0,0]
	v_mfma_scale_f32_16x16x128_f8f6f4 v[70:73], v[10:17], v[208:215], v[70:73], v197, v198 op_sel_hi:[0,0,0]
	v_mfma_scale_f32_16x16x128_f8f6f4 v[78:81], v[2:9], v[216:223], v[78:81], v197, v198 op_sel_hi:[0,0,0]
	v_mfma_scale_f32_16x16x128_f8f6f4 v[66:69], v[10:17], v[216:223], v[66:69], v197, v198 op_sel_hi:[0,0,0]
	v_mfma_scale_f32_16x16x128_f8f6f4 v[58:61], v[2:9], v[224:231], v[58:61], v197, v198 op_sel_hi:[0,0,0]
	v_mfma_scale_f32_16x16x128_f8f6f4 v[50:53], v[10:17], v[224:231], v[50:53], v197, v198 op_sel_hi:[0,0,0]
	v_mfma_scale_f32_16x16x128_f8f6f4 v[42:45], v[2:9], v[232:239], v[42:45], v197, v198 op_sel_hi:[0,0,0]
	v_mfma_scale_f32_16x16x128_f8f6f4 v[34:37], v[10:17], v[232:239], v[34:37], v197, v198 op_sel_hi:[0,0,0]
	s_setprio 0
	s_setprio 1
	s_nop 0
	v_mfma_scale_f32_16x16x128_f8f6f4 v[102:105], v[18:25], v[208:215], v[102:105], v197, v198 op_sel_hi:[0,0,0]
	v_mfma_scale_f32_16x16x128_f8f6f4 v[90:93], v[26:33], v[208:215], v[90:93], v197, v198 op_sel_hi:[0,0,0]
	v_mfma_scale_f32_16x16x128_f8f6f4 v[86:89], v[18:25], v[216:223], v[86:89], v197, v198 op_sel_hi:[0,0,0]
	v_mfma_scale_f32_16x16x128_f8f6f4 v[74:77], v[26:33], v[216:223], v[74:77], v197, v198 op_sel_hi:[0,0,0]
	v_mfma_scale_f32_16x16x128_f8f6f4 v[62:65], v[18:25], v[224:231], v[62:65], v197, v198 op_sel_hi:[0,0,0]
	v_mfma_scale_f32_16x16x128_f8f6f4 v[54:57], v[26:33], v[224:231], v[54:57], v197, v198 op_sel_hi:[0,0,0]
	v_mfma_scale_f32_16x16x128_f8f6f4 v[46:49], v[18:25], v[232:239], v[46:49], v197, v198 op_sel_hi:[0,0,0]
	v_mfma_scale_f32_16x16x128_f8f6f4 v[38:41], v[26:33], v[232:239], v[38:41], v197, v198 op_sel_hi:[0,0,0]
	s_setprio 0
	s_barrier
	s_add_i32 s51, s51, 2
	s_add_u32 s4, s4, 0x100
	s_addc_u32 s5, s5, 0
; #define PG8_STAGE(bufoff, gbase, voff) do { _Pragma("unroll") for (int _i = 0; _i < 2; ++_i) \
;         __builtin_amdgcn_global_load_lds((const unsigned*)((const char*)(gbase) + (voff)[_i]), (PG8_LAS unsigned*)(lds + (bufoff) + ldsw + _i * 8192), 16, 0, 0); } while (0)
; #define PG8_STAGE_A(bufoff, gbase, h, nx) do { if constexpr (Sched::GATHER) { const unsigned vv_[2] = {(nx) ? vAn[h][0] : vA[h][0], (nx) ? vAn[h][1] : vA[h][1]}; PG8_STAGE(bufoff, gbase, vv_); } \
;         else { PG8_STAGE(bufoff, (gbase) + (h) * hstep, voffA); } } while (0)
; #define PG8_LDA(dst, b, h) do { _Pragma("unroll") for (int m = 0; m < 4; ++m) _Pragma("unroll") for (int k = 0; k < 2; ++k) dst[m][k] = *(const PG8_LAS bf16x8*)(lds + PG8_SA(b, h) + aoff + m * 2048 + k * 1024); } while (0)
; #define PG8_LDB(dst, b, h) do { _Pragma("unroll") for (int n = 0; n < 2; ++n) _Pragma("unroll") for (int k = 0; k < 2; ++k) dst[n][k] = *(const PG8_LAS bf16x8*)(lds + PG8_SB(b, h) + boff + n * 2048 + k * 1024); } while (0)
; #define PG8_WAIT_V(n) asm volatile("s_waitcnt vmcnt(" #n ")" ::: "memory")
; #define PG8_WAIT_L(n) asm volatile("s_waitcnt lgkmcnt(" #n ")" ::: "memory")
; #define PG8_BAR __builtin_amdgcn_s_barrier()
; #define PG8_SCHED __builtin_amdgcn_sched_barrier(0)
;     ...
;             PG8_LDB(B0, 0, 0); PG8_LDB(B1, 0, 1); PG8_SCHED; PG8_LDA(At, 0, 0); PG8_STAGE_A(PG8_SA(1, 1), a1, 1, false);
;             PG8_WAIT_V(8); PG8_WAIT_L(0); PG8_BAR; PG8_MMA(0, 0, At, B0); PG8_MMA(0, 1, At, B1); PG8_BAR; PG8_SCHED;
;             PG8_LDA(At, 0, 1); PG8_STAGE(PG8_SB(0, 0), b2, voffB); PG8_STAGE(PG8_SB(0, 1), b2 + hstepB, voffB); PG8_STAGE_A(PG8_SA(0, 0), a2, 0, last);
;             PG8_WAIT_V(8); PG8_WAIT_L(0); PG8_BAR; PG8_MMA(1, 0, At, B0); PG8_MMA(1, 1, At, B1); PG8_BAR; PG8_SCHED;
.LBB0_841:
	ds_read_b128 v[26:29], v194
	ds_read_b128 v[30:33], v194 offset:1024
	ds_read_b128 v[18:21], v194 offset:2048
	ds_read_b128 v[22:25], v194 offset:3072
	ds_read_b128 v[10:13], v195
	ds_read_b128 v[14:17], v195 offset:1024
	ds_read_b128 v[2:5], v195 offset:2048
	ds_read_b128 v[6:9], v195 offset:3072
	s_add_u32 s20, s54, s4
	s_addc_u32 s21, s55, s5
	s_add_u32 s22, s20, 0x25400100
	s_addc_u32 s23, s21, 0
	s_add_u32 s52, s49, s4
	s_addc_u32 s53, s50, s5
	s_cmpk_eq_i32 s4, 0x300
	s_cselect_b64 vcc, -1, 0
	s_and_b64 s[20:21], vcc, exec
	s_cselect_b32 s23, s93, s23
	s_cselect_b32 s22, s92, s22
	s_cselect_b32 s21, s17, s53
	s_cselect_b32 s20, s48, s52
	s_mov_b32 m0, s36
	v_lshl_add_u64 v[232:233], v[180:181], 0, s[4:5]
	ds_read_b128 v[182:185], v196
	ds_read_b128 v[186:189], v196 offset:1024
	ds_read_b128 v[208:211], v196 offset:2048
	ds_read_b128 v[212:215], v196 offset:3072
	ds_read_b128 v[216:219], v196 offset:4096
	ds_read_b128 v[220:223], v196 offset:5120
	ds_read_b128 v[224:227], v196 offset:6144
	ds_read_b128 v[228:231], v196 offset:7168
	global_load_lds_dwordx4 v[232:233], off
	v_lshl_add_u64 v[232:233], v[178:179], 0, s[4:5]
	s_mov_b32 m0, s37
	s_nop 0
	global_load_lds_dwordx4 v[232:233], off
	s_waitcnt vmcnt(8)
	s_waitcnt lgkmcnt(0)
	s_barrier
	s_setprio 1
	v_mfma_scale_f32_16x16x128_f8f6f4 v[158:161], v[26:33], v[182:189], v[158:161], v197, v198 op_sel_hi:[0,0,0]
	v_mfma_scale_f32_16x16x128_f8f6f4 v[150:153], v[18:25], v[182:189], v[150:153], v197, v198 op_sel_hi:[0,0,0]
	v_mfma_scale_f32_16x16x128_f8f6f4 v[142:145], v[26:33], v[208:215], v[142:145], v197, v198 op_sel_hi:[0,0,0]
	v_mfma_scale_f32_16x16x128_f8f6f4 v[134:137], v[18:25], v[208:215], v[134:137], v197, v198 op_sel_hi:[0,0,0]
	v_mfma_scale_f32_16x16x128_f8f6f4 v[126:129], v[26:33], v[216:223], v[126:129], v197, v198 op_sel_hi:[0,0,0]
	v_mfma_scale_f32_16x16x128_f8f6f4 v[118:121], v[18:25], v[216:223], v[118:121], v197, v198 op_sel_hi:[0,0,0]
	v_mfma_scale_f32_16x16x128_f8f6f4 v[110:113], v[26:33], v[224:231], v[110:113], v197, v198 op_sel_hi:[0,0,0]
	v_mfma_scale_f32_16x16x128_f8f6f4 v[98:101], v[18:25], v[224:231], v[98:101], v197, v198 op_sel_hi:[0,0,0]
	s_setprio 0
	s_setprio 1
	s_nop 0
	v_mfma_scale_f32_16x16x128_f8f6f4 v[154:157], v[10:17], v[182:189], v[154:157], v197, v198 op_sel_hi:[0,0,0]
	v_mfma_scale_f32_16x16x128_f8f6f4 v[146:149], v[2:9], v[182:189], v[146:149], v197, v198 op_sel_hi:[0,0,0]
	v_mfma_scale_f32_16x16x128_f8f6f4 v[138:141], v[10:17], v[208:215], v[138:141], v197, v198 op_sel_hi:[0,0,0]
	v_mfma_scale_f32_16x16x128_f8f6f4 v[130:133], v[2:9], v[208:215], v[130:133], v197, v198 op_sel_hi:[0,0,0]
	v_mfma_scale_f32_16x16x128_f8f6f4 v[122:125], v[10:17], v[216:223], v[122:125], v197, v198 op_sel_hi:[0,0,0]
	v_mfma_scale_f32_16x16x128_f8f6f4 v[114:117], v[2:9], v[216:223], v[114:117], v197, v198 op_sel_hi:[0,0,0]
	v_mfma_scale_f32_16x16x128_f8f6f4 v[106:109], v[10:17], v[224:231], v[106:109], v197, v198 op_sel_hi:[0,0,0]
	v_mfma_scale_f32_16x16x128_f8f6f4 v[94:97], v[2:9], v[224:231], v[94:97], v197, v198 op_sel_hi:[0,0,0]
	s_setprio 0
	s_barrier
	s_mov_b32 m0, s38
	v_lshl_add_u64 v[182:183], s[20:21], 0, v[164:165]
	s_add_u32 s52, s20, 0x20000
	ds_read_b128 v[208:211], v196 offset:16384
	ds_read_b128 v[212:215], v196 offset:17408
	ds_read_b128 v[216:219], v196 offset:18432
	ds_read_b128 v[220:223], v196 offset:19456
	ds_read_b128 v[224:227], v196 offset:20480
	ds_read_b128 v[228:231], v196 offset:21504
	ds_read_b128 v[232:235], v196 offset:22528
	ds_read_b128 v[236:239], v196 offset:23552
	global_load_lds_dwordx4 v[182:183], off
	v_lshl_add_u64 v[184:185], s[20:21], 0, v[162:163]
	s_mov_b32 m0, s39
	s_addc_u32 s53, s21, 0
	global_load_lds_dwordx4 v[184:185], off
	v_lshl_add_u64 v[186:187], s[52:53], 0, v[164:165]
	s_mov_b32 m0, s40
	v_cndmask_b32_e32 v166, v206, v202, vcc
	global_load_lds_dwordx4 v[186:187], off
	v_lshl_add_u64 v[186:187], s[52:53], 0, v[162:163]
	s_mov_b32 m0, s41
	v_lshl_add_u64 v[188:189], s[22:23], 0, v[166:167]
	global_load_lds_dwordx4 v[186:187], off
	s_mov_b32 m0, s26
	v_cndmask_b32_e32 v186, v172, v203, vcc
	global_load_lds_dwordx4 v166, s[22:23]
	s_mov_b32 m0, s27
	v_mov_b32_e32 v187, v167
	global_load_lds_dwordx4 v186, s[22:23]
	s_waitcnt vmcnt(8)
	s_waitcnt lgkmcnt(0)
	v_lshl_add_u64 v[186:187], s[22:23], 0, v[186:187]
	s_barrier
	s_setprio 1
	s_nop 0
	s_waitcnt lgkmcnt(0)
	v_mfma_scale_f32_16x16x128_f8f6f4 v[82:85], v[26:33], v[208:215], v[82:85], v197, v198 op_sel_hi:[0,0,0]
	v_mfma_scale_f32_16x16x128_f8f6f4 v[70:73], v[18:25], v[208:215], v[70:73], v197, v198 op_sel_hi:[0,0,0]
	v_mfma_scale_f32_16x16x128_f8f6f4 v[78:81], v[26:33], v[216:223], v[78:81], v197, v198 op_sel_hi:[0,0,0]
	v_mfma_scale_f32_16x16x128_f8f6f4 v[66:69], v[18:25], v[216:223], v[66:69], v197, v198 op_sel_hi:[0,0,0]
	v_mfma_scale_f32_16x16x128_f8f6f4 v[58:61], v[26:33], v[224:231], v[58:61], v197, v198 op_sel_hi:[0,0,0]
	v_mfma_scale_f32_16x16x128_f8f6f4 v[50:53], v[18:25], v[224:231], v[50:53], v197, v198 op_sel_hi:[0,0,0]
	v_mfma_scale_f32_16x16x128_f8f6f4 v[42:45], v[26:33], v[232:239], v[42:45], v197, v198 op_sel_hi:[0,0,0]
	v_mfma_scale_f32_16x16x128_f8f6f4 v[34:37], v[18:25], v[232:239], v[34:37], v197, v198 op_sel_hi:[0,0,0]
	s_setprio 0
	s_setprio 1
	s_nop 0
	v_mfma_scale_f32_16x16x128_f8f6f4 v[102:105], v[10:17], v[208:215], v[102:105], v197, v198 op_sel_hi:[0,0,0]
	v_mfma_scale_f32_16x16x128_f8f6f4 v[90:93], v[2:9], v[208:215], v[90:93], v197, v198 op_sel_hi:[0,0,0]
	v_mfma_scale_f32_16x16x128_f8f6f4 v[86:89], v[10:17], v[216:223], v[86:89], v197, v198 op_sel_hi:[0,0,0]
	v_mfma_scale_f32_16x16x128_f8f6f4 v[74:77], v[2:9], v[216:223], v[74:77], v197, v198 op_sel_hi:[0,0,0]
	v_mfma_scale_f32_16x16x128_f8f6f4 v[62:65], v[10:17], v[224:231], v[62:65], v197, v198 op_sel_hi:[0,0,0]
	v_mfma_scale_f32_16x16x128_f8f6f4 v[54:57], v[2:9], v[224:231], v[54:57], v197, v198 op_sel_hi:[0,0,0]
	v_mfma_scale_f32_16x16x128_f8f6f4 v[46:49], v[10:17], v[232:239], v[46:49], v197, v198 op_sel_hi:[0,0,0]
	v_mfma_scale_f32_16x16x128_f8f6f4 v[38:41], v[2:9], v[232:239], v[38:41], v197, v198 op_sel_hi:[0,0,0]
	s_setprio 0
	s_barrier
; #define PG8_STAGE(bufoff, gbase, voff) do { _Pragma("unroll") for (int _i = 0; _i < 2; ++_i) \
;         __builtin_amdgcn_global_load_lds((const unsigned*)((const char*)(gbase) + (voff)[_i]), (PG8_LAS unsigned*)(lds + (bufoff) + ldsw + _i * 8192), 16, 0, 0); } while (0)
; #define PG8_STAGE_A(bufoff, gbase, h, nx) do { if constexpr (Sched::GATHER) { const unsigned vv_[2] = {(nx) ? vAn[h][0] : vA[h][0], (nx) ? vAn[h][1] : vA[h][1]}; PG8_STAGE(bufoff, gbase, vv_); } \
;         else { PG8_STAGE(bufoff, (gbase) + (h) * hstep, voffA); } } while (0)
; #define PG8_LDA(dst, b, h) do { _Pragma("unroll") for (int m = 0; m < 4; ++m) _Pragma("unroll") for (int k = 0; k < 2; ++k) dst[m][k] = *(const PG8_LAS bf16x8*)(lds + PG8_SA(b, h) + aoff + m * 2048 + k * 1024); } while (0)
; #define PG8_LDB(dst, b, h) do { _Pragma("unroll") for (int n = 0; n < 2; ++n) _Pragma("unroll") for (int k = 0; k < 2; ++k) dst[n][k] = *(const PG8_LAS bf16x8*)(lds + PG8_SB(b, h) + boff + n * 2048 + k * 1024); } while (0)
; #define PG8_WAIT_V(n) asm volatile("s_waitcnt vmcnt(" #n ")" ::: "memory")
; #define PG8_WAIT_L(n) asm volatile("s_waitcnt lgkmcnt(" #n ")" ::: "memory")
; #define PG8_BAR __builtin_amdgcn_s_barrier()
; #define PG8_SCHED __builtin_amdgcn_sched_barrier(0)
;     ...
;             PG8_LDB(B0, 1, 0); PG8_LDB(B1, 1, 1); PG8_SCHED; PG8_LDA(At, 1, 0); PG8_STAGE_A(PG8_SA(0, 1), a2, 1, last);
;             PG8_WAIT_V(8); PG8_WAIT_L(0); PG8_BAR; PG8_MMA(0, 0, At, B0); PG8_MMA(0, 1, At, B1); PG8_BAR; PG8_SCHED;
;             PG8_LDA(At, 1, 1); PG8_STAGE(PG8_SB(1, 0), b3, voffB); PG8_STAGE(PG8_SB(1, 1), b3 + hstepB, voffB); PG8_STAGE_A(PG8_SA(1, 0), a3, 0, last);
;             PG8_WAIT_V(8); PG8_WAIT_L(0); PG8_BAR; PG8_MMA(1, 0, At, B0); PG8_MMA(1, 1, At, B1); PG8_BAR; PG8_SCHED;
;     ...
;         }
;         if constexpr (F8) asm volatile("s_nop 15\n\ts_nop 15\n\ts_nop 15" ::: "memory");
;         if constexpr (ALIGN_EPI) { if (wr == 0) PG8_BAR; }
	ds_read_b128 v[2:5], v199
	ds_read_b128 v[6:9], v199 offset:1024
	ds_read_b128 v[10:13], v199 offset:2048
	ds_read_b128 v[14:17], v199 offset:3072
	ds_read_b128 v[18:21], v200
	ds_read_b128 v[22:25], v200 offset:1024
	ds_read_b128 v[26:29], v200 offset:2048
	ds_read_b128 v[30:33], v200 offset:3072
	s_mov_b32 m0, s28
	v_cndmask_b32_e32 v166, v174, v204, vcc
	ds_read_b128 v[208:211], v196 offset:32768
	ds_read_b128 v[212:215], v196 offset:33792
	ds_read_b128 v[216:219], v196 offset:34816
	ds_read_b128 v[220:223], v196 offset:35840
	ds_read_b128 v[224:227], v196 offset:36864
	ds_read_b128 v[228:231], v196 offset:37888
	ds_read_b128 v[232:235], v196 offset:38912
	ds_read_b128 v[236:239], v196 offset:39936
	v_cndmask_b32_e32 v175, v176, v205, vcc
	global_load_lds_dwordx4 v166, s[22:23]
	s_mov_b32 m0, s29
	s_nop 0
	global_load_lds_dwordx4 v175, s[22:23]
	s_waitcnt vmcnt(8)
	s_waitcnt lgkmcnt(0)
	s_barrier
	s_setprio 1
	v_mfma_scale_f32_16x16x128_f8f6f4 v[158:161], v[2:9], v[208:215], v[158:161], v197, v198 op_sel_hi:[0,0,0]
	v_mfma_scale_f32_16x16x128_f8f6f4 v[150:153], v[10:17], v[208:215], v[150:153], v197, v198 op_sel_hi:[0,0,0]
	v_mfma_scale_f32_16x16x128_f8f6f4 v[142:145], v[2:9], v[216:223], v[142:145], v197, v198 op_sel_hi:[0,0,0]
	v_mfma_scale_f32_16x16x128_f8f6f4 v[134:137], v[10:17], v[216:223], v[134:137], v197, v198 op_sel_hi:[0,0,0]
	v_mfma_scale_f32_16x16x128_f8f6f4 v[126:129], v[2:9], v[224:231], v[126:129], v197, v198 op_sel_hi:[0,0,0]
	v_mfma_scale_f32_16x16x128_f8f6f4 v[118:121], v[10:17], v[224:231], v[118:121], v197, v198 op_sel_hi:[0,0,0]
	v_mfma_scale_f32_16x16x128_f8f6f4 v[110:113], v[2:9], v[232:239], v[110:113], v197, v198 op_sel_hi:[0,0,0]
	v_mfma_scale_f32_16x16x128_f8f6f4 v[98:101], v[10:17], v[232:239], v[98:101], v197, v198 op_sel_hi:[0,0,0]
	s_setprio 0
	s_setprio 1
	s_nop 0
	v_mfma_scale_f32_16x16x128_f8f6f4 v[154:157], v[18:25], v[208:215], v[154:157], v197, v198 op_sel_hi:[0,0,0]
	v_mfma_scale_f32_16x16x128_f8f6f4 v[146:149], v[26:33], v[208:215], v[146:149], v197, v198 op_sel_hi:[0,0,0]
	v_mfma_scale_f32_16x16x128_f8f6f4 v[138:141], v[18:25], v[216:223], v[138:141], v197, v198 op_sel_hi:[0,0,0]
	v_mfma_scale_f32_16x16x128_f8f6f4 v[130:133], v[26:33], v[216:223], v[130:133], v197, v198 op_sel_hi:[0,0,0]
	v_mfma_scale_f32_16x16x128_f8f6f4 v[122:125], v[18:25], v[224:231], v[122:125], v197, v198 op_sel_hi:[0,0,0]
	v_mfma_scale_f32_16x16x128_f8f6f4 v[114:117], v[26:33], v[224:231], v[114:117], v197, v198 op_sel_hi:[0,0,0]
	v_mfma_scale_f32_16x16x128_f8f6f4 v[106:109], v[18:25], v[232:239], v[106:109], v197, v198 op_sel_hi:[0,0,0]
	v_mfma_scale_f32_16x16x128_f8f6f4 v[94:97], v[26:33], v[232:239], v[94:97], v197, v198 op_sel_hi:[0,0,0]
	s_setprio 0
	s_barrier
	s_mov_b32 m0, s42
	v_lshl_add_u64 v[182:183], v[182:183], 0, s[10:11]
	s_add_u32 s20, s20, 0x20080
	ds_read_b128 v[208:211], v196 offset:49152
	ds_read_b128 v[212:215], v196 offset:50176
	ds_read_b128 v[216:219], v196 offset:51200
	ds_read_b128 v[220:223], v196 offset:52224
	ds_read_b128 v[224:227], v196 offset:53248
	ds_read_b128 v[228:231], v196 offset:54272
	ds_read_b128 v[232:235], v196 offset:55296
	ds_read_b128 v[236:239], v196 offset:56320
	global_load_lds_dwordx4 v[182:183], off
	v_lshl_add_u64 v[182:183], v[184:185], 0, s[10:11]
	s_mov_b32 m0, s43
	s_addc_u32 s21, s21, 0
	global_load_lds_dwordx4 v[182:183], off
	v_lshl_add_u64 v[182:183], s[20:21], 0, v[164:165]
	s_mov_b32 m0, s44
	s_nop 0
	global_load_lds_dwordx4 v[182:183], off
	v_lshl_add_u64 v[182:183], s[20:21], 0, v[162:163]
	s_add_i32 m0, s44, 0x2000
	s_nop 0
	global_load_lds_dwordx4 v[182:183], off
	v_lshl_add_u64 v[182:183], v[188:189], 0, s[10:11]
	s_mov_b32 m0, s31
	s_nop 0
	global_load_lds_dwordx4 v[182:183], off
	v_lshl_add_u64 v[182:183], v[186:187], 0, s[10:11]
	s_mov_b32 m0, s34
	s_nop 0
	global_load_lds_dwordx4 v[182:183], off
	s_waitcnt vmcnt(8)
	s_waitcnt lgkmcnt(0)
	s_barrier
	s_setprio 1
	v_mfma_scale_f32_16x16x128_f8f6f4 v[82:85], v[2:9], v[208:215], v[82:85], v197, v198 op_sel_hi:[0,0,0]
	v_mfma_scale_f32_16x16x128_f8f6f4 v[70:73], v[10:17], v[208:215], v[70:73], v197, v198 op_sel_hi:[0,0,0]
	v_mfma_scale_f32_16x16x128_f8f6f4 v[78:81], v[2:9], v[216:223], v[78:81], v197, v198 op_sel_hi:[0,0,0]
	v_mfma_scale_f32_16x16x128_f8f6f4 v[66:69], v[10:17], v[216:223], v[66:69], v197, v198 op_sel_hi:[0,0,0]
	v_mfma_scale_f32_16x16x128_f8f6f4 v[58:61], v[2:9], v[224:231], v[58:61], v197, v198 op_sel_hi:[0,0,0]
	v_mfma_scale_f32_16x16x128_f8f6f4 v[50:53], v[10:17], v[224:231], v[50:53], v197, v198 op_sel_hi:[0,0,0]
	v_mfma_scale_f32_16x16x128_f8f6f4 v[42:45], v[2:9], v[232:239], v[42:45], v197, v198 op_sel_hi:[0,0,0]
	v_mfma_scale_f32_16x16x128_f8f6f4 v[34:37], v[10:17], v[232:239], v[34:37], v197, v198 op_sel_hi:[0,0,0]
	s_setprio 0
	s_setprio 1
	s_nop 0
	v_mfma_scale_f32_16x16x128_f8f6f4 v[102:105], v[18:25], v[208:215], v[102:105], v197, v198 op_sel_hi:[0,0,0]
	v_mfma_scale_f32_16x16x128_f8f6f4 v[90:93], v[26:33], v[208:215], v[90:93], v197, v198 op_sel_hi:[0,0,0]
	v_mfma_scale_f32_16x16x128_f8f6f4 v[86:89], v[18:25], v[216:223], v[86:89], v197, v198 op_sel_hi:[0,0,0]
	v_mfma_scale_f32_16x16x128_f8f6f4 v[74:77], v[26:33], v[216:223], v[74:77], v197, v198 op_sel_hi:[0,0,0]
	v_mfma_scale_f32_16x16x128_f8f6f4 v[62:65], v[18:25], v[224:231], v[62:65], v197, v198 op_sel_hi:[0,0,0]
	v_mfma_scale_f32_16x16x128_f8f6f4 v[54:57], v[26:33], v[224:231], v[54:57], v197, v198 op_sel_hi:[0,0,0]
	v_mfma_scale_f32_16x16x128_f8f6f4 v[46:49], v[18:25], v[232:239], v[46:49], v197, v198 op_sel_hi:[0,0,0]
	v_mfma_scale_f32_16x16x128_f8f6f4 v[38:41], v[26:33], v[232:239], v[38:41], v197, v198 op_sel_hi:[0,0,0]
	s_setprio 0
	s_barrier
	s_add_i32 s51, s51, 2
	s_add_u32 s4, s4, 0x100
	s_addc_u32 s5, s5, 0
	s_cmp_gt_u32 s51, 5
	s_cbranch_scc0 .LBB0_841
	s_and_b64 vcc, exec, s[14:15]
	s_cbranch_vccz .LBB0_844
	s_barrier

; #define PG8_STAGE(bufoff, gbase, voff) do { _Pragma("unroll") for (int _i = 0; _i < 2; ++_i) \
;         __builtin_amdgcn_global_load_lds((const unsigned*)((const char*)(gbase) + (voff)[_i]), (PG8_LAS unsigned*)(lds + (bufoff) + ldsw + _i * 8192), 16, 0, 0); } while (0)
; #define PG8_STAGE_A(bufoff, gbase, h, nx) do { if constexpr (Sched::GATHER) { const unsigned vv_[2] = {(nx) ? vAn[h][0] : vA[h][0], (nx) ? vAn[h][1] : vA[h][1]}; PG8_STAGE(bufoff, gbase, vv_); } \
;         else { PG8_STAGE(bufoff, (gbase) + (h) * hstep, voffA); } } while (0)
; #define PG8_LDA(dst, b, h) do { _Pragma("unroll") for (int m = 0; m < 4; ++m) _Pragma("unroll") for (int k = 0; k < 2; ++k) dst[m][k] = *(const PG8_LAS bf16x8*)(lds + PG8_SA(b, h) + aoff + m * 2048 + k * 1024); } while (0)
; #define PG8_WAIT_V(n) asm volatile("s_waitcnt vmcnt(" #n ")" ::: "memory")
; #define PG8_WAIT_L(n) asm volatile("s_waitcnt lgkmcnt(" #n ")" ::: "memory")
;     ...
;         const bool has_next = S.next(ui + 1, nxt);
;         const char* nA = Sched::GATHER ? cA : (has_next ? (const char*)g.A + (size_t)nxt.pm * tstep : cA);
;         if constexpr (Sched::GATHER) { if (has_next) { PG8_AOFF(vAn, ui + 1); } else { _Pragma("unroll") for (int h_ = 0; h_ < 2; ++h_) _Pragma("unroll") for (int i_ = 0; i_ < 2; ++i_) vAn[h_][i_] = vA[h_][i_]; } } const char* nB = has_next ? (const char*)g.Bt + (size_t)nxt.pb * tstep : cB;
; #pragma nounroll
;         for (int t = 0; t < nt; t += 2) {
;             const bool last = (t == nt - 2);
;             const char* a1 = cA + (size_t)(t + 1) * kstep;
;             const char* a2 = last ? nA : cA + (size_t)(t + 2) * kstep; const char* b2 = last ? nB : cB + (size_t)(t + 2) * kstep;
;             const char* a3 = a2 + kstep; const char* b3 = b2 + kstep;
;             if (last && has_next) S.a_ready(nxt);
;             if constexpr (SP2) {
;             PG8_LDB(B0, 0, 0); PG8_LDB(B1, 0, 1); PG8_SCHED; PG8_LDA(At, 0, 0); PG8_STAGE_A(PG8_SA(1, 1), a1, 1, false);
;             PG8_WAIT_V(8); PG8_WAIT_L(0); PG8_BAR; PG8_MMA(0, 0, At, B0); PG8_MMA(0, 1, At, B1); PG8_BAR; PG8_SCHED;
;             PG8_LDA(At, 0, 1); PG8_STAGE(PG8_SB(0, 0), b2, voffB); PG8_STAGE(PG8_SB(0, 1), b2 + hstepB, voffB); PG8_STAGE_A(PG8_SA(0, 0), a2, 0, last);
;             PG8_WAIT_V(8); PG8_WAIT_L(0); PG8_BAR; PG8_MMA(1, 0, At, B0); PG8_MMA(1, 1, At, B1); PG8_BAR; PG8_SCHED;
.LBB0_894:
	s_ashr_i32 s13, s12, 31
	s_lshl_b64 s[16:17], s[12:13], 19
	v_readlane_b32 s18, v255, 9
	v_readlane_b32 s19, v255, 10
	s_add_u32 s16, s18, s16
	s_addc_u32 s17, s19, s17
	s_and_b64 s[18:19], s[2:3], exec
	s_cselect_b32 s13, s17, s23
	s_cselect_b32 s21, s16, s22
	s_ashr_i32 s15, s14, 31
	s_lshl_b64 s[18:19], s[14:15], 19
	v_readlane_b32 s26, v254, 63
	v_readlane_b32 s27, v255, 0
	s_add_u32 s18, s26, s18
	s_addc_u32 s19, s27, s19
	s_and_b64 s[26:27], s[2:3], exec
	s_cselect_b32 s15, s19, s25
	s_cselect_b32 s44, s18, s24
	s_add_u32 s22, s22, 0x40080
	s_addc_u32 s23, s23, 0
	s_add_u32 s45, s24, 0x100
	s_addc_u32 s46, s25, 0
	s_mov_b32 s47, -2
	ds_read_b128 v[26:29], v188
	ds_read_b128 v[30:33], v188 offset:1024
	ds_read_b128 v[18:21], v188 offset:2048
	ds_read_b128 v[22:25], v188 offset:3072
	ds_read_b128 v[10:13], v189
	ds_read_b128 v[14:17], v189 offset:1024
	ds_read_b128 v[2:5], v189 offset:2048
	ds_read_b128 v[6:9], v189 offset:3072
	s_add_u32 s24, s22, 0xfffc0080
	s_addc_u32 s25, s23, -1
	s_cmp_eq_u32 s47, 12
	s_cselect_b32 s27, s13, s25
	s_cselect_b32 s26, s21, s24
	s_cselect_b32 s25, s15, s46
	s_cselect_b32 s24, s44, s45
	v_lshl_add_u64 v[218:219], s[22:23], 0, v[170:171]
	s_add_i32 m0, s29, 0xc000
	ds_read_b128 v[178:181], v190
	ds_read_b128 v[182:185], v190 offset:1024
	ds_read_b128 v[194:197], v190 offset:2048
	ds_read_b128 v[198:201], v190 offset:3072
	ds_read_b128 v[202:205], v190 offset:4096
	ds_read_b128 v[206:209], v190 offset:5120
	ds_read_b128 v[210:213], v190 offset:6144
	ds_read_b128 v[214:217], v190 offset:7168
	global_load_lds_dwordx4 v[218:219], off
	v_lshl_add_u64 v[218:219], s[22:23], 0, v[172:173]
	s_add_i32 m0, s29, 0xe000
	s_nop 0
	global_load_lds_dwordx4 v[218:219], off
	s_waitcnt vmcnt(8)
	s_waitcnt lgkmcnt(0)
	s_barrier
	s_setprio 1
	v_mfma_scale_f32_16x16x128_f8f6f4 v[158:161], v[26:33], v[178:185], 0, v191, v192 op_sel_hi:[0,0,0]
	v_mfma_scale_f32_16x16x128_f8f6f4 v[154:157], v[18:25], v[178:185], 0, v191, v192 op_sel_hi:[0,0,0]
	v_mfma_scale_f32_16x16x128_f8f6f4 v[142:145], v[26:33], v[194:201], 0, v191, v192 op_sel_hi:[0,0,0]
	v_mfma_scale_f32_16x16x128_f8f6f4 v[138:141], v[18:25], v[194:201], 0, v191, v192 op_sel_hi:[0,0,0]
	v_mfma_scale_f32_16x16x128_f8f6f4 v[126:129], v[26:33], v[202:209], 0, v191, v192 op_sel_hi:[0,0,0]
	v_mfma_scale_f32_16x16x128_f8f6f4 v[122:125], v[18:25], v[202:209], 0, v191, v192 op_sel_hi:[0,0,0]
	v_mfma_scale_f32_16x16x128_f8f6f4 v[110:113], v[26:33], v[210:217], 0, v191, v192 op_sel_hi:[0,0,0]
	v_mfma_scale_f32_16x16x128_f8f6f4 v[106:109], v[18:25], v[210:217], 0, v191, v192 op_sel_hi:[0,0,0]
	s_setprio 0
	s_setprio 1
	s_nop 0
	v_mfma_scale_f32_16x16x128_f8f6f4 v[150:153], v[10:17], v[178:185], 0, v191, v192 op_sel_hi:[0,0,0]
	v_mfma_scale_f32_16x16x128_f8f6f4 v[146:149], v[2:9], v[178:185], 0, v191, v192 op_sel_hi:[0,0,0]
	v_mfma_scale_f32_16x16x128_f8f6f4 v[134:137], v[10:17], v[194:201], 0, v191, v192 op_sel_hi:[0,0,0]
	v_mfma_scale_f32_16x16x128_f8f6f4 v[130:133], v[2:9], v[194:201], 0, v191, v192 op_sel_hi:[0,0,0]
	v_mfma_scale_f32_16x16x128_f8f6f4 v[118:121], v[10:17], v[202:209], 0, v191, v192 op_sel_hi:[0,0,0]
	v_mfma_scale_f32_16x16x128_f8f6f4 v[114:117], v[2:9], v[202:209], 0, v191, v192 op_sel_hi:[0,0,0]
	v_mfma_scale_f32_16x16x128_f8f6f4 v[102:105], v[10:17], v[210:217], 0, v191, v192 op_sel_hi:[0,0,0]
	v_mfma_scale_f32_16x16x128_f8f6f4 v[98:101], v[2:9], v[210:217], 0, v191, v192 op_sel_hi:[0,0,0]
	s_setprio 0
	s_barrier
	s_add_i32 s48, s40, s28
	v_lshl_add_u64 v[178:179], s[24:25], 0, v[166:167]
	s_mov_b32 m0, s48
	ds_read_b128 v[194:197], v190 offset:16384
	ds_read_b128 v[198:201], v190 offset:17408
	ds_read_b128 v[202:205], v190 offset:18432
	ds_read_b128 v[206:209], v190 offset:19456
	ds_read_b128 v[210:213], v190 offset:20480
	ds_read_b128 v[214:217], v190 offset:21504
	ds_read_b128 v[218:221], v190 offset:22528
	ds_read_b128 v[222:225], v190 offset:23552
	global_load_lds_dwordx4 v[178:179], off
	s_add_i32 m0, s48, 0x2000
	s_add_u32 s48, s24, 0x4000
	v_lshl_add_u64 v[180:181], s[24:25], 0, v[162:163]
	s_addc_u32 s49, s25, 0
	s_add_i32 s50, s41, s28
	global_load_lds_dwordx4 v[180:181], off
	v_lshl_add_u64 v[182:183], s[48:49], 0, v[166:167]
	s_mov_b32 m0, s50
	v_lshl_add_u64 v[184:185], s[26:27], 0, v[164:165]
	global_load_lds_dwordx4 v[182:183], off
	v_lshl_add_u64 v[182:183], s[48:49], 0, v[162:163]
	s_add_i32 m0, s50, 0x2000
	s_nop 0
	global_load_lds_dwordx4 v[182:183], off
	v_lshl_add_u64 v[182:183], s[26:27], 0, v[168:169]
	s_mov_b32 m0, s29
	s_nop 0
	global_load_lds_dwordx4 v[182:183], off
	s_mov_b32 m0, s30
	s_nop 0
	global_load_lds_dwordx4 v[184:185], off
	s_waitcnt vmcnt(8)
	s_waitcnt lgkmcnt(0)
	s_barrier
	s_setprio 1
	v_mfma_scale_f32_16x16x128_f8f6f4 v[94:97], v[26:33], v[194:201], 0, v191, v192 op_sel_hi:[0,0,0]
	v_mfma_scale_f32_16x16x128_f8f6f4 v[90:93], v[18:25], v[194:201], 0, v191, v192 op_sel_hi:[0,0,0]
	v_mfma_scale_f32_16x16x128_f8f6f4 v[78:81], v[26:33], v[202:209], 0, v191, v192 op_sel_hi:[0,0,0]
	v_mfma_scale_f32_16x16x128_f8f6f4 v[74:77], v[18:25], v[202:209], 0, v191, v192 op_sel_hi:[0,0,0]
	v_mfma_scale_f32_16x16x128_f8f6f4 v[62:65], v[26:33], v[210:217], 0, v191, v192 op_sel_hi:[0,0,0]
	v_mfma_scale_f32_16x16x128_f8f6f4 v[58:61], v[18:25], v[210:217], 0, v191, v192 op_sel_hi:[0,0,0]
	v_mfma_scale_f32_16x16x128_f8f6f4 v[46:49], v[26:33], v[218:225], 0, v191, v192 op_sel_hi:[0,0,0]
	v_mfma_scale_f32_16x16x128_f8f6f4 v[42:45], v[18:25], v[218:225], 0, v191, v192 op_sel_hi:[0,0,0]
	s_setprio 0
	s_setprio 1
	s_nop 0
	v_mfma_scale_f32_16x16x128_f8f6f4 v[86:89], v[10:17], v[194:201], 0, v191, v192 op_sel_hi:[0,0,0]
	v_mfma_scale_f32_16x16x128_f8f6f4 v[82:85], v[2:9], v[194:201], 0, v191, v192 op_sel_hi:[0,0,0]
	v_mfma_scale_f32_16x16x128_f8f6f4 v[70:73], v[10:17], v[202:209], 0, v191, v192 op_sel_hi:[0,0,0]
	v_mfma_scale_f32_16x16x128_f8f6f4 v[66:69], v[2:9], v[202:209], 0, v191, v192 op_sel_hi:[0,0,0]
	v_mfma_scale_f32_16x16x128_f8f6f4 v[54:57], v[10:17], v[210:217], 0, v191, v192 op_sel_hi:[0,0,0]
	v_mfma_scale_f32_16x16x128_f8f6f4 v[50:53], v[2:9], v[210:217], 0, v191, v192 op_sel_hi:[0,0,0]
	v_mfma_scale_f32_16x16x128_f8f6f4 v[38:41], v[10:17], v[218:225], 0, v191, v192 op_sel_hi:[0,0,0]
	v_mfma_scale_f32_16x16x128_f8f6f4 v[34:37], v[2:9], v[218:225], 0, v191, v192 op_sel_hi:[0,0,0]
	s_setprio 0
	s_barrier
; #define PG8_STAGE(bufoff, gbase, voff) do { _Pragma("unroll") for (int _i = 0; _i < 2; ++_i) \
;         __builtin_amdgcn_global_load_lds((const unsigned*)((const char*)(gbase) + (voff)[_i]), (PG8_LAS unsigned*)(lds + (bufoff) + ldsw + _i * 8192), 16, 0, 0); } while (0)
; #define PG8_STAGE_A(bufoff, gbase, h, nx) do { if constexpr (Sched::GATHER) { const unsigned vv_[2] = {(nx) ? vAn[h][0] : vA[h][0], (nx) ? vAn[h][1] : vA[h][1]}; PG8_STAGE(bufoff, gbase, vv_); } \
;         else { PG8_STAGE(bufoff, (gbase) + (h) * hstep, voffA); } } while (0)
; #define PG8_LDA(dst, b, h) do { _Pragma("unroll") for (int m = 0; m < 4; ++m) _Pragma("unroll") for (int k = 0; k < 2; ++k) dst[m][k] = *(const PG8_LAS bf16x8*)(lds + PG8_SA(b, h) + aoff + m * 2048 + k * 1024); } while (0)
; #define PG8_LDB(dst, b, h) do { _Pragma("unroll") for (int n = 0; n < 2; ++n) _Pragma("unroll") for (int k = 0; k < 2; ++k) dst[n][k] = *(const PG8_LAS bf16x8*)(lds + PG8_SB(b, h) + boff + n * 2048 + k * 1024); } while (0)
; #define PG8_WAIT_V(n) asm volatile("s_waitcnt vmcnt(" #n ")" ::: "memory")
; #define PG8_WAIT_L(n) asm volatile("s_waitcnt lgkmcnt(" #n ")" ::: "memory")
; #define PG8_BAR __builtin_amdgcn_s_barrier()
; #define PG8_SCHED __builtin_amdgcn_sched_barrier(0)
;     ...
;             PG8_LDB(B0, 1, 0); PG8_LDB(B1, 1, 1); PG8_SCHED; PG8_LDA(At, 1, 0); PG8_STAGE_A(PG8_SA(0, 1), a2, 1, last);
;             PG8_WAIT_V(8); PG8_WAIT_L(0); PG8_BAR; PG8_MMA(0, 0, At, B0); PG8_MMA(0, 1, At, B1); PG8_BAR; PG8_SCHED;
;             PG8_LDA(At, 1, 1); PG8_STAGE(PG8_SB(1, 0), b3, voffB); PG8_STAGE(PG8_SB(1, 1), b3 + hstepB, voffB); PG8_STAGE_A(PG8_SA(1, 0), a3, 0, last);
;             PG8_WAIT_V(8); PG8_WAIT_L(0); PG8_BAR; PG8_MMA(1, 0, At, B0); PG8_MMA(1, 1, At, B1); PG8_BAR; PG8_SCHED;
	s_add_i32 s48, 0, 0x18000
	s_add_i32 s49, 0, 0x1c000
	v_add_u32_e32 v14, s48, v186
	v_add_u32_e32 v30, s49, v186
	ds_read_b128 v[2:5], v14
	ds_read_b128 v[6:9], v14 offset:1024
	ds_read_b128 v[10:13], v14 offset:2048
	ds_read_b128 v[14:17], v14 offset:3072
	ds_read_b128 v[18:21], v30
	ds_read_b128 v[22:25], v30 offset:1024
	ds_read_b128 v[26:29], v30 offset:2048
	ds_read_b128 v[30:33], v30 offset:3072
	s_add_u32 s26, s26, 0x40000
	s_addc_u32 s27, s27, 0
	s_mov_b32 m0, s31
	v_lshl_add_u64 v[226:227], s[26:27], 0, v[168:169]
	ds_read_b128 v[194:197], v190 offset:32768
	ds_read_b128 v[198:201], v190 offset:33792
	ds_read_b128 v[202:205], v190 offset:34816
	ds_read_b128 v[206:209], v190 offset:35840
	ds_read_b128 v[210:213], v190 offset:36864
	ds_read_b128 v[214:217], v190 offset:37888
	ds_read_b128 v[218:221], v190 offset:38912
	ds_read_b128 v[222:225], v190 offset:39936
	global_load_lds_dwordx4 v[226:227], off
	v_lshl_add_u64 v[226:227], s[26:27], 0, v[164:165]
	s_mov_b32 m0, s34
	s_nop 0
	global_load_lds_dwordx4 v[226:227], off
	s_waitcnt vmcnt(8)
	s_waitcnt lgkmcnt(0)
	s_barrier
	s_setprio 1
	v_mfma_scale_f32_16x16x128_f8f6f4 v[158:161], v[2:9], v[194:201], v[158:161], v191, v192 op_sel_hi:[0,0,0]
	v_mfma_scale_f32_16x16x128_f8f6f4 v[154:157], v[10:17], v[194:201], v[154:157], v191, v192 op_sel_hi:[0,0,0]
	v_mfma_scale_f32_16x16x128_f8f6f4 v[142:145], v[2:9], v[202:209], v[142:145], v191, v192 op_sel_hi:[0,0,0]
	v_mfma_scale_f32_16x16x128_f8f6f4 v[138:141], v[10:17], v[202:209], v[138:141], v191, v192 op_sel_hi:[0,0,0]
	v_mfma_scale_f32_16x16x128_f8f6f4 v[126:129], v[2:9], v[210:217], v[126:129], v191, v192 op_sel_hi:[0,0,0]
	v_mfma_scale_f32_16x16x128_f8f6f4 v[122:125], v[10:17], v[210:217], v[122:125], v191, v192 op_sel_hi:[0,0,0]
	v_mfma_scale_f32_16x16x128_f8f6f4 v[110:113], v[2:9], v[218:225], v[110:113], v191, v192 op_sel_hi:[0,0,0]
	v_mfma_scale_f32_16x16x128_f8f6f4 v[106:109], v[10:17], v[218:225], v[106:109], v191, v192 op_sel_hi:[0,0,0]
	s_setprio 0
	s_setprio 1
	s_nop 0
	v_mfma_scale_f32_16x16x128_f8f6f4 v[150:153], v[18:25], v[194:201], v[150:153], v191, v192 op_sel_hi:[0,0,0]
	v_mfma_scale_f32_16x16x128_f8f6f4 v[146:149], v[26:33], v[194:201], v[146:149], v191, v192 op_sel_hi:[0,0,0]
	v_mfma_scale_f32_16x16x128_f8f6f4 v[134:137], v[18:25], v[202:209], v[134:137], v191, v192 op_sel_hi:[0,0,0]
	v_mfma_scale_f32_16x16x128_f8f6f4 v[130:133], v[26:33], v[202:209], v[130:133], v191, v192 op_sel_hi:[0,0,0]
	v_mfma_scale_f32_16x16x128_f8f6f4 v[118:121], v[18:25], v[210:217], v[118:121], v191, v192 op_sel_hi:[0,0,0]
	v_mfma_scale_f32_16x16x128_f8f6f4 v[114:117], v[26:33], v[210:217], v[114:117], v191, v192 op_sel_hi:[0,0,0]
	v_mfma_scale_f32_16x16x128_f8f6f4 v[102:105], v[18:25], v[218:225], v[102:105], v191, v192 op_sel_hi:[0,0,0]
	v_mfma_scale_f32_16x16x128_f8f6f4 v[98:101], v[26:33], v[218:225], v[98:101], v191, v192 op_sel_hi:[0,0,0]
	s_setprio 0
	s_barrier
	s_add_i32 s26, s48, s28
	v_lshl_add_u64 v[178:179], v[178:179], 0, s[8:9]
	s_mov_b32 m0, s26
	ds_read_b128 v[194:197], v190 offset:49152
	ds_read_b128 v[198:201], v190 offset:50176
	ds_read_b128 v[202:205], v190 offset:51200
	ds_read_b128 v[206:209], v190 offset:52224
	ds_read_b128 v[210:213], v190 offset:53248
	ds_read_b128 v[214:217], v190 offset:54272
	ds_read_b128 v[218:221], v190 offset:55296
	ds_read_b128 v[222:225], v190 offset:56320
	global_load_lds_dwordx4 v[178:179], off
	s_add_i32 m0, s26, 0x2000
	s_add_u32 s24, s24, 0x4080
	v_lshl_add_u64 v[178:179], v[180:181], 0, s[8:9]
	s_addc_u32 s25, s25, 0
	s_add_i32 s26, s49, s28
	global_load_lds_dwordx4 v[178:179], off
	v_lshl_add_u64 v[178:179], s[24:25], 0, v[166:167]
	s_mov_b32 m0, s26
	s_nop 0
	global_load_lds_dwordx4 v[178:179], off
	v_lshl_add_u64 v[178:179], s[24:25], 0, v[162:163]
	s_add_i32 m0, s26, 0x2000
	s_nop 0
	global_load_lds_dwordx4 v[178:179], off
	v_lshl_add_u64 v[178:179], v[182:183], 0, s[8:9]
	s_mov_b32 m0, s38
	s_nop 0
	global_load_lds_dwordx4 v[178:179], off
	v_lshl_add_u64 v[178:179], v[184:185], 0, s[8:9]
	s_mov_b32 m0, s39
	s_nop 0
	global_load_lds_dwordx4 v[178:179], off
	s_waitcnt vmcnt(8)
	s_waitcnt lgkmcnt(0)
	s_barrier
	s_setprio 1
	v_mfma_scale_f32_16x16x128_f8f6f4 v[94:97], v[2:9], v[194:201], v[94:97], v191, v192 op_sel_hi:[0,0,0]
	v_mfma_scale_f32_16x16x128_f8f6f4 v[90:93], v[10:17], v[194:201], v[90:93], v191, v192 op_sel_hi:[0,0,0]
	v_mfma_scale_f32_16x16x128_f8f6f4 v[78:81], v[2:9], v[202:209], v[78:81], v191, v192 op_sel_hi:[0,0,0]
	v_mfma_scale_f32_16x16x128_f8f6f4 v[74:77], v[10:17], v[202:209], v[74:77], v191, v192 op_sel_hi:[0,0,0]
	v_mfma_scale_f32_16x16x128_f8f6f4 v[62:65], v[2:9], v[210:217], v[62:65], v191, v192 op_sel_hi:[0,0,0]
	v_mfma_scale_f32_16x16x128_f8f6f4 v[58:61], v[10:17], v[210:217], v[58:61], v191, v192 op_sel_hi:[0,0,0]
	v_mfma_scale_f32_16x16x128_f8f6f4 v[46:49], v[2:9], v[218:225], v[46:49], v191, v192 op_sel_hi:[0,0,0]
	v_mfma_scale_f32_16x16x128_f8f6f4 v[42:45], v[10:17], v[218:225], v[42:45], v191, v192 op_sel_hi:[0,0,0]
	s_setprio 0
	s_setprio 1
	s_nop 0
	v_mfma_scale_f32_16x16x128_f8f6f4 v[86:89], v[18:25], v[194:201], v[86:89], v191, v192 op_sel_hi:[0,0,0]
	v_mfma_scale_f32_16x16x128_f8f6f4 v[82:85], v[26:33], v[194:201], v[82:85], v191, v192 op_sel_hi:[0,0,0]
	v_mfma_scale_f32_16x16x128_f8f6f4 v[70:73], v[18:25], v[202:209], v[70:73], v191, v192 op_sel_hi:[0,0,0]
	v_mfma_scale_f32_16x16x128_f8f6f4 v[66:69], v[26:33], v[202:209], v[66:69], v191, v192 op_sel_hi:[0,0,0]
	v_mfma_scale_f32_16x16x128_f8f6f4 v[54:57], v[18:25], v[210:217], v[54:57], v191, v192 op_sel_hi:[0,0,0]
	v_mfma_scale_f32_16x16x128_f8f6f4 v[50:53], v[26:33], v[210:217], v[50:53], v191, v192 op_sel_hi:[0,0,0]
	v_mfma_scale_f32_16x16x128_f8f6f4 v[38:41], v[18:25], v[218:225], v[38:41], v191, v192 op_sel_hi:[0,0,0]
	v_mfma_scale_f32_16x16x128_f8f6f4 v[34:37], v[26:33], v[218:225], v[34:37], v191, v192 op_sel_hi:[0,0,0]
	s_setprio 0
	s_barrier
	s_add_i32 s47, s47, 2
	s_add_u32 s22, s22, 0x100
	s_addc_u32 s23, s23, 0
	s_add_u32 s45, s45, 0x100
	s_addc_u32 s46, s46, 0
; #define PG8_STAGE(bufoff, gbase, voff) do { _Pragma("unroll") for (int _i = 0; _i < 2; ++_i) \
;         __builtin_amdgcn_global_load_lds((const unsigned*)((const char*)(gbase) + (voff)[_i]), (PG8_LAS unsigned*)(lds + (bufoff) + ldsw + _i * 8192), 16, 0, 0); } while (0)
; #define PG8_STAGE_A(bufoff, gbase, h, nx) do { if constexpr (Sched::GATHER) { const unsigned vv_[2] = {(nx) ? vAn[h][0] : vA[h][0], (nx) ? vAn[h][1] : vA[h][1]}; PG8_STAGE(bufoff, gbase, vv_); } \
;         else { PG8_STAGE(bufoff, (gbase) + (h) * hstep, voffA); } } while (0)
; #define PG8_LDA(dst, b, h) do { _Pragma("unroll") for (int m = 0; m < 4; ++m) _Pragma("unroll") for (int k = 0; k < 2; ++k) dst[m][k] = *(const PG8_LAS bf16x8*)(lds + PG8_SA(b, h) + aoff + m * 2048 + k * 1024); } while (0)
; #define PG8_LDB(dst, b, h) do { _Pragma("unroll") for (int n = 0; n < 2; ++n) _Pragma("unroll") for (int k = 0; k < 2; ++k) dst[n][k] = *(const PG8_LAS bf16x8*)(lds + PG8_SB(b, h) + boff + n * 2048 + k * 1024); } while (0)
; #define PG8_WAIT_V(n) asm volatile("s_waitcnt vmcnt(" #n ")" ::: "memory")
; #define PG8_WAIT_L(n) asm volatile("s_waitcnt lgkmcnt(" #n ")" ::: "memory")
; #define PG8_BAR __builtin_amdgcn_s_barrier()
; #define PG8_SCHED __builtin_amdgcn_sched_barrier(0)
;     ...
;             PG8_LDB(B0, 0, 0); PG8_LDB(B1, 0, 1); PG8_SCHED; PG8_LDA(At, 0, 0); PG8_STAGE_A(PG8_SA(1, 1), a1, 1, false);
;             PG8_WAIT_V(8); PG8_WAIT_L(0); PG8_BAR; PG8_MMA(0, 0, At, B0); PG8_MMA(0, 1, At, B1); PG8_BAR; PG8_SCHED;
;             PG8_LDA(At, 0, 1); PG8_STAGE(PG8_SB(0, 0), b2, voffB); PG8_STAGE(PG8_SB(0, 1), b2 + hstepB, voffB); PG8_STAGE_A(PG8_SA(0, 0), a2, 0, last);
;             PG8_WAIT_V(8); PG8_WAIT_L(0); PG8_BAR; PG8_MMA(1, 0, At, B0); PG8_MMA(1, 1, At, B1); PG8_BAR; PG8_SCHED;
.LBB0_895:
	ds_read_b128 v[26:29], v188
	ds_read_b128 v[30:33], v188 offset:1024
	ds_read_b128 v[18:21], v188 offset:2048
	ds_read_b128 v[22:25], v188 offset:3072
	ds_read_b128 v[10:13], v189
	ds_read_b128 v[14:17], v189 offset:1024
	ds_read_b128 v[2:5], v189 offset:2048
	ds_read_b128 v[6:9], v189 offset:3072
	s_add_u32 s24, s22, 0xfffc0080
	s_addc_u32 s25, s23, -1
	s_cmp_eq_u32 s47, 12
	s_cselect_b32 s27, s13, s25
	s_cselect_b32 s26, s21, s24
	s_cselect_b32 s25, s15, s46
	s_cselect_b32 s24, s44, s45
	v_lshl_add_u64 v[218:219], s[22:23], 0, v[170:171]
	s_add_i32 m0, s29, 0xc000
	ds_read_b128 v[178:181], v190
	ds_read_b128 v[182:185], v190 offset:1024
	ds_read_b128 v[194:197], v190 offset:2048
	ds_read_b128 v[198:201], v190 offset:3072
	ds_read_b128 v[202:205], v190 offset:4096
	ds_read_b128 v[206:209], v190 offset:5120
	ds_read_b128 v[210:213], v190 offset:6144
	ds_read_b128 v[214:217], v190 offset:7168
	global_load_lds_dwordx4 v[218:219], off
	v_lshl_add_u64 v[218:219], s[22:23], 0, v[172:173]
	s_add_i32 m0, s29, 0xe000
	s_nop 0
	global_load_lds_dwordx4 v[218:219], off
	s_waitcnt vmcnt(8)
	s_waitcnt lgkmcnt(0)
	s_barrier
	s_setprio 1
	v_mfma_scale_f32_16x16x128_f8f6f4 v[158:161], v[26:33], v[178:185], v[158:161], v191, v192 op_sel_hi:[0,0,0]
	v_mfma_scale_f32_16x16x128_f8f6f4 v[154:157], v[18:25], v[178:185], v[154:157], v191, v192 op_sel_hi:[0,0,0]
	v_mfma_scale_f32_16x16x128_f8f6f4 v[142:145], v[26:33], v[194:201], v[142:145], v191, v192 op_sel_hi:[0,0,0]
	v_mfma_scale_f32_16x16x128_f8f6f4 v[138:141], v[18:25], v[194:201], v[138:141], v191, v192 op_sel_hi:[0,0,0]
	v_mfma_scale_f32_16x16x128_f8f6f4 v[126:129], v[26:33], v[202:209], v[126:129], v191, v192 op_sel_hi:[0,0,0]
	v_mfma_scale_f32_16x16x128_f8f6f4 v[122:125], v[18:25], v[202:209], v[122:125], v191, v192 op_sel_hi:[0,0,0]
	v_mfma_scale_f32_16x16x128_f8f6f4 v[110:113], v[26:33], v[210:217], v[110:113], v191, v192 op_sel_hi:[0,0,0]
	v_mfma_scale_f32_16x16x128_f8f6f4 v[106:109], v[18:25], v[210:217], v[106:109], v191, v192 op_sel_hi:[0,0,0]
	s_setprio 0
	s_setprio 1
	s_nop 0
	v_mfma_scale_f32_16x16x128_f8f6f4 v[150:153], v[10:17], v[178:185], v[150:153], v191, v192 op_sel_hi:[0,0,0]
	v_mfma_scale_f32_16x16x128_f8f6f4 v[146:149], v[2:9], v[178:185], v[146:149], v191, v192 op_sel_hi:[0,0,0]
	v_mfma_scale_f32_16x16x128_f8f6f4 v[134:137], v[10:17], v[194:201], v[134:137], v191, v192 op_sel_hi:[0,0,0]
	v_mfma_scale_f32_16x16x128_f8f6f4 v[130:133], v[2:9], v[194:201], v[130:133], v191, v192 op_sel_hi:[0,0,0]
	v_mfma_scale_f32_16x16x128_f8f6f4 v[118:121], v[10:17], v[202:209], v[118:121], v191, v192 op_sel_hi:[0,0,0]
	v_mfma_scale_f32_16x16x128_f8f6f4 v[114:117], v[2:9], v[202:209], v[114:117], v191, v192 op_sel_hi:[0,0,0]
	v_mfma_scale_f32_16x16x128_f8f6f4 v[102:105], v[10:17], v[210:217], v[102:105], v191, v192 op_sel_hi:[0,0,0]
	v_mfma_scale_f32_16x16x128_f8f6f4 v[98:101], v[2:9], v[210:217], v[98:101], v191, v192 op_sel_hi:[0,0,0]
	s_setprio 0
	s_barrier
	s_add_i32 s48, s40, s28
	v_lshl_add_u64 v[178:179], s[24:25], 0, v[166:167]
	s_mov_b32 m0, s48
	ds_read_b128 v[194:197], v190 offset:16384
	ds_read_b128 v[198:201], v190 offset:17408
	ds_read_b128 v[202:205], v190 offset:18432
	ds_read_b128 v[206:209], v190 offset:19456
	ds_read_b128 v[210:213], v190 offset:20480
	ds_read_b128 v[214:217], v190 offset:21504
	ds_read_b128 v[218:221], v190 offset:22528
	ds_read_b128 v[222:225], v190 offset:23552
	global_load_lds_dwordx4 v[178:179], off
	s_add_i32 m0, s48, 0x2000
	s_add_u32 s48, s24, 0x4000
	v_lshl_add_u64 v[180:181], s[24:25], 0, v[162:163]
	s_addc_u32 s49, s25, 0
	s_add_i32 s50, s41, s28
	global_load_lds_dwordx4 v[180:181], off
	v_lshl_add_u64 v[182:183], s[48:49], 0, v[166:167]
	s_mov_b32 m0, s50
	v_lshl_add_u64 v[184:185], s[26:27], 0, v[164:165]
	global_load_lds_dwordx4 v[182:183], off
	v_lshl_add_u64 v[182:183], s[48:49], 0, v[162:163]
	s_add_i32 m0, s50, 0x2000
	s_nop 0
	global_load_lds_dwordx4 v[182:183], off
	v_lshl_add_u64 v[182:183], s[26:27], 0, v[168:169]
	s_mov_b32 m0, s29
	s_nop 0
	global_load_lds_dwordx4 v[182:183], off
	s_mov_b32 m0, s30
	s_nop 0
	global_load_lds_dwordx4 v[184:185], off
	s_waitcnt vmcnt(8)
	s_waitcnt lgkmcnt(0)
	s_barrier
	s_setprio 1
	v_mfma_scale_f32_16x16x128_f8f6f4 v[94:97], v[26:33], v[194:201], v[94:97], v191, v192 op_sel_hi:[0,0,0]
	v_mfma_scale_f32_16x16x128_f8f6f4 v[90:93], v[18:25], v[194:201], v[90:93], v191, v192 op_sel_hi:[0,0,0]
	v_mfma_scale_f32_16x16x128_f8f6f4 v[78:81], v[26:33], v[202:209], v[78:81], v191, v192 op_sel_hi:[0,0,0]
	v_mfma_scale_f32_16x16x128_f8f6f4 v[74:77], v[18:25], v[202:209], v[74:77], v191, v192 op_sel_hi:[0,0,0]
	v_mfma_scale_f32_16x16x128_f8f6f4 v[62:65], v[26:33], v[210:217], v[62:65], v191, v192 op_sel_hi:[0,0,0]
	v_mfma_scale_f32_16x16x128_f8f6f4 v[58:61], v[18:25], v[210:217], v[58:61], v191, v192 op_sel_hi:[0,0,0]
	v_mfma_scale_f32_16x16x128_f8f6f4 v[46:49], v[26:33], v[218:225], v[46:49], v191, v192 op_sel_hi:[0,0,0]
	v_mfma_scale_f32_16x16x128_f8f6f4 v[42:45], v[18:25], v[218:225], v[42:45], v191, v192 op_sel_hi:[0,0,0]
	s_setprio 0
	s_setprio 1
	s_nop 0
	v_mfma_scale_f32_16x16x128_f8f6f4 v[86:89], v[10:17], v[194:201], v[86:89], v191, v192 op_sel_hi:[0,0,0]
	v_mfma_scale_f32_16x16x128_f8f6f4 v[82:85], v[2:9], v[194:201], v[82:85], v191, v192 op_sel_hi:[0,0,0]
	v_mfma_scale_f32_16x16x128_f8f6f4 v[70:73], v[10:17], v[202:209], v[70:73], v191, v192 op_sel_hi:[0,0,0]
	v_mfma_scale_f32_16x16x128_f8f6f4 v[66:69], v[2:9], v[202:209], v[66:69], v191, v192 op_sel_hi:[0,0,0]
	v_mfma_scale_f32_16x16x128_f8f6f4 v[54:57], v[10:17], v[210:217], v[54:57], v191, v192 op_sel_hi:[0,0,0]
	v_mfma_scale_f32_16x16x128_f8f6f4 v[50:53], v[2:9], v[210:217], v[50:53], v191, v192 op_sel_hi:[0,0,0]
	v_mfma_scale_f32_16x16x128_f8f6f4 v[38:41], v[10:17], v[218:225], v[38:41], v191, v192 op_sel_hi:[0,0,0]
	v_mfma_scale_f32_16x16x128_f8f6f4 v[34:37], v[2:9], v[218:225], v[34:37], v191, v192 op_sel_hi:[0,0,0]
	s_setprio 0
	s_barrier
; #define PG8_STAGE(bufoff, gbase, voff) do { _Pragma("unroll") for (int _i = 0; _i < 2; ++_i) \
;         __builtin_amdgcn_global_load_lds((const unsigned*)((const char*)(gbase) + (voff)[_i]), (PG8_LAS unsigned*)(lds + (bufoff) + ldsw + _i * 8192), 16, 0, 0); } while (0)
; #define PG8_STAGE_A(bufoff, gbase, h, nx) do { if constexpr (Sched::GATHER) { const unsigned vv_[2] = {(nx) ? vAn[h][0] : vA[h][0], (nx) ? vAn[h][1] : vA[h][1]}; PG8_STAGE(bufoff, gbase, vv_); } \
;         else { PG8_STAGE(bufoff, (gbase) + (h) * hstep, voffA); } } while (0)
; #define PG8_LDA(dst, b, h) do { _Pragma("unroll") for (int m = 0; m < 4; ++m) _Pragma("unroll") for (int k = 0; k < 2; ++k) dst[m][k] = *(const PG8_LAS bf16x8*)(lds + PG8_SA(b, h) + aoff + m * 2048 + k * 1024); } while (0)
; #define PG8_LDB(dst, b, h) do { _Pragma("unroll") for (int n = 0; n < 2; ++n) _Pragma("unroll") for (int k = 0; k < 2; ++k) dst[n][k] = *(const PG8_LAS bf16x8*)(lds + PG8_SB(b, h) + boff + n * 2048 + k * 1024); } while (0)
; #define PG8_WAIT_V(n) asm volatile("s_waitcnt vmcnt(" #n ")" ::: "memory")
; #define PG8_WAIT_L(n) asm volatile("s_waitcnt lgkmcnt(" #n ")" ::: "memory")
; #define PG8_BAR __builtin_amdgcn_s_barrier()
; #define PG8_SCHED __builtin_amdgcn_sched_barrier(0)
;     ...
;             PG8_LDB(B0, 1, 0); PG8_LDB(B1, 1, 1); PG8_SCHED; PG8_LDA(At, 1, 0); PG8_STAGE_A(PG8_SA(0, 1), a2, 1, last);
;             PG8_WAIT_V(8); PG8_WAIT_L(0); PG8_BAR; PG8_MMA(0, 0, At, B0); PG8_MMA(0, 1, At, B1); PG8_BAR; PG8_SCHED;
;             PG8_LDA(At, 1, 1); PG8_STAGE(PG8_SB(1, 0), b3, voffB); PG8_STAGE(PG8_SB(1, 1), b3 + hstepB, voffB); PG8_STAGE_A(PG8_SA(1, 0), a3, 0, last);
;             PG8_WAIT_V(8); PG8_WAIT_L(0); PG8_BAR; PG8_MMA(1, 0, At, B0); PG8_MMA(1, 1, At, B1); PG8_BAR; PG8_SCHED;
;     __device__ __forceinline__ void operator()(const f32x4 (&acc)[2][2][4][2], const Unit& u, int wr, int wc, int fr, int fq) const {
;     ...
;             for (int m = 0; m < 4; ++m) { const int row = row0 + ai * HALF + m * 16; const float gt = gate[row] * YSCALE; unsigned char* rowp = O + (size_t)row * ldc + col0;
	s_add_i32 s48, 0, 0x18000
	s_add_i32 s49, 0, 0x1c000
	v_add_u32_e32 v14, s48, v186
	v_add_u32_e32 v30, s49, v186
	ds_read_b128 v[2:5], v14
	ds_read_b128 v[6:9], v14 offset:1024
	ds_read_b128 v[10:13], v14 offset:2048
	ds_read_b128 v[14:17], v14 offset:3072
	ds_read_b128 v[18:21], v30
	ds_read_b128 v[22:25], v30 offset:1024
	ds_read_b128 v[26:29], v30 offset:2048
	ds_read_b128 v[30:33], v30 offset:3072
	s_add_u32 s26, s26, 0x40000
	s_addc_u32 s27, s27, 0
	s_mov_b32 m0, s31
	v_lshl_add_u64 v[226:227], s[26:27], 0, v[168:169]
	ds_read_b128 v[194:197], v190 offset:32768
	ds_read_b128 v[198:201], v190 offset:33792
	ds_read_b128 v[202:205], v190 offset:34816
	ds_read_b128 v[206:209], v190 offset:35840
	ds_read_b128 v[210:213], v190 offset:36864
	ds_read_b128 v[214:217], v190 offset:37888
	ds_read_b128 v[218:221], v190 offset:38912
	ds_read_b128 v[222:225], v190 offset:39936
	global_load_lds_dwordx4 v[226:227], off
	v_lshl_add_u64 v[226:227], s[26:27], 0, v[164:165]
	s_mov_b32 m0, s34
	s_nop 0
	global_load_lds_dwordx4 v[226:227], off
	s_waitcnt vmcnt(8)
	s_waitcnt lgkmcnt(0)
	s_barrier
	s_setprio 1
	v_mfma_scale_f32_16x16x128_f8f6f4 v[158:161], v[2:9], v[194:201], v[158:161], v191, v192 op_sel_hi:[0,0,0]
	v_mfma_scale_f32_16x16x128_f8f6f4 v[154:157], v[10:17], v[194:201], v[154:157], v191, v192 op_sel_hi:[0,0,0]
	v_mfma_scale_f32_16x16x128_f8f6f4 v[142:145], v[2:9], v[202:209], v[142:145], v191, v192 op_sel_hi:[0,0,0]
	v_mfma_scale_f32_16x16x128_f8f6f4 v[138:141], v[10:17], v[202:209], v[138:141], v191, v192 op_sel_hi:[0,0,0]
	v_mfma_scale_f32_16x16x128_f8f6f4 v[126:129], v[2:9], v[210:217], v[126:129], v191, v192 op_sel_hi:[0,0,0]
	v_mfma_scale_f32_16x16x128_f8f6f4 v[122:125], v[10:17], v[210:217], v[122:125], v191, v192 op_sel_hi:[0,0,0]
	v_mfma_scale_f32_16x16x128_f8f6f4 v[110:113], v[2:9], v[218:225], v[110:113], v191, v192 op_sel_hi:[0,0,0]
	v_mfma_scale_f32_16x16x128_f8f6f4 v[106:109], v[10:17], v[218:225], v[106:109], v191, v192 op_sel_hi:[0,0,0]
	s_setprio 0
	s_setprio 1
	s_nop 0
	v_mfma_scale_f32_16x16x128_f8f6f4 v[150:153], v[18:25], v[194:201], v[150:153], v191, v192 op_sel_hi:[0,0,0]
	v_mfma_scale_f32_16x16x128_f8f6f4 v[146:149], v[26:33], v[194:201], v[146:149], v191, v192 op_sel_hi:[0,0,0]
	v_mfma_scale_f32_16x16x128_f8f6f4 v[134:137], v[18:25], v[202:209], v[134:137], v191, v192 op_sel_hi:[0,0,0]
	v_mfma_scale_f32_16x16x128_f8f6f4 v[130:133], v[26:33], v[202:209], v[130:133], v191, v192 op_sel_hi:[0,0,0]
	v_mfma_scale_f32_16x16x128_f8f6f4 v[118:121], v[18:25], v[210:217], v[118:121], v191, v192 op_sel_hi:[0,0,0]
	v_mfma_scale_f32_16x16x128_f8f6f4 v[114:117], v[26:33], v[210:217], v[114:117], v191, v192 op_sel_hi:[0,0,0]
	v_mfma_scale_f32_16x16x128_f8f6f4 v[102:105], v[18:25], v[218:225], v[102:105], v191, v192 op_sel_hi:[0,0,0]
	v_mfma_scale_f32_16x16x128_f8f6f4 v[98:101], v[26:33], v[218:225], v[98:101], v191, v192 op_sel_hi:[0,0,0]
	s_setprio 0
	s_barrier
	s_add_i32 s26, s48, s28
	v_lshl_add_u64 v[178:179], v[178:179], 0, s[8:9]
	s_mov_b32 m0, s26
	ds_read_b128 v[194:197], v190 offset:49152
	ds_read_b128 v[198:201], v190 offset:50176
	ds_read_b128 v[202:205], v190 offset:51200
	ds_read_b128 v[206:209], v190 offset:52224
	ds_read_b128 v[210:213], v190 offset:53248
	ds_read_b128 v[214:217], v190 offset:54272
	ds_read_b128 v[218:221], v190 offset:55296
	ds_read_b128 v[222:225], v190 offset:56320
	global_load_lds_dwordx4 v[178:179], off
	s_add_i32 m0, s26, 0x2000
	s_add_u32 s24, s24, 0x4080
	v_lshl_add_u64 v[178:179], v[180:181], 0, s[8:9]
	s_addc_u32 s25, s25, 0
	s_add_i32 s26, s49, s28
	global_load_lds_dwordx4 v[178:179], off
	v_lshl_add_u64 v[178:179], s[24:25], 0, v[166:167]
	s_mov_b32 m0, s26
	s_nop 0
	global_load_lds_dwordx4 v[178:179], off
	v_lshl_add_u64 v[178:179], s[24:25], 0, v[162:163]
	s_add_i32 m0, s26, 0x2000
	s_nop 0
	global_load_lds_dwordx4 v[178:179], off
	v_lshl_add_u64 v[178:179], v[182:183], 0, s[8:9]
	s_mov_b32 m0, s38
	s_nop 0
	global_load_lds_dwordx4 v[178:179], off
	v_lshl_add_u64 v[178:179], v[184:185], 0, s[8:9]
	s_mov_b32 m0, s39
	s_nop 0
	global_load_lds_dwordx4 v[178:179], off
	s_waitcnt vmcnt(8)
	s_cmp_eq_u32 s47, 12
	s_cbranch_scc0 .Lgate9_skip
	v_lshl_add_u32 v236, s20, 8, v1
	v_ashrrev_i32_e32 v237, 31, v236
	v_lshl_add_u64 v[236:237], v[236:237], 2, s[0:1]
	global_load_dword v228, v[236:237], off
	global_load_dword v229, v[236:237], off offset:64
	global_load_dword v230, v[236:237], off offset:128
	global_load_dword v231, v[236:237], off offset:192
	global_load_dword v232, v[236:237], off offset:512
	global_load_dword v233, v[236:237], off offset:576
	global_load_dword v234, v[236:237], off offset:640
	global_load_dword v235, v[236:237], off offset:704
.Lgate9_skip:
	s_waitcnt lgkmcnt(0)
	s_barrier
	s_setprio 1
	v_mfma_scale_f32_16x16x128_f8f6f4 v[94:97], v[2:9], v[194:201], v[94:97], v191, v192 op_sel_hi:[0,0,0]
	v_mfma_scale_f32_16x16x128_f8f6f4 v[90:93], v[10:17], v[194:201], v[90:93], v191, v192 op_sel_hi:[0,0,0]
	v_mfma_scale_f32_16x16x128_f8f6f4 v[78:81], v[2:9], v[202:209], v[78:81], v191, v192 op_sel_hi:[0,0,0]
	v_mfma_scale_f32_16x16x128_f8f6f4 v[74:77], v[10:17], v[202:209], v[74:77], v191, v192 op_sel_hi:[0,0,0]
	v_mfma_scale_f32_16x16x128_f8f6f4 v[62:65], v[2:9], v[210:217], v[62:65], v191, v192 op_sel_hi:[0,0,0]
	v_mfma_scale_f32_16x16x128_f8f6f4 v[58:61], v[10:17], v[210:217], v[58:61], v191, v192 op_sel_hi:[0,0,0]
	v_mfma_scale_f32_16x16x128_f8f6f4 v[46:49], v[2:9], v[218:225], v[46:49], v191, v192 op_sel_hi:[0,0,0]
	v_mfma_scale_f32_16x16x128_f8f6f4 v[42:45], v[10:17], v[218:225], v[42:45], v191, v192 op_sel_hi:[0,0,0]
	s_setprio 0
	s_setprio 1
	s_nop 0
	v_mfma_scale_f32_16x16x128_f8f6f4 v[86:89], v[18:25], v[194:201], v[86:89], v191, v192 op_sel_hi:[0,0,0]
	v_mfma_scale_f32_16x16x128_f8f6f4 v[82:85], v[26:33], v[194:201], v[82:85], v191, v192 op_sel_hi:[0,0,0]
	v_mfma_scale_f32_16x16x128_f8f6f4 v[70:73], v[18:25], v[202:209], v[70:73], v191, v192 op_sel_hi:[0,0,0]
	v_mfma_scale_f32_16x16x128_f8f6f4 v[66:69], v[26:33], v[202:209], v[66:69], v191, v192 op_sel_hi:[0,0,0]
	v_mfma_scale_f32_16x16x128_f8f6f4 v[54:57], v[18:25], v[210:217], v[54:57], v191, v192 op_sel_hi:[0,0,0]
	v_mfma_scale_f32_16x16x128_f8f6f4 v[50:53], v[26:33], v[210:217], v[50:53], v191, v192 op_sel_hi:[0,0,0]
	v_mfma_scale_f32_16x16x128_f8f6f4 v[38:41], v[18:25], v[218:225], v[38:41], v191, v192 op_sel_hi:[0,0,0]
	v_mfma_scale_f32_16x16x128_f8f6f4 v[34:37], v[26:33], v[218:225], v[34:37], v191, v192 op_sel_hi:[0,0,0]
	s_setprio 0
	s_barrier
	s_add_i32 s47, s47, 2
	s_add_u32 s22, s22, 0x100
	s_addc_u32 s23, s23, 0
	s_add_u32 s45, s45, 0x100
	s_addc_u32 s46, s46, 0
	s_cmp_gt_u32 s47, 13
	s_cbranch_scc0 .LBB0_895
	s_and_b64 vcc, exec, s[10:11]
	s_cbranch_vccz .LBB0_898
	s_barrier

; #define PG8_STAGE(bufoff, gbase, voff) do { _Pragma("unroll") for (int _i = 0; _i < 2; ++_i) \
;         __builtin_amdgcn_global_load_lds((const unsigned*)((const char*)(gbase) + (voff)[_i]), (PG8_LAS unsigned*)(lds + (bufoff) + ldsw + _i * 8192), 16, 0, 0); } while (0)
; #define PG8_STAGE_A(bufoff, gbase, h, nx) do { if constexpr (Sched::GATHER) { const unsigned vv_[2] = {(nx) ? vAn[h][0] : vA[h][0], (nx) ? vAn[h][1] : vA[h][1]}; PG8_STAGE(bufoff, gbase, vv_); } \
;         else { PG8_STAGE(bufoff, (gbase) + (h) * hstep, voffA); } } while (0)
; #define PG8_LDA(dst, b, h) do { _Pragma("unroll") for (int m = 0; m < 4; ++m) _Pragma("unroll") for (int k = 0; k < 2; ++k) dst[m][k] = *(const PG8_LAS bf16x8*)(lds + PG8_SA(b, h) + aoff + m * 2048 + k * 1024); } while (0)
; #define PG8_WAIT_V(n) asm volatile("s_waitcnt vmcnt(" #n ")" ::: "memory")
; #define PG8_WAIT_L(n) asm volatile("s_waitcnt lgkmcnt(" #n ")" ::: "memory")
;     ...
;         const bool has_next = S.next(ui + 1, nxt);
;         const char* nA = Sched::GATHER ? cA : (has_next ? (const char*)g.A + (size_t)nxt.pm * tstep : cA);
;         if constexpr (Sched::GATHER) { if (has_next) { PG8_AOFF(vAn, ui + 1); } else { _Pragma("unroll") for (int h_ = 0; h_ < 2; ++h_) _Pragma("unroll") for (int i_ = 0; i_ < 2; ++i_) vAn[h_][i_] = vA[h_][i_]; } } const char* nB = has_next ? (const char*)g.Bt + (size_t)nxt.pb * tstep : cB;
; #pragma nounroll
;         for (int t = 0; t < nt; t += 2) {
;             const bool last = (t == nt - 2);
;             const char* a1 = cA + (size_t)(t + 1) * kstep;
;             const char* a2 = last ? nA : cA + (size_t)(t + 2) * kstep; const char* b2 = last ? nB : cB + (size_t)(t + 2) * kstep;
;             const char* a3 = a2 + kstep; const char* b3 = b2 + kstep;
;             if (last && has_next) S.a_ready(nxt);
;             if constexpr (SP2) {
;             PG8_LDB(B0, 0, 0); PG8_LDB(B1, 0, 1); PG8_SCHED; PG8_LDA(At, 0, 0); PG8_STAGE_A(PG8_SA(1, 1), a1, 1, false);
;             PG8_WAIT_V(8); PG8_WAIT_L(0); PG8_BAR; PG8_MMA(0, 0, At, B0); PG8_MMA(0, 1, At, B1); PG8_BAR; PG8_SCHED;
;             PG8_LDA(At, 0, 1); PG8_STAGE(PG8_SB(0, 0), b2, voffB); PG8_STAGE(PG8_SB(0, 1), b2 + hstepB, voffB); PG8_STAGE_A(PG8_SA(0, 0), a2, 0, last);
;             PG8_WAIT_V(8); PG8_WAIT_L(0); PG8_BAR; PG8_MMA(1, 0, At, B0); PG8_MMA(1, 1, At, B1); PG8_BAR; PG8_SCHED;
.LBB0_1025:
	s_ashr_i32 s45, s44, 31
	s_lshl_b64 s[46:47], s[44:45], 18
	s_add_u32 s46, s88, s46
	s_addc_u32 s47, s89, s47
	s_and_b64 s[48:49], s[2:3], exec
	s_cselect_b32 s5, s47, s7
	s_cselect_b32 s33, s46, s6
	s_ashr_i32 s43, s42, 31
	s_lshl_b64 s[48:49], s[42:43], 18
	v_readlane_b32 s54, v254, 55
	v_readlane_b32 s55, v254, 56
	s_add_u32 s48, s54, s48
	s_addc_u32 s49, s55, s49
	s_and_b64 s[54:55], s[2:3], exec
	s_cselect_b32 s43, s49, s53
	s_cselect_b32 s45, s48, s52
	s_add_u32 s6, s6, 0x20080
	s_addc_u32 s7, s7, 0
	s_add_u32 s71, s52, 0x100
	s_addc_u32 s72, s53, 0
	s_mov_b32 s73, -2
	ds_read_b128 v[26:29], v188
	ds_read_b128 v[30:33], v188 offset:1024
	ds_read_b128 v[18:21], v188 offset:2048
	ds_read_b128 v[22:25], v188 offset:3072
	ds_read_b128 v[10:13], v189
	ds_read_b128 v[14:17], v189 offset:1024
	ds_read_b128 v[2:5], v189 offset:2048
	ds_read_b128 v[6:9], v189 offset:3072
	s_add_u32 s52, s6, 0xfffe0080
	s_addc_u32 s53, s7, -1
	s_cmp_eq_u32 s73, 4
	s_cselect_b32 s55, s5, s53
	s_cselect_b32 s54, s33, s52
	s_cselect_b32 s53, s43, s72
	s_cselect_b32 s52, s45, s71
	v_lshl_add_u64 v[220:221], s[6:7], 0, v[170:171]
	s_add_i32 m0, s51, 0xc000
	ds_read_b128 v[178:181], v190
	ds_read_b128 v[182:185], v190 offset:1024
	ds_read_b128 v[196:199], v190 offset:2048
	ds_read_b128 v[200:203], v190 offset:3072
	ds_read_b128 v[204:207], v190 offset:4096
	ds_read_b128 v[208:211], v190 offset:5120
	ds_read_b128 v[212:215], v190 offset:6144
	ds_read_b128 v[216:219], v190 offset:7168
	global_load_lds_dwordx4 v[220:221], off
	v_lshl_add_u64 v[220:221], s[6:7], 0, v[172:173]
	s_add_i32 m0, s51, 0xe000
	s_nop 0
	global_load_lds_dwordx4 v[220:221], off
	s_waitcnt vmcnt(8)
	s_waitcnt lgkmcnt(0)
	s_barrier
	s_setprio 1
	v_mfma_scale_f32_16x16x128_f8f6f4 v[158:161], v[26:33], v[178:185], 0, v191, v192 op_sel_hi:[0,0,0]
	v_mfma_scale_f32_16x16x128_f8f6f4 v[154:157], v[18:25], v[178:185], 0, v191, v192 op_sel_hi:[0,0,0]
	v_mfma_scale_f32_16x16x128_f8f6f4 v[142:145], v[26:33], v[196:203], 0, v191, v192 op_sel_hi:[0,0,0]
	v_mfma_scale_f32_16x16x128_f8f6f4 v[138:141], v[18:25], v[196:203], 0, v191, v192 op_sel_hi:[0,0,0]
	v_mfma_scale_f32_16x16x128_f8f6f4 v[126:129], v[26:33], v[204:211], 0, v191, v192 op_sel_hi:[0,0,0]
	v_mfma_scale_f32_16x16x128_f8f6f4 v[122:125], v[18:25], v[204:211], 0, v191, v192 op_sel_hi:[0,0,0]
	v_mfma_scale_f32_16x16x128_f8f6f4 v[110:113], v[26:33], v[212:219], 0, v191, v192 op_sel_hi:[0,0,0]
	v_mfma_scale_f32_16x16x128_f8f6f4 v[106:109], v[18:25], v[212:219], 0, v191, v192 op_sel_hi:[0,0,0]
	s_setprio 0
	s_setprio 1
	s_nop 0
	v_mfma_scale_f32_16x16x128_f8f6f4 v[150:153], v[10:17], v[178:185], 0, v191, v192 op_sel_hi:[0,0,0]
	v_mfma_scale_f32_16x16x128_f8f6f4 v[146:149], v[2:9], v[178:185], 0, v191, v192 op_sel_hi:[0,0,0]
	v_mfma_scale_f32_16x16x128_f8f6f4 v[134:137], v[10:17], v[196:203], 0, v191, v192 op_sel_hi:[0,0,0]
	v_mfma_scale_f32_16x16x128_f8f6f4 v[130:133], v[2:9], v[196:203], 0, v191, v192 op_sel_hi:[0,0,0]
	v_mfma_scale_f32_16x16x128_f8f6f4 v[118:121], v[10:17], v[204:211], 0, v191, v192 op_sel_hi:[0,0,0]
	v_mfma_scale_f32_16x16x128_f8f6f4 v[114:117], v[2:9], v[204:211], 0, v191, v192 op_sel_hi:[0,0,0]
	v_mfma_scale_f32_16x16x128_f8f6f4 v[102:105], v[10:17], v[212:219], 0, v191, v192 op_sel_hi:[0,0,0]
	v_mfma_scale_f32_16x16x128_f8f6f4 v[98:101], v[2:9], v[212:219], 0, v191, v192 op_sel_hi:[0,0,0]
	s_setprio 0
	s_barrier
	s_add_i32 s74, s67, s56
	v_lshl_add_u64 v[178:179], s[52:53], 0, v[164:165]
	s_mov_b32 m0, s74
	ds_read_b128 v[196:199], v190 offset:16384
	ds_read_b128 v[200:203], v190 offset:17408
	ds_read_b128 v[204:207], v190 offset:18432
	ds_read_b128 v[208:211], v190 offset:19456
	ds_read_b128 v[212:215], v190 offset:20480
	ds_read_b128 v[216:219], v190 offset:21504
	ds_read_b128 v[220:223], v190 offset:22528
	ds_read_b128 v[224:227], v190 offset:23552
	global_load_lds_dwordx4 v[178:179], off
	s_add_i32 m0, s74, 0x2000
	s_add_u32 s74, s52, 0x8000
	v_lshl_add_u64 v[180:181], s[52:53], 0, v[168:169]
	s_addc_u32 s75, s53, 0
	s_add_i32 s76, s68, s56
	global_load_lds_dwordx4 v[180:181], off
	v_lshl_add_u64 v[182:183], s[74:75], 0, v[164:165]
	s_mov_b32 m0, s76
	v_lshl_add_u64 v[184:185], s[54:55], 0, v[166:167]
	global_load_lds_dwordx4 v[182:183], off
	v_lshl_add_u64 v[182:183], s[74:75], 0, v[168:169]
	s_add_i32 m0, s76, 0x2000
	s_nop 0
	global_load_lds_dwordx4 v[182:183], off
	v_lshl_add_u64 v[182:183], s[54:55], 0, v[162:163]
	s_mov_b32 m0, s51
	s_nop 0
	global_load_lds_dwordx4 v[182:183], off
	s_mov_b32 m0, s57
	s_nop 0
	global_load_lds_dwordx4 v[184:185], off
	s_waitcnt vmcnt(8)
	s_waitcnt lgkmcnt(0)
	s_barrier
	s_setprio 1
	v_mfma_scale_f32_16x16x128_f8f6f4 v[94:97], v[26:33], v[196:203], 0, v191, v192 op_sel_hi:[0,0,0]
	v_mfma_scale_f32_16x16x128_f8f6f4 v[90:93], v[18:25], v[196:203], 0, v191, v192 op_sel_hi:[0,0,0]
	v_mfma_scale_f32_16x16x128_f8f6f4 v[78:81], v[26:33], v[204:211], 0, v191, v192 op_sel_hi:[0,0,0]
	v_mfma_scale_f32_16x16x128_f8f6f4 v[74:77], v[18:25], v[204:211], 0, v191, v192 op_sel_hi:[0,0,0]
	v_mfma_scale_f32_16x16x128_f8f6f4 v[62:65], v[26:33], v[212:219], 0, v191, v192 op_sel_hi:[0,0,0]
	v_mfma_scale_f32_16x16x128_f8f6f4 v[58:61], v[18:25], v[212:219], 0, v191, v192 op_sel_hi:[0,0,0]
	v_mfma_scale_f32_16x16x128_f8f6f4 v[46:49], v[26:33], v[220:227], 0, v191, v192 op_sel_hi:[0,0,0]
	v_mfma_scale_f32_16x16x128_f8f6f4 v[42:45], v[18:25], v[220:227], 0, v191, v192 op_sel_hi:[0,0,0]
	s_setprio 0
	s_setprio 1
	s_nop 0
	v_mfma_scale_f32_16x16x128_f8f6f4 v[86:89], v[10:17], v[196:203], 0, v191, v192 op_sel_hi:[0,0,0]
	v_mfma_scale_f32_16x16x128_f8f6f4 v[82:85], v[2:9], v[196:203], 0, v191, v192 op_sel_hi:[0,0,0]
	v_mfma_scale_f32_16x16x128_f8f6f4 v[70:73], v[10:17], v[204:211], 0, v191, v192 op_sel_hi:[0,0,0]
	v_mfma_scale_f32_16x16x128_f8f6f4 v[66:69], v[2:9], v[204:211], 0, v191, v192 op_sel_hi:[0,0,0]
	v_mfma_scale_f32_16x16x128_f8f6f4 v[54:57], v[10:17], v[212:219], 0, v191, v192 op_sel_hi:[0,0,0]
	v_mfma_scale_f32_16x16x128_f8f6f4 v[50:53], v[2:9], v[212:219], 0, v191, v192 op_sel_hi:[0,0,0]
	v_mfma_scale_f32_16x16x128_f8f6f4 v[38:41], v[10:17], v[220:227], 0, v191, v192 op_sel_hi:[0,0,0]
	v_mfma_scale_f32_16x16x128_f8f6f4 v[34:37], v[2:9], v[220:227], 0, v191, v192 op_sel_hi:[0,0,0]
	s_setprio 0
	s_barrier
; #define PG8_STAGE(bufoff, gbase, voff) do { _Pragma("unroll") for (int _i = 0; _i < 2; ++_i) \
;         __builtin_amdgcn_global_load_lds((const unsigned*)((const char*)(gbase) + (voff)[_i]), (PG8_LAS unsigned*)(lds + (bufoff) + ldsw + _i * 8192), 16, 0, 0); } while (0)
; #define PG8_STAGE_A(bufoff, gbase, h, nx) do { if constexpr (Sched::GATHER) { const unsigned vv_[2] = {(nx) ? vAn[h][0] : vA[h][0], (nx) ? vAn[h][1] : vA[h][1]}; PG8_STAGE(bufoff, gbase, vv_); } \
;         else { PG8_STAGE(bufoff, (gbase) + (h) * hstep, voffA); } } while (0)
; #define PG8_LDA(dst, b, h) do { _Pragma("unroll") for (int m = 0; m < 4; ++m) _Pragma("unroll") for (int k = 0; k < 2; ++k) dst[m][k] = *(const PG8_LAS bf16x8*)(lds + PG8_SA(b, h) + aoff + m * 2048 + k * 1024); } while (0)
; #define PG8_LDB(dst, b, h) do { _Pragma("unroll") for (int n = 0; n < 2; ++n) _Pragma("unroll") for (int k = 0; k < 2; ++k) dst[n][k] = *(const PG8_LAS bf16x8*)(lds + PG8_SB(b, h) + boff + n * 2048 + k * 1024); } while (0)
; #define PG8_WAIT_V(n) asm volatile("s_waitcnt vmcnt(" #n ")" ::: "memory")
; #define PG8_WAIT_L(n) asm volatile("s_waitcnt lgkmcnt(" #n ")" ::: "memory")
; #define PG8_BAR __builtin_amdgcn_s_barrier()
; #define PG8_SCHED __builtin_amdgcn_sched_barrier(0)
;     ...
;             PG8_LDB(B0, 1, 0); PG8_LDB(B1, 1, 1); PG8_SCHED; PG8_LDA(At, 1, 0); PG8_STAGE_A(PG8_SA(0, 1), a2, 1, last);
;             PG8_WAIT_V(8); PG8_WAIT_L(0); PG8_BAR; PG8_MMA(0, 0, At, B0); PG8_MMA(0, 1, At, B1); PG8_BAR; PG8_SCHED;
;             PG8_LDA(At, 1, 1); PG8_STAGE(PG8_SB(1, 0), b3, voffB); PG8_STAGE(PG8_SB(1, 1), b3 + hstepB, voffB); PG8_STAGE_A(PG8_SA(1, 0), a3, 0, last);
;             PG8_WAIT_V(8); PG8_WAIT_L(0); PG8_BAR; PG8_MMA(1, 0, At, B0); PG8_MMA(1, 1, At, B1); PG8_BAR; PG8_SCHED;
	s_add_i32 s74, 0, 0x18000
	s_add_i32 s75, 0, 0x1c000
	v_add_u32_e32 v14, s74, v187
	v_add_u32_e32 v30, s75, v187
	ds_read_b128 v[2:5], v14
	ds_read_b128 v[6:9], v14 offset:1024
	ds_read_b128 v[10:13], v14 offset:2048
	ds_read_b128 v[14:17], v14 offset:3072
	ds_read_b128 v[18:21], v30
	ds_read_b128 v[22:25], v30 offset:1024
	ds_read_b128 v[26:29], v30 offset:2048
	ds_read_b128 v[30:33], v30 offset:3072
	s_add_u32 s54, s54, 0x20000
	s_addc_u32 s55, s55, 0
	s_mov_b32 m0, s58
	v_lshl_add_u64 v[228:229], s[54:55], 0, v[162:163]
	ds_read_b128 v[196:199], v190 offset:32768
	ds_read_b128 v[200:203], v190 offset:33792
	ds_read_b128 v[204:207], v190 offset:34816
	ds_read_b128 v[208:211], v190 offset:35840
	ds_read_b128 v[212:215], v190 offset:36864
	ds_read_b128 v[216:219], v190 offset:37888
	ds_read_b128 v[220:223], v190 offset:38912
	ds_read_b128 v[224:227], v190 offset:39936
	global_load_lds_dwordx4 v[228:229], off
	v_lshl_add_u64 v[228:229], s[54:55], 0, v[166:167]
	s_mov_b32 m0, s59
	s_nop 0
	global_load_lds_dwordx4 v[228:229], off
	s_waitcnt vmcnt(8)
	s_waitcnt lgkmcnt(0)
	s_barrier
	s_setprio 1
	v_mfma_scale_f32_16x16x128_f8f6f4 v[158:161], v[2:9], v[196:203], v[158:161], v191, v192 op_sel_hi:[0,0,0]
	v_mfma_scale_f32_16x16x128_f8f6f4 v[154:157], v[10:17], v[196:203], v[154:157], v191, v192 op_sel_hi:[0,0,0]
	v_mfma_scale_f32_16x16x128_f8f6f4 v[142:145], v[2:9], v[204:211], v[142:145], v191, v192 op_sel_hi:[0,0,0]
	v_mfma_scale_f32_16x16x128_f8f6f4 v[138:141], v[10:17], v[204:211], v[138:141], v191, v192 op_sel_hi:[0,0,0]
	v_mfma_scale_f32_16x16x128_f8f6f4 v[126:129], v[2:9], v[212:219], v[126:129], v191, v192 op_sel_hi:[0,0,0]
	v_mfma_scale_f32_16x16x128_f8f6f4 v[122:125], v[10:17], v[212:219], v[122:125], v191, v192 op_sel_hi:[0,0,0]
	v_mfma_scale_f32_16x16x128_f8f6f4 v[110:113], v[2:9], v[220:227], v[110:113], v191, v192 op_sel_hi:[0,0,0]
	v_mfma_scale_f32_16x16x128_f8f6f4 v[106:109], v[10:17], v[220:227], v[106:109], v191, v192 op_sel_hi:[0,0,0]
	s_setprio 0
	s_setprio 1
	s_nop 0
	v_mfma_scale_f32_16x16x128_f8f6f4 v[150:153], v[18:25], v[196:203], v[150:153], v191, v192 op_sel_hi:[0,0,0]
	v_mfma_scale_f32_16x16x128_f8f6f4 v[146:149], v[26:33], v[196:203], v[146:149], v191, v192 op_sel_hi:[0,0,0]
	v_mfma_scale_f32_16x16x128_f8f6f4 v[134:137], v[18:25], v[204:211], v[134:137], v191, v192 op_sel_hi:[0,0,0]
	v_mfma_scale_f32_16x16x128_f8f6f4 v[130:133], v[26:33], v[204:211], v[130:133], v191, v192 op_sel_hi:[0,0,0]
	v_mfma_scale_f32_16x16x128_f8f6f4 v[118:121], v[18:25], v[212:219], v[118:121], v191, v192 op_sel_hi:[0,0,0]
	v_mfma_scale_f32_16x16x128_f8f6f4 v[114:117], v[26:33], v[212:219], v[114:117], v191, v192 op_sel_hi:[0,0,0]
	v_mfma_scale_f32_16x16x128_f8f6f4 v[102:105], v[18:25], v[220:227], v[102:105], v191, v192 op_sel_hi:[0,0,0]
	v_mfma_scale_f32_16x16x128_f8f6f4 v[98:101], v[26:33], v[220:227], v[98:101], v191, v192 op_sel_hi:[0,0,0]
	s_setprio 0
	s_barrier
	s_add_i32 s54, s74, s56
	v_lshl_add_u64 v[178:179], v[178:179], 0, s[18:19]
	s_mov_b32 m0, s54
	ds_read_b128 v[196:199], v190 offset:49152
	ds_read_b128 v[200:203], v190 offset:50176
	ds_read_b128 v[204:207], v190 offset:51200
	ds_read_b128 v[208:211], v190 offset:52224
	ds_read_b128 v[212:215], v190 offset:53248
	ds_read_b128 v[216:219], v190 offset:54272
	ds_read_b128 v[220:223], v190 offset:55296
	ds_read_b128 v[224:227], v190 offset:56320
	global_load_lds_dwordx4 v[178:179], off
	s_add_i32 m0, s54, 0x2000
	s_add_u32 s52, s52, 0x8080
	v_lshl_add_u64 v[178:179], v[180:181], 0, s[18:19]
	s_addc_u32 s53, s53, 0
	s_add_i32 s54, s75, s56
	global_load_lds_dwordx4 v[178:179], off
	v_lshl_add_u64 v[178:179], s[52:53], 0, v[164:165]
	s_mov_b32 m0, s54
	s_nop 0
	global_load_lds_dwordx4 v[178:179], off
	v_lshl_add_u64 v[178:179], s[52:53], 0, v[168:169]
	s_add_i32 m0, s54, 0x2000
	s_nop 0
	global_load_lds_dwordx4 v[178:179], off
	v_lshl_add_u64 v[178:179], v[182:183], 0, s[18:19]
	s_mov_b32 m0, s64
	s_nop 0
	global_load_lds_dwordx4 v[178:179], off
	v_lshl_add_u64 v[178:179], v[184:185], 0, s[18:19]
	s_mov_b32 m0, s65
	s_nop 0
	global_load_lds_dwordx4 v[178:179], off
	s_waitcnt vmcnt(8)
	s_waitcnt lgkmcnt(0)
	s_barrier
	s_setprio 1
	v_mfma_scale_f32_16x16x128_f8f6f4 v[94:97], v[2:9], v[196:203], v[94:97], v191, v192 op_sel_hi:[0,0,0]
	v_mfma_scale_f32_16x16x128_f8f6f4 v[90:93], v[10:17], v[196:203], v[90:93], v191, v192 op_sel_hi:[0,0,0]
	v_mfma_scale_f32_16x16x128_f8f6f4 v[78:81], v[2:9], v[204:211], v[78:81], v191, v192 op_sel_hi:[0,0,0]
	v_mfma_scale_f32_16x16x128_f8f6f4 v[74:77], v[10:17], v[204:211], v[74:77], v191, v192 op_sel_hi:[0,0,0]
	v_mfma_scale_f32_16x16x128_f8f6f4 v[62:65], v[2:9], v[212:219], v[62:65], v191, v192 op_sel_hi:[0,0,0]
	v_mfma_scale_f32_16x16x128_f8f6f4 v[58:61], v[10:17], v[212:219], v[58:61], v191, v192 op_sel_hi:[0,0,0]
	v_mfma_scale_f32_16x16x128_f8f6f4 v[46:49], v[2:9], v[220:227], v[46:49], v191, v192 op_sel_hi:[0,0,0]
	v_mfma_scale_f32_16x16x128_f8f6f4 v[42:45], v[10:17], v[220:227], v[42:45], v191, v192 op_sel_hi:[0,0,0]
	s_setprio 0
	s_setprio 1
	s_nop 0
	v_mfma_scale_f32_16x16x128_f8f6f4 v[86:89], v[18:25], v[196:203], v[86:89], v191, v192 op_sel_hi:[0,0,0]
	v_mfma_scale_f32_16x16x128_f8f6f4 v[82:85], v[26:33], v[196:203], v[82:85], v191, v192 op_sel_hi:[0,0,0]
	v_mfma_scale_f32_16x16x128_f8f6f4 v[70:73], v[18:25], v[204:211], v[70:73], v191, v192 op_sel_hi:[0,0,0]
	v_mfma_scale_f32_16x16x128_f8f6f4 v[66:69], v[26:33], v[204:211], v[66:69], v191, v192 op_sel_hi:[0,0,0]
	v_mfma_scale_f32_16x16x128_f8f6f4 v[54:57], v[18:25], v[212:219], v[54:57], v191, v192 op_sel_hi:[0,0,0]
	v_mfma_scale_f32_16x16x128_f8f6f4 v[50:53], v[26:33], v[212:219], v[50:53], v191, v192 op_sel_hi:[0,0,0]
	v_mfma_scale_f32_16x16x128_f8f6f4 v[38:41], v[18:25], v[220:227], v[38:41], v191, v192 op_sel_hi:[0,0,0]
	v_mfma_scale_f32_16x16x128_f8f6f4 v[34:37], v[26:33], v[220:227], v[34:37], v191, v192 op_sel_hi:[0,0,0]
	s_setprio 0
	s_barrier
	s_add_i32 s73, s73, 2
	s_add_u32 s6, s6, 0x100
	s_addc_u32 s7, s7, 0
	s_add_u32 s71, s71, 0x100
	s_addc_u32 s72, s72, 0
; #define PG8_STAGE(bufoff, gbase, voff) do { _Pragma("unroll") for (int _i = 0; _i < 2; ++_i) \
;         __builtin_amdgcn_global_load_lds((const unsigned*)((const char*)(gbase) + (voff)[_i]), (PG8_LAS unsigned*)(lds + (bufoff) + ldsw + _i * 8192), 16, 0, 0); } while (0)
; #define PG8_STAGE_A(bufoff, gbase, h, nx) do { if constexpr (Sched::GATHER) { const unsigned vv_[2] = {(nx) ? vAn[h][0] : vA[h][0], (nx) ? vAn[h][1] : vA[h][1]}; PG8_STAGE(bufoff, gbase, vv_); } \
;         else { PG8_STAGE(bufoff, (gbase) + (h) * hstep, voffA); } } while (0)
; #define PG8_LDA(dst, b, h) do { _Pragma("unroll") for (int m = 0; m < 4; ++m) _Pragma("unroll") for (int k = 0; k < 2; ++k) dst[m][k] = *(const PG8_LAS bf16x8*)(lds + PG8_SA(b, h) + aoff + m * 2048 + k * 1024); } while (0)
; #define PG8_LDB(dst, b, h) do { _Pragma("unroll") for (int n = 0; n < 2; ++n) _Pragma("unroll") for (int k = 0; k < 2; ++k) dst[n][k] = *(const PG8_LAS bf16x8*)(lds + PG8_SB(b, h) + boff + n * 2048 + k * 1024); } while (0)
; #define PG8_WAIT_V(n) asm volatile("s_waitcnt vmcnt(" #n ")" ::: "memory")
; #define PG8_WAIT_L(n) asm volatile("s_waitcnt lgkmcnt(" #n ")" ::: "memory")
; #define PG8_BAR __builtin_amdgcn_s_barrier()
; #define PG8_SCHED __builtin_amdgcn_sched_barrier(0)
;     ...
;             PG8_LDB(B0, 0, 0); PG8_LDB(B1, 0, 1); PG8_SCHED; PG8_LDA(At, 0, 0); PG8_STAGE_A(PG8_SA(1, 1), a1, 1, false);
;             PG8_WAIT_V(8); PG8_WAIT_L(0); PG8_BAR; PG8_MMA(0, 0, At, B0); PG8_MMA(0, 1, At, B1); PG8_BAR; PG8_SCHED;
;             PG8_LDA(At, 0, 1); PG8_STAGE(PG8_SB(0, 0), b2, voffB); PG8_STAGE(PG8_SB(0, 1), b2 + hstepB, voffB); PG8_STAGE_A(PG8_SA(0, 0), a2, 0, last);
;             PG8_WAIT_V(8); PG8_WAIT_L(0); PG8_BAR; PG8_MMA(1, 0, At, B0); PG8_MMA(1, 1, At, B1); PG8_BAR; PG8_SCHED;
.LBB0_1026:
	ds_read_b128 v[26:29], v188
	ds_read_b128 v[30:33], v188 offset:1024
	ds_read_b128 v[18:21], v188 offset:2048
	ds_read_b128 v[22:25], v188 offset:3072
	ds_read_b128 v[10:13], v189
	ds_read_b128 v[14:17], v189 offset:1024
	ds_read_b128 v[2:5], v189 offset:2048
	ds_read_b128 v[6:9], v189 offset:3072
	s_add_u32 s52, s6, 0xfffe0080
	s_addc_u32 s53, s7, -1
	s_cmp_eq_u32 s73, 4
	s_cselect_b32 s55, s5, s53
	s_cselect_b32 s54, s33, s52
	s_cselect_b32 s53, s43, s72
	s_cselect_b32 s52, s45, s71
	v_lshl_add_u64 v[220:221], s[6:7], 0, v[170:171]
	s_add_i32 m0, s51, 0xc000
	ds_read_b128 v[178:181], v190
	ds_read_b128 v[182:185], v190 offset:1024
	ds_read_b128 v[196:199], v190 offset:2048
	ds_read_b128 v[200:203], v190 offset:3072
	ds_read_b128 v[204:207], v190 offset:4096
	ds_read_b128 v[208:211], v190 offset:5120
	ds_read_b128 v[212:215], v190 offset:6144
	ds_read_b128 v[216:219], v190 offset:7168
	global_load_lds_dwordx4 v[220:221], off
	v_lshl_add_u64 v[220:221], s[6:7], 0, v[172:173]
	s_add_i32 m0, s51, 0xe000
	s_nop 0
	global_load_lds_dwordx4 v[220:221], off
	s_waitcnt vmcnt(8)
	s_waitcnt lgkmcnt(0)
	s_barrier
	s_setprio 1
	v_mfma_scale_f32_16x16x128_f8f6f4 v[158:161], v[26:33], v[178:185], v[158:161], v191, v192 op_sel_hi:[0,0,0]
	v_mfma_scale_f32_16x16x128_f8f6f4 v[154:157], v[18:25], v[178:185], v[154:157], v191, v192 op_sel_hi:[0,0,0]
	v_mfma_scale_f32_16x16x128_f8f6f4 v[142:145], v[26:33], v[196:203], v[142:145], v191, v192 op_sel_hi:[0,0,0]
	v_mfma_scale_f32_16x16x128_f8f6f4 v[138:141], v[18:25], v[196:203], v[138:141], v191, v192 op_sel_hi:[0,0,0]
	v_mfma_scale_f32_16x16x128_f8f6f4 v[126:129], v[26:33], v[204:211], v[126:129], v191, v192 op_sel_hi:[0,0,0]
	v_mfma_scale_f32_16x16x128_f8f6f4 v[122:125], v[18:25], v[204:211], v[122:125], v191, v192 op_sel_hi:[0,0,0]
	v_mfma_scale_f32_16x16x128_f8f6f4 v[110:113], v[26:33], v[212:219], v[110:113], v191, v192 op_sel_hi:[0,0,0]
	v_mfma_scale_f32_16x16x128_f8f6f4 v[106:109], v[18:25], v[212:219], v[106:109], v191, v192 op_sel_hi:[0,0,0]
	s_setprio 0
	s_setprio 1
	s_nop 0
	v_mfma_scale_f32_16x16x128_f8f6f4 v[150:153], v[10:17], v[178:185], v[150:153], v191, v192 op_sel_hi:[0,0,0]
	v_mfma_scale_f32_16x16x128_f8f6f4 v[146:149], v[2:9], v[178:185], v[146:149], v191, v192 op_sel_hi:[0,0,0]
	v_mfma_scale_f32_16x16x128_f8f6f4 v[134:137], v[10:17], v[196:203], v[134:137], v191, v192 op_sel_hi:[0,0,0]
	v_mfma_scale_f32_16x16x128_f8f6f4 v[130:133], v[2:9], v[196:203], v[130:133], v191, v192 op_sel_hi:[0,0,0]
	v_mfma_scale_f32_16x16x128_f8f6f4 v[118:121], v[10:17], v[204:211], v[118:121], v191, v192 op_sel_hi:[0,0,0]
	v_mfma_scale_f32_16x16x128_f8f6f4 v[114:117], v[2:9], v[204:211], v[114:117], v191, v192 op_sel_hi:[0,0,0]
	v_mfma_scale_f32_16x16x128_f8f6f4 v[102:105], v[10:17], v[212:219], v[102:105], v191, v192 op_sel_hi:[0,0,0]
	v_mfma_scale_f32_16x16x128_f8f6f4 v[98:101], v[2:9], v[212:219], v[98:101], v191, v192 op_sel_hi:[0,0,0]
	s_setprio 0
	s_barrier
	s_add_i32 s74, s67, s56
	v_lshl_add_u64 v[178:179], s[52:53], 0, v[164:165]
	s_mov_b32 m0, s74
	ds_read_b128 v[196:199], v190 offset:16384
	ds_read_b128 v[200:203], v190 offset:17408
	ds_read_b128 v[204:207], v190 offset:18432
	ds_read_b128 v[208:211], v190 offset:19456
	ds_read_b128 v[212:215], v190 offset:20480
	ds_read_b128 v[216:219], v190 offset:21504
	ds_read_b128 v[220:223], v190 offset:22528
	ds_read_b128 v[224:227], v190 offset:23552
	global_load_lds_dwordx4 v[178:179], off
	s_add_i32 m0, s74, 0x2000
	s_add_u32 s74, s52, 0x8000
	v_lshl_add_u64 v[180:181], s[52:53], 0, v[168:169]
	s_addc_u32 s75, s53, 0
	s_add_i32 s76, s68, s56
	global_load_lds_dwordx4 v[180:181], off
	v_lshl_add_u64 v[182:183], s[74:75], 0, v[164:165]
	s_mov_b32 m0, s76
	v_lshl_add_u64 v[184:185], s[54:55], 0, v[166:167]
	global_load_lds_dwordx4 v[182:183], off
	v_lshl_add_u64 v[182:183], s[74:75], 0, v[168:169]
	s_add_i32 m0, s76, 0x2000
	s_nop 0
	global_load_lds_dwordx4 v[182:183], off
	v_lshl_add_u64 v[182:183], s[54:55], 0, v[162:163]
	s_mov_b32 m0, s51
	s_nop 0
	global_load_lds_dwordx4 v[182:183], off
	s_mov_b32 m0, s57
	s_nop 0
	global_load_lds_dwordx4 v[184:185], off
	s_waitcnt vmcnt(8)
	s_waitcnt lgkmcnt(0)
	s_barrier
	s_setprio 1
	v_mfma_scale_f32_16x16x128_f8f6f4 v[94:97], v[26:33], v[196:203], v[94:97], v191, v192 op_sel_hi:[0,0,0]
	v_mfma_scale_f32_16x16x128_f8f6f4 v[90:93], v[18:25], v[196:203], v[90:93], v191, v192 op_sel_hi:[0,0,0]
	v_mfma_scale_f32_16x16x128_f8f6f4 v[78:81], v[26:33], v[204:211], v[78:81], v191, v192 op_sel_hi:[0,0,0]
	v_mfma_scale_f32_16x16x128_f8f6f4 v[74:77], v[18:25], v[204:211], v[74:77], v191, v192 op_sel_hi:[0,0,0]
	v_mfma_scale_f32_16x16x128_f8f6f4 v[62:65], v[26:33], v[212:219], v[62:65], v191, v192 op_sel_hi:[0,0,0]
	v_mfma_scale_f32_16x16x128_f8f6f4 v[58:61], v[18:25], v[212:219], v[58:61], v191, v192 op_sel_hi:[0,0,0]
	v_mfma_scale_f32_16x16x128_f8f6f4 v[46:49], v[26:33], v[220:227], v[46:49], v191, v192 op_sel_hi:[0,0,0]
	v_mfma_scale_f32_16x16x128_f8f6f4 v[42:45], v[18:25], v[220:227], v[42:45], v191, v192 op_sel_hi:[0,0,0]
	s_setprio 0
	s_setprio 1
	s_nop 0
	v_mfma_scale_f32_16x16x128_f8f6f4 v[86:89], v[10:17], v[196:203], v[86:89], v191, v192 op_sel_hi:[0,0,0]
	v_mfma_scale_f32_16x16x128_f8f6f4 v[82:85], v[2:9], v[196:203], v[82:85], v191, v192 op_sel_hi:[0,0,0]
	v_mfma_scale_f32_16x16x128_f8f6f4 v[70:73], v[10:17], v[204:211], v[70:73], v191, v192 op_sel_hi:[0,0,0]
	v_mfma_scale_f32_16x16x128_f8f6f4 v[66:69], v[2:9], v[204:211], v[66:69], v191, v192 op_sel_hi:[0,0,0]
	v_mfma_scale_f32_16x16x128_f8f6f4 v[54:57], v[10:17], v[212:219], v[54:57], v191, v192 op_sel_hi:[0,0,0]
	v_mfma_scale_f32_16x16x128_f8f6f4 v[50:53], v[2:9], v[212:219], v[50:53], v191, v192 op_sel_hi:[0,0,0]
	v_mfma_scale_f32_16x16x128_f8f6f4 v[38:41], v[10:17], v[220:227], v[38:41], v191, v192 op_sel_hi:[0,0,0]
	v_mfma_scale_f32_16x16x128_f8f6f4 v[34:37], v[2:9], v[220:227], v[34:37], v191, v192 op_sel_hi:[0,0,0]
	s_setprio 0
	s_barrier
; #define PG8_STAGE(bufoff, gbase, voff) do { _Pragma("unroll") for (int _i = 0; _i < 2; ++_i) \
;         __builtin_amdgcn_global_load_lds((const unsigned*)((const char*)(gbase) + (voff)[_i]), (PG8_LAS unsigned*)(lds + (bufoff) + ldsw + _i * 8192), 16, 0, 0); } while (0)
; #define PG8_STAGE_A(bufoff, gbase, h, nx) do { if constexpr (Sched::GATHER) { const unsigned vv_[2] = {(nx) ? vAn[h][0] : vA[h][0], (nx) ? vAn[h][1] : vA[h][1]}; PG8_STAGE(bufoff, gbase, vv_); } \
;         else { PG8_STAGE(bufoff, (gbase) + (h) * hstep, voffA); } } while (0)
; #define PG8_LDA(dst, b, h) do { _Pragma("unroll") for (int m = 0; m < 4; ++m) _Pragma("unroll") for (int k = 0; k < 2; ++k) dst[m][k] = *(const PG8_LAS bf16x8*)(lds + PG8_SA(b, h) + aoff + m * 2048 + k * 1024); } while (0)
; #define PG8_LDB(dst, b, h) do { _Pragma("unroll") for (int n = 0; n < 2; ++n) _Pragma("unroll") for (int k = 0; k < 2; ++k) dst[n][k] = *(const PG8_LAS bf16x8*)(lds + PG8_SB(b, h) + boff + n * 2048 + k * 1024); } while (0)
; #define PG8_WAIT_V(n) asm volatile("s_waitcnt vmcnt(" #n ")" ::: "memory")
; #define PG8_WAIT_L(n) asm volatile("s_waitcnt lgkmcnt(" #n ")" ::: "memory")
; #define PG8_BAR __builtin_amdgcn_s_barrier()
; #define PG8_SCHED __builtin_amdgcn_sched_barrier(0)
;     ...
;             PG8_LDB(B0, 1, 0); PG8_LDB(B1, 1, 1); PG8_SCHED; PG8_LDA(At, 1, 0); PG8_STAGE_A(PG8_SA(0, 1), a2, 1, last);
;             PG8_WAIT_V(8); PG8_WAIT_L(0); PG8_BAR; PG8_MMA(0, 0, At, B0); PG8_MMA(0, 1, At, B1); PG8_BAR; PG8_SCHED;
;             PG8_LDA(At, 1, 1); PG8_STAGE(PG8_SB(1, 0), b3, voffB); PG8_STAGE(PG8_SB(1, 1), b3 + hstepB, voffB); PG8_STAGE_A(PG8_SA(1, 0), a3, 0, last);
;             PG8_WAIT_V(8); PG8_WAIT_L(0); PG8_BAR; PG8_MMA(1, 0, At, B0); PG8_MMA(1, 1, At, B1); PG8_BAR; PG8_SCHED;
;     ...
;         }
;         if constexpr (F8) asm volatile("s_nop 15\n\ts_nop 15\n\ts_nop 15" ::: "memory");
;         if constexpr (ALIGN_EPI) { if (wr == 0) PG8_BAR; }
	s_add_i32 s74, 0, 0x18000
	s_add_i32 s75, 0, 0x1c000
	v_add_u32_e32 v14, s74, v187
	v_add_u32_e32 v30, s75, v187
	ds_read_b128 v[2:5], v14
	ds_read_b128 v[6:9], v14 offset:1024
	ds_read_b128 v[10:13], v14 offset:2048
	ds_read_b128 v[14:17], v14 offset:3072
	ds_read_b128 v[18:21], v30
	ds_read_b128 v[22:25], v30 offset:1024
	ds_read_b128 v[26:29], v30 offset:2048
	ds_read_b128 v[30:33], v30 offset:3072
	s_add_u32 s54, s54, 0x20000
	s_addc_u32 s55, s55, 0
	s_mov_b32 m0, s58
	v_lshl_add_u64 v[228:229], s[54:55], 0, v[162:163]
	ds_read_b128 v[196:199], v190 offset:32768
	ds_read_b128 v[200:203], v190 offset:33792
	ds_read_b128 v[204:207], v190 offset:34816
	ds_read_b128 v[208:211], v190 offset:35840
	ds_read_b128 v[212:215], v190 offset:36864
	ds_read_b128 v[216:219], v190 offset:37888
	ds_read_b128 v[220:223], v190 offset:38912
	ds_read_b128 v[224:227], v190 offset:39936
	global_load_lds_dwordx4 v[228:229], off
	v_lshl_add_u64 v[228:229], s[54:55], 0, v[166:167]
	s_mov_b32 m0, s59
	s_nop 0
	global_load_lds_dwordx4 v[228:229], off
	s_waitcnt vmcnt(8)
	s_waitcnt lgkmcnt(0)
	s_barrier
	s_setprio 1
	v_mfma_scale_f32_16x16x128_f8f6f4 v[158:161], v[2:9], v[196:203], v[158:161], v191, v192 op_sel_hi:[0,0,0]
	v_mfma_scale_f32_16x16x128_f8f6f4 v[154:157], v[10:17], v[196:203], v[154:157], v191, v192 op_sel_hi:[0,0,0]
	v_mfma_scale_f32_16x16x128_f8f6f4 v[142:145], v[2:9], v[204:211], v[142:145], v191, v192 op_sel_hi:[0,0,0]
	v_mfma_scale_f32_16x16x128_f8f6f4 v[138:141], v[10:17], v[204:211], v[138:141], v191, v192 op_sel_hi:[0,0,0]
	v_mfma_scale_f32_16x16x128_f8f6f4 v[126:129], v[2:9], v[212:219], v[126:129], v191, v192 op_sel_hi:[0,0,0]
	v_mfma_scale_f32_16x16x128_f8f6f4 v[122:125], v[10:17], v[212:219], v[122:125], v191, v192 op_sel_hi:[0,0,0]
	v_mfma_scale_f32_16x16x128_f8f6f4 v[110:113], v[2:9], v[220:227], v[110:113], v191, v192 op_sel_hi:[0,0,0]
	v_mfma_scale_f32_16x16x128_f8f6f4 v[106:109], v[10:17], v[220:227], v[106:109], v191, v192 op_sel_hi:[0,0,0]
	s_setprio 0
	s_setprio 1
	s_nop 0
	v_mfma_scale_f32_16x16x128_f8f6f4 v[150:153], v[18:25], v[196:203], v[150:153], v191, v192 op_sel_hi:[0,0,0]
	v_mfma_scale_f32_16x16x128_f8f6f4 v[146:149], v[26:33], v[196:203], v[146:149], v191, v192 op_sel_hi:[0,0,0]
	v_mfma_scale_f32_16x16x128_f8f6f4 v[134:137], v[18:25], v[204:211], v[134:137], v191, v192 op_sel_hi:[0,0,0]
	v_mfma_scale_f32_16x16x128_f8f6f4 v[130:133], v[26:33], v[204:211], v[130:133], v191, v192 op_sel_hi:[0,0,0]
	v_mfma_scale_f32_16x16x128_f8f6f4 v[118:121], v[18:25], v[212:219], v[118:121], v191, v192 op_sel_hi:[0,0,0]
	v_mfma_scale_f32_16x16x128_f8f6f4 v[114:117], v[26:33], v[212:219], v[114:117], v191, v192 op_sel_hi:[0,0,0]
	v_mfma_scale_f32_16x16x128_f8f6f4 v[102:105], v[18:25], v[220:227], v[102:105], v191, v192 op_sel_hi:[0,0,0]
	v_mfma_scale_f32_16x16x128_f8f6f4 v[98:101], v[26:33], v[220:227], v[98:101], v191, v192 op_sel_hi:[0,0,0]
	s_setprio 0
	s_barrier
	s_add_i32 s54, s74, s56
	v_lshl_add_u64 v[178:179], v[178:179], 0, s[18:19]
	s_mov_b32 m0, s54
	ds_read_b128 v[196:199], v190 offset:49152
	ds_read_b128 v[200:203], v190 offset:50176
	ds_read_b128 v[204:207], v190 offset:51200
	ds_read_b128 v[208:211], v190 offset:52224
	ds_read_b128 v[212:215], v190 offset:53248
	ds_read_b128 v[216:219], v190 offset:54272
	ds_read_b128 v[220:223], v190 offset:55296
	ds_read_b128 v[224:227], v190 offset:56320
	global_load_lds_dwordx4 v[178:179], off
	s_add_i32 m0, s54, 0x2000
	s_add_u32 s52, s52, 0x8080
	v_lshl_add_u64 v[178:179], v[180:181], 0, s[18:19]
	s_addc_u32 s53, s53, 0
	s_add_i32 s54, s75, s56
	global_load_lds_dwordx4 v[178:179], off
	v_lshl_add_u64 v[178:179], s[52:53], 0, v[164:165]
	s_mov_b32 m0, s54
	s_nop 0
	global_load_lds_dwordx4 v[178:179], off
	v_lshl_add_u64 v[178:179], s[52:53], 0, v[168:169]
	s_add_i32 m0, s54, 0x2000
	s_nop 0
	global_load_lds_dwordx4 v[178:179], off
	v_lshl_add_u64 v[178:179], v[182:183], 0, s[18:19]
	s_mov_b32 m0, s64
	s_nop 0
	global_load_lds_dwordx4 v[178:179], off
	v_lshl_add_u64 v[178:179], v[184:185], 0, s[18:19]
	s_mov_b32 m0, s65
	s_nop 0
	global_load_lds_dwordx4 v[178:179], off
	s_waitcnt vmcnt(8)
	s_waitcnt lgkmcnt(0)
	s_barrier
	s_setprio 1
	v_mfma_scale_f32_16x16x128_f8f6f4 v[94:97], v[2:9], v[196:203], v[94:97], v191, v192 op_sel_hi:[0,0,0]
	v_mfma_scale_f32_16x16x128_f8f6f4 v[90:93], v[10:17], v[196:203], v[90:93], v191, v192 op_sel_hi:[0,0,0]
	v_mfma_scale_f32_16x16x128_f8f6f4 v[78:81], v[2:9], v[204:211], v[78:81], v191, v192 op_sel_hi:[0,0,0]
	v_mfma_scale_f32_16x16x128_f8f6f4 v[74:77], v[10:17], v[204:211], v[74:77], v191, v192 op_sel_hi:[0,0,0]
	v_mfma_scale_f32_16x16x128_f8f6f4 v[62:65], v[2:9], v[212:219], v[62:65], v191, v192 op_sel_hi:[0,0,0]
	v_mfma_scale_f32_16x16x128_f8f6f4 v[58:61], v[10:17], v[212:219], v[58:61], v191, v192 op_sel_hi:[0,0,0]
	v_mfma_scale_f32_16x16x128_f8f6f4 v[46:49], v[2:9], v[220:227], v[46:49], v191, v192 op_sel_hi:[0,0,0]
	v_mfma_scale_f32_16x16x128_f8f6f4 v[42:45], v[10:17], v[220:227], v[42:45], v191, v192 op_sel_hi:[0,0,0]
	s_setprio 0
	s_setprio 1
	s_nop 0
	v_mfma_scale_f32_16x16x128_f8f6f4 v[86:89], v[18:25], v[196:203], v[86:89], v191, v192 op_sel_hi:[0,0,0]
	v_mfma_scale_f32_16x16x128_f8f6f4 v[82:85], v[26:33], v[196:203], v[82:85], v191, v192 op_sel_hi:[0,0,0]
	v_mfma_scale_f32_16x16x128_f8f6f4 v[70:73], v[18:25], v[204:211], v[70:73], v191, v192 op_sel_hi:[0,0,0]
	v_mfma_scale_f32_16x16x128_f8f6f4 v[66:69], v[26:33], v[204:211], v[66:69], v191, v192 op_sel_hi:[0,0,0]
	v_mfma_scale_f32_16x16x128_f8f6f4 v[54:57], v[18:25], v[212:219], v[54:57], v191, v192 op_sel_hi:[0,0,0]
	v_mfma_scale_f32_16x16x128_f8f6f4 v[50:53], v[26:33], v[212:219], v[50:53], v191, v192 op_sel_hi:[0,0,0]
	v_mfma_scale_f32_16x16x128_f8f6f4 v[38:41], v[18:25], v[220:227], v[38:41], v191, v192 op_sel_hi:[0,0,0]
	v_mfma_scale_f32_16x16x128_f8f6f4 v[34:37], v[26:33], v[220:227], v[34:37], v191, v192 op_sel_hi:[0,0,0]
	s_setprio 0
	s_barrier
	s_add_i32 s73, s73, 2
	s_add_u32 s6, s6, 0x100
	s_addc_u32 s7, s7, 0
	s_add_u32 s71, s71, 0x100
	s_addc_u32 s72, s72, 0
	s_cmp_gt_u32 s73, 5
	s_cbranch_scc0 .LBB0_1026
	s_and_b64 vcc, exec, s[20:21]
	s_cbranch_vccz .LBB0_1029
	s_barrier

; #define PG8_STAGE(bufoff, gbase, voff) do { _Pragma("unroll") for (int _i = 0; _i < 2; ++_i) \
;         __builtin_amdgcn_global_load_lds((const unsigned*)((const char*)(gbase) + (voff)[_i]), (PG8_LAS unsigned*)(lds + (bufoff) + ldsw + _i * 8192), 16, 0, 0); } while (0)
; #define PG8_STAGE_A(bufoff, gbase, h, nx) do { if constexpr (Sched::GATHER) { const unsigned vv_[2] = {(nx) ? vAn[h][0] : vA[h][0], (nx) ? vAn[h][1] : vA[h][1]}; PG8_STAGE(bufoff, gbase, vv_); } \
;         else { PG8_STAGE(bufoff, (gbase) + (h) * hstep, voffA); } } while (0)
; #define PG8_LDA(dst, b, h) do { _Pragma("unroll") for (int m = 0; m < 4; ++m) _Pragma("unroll") for (int k = 0; k < 2; ++k) dst[m][k] = *(const PG8_LAS bf16x8*)(lds + PG8_SA(b, h) + aoff + m * 2048 + k * 1024); } while (0)
; #define PG8_WAIT_V(n) asm volatile("s_waitcnt vmcnt(" #n ")" ::: "memory")
; #define PG8_WAIT_L(n) asm volatile("s_waitcnt lgkmcnt(" #n ")" ::: "memory")
;     ...
;         const bool has_next = S.next(ui + 1, nxt);
;         const char* nA = Sched::GATHER ? cA : (has_next ? (const char*)g.A + (size_t)nxt.pm * tstep : cA);
;         if constexpr (Sched::GATHER) { if (has_next) { PG8_AOFF(vAn, ui + 1); } else { _Pragma("unroll") for (int h_ = 0; h_ < 2; ++h_) _Pragma("unroll") for (int i_ = 0; i_ < 2; ++i_) vAn[h_][i_] = vA[h_][i_]; } } const char* nB = has_next ? (const char*)g.Bt + (size_t)nxt.pb * tstep : cB;
; #pragma nounroll
;         for (int t = 0; t < nt; t += 2) {
;             const bool last = (t == nt - 2);
;             const char* a1 = cA + (size_t)(t + 1) * kstep;
;             const char* a2 = last ? nA : cA + (size_t)(t + 2) * kstep; const char* b2 = last ? nB : cB + (size_t)(t + 2) * kstep;
;             const char* a3 = a2 + kstep; const char* b3 = b2 + kstep;
;             if (last && has_next) S.a_ready(nxt);
;             if constexpr (SP2) {
;             PG8_LDB(B0, 0, 0); PG8_LDB(B1, 0, 1); PG8_SCHED; PG8_LDA(At, 0, 0); PG8_STAGE_A(PG8_SA(1, 1), a1, 1, false);
;             PG8_WAIT_V(8); PG8_WAIT_L(0); PG8_BAR; PG8_MMA(0, 0, At, B0); PG8_MMA(0, 1, At, B1); PG8_BAR; PG8_SCHED;
;             PG8_LDA(At, 0, 1); PG8_STAGE(PG8_SB(0, 0), b2, voffB); PG8_STAGE(PG8_SB(0, 1), b2 + hstepB, voffB); PG8_STAGE_A(PG8_SA(0, 0), a2, 0, last);
;             PG8_WAIT_V(8); PG8_WAIT_L(0); PG8_BAR; PG8_MMA(1, 0, At, B0); PG8_MMA(1, 1, At, B1); PG8_BAR; PG8_SCHED;
.LBB0_1204:
	s_ashr_i32 s17, s16, 31
	s_lshl_b64 s[18:19], s[16:17], 18
	v_readlane_b32 s20, v255, 21
	v_readlane_b32 s21, v255, 22
	s_add_u32 s18, s20, s18
	s_addc_u32 s19, s21, s19
	s_and_b64 s[20:21], s[2:3], exec
	s_cselect_b32 s17, s19, s25
	s_cselect_b32 s44, s18, s24
	s_ashr_i32 s15, s14, 31
	s_lshl_b64 s[20:21], s[14:15], 18
	v_readlane_b32 s28, v254, 57
	v_readlane_b32 s29, v254, 58
	s_add_u32 s20, s28, s20
	s_addc_u32 s21, s29, s21
	s_and_b64 s[28:29], s[2:3], exec
	s_cselect_b32 s15, s21, s27
	s_cselect_b32 s45, s20, s26
	s_add_u32 s24, s24, 0x20080
	s_addc_u32 s25, s25, 0
	s_add_u32 s46, s26, 0x100
	s_addc_u32 s47, s27, 0
	s_mov_b32 s48, -2
	ds_read_b128 v[26:29], v188
	ds_read_b128 v[30:33], v188 offset:1024
	ds_read_b128 v[18:21], v188 offset:2048
	ds_read_b128 v[22:25], v188 offset:3072
	ds_read_b128 v[10:13], v189
	ds_read_b128 v[14:17], v189 offset:1024
	ds_read_b128 v[2:5], v189 offset:2048
	ds_read_b128 v[6:9], v189 offset:3072
	s_add_u32 s26, s24, 0xfffe0080
	s_addc_u32 s27, s25, -1
	s_cmp_eq_u32 s48, 4
	s_cselect_b32 s29, s17, s27
	s_cselect_b32 s28, s44, s26
	s_cselect_b32 s27, s15, s47
	s_cselect_b32 s26, s45, s46
	v_lshl_add_u64 v[218:219], s[24:25], 0, v[170:171]
	s_add_i32 m0, s23, 0xc000
	ds_read_b128 v[178:181], v190
	ds_read_b128 v[182:185], v190 offset:1024
	ds_read_b128 v[194:197], v190 offset:2048
	ds_read_b128 v[198:201], v190 offset:3072
	ds_read_b128 v[202:205], v190 offset:4096
	ds_read_b128 v[206:209], v190 offset:5120
	ds_read_b128 v[210:213], v190 offset:6144
	ds_read_b128 v[214:217], v190 offset:7168
	global_load_lds_dwordx4 v[218:219], off
	v_lshl_add_u64 v[218:219], s[24:25], 0, v[172:173]
	s_add_i32 m0, s23, 0xe000
	s_nop 0
	global_load_lds_dwordx4 v[218:219], off
	s_waitcnt vmcnt(8)
	s_waitcnt lgkmcnt(0)
	s_barrier
	s_setprio 1
	v_mfma_scale_f32_16x16x128_f8f6f4 v[158:161], v[26:33], v[178:185], 0, v191, v192 op_sel_hi:[0,0,0]
	v_mfma_scale_f32_16x16x128_f8f6f4 v[154:157], v[18:25], v[178:185], 0, v191, v192 op_sel_hi:[0,0,0]
	v_mfma_scale_f32_16x16x128_f8f6f4 v[142:145], v[26:33], v[194:201], 0, v191, v192 op_sel_hi:[0,0,0]
	v_mfma_scale_f32_16x16x128_f8f6f4 v[138:141], v[18:25], v[194:201], 0, v191, v192 op_sel_hi:[0,0,0]
	v_mfma_scale_f32_16x16x128_f8f6f4 v[126:129], v[26:33], v[202:209], 0, v191, v192 op_sel_hi:[0,0,0]
	v_mfma_scale_f32_16x16x128_f8f6f4 v[122:125], v[18:25], v[202:209], 0, v191, v192 op_sel_hi:[0,0,0]
	v_mfma_scale_f32_16x16x128_f8f6f4 v[110:113], v[26:33], v[210:217], 0, v191, v192 op_sel_hi:[0,0,0]
	v_mfma_scale_f32_16x16x128_f8f6f4 v[106:109], v[18:25], v[210:217], 0, v191, v192 op_sel_hi:[0,0,0]
	s_setprio 0
	s_setprio 1
	s_nop 0
	v_mfma_scale_f32_16x16x128_f8f6f4 v[150:153], v[10:17], v[178:185], 0, v191, v192 op_sel_hi:[0,0,0]
	v_mfma_scale_f32_16x16x128_f8f6f4 v[146:149], v[2:9], v[178:185], 0, v191, v192 op_sel_hi:[0,0,0]
	v_mfma_scale_f32_16x16x128_f8f6f4 v[134:137], v[10:17], v[194:201], 0, v191, v192 op_sel_hi:[0,0,0]
	v_mfma_scale_f32_16x16x128_f8f6f4 v[130:133], v[2:9], v[194:201], 0, v191, v192 op_sel_hi:[0,0,0]
	v_mfma_scale_f32_16x16x128_f8f6f4 v[118:121], v[10:17], v[202:209], 0, v191, v192 op_sel_hi:[0,0,0]
	v_mfma_scale_f32_16x16x128_f8f6f4 v[114:117], v[2:9], v[202:209], 0, v191, v192 op_sel_hi:[0,0,0]
	v_mfma_scale_f32_16x16x128_f8f6f4 v[102:105], v[10:17], v[210:217], 0, v191, v192 op_sel_hi:[0,0,0]
	v_mfma_scale_f32_16x16x128_f8f6f4 v[98:101], v[2:9], v[210:217], 0, v191, v192 op_sel_hi:[0,0,0]
	s_setprio 0
	s_barrier
	s_add_i32 s49, s41, s30
	v_lshl_add_u64 v[178:179], s[26:27], 0, v[164:165]
	s_mov_b32 m0, s49
	ds_read_b128 v[194:197], v190 offset:16384
	ds_read_b128 v[198:201], v190 offset:17408
	ds_read_b128 v[202:205], v190 offset:18432
	ds_read_b128 v[206:209], v190 offset:19456
	ds_read_b128 v[210:213], v190 offset:20480
	ds_read_b128 v[214:217], v190 offset:21504
	ds_read_b128 v[218:221], v190 offset:22528
	ds_read_b128 v[222:225], v190 offset:23552
	global_load_lds_dwordx4 v[178:179], off
	s_add_i32 m0, s49, 0x2000
	s_add_u32 s50, s26, 0x2000
	v_lshl_add_u64 v[180:181], s[26:27], 0, v[168:169]
	s_addc_u32 s51, s27, 0
	s_add_i32 s49, s42, s30
	global_load_lds_dwordx4 v[180:181], off
	v_lshl_add_u64 v[182:183], s[50:51], 0, v[164:165]
	s_mov_b32 m0, s49
	v_lshl_add_u64 v[184:185], s[28:29], 0, v[166:167]
	global_load_lds_dwordx4 v[182:183], off
	v_lshl_add_u64 v[182:183], s[50:51], 0, v[168:169]
	s_add_i32 m0, s49, 0x2000
	s_nop 0
	global_load_lds_dwordx4 v[182:183], off
	v_lshl_add_u64 v[182:183], s[28:29], 0, v[162:163]
	s_mov_b32 m0, s23
	s_nop 0
	global_load_lds_dwordx4 v[182:183], off
	s_mov_b32 m0, s34
	s_nop 0
	global_load_lds_dwordx4 v[184:185], off
	s_waitcnt vmcnt(8)
	s_waitcnt lgkmcnt(0)
	s_barrier
	s_setprio 1
	v_mfma_scale_f32_16x16x128_f8f6f4 v[94:97], v[26:33], v[194:201], 0, v191, v192 op_sel_hi:[0,0,0]
	v_mfma_scale_f32_16x16x128_f8f6f4 v[90:93], v[18:25], v[194:201], 0, v191, v192 op_sel_hi:[0,0,0]
	v_mfma_scale_f32_16x16x128_f8f6f4 v[78:81], v[26:33], v[202:209], 0, v191, v192 op_sel_hi:[0,0,0]
	v_mfma_scale_f32_16x16x128_f8f6f4 v[74:77], v[18:25], v[202:209], 0, v191, v192 op_sel_hi:[0,0,0]
	v_mfma_scale_f32_16x16x128_f8f6f4 v[62:65], v[26:33], v[210:217], 0, v191, v192 op_sel_hi:[0,0,0]
	v_mfma_scale_f32_16x16x128_f8f6f4 v[58:61], v[18:25], v[210:217], 0, v191, v192 op_sel_hi:[0,0,0]
	v_mfma_scale_f32_16x16x128_f8f6f4 v[46:49], v[26:33], v[218:225], 0, v191, v192 op_sel_hi:[0,0,0]
	v_mfma_scale_f32_16x16x128_f8f6f4 v[42:45], v[18:25], v[218:225], 0, v191, v192 op_sel_hi:[0,0,0]
	s_setprio 0
	s_setprio 1
	s_nop 0
	v_mfma_scale_f32_16x16x128_f8f6f4 v[86:89], v[10:17], v[194:201], 0, v191, v192 op_sel_hi:[0,0,0]
	v_mfma_scale_f32_16x16x128_f8f6f4 v[82:85], v[2:9], v[194:201], 0, v191, v192 op_sel_hi:[0,0,0]
	v_mfma_scale_f32_16x16x128_f8f6f4 v[70:73], v[10:17], v[202:209], 0, v191, v192 op_sel_hi:[0,0,0]
	v_mfma_scale_f32_16x16x128_f8f6f4 v[66:69], v[2:9], v[202:209], 0, v191, v192 op_sel_hi:[0,0,0]
	v_mfma_scale_f32_16x16x128_f8f6f4 v[54:57], v[10:17], v[210:217], 0, v191, v192 op_sel_hi:[0,0,0]
	v_mfma_scale_f32_16x16x128_f8f6f4 v[50:53], v[2:9], v[210:217], 0, v191, v192 op_sel_hi:[0,0,0]
	v_mfma_scale_f32_16x16x128_f8f6f4 v[38:41], v[10:17], v[218:225], 0, v191, v192 op_sel_hi:[0,0,0]
	v_mfma_scale_f32_16x16x128_f8f6f4 v[34:37], v[2:9], v[218:225], 0, v191, v192 op_sel_hi:[0,0,0]
	s_setprio 0
	s_barrier
; #define PG8_STAGE(bufoff, gbase, voff) do { _Pragma("unroll") for (int _i = 0; _i < 2; ++_i) \
;         __builtin_amdgcn_global_load_lds((const unsigned*)((const char*)(gbase) + (voff)[_i]), (PG8_LAS unsigned*)(lds + (bufoff) + ldsw + _i * 8192), 16, 0, 0); } while (0)
; #define PG8_STAGE_A(bufoff, gbase, h, nx) do { if constexpr (Sched::GATHER) { const unsigned vv_[2] = {(nx) ? vAn[h][0] : vA[h][0], (nx) ? vAn[h][1] : vA[h][1]}; PG8_STAGE(bufoff, gbase, vv_); } \
;         else { PG8_STAGE(bufoff, (gbase) + (h) * hstep, voffA); } } while (0)
; #define PG8_LDA(dst, b, h) do { _Pragma("unroll") for (int m = 0; m < 4; ++m) _Pragma("unroll") for (int k = 0; k < 2; ++k) dst[m][k] = *(const PG8_LAS bf16x8*)(lds + PG8_SA(b, h) + aoff + m * 2048 + k * 1024); } while (0)
; #define PG8_LDB(dst, b, h) do { _Pragma("unroll") for (int n = 0; n < 2; ++n) _Pragma("unroll") for (int k = 0; k < 2; ++k) dst[n][k] = *(const PG8_LAS bf16x8*)(lds + PG8_SB(b, h) + boff + n * 2048 + k * 1024); } while (0)
; #define PG8_WAIT_V(n) asm volatile("s_waitcnt vmcnt(" #n ")" ::: "memory")
; #define PG8_WAIT_L(n) asm volatile("s_waitcnt lgkmcnt(" #n ")" ::: "memory")
; #define PG8_BAR __builtin_amdgcn_s_barrier()
; #define PG8_SCHED __builtin_amdgcn_sched_barrier(0)
;     ...
;             PG8_LDB(B0, 1, 0); PG8_LDB(B1, 1, 1); PG8_SCHED; PG8_LDA(At, 1, 0); PG8_STAGE_A(PG8_SA(0, 1), a2, 1, last);
;             PG8_WAIT_V(8); PG8_WAIT_L(0); PG8_BAR; PG8_MMA(0, 0, At, B0); PG8_MMA(0, 1, At, B1); PG8_BAR; PG8_SCHED;
;             PG8_LDA(At, 1, 1); PG8_STAGE(PG8_SB(1, 0), b3, voffB); PG8_STAGE(PG8_SB(1, 1), b3 + hstepB, voffB); PG8_STAGE_A(PG8_SA(1, 0), a3, 0, last);
;             PG8_WAIT_V(8); PG8_WAIT_L(0); PG8_BAR; PG8_MMA(1, 0, At, B0); PG8_MMA(1, 1, At, B1); PG8_BAR; PG8_SCHED;
	s_add_i32 s49, 0, 0x18000
	s_add_i32 s50, 0, 0x1c000
	v_add_u32_e32 v14, s49, v186
	v_add_u32_e32 v30, s50, v186
	ds_read_b128 v[2:5], v14
	ds_read_b128 v[6:9], v14 offset:1024
	ds_read_b128 v[10:13], v14 offset:2048
	ds_read_b128 v[14:17], v14 offset:3072
	ds_read_b128 v[18:21], v30
	ds_read_b128 v[22:25], v30 offset:1024
	ds_read_b128 v[26:29], v30 offset:2048
	ds_read_b128 v[30:33], v30 offset:3072
	s_add_u32 s28, s28, 0x20000
	s_addc_u32 s29, s29, 0
	s_mov_b32 m0, s35
	v_lshl_add_u64 v[226:227], s[28:29], 0, v[162:163]
	ds_read_b128 v[194:197], v190 offset:32768
	ds_read_b128 v[198:201], v190 offset:33792
	ds_read_b128 v[202:205], v190 offset:34816
	ds_read_b128 v[206:209], v190 offset:35840
	ds_read_b128 v[210:213], v190 offset:36864
	ds_read_b128 v[214:217], v190 offset:37888
	ds_read_b128 v[218:221], v190 offset:38912
	ds_read_b128 v[222:225], v190 offset:39936
	global_load_lds_dwordx4 v[226:227], off
	v_lshl_add_u64 v[226:227], s[28:29], 0, v[166:167]
	s_mov_b32 m0, s36
	s_nop 0
	global_load_lds_dwordx4 v[226:227], off
	s_waitcnt vmcnt(8)
	s_waitcnt lgkmcnt(0)
	s_barrier
	s_setprio 1
	v_mfma_scale_f32_16x16x128_f8f6f4 v[158:161], v[2:9], v[194:201], v[158:161], v191, v192 op_sel_hi:[0,0,0]
	v_mfma_scale_f32_16x16x128_f8f6f4 v[154:157], v[10:17], v[194:201], v[154:157], v191, v192 op_sel_hi:[0,0,0]
	v_mfma_scale_f32_16x16x128_f8f6f4 v[142:145], v[2:9], v[202:209], v[142:145], v191, v192 op_sel_hi:[0,0,0]
	v_mfma_scale_f32_16x16x128_f8f6f4 v[138:141], v[10:17], v[202:209], v[138:141], v191, v192 op_sel_hi:[0,0,0]
	v_mfma_scale_f32_16x16x128_f8f6f4 v[126:129], v[2:9], v[210:217], v[126:129], v191, v192 op_sel_hi:[0,0,0]
	v_mfma_scale_f32_16x16x128_f8f6f4 v[122:125], v[10:17], v[210:217], v[122:125], v191, v192 op_sel_hi:[0,0,0]
	v_mfma_scale_f32_16x16x128_f8f6f4 v[110:113], v[2:9], v[218:225], v[110:113], v191, v192 op_sel_hi:[0,0,0]
	v_mfma_scale_f32_16x16x128_f8f6f4 v[106:109], v[10:17], v[218:225], v[106:109], v191, v192 op_sel_hi:[0,0,0]
	s_setprio 0
	s_setprio 1
	s_nop 0
	v_mfma_scale_f32_16x16x128_f8f6f4 v[150:153], v[18:25], v[194:201], v[150:153], v191, v192 op_sel_hi:[0,0,0]
	v_mfma_scale_f32_16x16x128_f8f6f4 v[146:149], v[26:33], v[194:201], v[146:149], v191, v192 op_sel_hi:[0,0,0]
	v_mfma_scale_f32_16x16x128_f8f6f4 v[134:137], v[18:25], v[202:209], v[134:137], v191, v192 op_sel_hi:[0,0,0]
	v_mfma_scale_f32_16x16x128_f8f6f4 v[130:133], v[26:33], v[202:209], v[130:133], v191, v192 op_sel_hi:[0,0,0]
	v_mfma_scale_f32_16x16x128_f8f6f4 v[118:121], v[18:25], v[210:217], v[118:121], v191, v192 op_sel_hi:[0,0,0]
	v_mfma_scale_f32_16x16x128_f8f6f4 v[114:117], v[26:33], v[210:217], v[114:117], v191, v192 op_sel_hi:[0,0,0]
	v_mfma_scale_f32_16x16x128_f8f6f4 v[102:105], v[18:25], v[218:225], v[102:105], v191, v192 op_sel_hi:[0,0,0]
	v_mfma_scale_f32_16x16x128_f8f6f4 v[98:101], v[26:33], v[218:225], v[98:101], v191, v192 op_sel_hi:[0,0,0]
	s_setprio 0
	s_barrier
	s_add_i32 s28, s49, s30
	v_lshl_add_u64 v[178:179], v[178:179], 0, s[8:9]
	s_mov_b32 m0, s28
	ds_read_b128 v[194:197], v190 offset:49152
	ds_read_b128 v[198:201], v190 offset:50176
	ds_read_b128 v[202:205], v190 offset:51200
	ds_read_b128 v[206:209], v190 offset:52224
	ds_read_b128 v[210:213], v190 offset:53248
	ds_read_b128 v[214:217], v190 offset:54272
	ds_read_b128 v[218:221], v190 offset:55296
	ds_read_b128 v[222:225], v190 offset:56320
	global_load_lds_dwordx4 v[178:179], off
	s_add_i32 m0, s28, 0x2000
	s_add_u32 s26, s26, 0x2080
	v_lshl_add_u64 v[178:179], v[180:181], 0, s[8:9]
	s_addc_u32 s27, s27, 0
	s_add_i32 s28, s50, s30
	global_load_lds_dwordx4 v[178:179], off
	v_lshl_add_u64 v[178:179], s[26:27], 0, v[164:165]
	s_mov_b32 m0, s28
	s_nop 0
	global_load_lds_dwordx4 v[178:179], off
	v_lshl_add_u64 v[178:179], s[26:27], 0, v[168:169]
	s_add_i32 m0, s28, 0x2000
	s_nop 0
	global_load_lds_dwordx4 v[178:179], off
	v_lshl_add_u64 v[178:179], v[182:183], 0, s[8:9]
	s_mov_b32 m0, s39
	s_nop 0
	global_load_lds_dwordx4 v[178:179], off
	v_lshl_add_u64 v[178:179], v[184:185], 0, s[8:9]
	s_mov_b32 m0, s40
	s_nop 0
	global_load_lds_dwordx4 v[178:179], off
	s_waitcnt vmcnt(8)
	s_waitcnt lgkmcnt(0)
	s_barrier
	s_setprio 1
	v_mfma_scale_f32_16x16x128_f8f6f4 v[94:97], v[2:9], v[194:201], v[94:97], v191, v192 op_sel_hi:[0,0,0]
	v_mfma_scale_f32_16x16x128_f8f6f4 v[90:93], v[10:17], v[194:201], v[90:93], v191, v192 op_sel_hi:[0,0,0]
	v_mfma_scale_f32_16x16x128_f8f6f4 v[78:81], v[2:9], v[202:209], v[78:81], v191, v192 op_sel_hi:[0,0,0]
	v_mfma_scale_f32_16x16x128_f8f6f4 v[74:77], v[10:17], v[202:209], v[74:77], v191, v192 op_sel_hi:[0,0,0]
	v_mfma_scale_f32_16x16x128_f8f6f4 v[62:65], v[2:9], v[210:217], v[62:65], v191, v192 op_sel_hi:[0,0,0]
	v_mfma_scale_f32_16x16x128_f8f6f4 v[58:61], v[10:17], v[210:217], v[58:61], v191, v192 op_sel_hi:[0,0,0]
	v_mfma_scale_f32_16x16x128_f8f6f4 v[46:49], v[2:9], v[218:225], v[46:49], v191, v192 op_sel_hi:[0,0,0]
	v_mfma_scale_f32_16x16x128_f8f6f4 v[42:45], v[10:17], v[218:225], v[42:45], v191, v192 op_sel_hi:[0,0,0]
	s_setprio 0
	s_setprio 1
	s_nop 0
	v_mfma_scale_f32_16x16x128_f8f6f4 v[86:89], v[18:25], v[194:201], v[86:89], v191, v192 op_sel_hi:[0,0,0]
	v_mfma_scale_f32_16x16x128_f8f6f4 v[82:85], v[26:33], v[194:201], v[82:85], v191, v192 op_sel_hi:[0,0,0]
	v_mfma_scale_f32_16x16x128_f8f6f4 v[70:73], v[18:25], v[202:209], v[70:73], v191, v192 op_sel_hi:[0,0,0]
	v_mfma_scale_f32_16x16x128_f8f6f4 v[66:69], v[26:33], v[202:209], v[66:69], v191, v192 op_sel_hi:[0,0,0]
	v_mfma_scale_f32_16x16x128_f8f6f4 v[54:57], v[18:25], v[210:217], v[54:57], v191, v192 op_sel_hi:[0,0,0]
	v_mfma_scale_f32_16x16x128_f8f6f4 v[50:53], v[26:33], v[210:217], v[50:53], v191, v192 op_sel_hi:[0,0,0]
	v_mfma_scale_f32_16x16x128_f8f6f4 v[38:41], v[18:25], v[218:225], v[38:41], v191, v192 op_sel_hi:[0,0,0]
	v_mfma_scale_f32_16x16x128_f8f6f4 v[34:37], v[26:33], v[218:225], v[34:37], v191, v192 op_sel_hi:[0,0,0]
	s_setprio 0
	s_barrier
	s_add_i32 s48, s48, 2
	s_add_u32 s24, s24, 0x100
	s_addc_u32 s25, s25, 0
	s_add_u32 s46, s46, 0x100
	s_addc_u32 s47, s47, 0
; #define PG8_STAGE(bufoff, gbase, voff) do { _Pragma("unroll") for (int _i = 0; _i < 2; ++_i) \
;         __builtin_amdgcn_global_load_lds((const unsigned*)((const char*)(gbase) + (voff)[_i]), (PG8_LAS unsigned*)(lds + (bufoff) + ldsw + _i * 8192), 16, 0, 0); } while (0)
; #define PG8_STAGE_A(bufoff, gbase, h, nx) do { if constexpr (Sched::GATHER) { const unsigned vv_[2] = {(nx) ? vAn[h][0] : vA[h][0], (nx) ? vAn[h][1] : vA[h][1]}; PG8_STAGE(bufoff, gbase, vv_); } \
;         else { PG8_STAGE(bufoff, (gbase) + (h) * hstep, voffA); } } while (0)
; #define PG8_LDA(dst, b, h) do { _Pragma("unroll") for (int m = 0; m < 4; ++m) _Pragma("unroll") for (int k = 0; k < 2; ++k) dst[m][k] = *(const PG8_LAS bf16x8*)(lds + PG8_SA(b, h) + aoff + m * 2048 + k * 1024); } while (0)
; #define PG8_LDB(dst, b, h) do { _Pragma("unroll") for (int n = 0; n < 2; ++n) _Pragma("unroll") for (int k = 0; k < 2; ++k) dst[n][k] = *(const PG8_LAS bf16x8*)(lds + PG8_SB(b, h) + boff + n * 2048 + k * 1024); } while (0)
; #define PG8_WAIT_V(n) asm volatile("s_waitcnt vmcnt(" #n ")" ::: "memory")
; #define PG8_WAIT_L(n) asm volatile("s_waitcnt lgkmcnt(" #n ")" ::: "memory")
; #define PG8_BAR __builtin_amdgcn_s_barrier()
; #define PG8_SCHED __builtin_amdgcn_sched_barrier(0)
;     ...
;             PG8_LDB(B0, 0, 0); PG8_LDB(B1, 0, 1); PG8_SCHED; PG8_LDA(At, 0, 0); PG8_STAGE_A(PG8_SA(1, 1), a1, 1, false);
;             PG8_WAIT_V(8); PG8_WAIT_L(0); PG8_BAR; PG8_MMA(0, 0, At, B0); PG8_MMA(0, 1, At, B1); PG8_BAR; PG8_SCHED;
;             PG8_LDA(At, 0, 1); PG8_STAGE(PG8_SB(0, 0), b2, voffB); PG8_STAGE(PG8_SB(0, 1), b2 + hstepB, voffB); PG8_STAGE_A(PG8_SA(0, 0), a2, 0, last);
;             PG8_WAIT_V(8); PG8_WAIT_L(0); PG8_BAR; PG8_MMA(1, 0, At, B0); PG8_MMA(1, 1, At, B1); PG8_BAR; PG8_SCHED;
.LBB0_1205:
	ds_read_b128 v[26:29], v188
	ds_read_b128 v[30:33], v188 offset:1024
	ds_read_b128 v[18:21], v188 offset:2048
	ds_read_b128 v[22:25], v188 offset:3072
	ds_read_b128 v[10:13], v189
	ds_read_b128 v[14:17], v189 offset:1024
	ds_read_b128 v[2:5], v189 offset:2048
	ds_read_b128 v[6:9], v189 offset:3072
	s_add_u32 s26, s24, 0xfffe0080
	s_addc_u32 s27, s25, -1
	s_cmp_eq_u32 s48, 4
	s_cselect_b32 s29, s17, s27
	s_cselect_b32 s28, s44, s26
	s_cselect_b32 s27, s15, s47
	s_cselect_b32 s26, s45, s46
	v_lshl_add_u64 v[218:219], s[24:25], 0, v[170:171]
	s_add_i32 m0, s23, 0xc000
	ds_read_b128 v[178:181], v190
	ds_read_b128 v[182:185], v190 offset:1024
	ds_read_b128 v[194:197], v190 offset:2048
	ds_read_b128 v[198:201], v190 offset:3072
	ds_read_b128 v[202:205], v190 offset:4096
	ds_read_b128 v[206:209], v190 offset:5120
	ds_read_b128 v[210:213], v190 offset:6144
	ds_read_b128 v[214:217], v190 offset:7168
	global_load_lds_dwordx4 v[218:219], off
	v_lshl_add_u64 v[218:219], s[24:25], 0, v[172:173]
	s_add_i32 m0, s23, 0xe000
	s_nop 0
	global_load_lds_dwordx4 v[218:219], off
	s_waitcnt vmcnt(8)
	s_waitcnt lgkmcnt(0)
	s_barrier
	s_setprio 1
	v_mfma_scale_f32_16x16x128_f8f6f4 v[158:161], v[26:33], v[178:185], v[158:161], v191, v192 op_sel_hi:[0,0,0]
	v_mfma_scale_f32_16x16x128_f8f6f4 v[154:157], v[18:25], v[178:185], v[154:157], v191, v192 op_sel_hi:[0,0,0]
	v_mfma_scale_f32_16x16x128_f8f6f4 v[142:145], v[26:33], v[194:201], v[142:145], v191, v192 op_sel_hi:[0,0,0]
	v_mfma_scale_f32_16x16x128_f8f6f4 v[138:141], v[18:25], v[194:201], v[138:141], v191, v192 op_sel_hi:[0,0,0]
	v_mfma_scale_f32_16x16x128_f8f6f4 v[126:129], v[26:33], v[202:209], v[126:129], v191, v192 op_sel_hi:[0,0,0]
	v_mfma_scale_f32_16x16x128_f8f6f4 v[122:125], v[18:25], v[202:209], v[122:125], v191, v192 op_sel_hi:[0,0,0]
	v_mfma_scale_f32_16x16x128_f8f6f4 v[110:113], v[26:33], v[210:217], v[110:113], v191, v192 op_sel_hi:[0,0,0]
	v_mfma_scale_f32_16x16x128_f8f6f4 v[106:109], v[18:25], v[210:217], v[106:109], v191, v192 op_sel_hi:[0,0,0]
	s_setprio 0
	s_setprio 1
	s_nop 0
	v_mfma_scale_f32_16x16x128_f8f6f4 v[150:153], v[10:17], v[178:185], v[150:153], v191, v192 op_sel_hi:[0,0,0]
	v_mfma_scale_f32_16x16x128_f8f6f4 v[146:149], v[2:9], v[178:185], v[146:149], v191, v192 op_sel_hi:[0,0,0]
	v_mfma_scale_f32_16x16x128_f8f6f4 v[134:137], v[10:17], v[194:201], v[134:137], v191, v192 op_sel_hi:[0,0,0]
	v_mfma_scale_f32_16x16x128_f8f6f4 v[130:133], v[2:9], v[194:201], v[130:133], v191, v192 op_sel_hi:[0,0,0]
	v_mfma_scale_f32_16x16x128_f8f6f4 v[118:121], v[10:17], v[202:209], v[118:121], v191, v192 op_sel_hi:[0,0,0]
	v_mfma_scale_f32_16x16x128_f8f6f4 v[114:117], v[2:9], v[202:209], v[114:117], v191, v192 op_sel_hi:[0,0,0]
	v_mfma_scale_f32_16x16x128_f8f6f4 v[102:105], v[10:17], v[210:217], v[102:105], v191, v192 op_sel_hi:[0,0,0]
	v_mfma_scale_f32_16x16x128_f8f6f4 v[98:101], v[2:9], v[210:217], v[98:101], v191, v192 op_sel_hi:[0,0,0]
	s_setprio 0
	s_barrier
	s_add_i32 s49, s41, s30
	v_lshl_add_u64 v[178:179], s[26:27], 0, v[164:165]
	s_mov_b32 m0, s49
	ds_read_b128 v[194:197], v190 offset:16384
	ds_read_b128 v[198:201], v190 offset:17408
	ds_read_b128 v[202:205], v190 offset:18432
	ds_read_b128 v[206:209], v190 offset:19456
	ds_read_b128 v[210:213], v190 offset:20480
	ds_read_b128 v[214:217], v190 offset:21504
	ds_read_b128 v[218:221], v190 offset:22528
	ds_read_b128 v[222:225], v190 offset:23552
	global_load_lds_dwordx4 v[178:179], off
	s_add_i32 m0, s49, 0x2000
	s_add_u32 s50, s26, 0x2000
	v_lshl_add_u64 v[180:181], s[26:27], 0, v[168:169]
	s_addc_u32 s51, s27, 0
	s_add_i32 s49, s42, s30
	global_load_lds_dwordx4 v[180:181], off
	v_lshl_add_u64 v[182:183], s[50:51], 0, v[164:165]
	s_mov_b32 m0, s49
	v_lshl_add_u64 v[184:185], s[28:29], 0, v[166:167]
	global_load_lds_dwordx4 v[182:183], off
	v_lshl_add_u64 v[182:183], s[50:51], 0, v[168:169]
	s_add_i32 m0, s49, 0x2000
	s_nop 0
	global_load_lds_dwordx4 v[182:183], off
	v_lshl_add_u64 v[182:183], s[28:29], 0, v[162:163]
	s_mov_b32 m0, s23
	s_nop 0
	global_load_lds_dwordx4 v[182:183], off
	s_mov_b32 m0, s34
	s_nop 0
	global_load_lds_dwordx4 v[184:185], off
	s_waitcnt vmcnt(8)
	s_waitcnt lgkmcnt(0)
	s_barrier
	s_setprio 1
	v_mfma_scale_f32_16x16x128_f8f6f4 v[94:97], v[26:33], v[194:201], v[94:97], v191, v192 op_sel_hi:[0,0,0]
	v_mfma_scale_f32_16x16x128_f8f6f4 v[90:93], v[18:25], v[194:201], v[90:93], v191, v192 op_sel_hi:[0,0,0]
	v_mfma_scale_f32_16x16x128_f8f6f4 v[78:81], v[26:33], v[202:209], v[78:81], v191, v192 op_sel_hi:[0,0,0]
	v_mfma_scale_f32_16x16x128_f8f6f4 v[74:77], v[18:25], v[202:209], v[74:77], v191, v192 op_sel_hi:[0,0,0]
	v_mfma_scale_f32_16x16x128_f8f6f4 v[62:65], v[26:33], v[210:217], v[62:65], v191, v192 op_sel_hi:[0,0,0]
	v_mfma_scale_f32_16x16x128_f8f6f4 v[58:61], v[18:25], v[210:217], v[58:61], v191, v192 op_sel_hi:[0,0,0]
	v_mfma_scale_f32_16x16x128_f8f6f4 v[46:49], v[26:33], v[218:225], v[46:49], v191, v192 op_sel_hi:[0,0,0]
	v_mfma_scale_f32_16x16x128_f8f6f4 v[42:45], v[18:25], v[218:225], v[42:45], v191, v192 op_sel_hi:[0,0,0]
	s_setprio 0
	s_setprio 1
	s_nop 0
	v_mfma_scale_f32_16x16x128_f8f6f4 v[86:89], v[10:17], v[194:201], v[86:89], v191, v192 op_sel_hi:[0,0,0]
	v_mfma_scale_f32_16x16x128_f8f6f4 v[82:85], v[2:9], v[194:201], v[82:85], v191, v192 op_sel_hi:[0,0,0]
	v_mfma_scale_f32_16x16x128_f8f6f4 v[70:73], v[10:17], v[202:209], v[70:73], v191, v192 op_sel_hi:[0,0,0]
	v_mfma_scale_f32_16x16x128_f8f6f4 v[66:69], v[2:9], v[202:209], v[66:69], v191, v192 op_sel_hi:[0,0,0]
	v_mfma_scale_f32_16x16x128_f8f6f4 v[54:57], v[10:17], v[210:217], v[54:57], v191, v192 op_sel_hi:[0,0,0]
	v_mfma_scale_f32_16x16x128_f8f6f4 v[50:53], v[2:9], v[210:217], v[50:53], v191, v192 op_sel_hi:[0,0,0]
	v_mfma_scale_f32_16x16x128_f8f6f4 v[38:41], v[10:17], v[218:225], v[38:41], v191, v192 op_sel_hi:[0,0,0]
	v_mfma_scale_f32_16x16x128_f8f6f4 v[34:37], v[2:9], v[218:225], v[34:37], v191, v192 op_sel_hi:[0,0,0]
	s_setprio 0
	s_barrier
; #define PG8_STAGE(bufoff, gbase, voff) do { _Pragma("unroll") for (int _i = 0; _i < 2; ++_i) \
;         __builtin_amdgcn_global_load_lds((const unsigned*)((const char*)(gbase) + (voff)[_i]), (PG8_LAS unsigned*)(lds + (bufoff) + ldsw + _i * 8192), 16, 0, 0); } while (0)
; #define PG8_STAGE_A(bufoff, gbase, h, nx) do { if constexpr (Sched::GATHER) { const unsigned vv_[2] = {(nx) ? vAn[h][0] : vA[h][0], (nx) ? vAn[h][1] : vA[h][1]}; PG8_STAGE(bufoff, gbase, vv_); } \
;         else { PG8_STAGE(bufoff, (gbase) + (h) * hstep, voffA); } } while (0)
; #define PG8_LDA(dst, b, h) do { _Pragma("unroll") for (int m = 0; m < 4; ++m) _Pragma("unroll") for (int k = 0; k < 2; ++k) dst[m][k] = *(const PG8_LAS bf16x8*)(lds + PG8_SA(b, h) + aoff + m * 2048 + k * 1024); } while (0)
; #define PG8_LDB(dst, b, h) do { _Pragma("unroll") for (int n = 0; n < 2; ++n) _Pragma("unroll") for (int k = 0; k < 2; ++k) dst[n][k] = *(const PG8_LAS bf16x8*)(lds + PG8_SB(b, h) + boff + n * 2048 + k * 1024); } while (0)
; #define PG8_WAIT_V(n) asm volatile("s_waitcnt vmcnt(" #n ")" ::: "memory")
; #define PG8_WAIT_L(n) asm volatile("s_waitcnt lgkmcnt(" #n ")" ::: "memory")
; #define PG8_BAR __builtin_amdgcn_s_barrier()
; #define PG8_SCHED __builtin_amdgcn_sched_barrier(0)
;     ...
;             PG8_LDB(B0, 1, 0); PG8_LDB(B1, 1, 1); PG8_SCHED; PG8_LDA(At, 1, 0); PG8_STAGE_A(PG8_SA(0, 1), a2, 1, last);
;             PG8_WAIT_V(8); PG8_WAIT_L(0); PG8_BAR; PG8_MMA(0, 0, At, B0); PG8_MMA(0, 1, At, B1); PG8_BAR; PG8_SCHED;
;             PG8_LDA(At, 1, 1); PG8_STAGE(PG8_SB(1, 0), b3, voffB); PG8_STAGE(PG8_SB(1, 1), b3 + hstepB, voffB); PG8_STAGE_A(PG8_SA(1, 0), a3, 0, last);
;             PG8_WAIT_V(8); PG8_WAIT_L(0); PG8_BAR; PG8_MMA(1, 0, At, B0); PG8_MMA(1, 1, At, B1); PG8_BAR; PG8_SCHED;
;     ...
;         }
;         if constexpr (F8) asm volatile("s_nop 15\n\ts_nop 15\n\ts_nop 15" ::: "memory");
;         if constexpr (ALIGN_EPI) { if (wr == 0) PG8_BAR; }
	s_add_i32 s49, 0, 0x18000
	s_add_i32 s50, 0, 0x1c000
	v_add_u32_e32 v14, s49, v186
	v_add_u32_e32 v30, s50, v186
	ds_read_b128 v[2:5], v14
	ds_read_b128 v[6:9], v14 offset:1024
	ds_read_b128 v[10:13], v14 offset:2048
	ds_read_b128 v[14:17], v14 offset:3072
	ds_read_b128 v[18:21], v30
	ds_read_b128 v[22:25], v30 offset:1024
	ds_read_b128 v[26:29], v30 offset:2048
	ds_read_b128 v[30:33], v30 offset:3072
	s_add_u32 s28, s28, 0x20000
	s_addc_u32 s29, s29, 0
	s_mov_b32 m0, s35
	v_lshl_add_u64 v[226:227], s[28:29], 0, v[162:163]
	ds_read_b128 v[194:197], v190 offset:32768
	ds_read_b128 v[198:201], v190 offset:33792
	ds_read_b128 v[202:205], v190 offset:34816
	ds_read_b128 v[206:209], v190 offset:35840
	ds_read_b128 v[210:213], v190 offset:36864
	ds_read_b128 v[214:217], v190 offset:37888
	ds_read_b128 v[218:221], v190 offset:38912
	ds_read_b128 v[222:225], v190 offset:39936
	global_load_lds_dwordx4 v[226:227], off
	v_lshl_add_u64 v[226:227], s[28:29], 0, v[166:167]
	s_mov_b32 m0, s36
	s_nop 0
	global_load_lds_dwordx4 v[226:227], off
	s_waitcnt vmcnt(8)
	s_waitcnt lgkmcnt(0)
	s_barrier
	s_setprio 1
	v_mfma_scale_f32_16x16x128_f8f6f4 v[158:161], v[2:9], v[194:201], v[158:161], v191, v192 op_sel_hi:[0,0,0]
	v_mfma_scale_f32_16x16x128_f8f6f4 v[154:157], v[10:17], v[194:201], v[154:157], v191, v192 op_sel_hi:[0,0,0]
	v_mfma_scale_f32_16x16x128_f8f6f4 v[142:145], v[2:9], v[202:209], v[142:145], v191, v192 op_sel_hi:[0,0,0]
	v_mfma_scale_f32_16x16x128_f8f6f4 v[138:141], v[10:17], v[202:209], v[138:141], v191, v192 op_sel_hi:[0,0,0]
	v_mfma_scale_f32_16x16x128_f8f6f4 v[126:129], v[2:9], v[210:217], v[126:129], v191, v192 op_sel_hi:[0,0,0]
	v_mfma_scale_f32_16x16x128_f8f6f4 v[122:125], v[10:17], v[210:217], v[122:125], v191, v192 op_sel_hi:[0,0,0]
	v_mfma_scale_f32_16x16x128_f8f6f4 v[110:113], v[2:9], v[218:225], v[110:113], v191, v192 op_sel_hi:[0,0,0]
	v_mfma_scale_f32_16x16x128_f8f6f4 v[106:109], v[10:17], v[218:225], v[106:109], v191, v192 op_sel_hi:[0,0,0]
	s_setprio 0
	s_setprio 1
	s_nop 0
	v_mfma_scale_f32_16x16x128_f8f6f4 v[150:153], v[18:25], v[194:201], v[150:153], v191, v192 op_sel_hi:[0,0,0]
	v_mfma_scale_f32_16x16x128_f8f6f4 v[146:149], v[26:33], v[194:201], v[146:149], v191, v192 op_sel_hi:[0,0,0]
	v_mfma_scale_f32_16x16x128_f8f6f4 v[134:137], v[18:25], v[202:209], v[134:137], v191, v192 op_sel_hi:[0,0,0]
	v_mfma_scale_f32_16x16x128_f8f6f4 v[130:133], v[26:33], v[202:209], v[130:133], v191, v192 op_sel_hi:[0,0,0]
	v_mfma_scale_f32_16x16x128_f8f6f4 v[118:121], v[18:25], v[210:217], v[118:121], v191, v192 op_sel_hi:[0,0,0]
	v_mfma_scale_f32_16x16x128_f8f6f4 v[114:117], v[26:33], v[210:217], v[114:117], v191, v192 op_sel_hi:[0,0,0]
	v_mfma_scale_f32_16x16x128_f8f6f4 v[102:105], v[18:25], v[218:225], v[102:105], v191, v192 op_sel_hi:[0,0,0]
	v_mfma_scale_f32_16x16x128_f8f6f4 v[98:101], v[26:33], v[218:225], v[98:101], v191, v192 op_sel_hi:[0,0,0]
	s_setprio 0
	s_barrier
	s_add_i32 s28, s49, s30
	v_lshl_add_u64 v[178:179], v[178:179], 0, s[8:9]
	s_mov_b32 m0, s28
	ds_read_b128 v[194:197], v190 offset:49152
	ds_read_b128 v[198:201], v190 offset:50176
	ds_read_b128 v[202:205], v190 offset:51200
	ds_read_b128 v[206:209], v190 offset:52224
	ds_read_b128 v[210:213], v190 offset:53248
	ds_read_b128 v[214:217], v190 offset:54272
	ds_read_b128 v[218:221], v190 offset:55296
	ds_read_b128 v[222:225], v190 offset:56320
	global_load_lds_dwordx4 v[178:179], off
	s_add_i32 m0, s28, 0x2000
	s_add_u32 s26, s26, 0x2080
	v_lshl_add_u64 v[178:179], v[180:181], 0, s[8:9]
	s_addc_u32 s27, s27, 0
	s_add_i32 s28, s50, s30
	global_load_lds_dwordx4 v[178:179], off
	v_lshl_add_u64 v[178:179], s[26:27], 0, v[164:165]
	s_mov_b32 m0, s28
	s_nop 0
	global_load_lds_dwordx4 v[178:179], off
	v_lshl_add_u64 v[178:179], s[26:27], 0, v[168:169]
	s_add_i32 m0, s28, 0x2000
	s_nop 0
	global_load_lds_dwordx4 v[178:179], off
	v_lshl_add_u64 v[178:179], v[182:183], 0, s[8:9]
	s_mov_b32 m0, s39
	s_nop 0
	global_load_lds_dwordx4 v[178:179], off
	v_lshl_add_u64 v[178:179], v[184:185], 0, s[8:9]
	s_mov_b32 m0, s40
	s_nop 0
	global_load_lds_dwordx4 v[178:179], off
	s_waitcnt vmcnt(8)
	s_waitcnt lgkmcnt(0)
	s_barrier
	s_setprio 1
	v_mfma_scale_f32_16x16x128_f8f6f4 v[94:97], v[2:9], v[194:201], v[94:97], v191, v192 op_sel_hi:[0,0,0]
	v_mfma_scale_f32_16x16x128_f8f6f4 v[90:93], v[10:17], v[194:201], v[90:93], v191, v192 op_sel_hi:[0,0,0]
	v_mfma_scale_f32_16x16x128_f8f6f4 v[78:81], v[2:9], v[202:209], v[78:81], v191, v192 op_sel_hi:[0,0,0]
	v_mfma_scale_f32_16x16x128_f8f6f4 v[74:77], v[10:17], v[202:209], v[74:77], v191, v192 op_sel_hi:[0,0,0]
	v_mfma_scale_f32_16x16x128_f8f6f4 v[62:65], v[2:9], v[210:217], v[62:65], v191, v192 op_sel_hi:[0,0,0]
	v_mfma_scale_f32_16x16x128_f8f6f4 v[58:61], v[10:17], v[210:217], v[58:61], v191, v192 op_sel_hi:[0,0,0]
	v_mfma_scale_f32_16x16x128_f8f6f4 v[46:49], v[2:9], v[218:225], v[46:49], v191, v192 op_sel_hi:[0,0,0]
	v_mfma_scale_f32_16x16x128_f8f6f4 v[42:45], v[10:17], v[218:225], v[42:45], v191, v192 op_sel_hi:[0,0,0]
	s_setprio 0
	s_setprio 1
	s_nop 0
	v_mfma_scale_f32_16x16x128_f8f6f4 v[86:89], v[18:25], v[194:201], v[86:89], v191, v192 op_sel_hi:[0,0,0]
	v_mfma_scale_f32_16x16x128_f8f6f4 v[82:85], v[26:33], v[194:201], v[82:85], v191, v192 op_sel_hi:[0,0,0]
	v_mfma_scale_f32_16x16x128_f8f6f4 v[70:73], v[18:25], v[202:209], v[70:73], v191, v192 op_sel_hi:[0,0,0]
	v_mfma_scale_f32_16x16x128_f8f6f4 v[66:69], v[26:33], v[202:209], v[66:69], v191, v192 op_sel_hi:[0,0,0]
	v_mfma_scale_f32_16x16x128_f8f6f4 v[54:57], v[18:25], v[210:217], v[54:57], v191, v192 op_sel_hi:[0,0,0]
	v_mfma_scale_f32_16x16x128_f8f6f4 v[50:53], v[26:33], v[210:217], v[50:53], v191, v192 op_sel_hi:[0,0,0]
	v_mfma_scale_f32_16x16x128_f8f6f4 v[38:41], v[18:25], v[218:225], v[38:41], v191, v192 op_sel_hi:[0,0,0]
	v_mfma_scale_f32_16x16x128_f8f6f4 v[34:37], v[26:33], v[218:225], v[34:37], v191, v192 op_sel_hi:[0,0,0]
	s_setprio 0
	s_barrier
	s_add_i32 s48, s48, 2
	s_add_u32 s24, s24, 0x100
	s_addc_u32 s25, s25, 0
	s_add_u32 s46, s46, 0x100
	s_addc_u32 s47, s47, 0
	s_cmp_gt_u32 s48, 5
	s_cbranch_scc0 .LBB0_1205
	s_and_b64 vcc, exec, s[10:11]
	s_cbranch_vccz .LBB0_1208
	s_barrier

; #define PG8_STAGE(bufoff, gbase, voff) do { _Pragma("unroll") for (int _i = 0; _i < 2; ++_i) \
;         __builtin_amdgcn_global_load_lds((const unsigned*)((const char*)(gbase) + (voff)[_i]), (PG8_LAS unsigned*)(lds + (bufoff) + ldsw + _i * 8192), 16, 0, 0); } while (0)
; #define PG8_STAGE_A(bufoff, gbase, h, nx) do { if constexpr (Sched::GATHER) { const unsigned vv_[2] = {(nx) ? vAn[h][0] : vA[h][0], (nx) ? vAn[h][1] : vA[h][1]}; PG8_STAGE(bufoff, gbase, vv_); } \
;         else { PG8_STAGE(bufoff, (gbase) + (h) * hstep, voffA); } } while (0)
; #define PG8_LDA(dst, b, h) do { _Pragma("unroll") for (int m = 0; m < 4; ++m) _Pragma("unroll") for (int k = 0; k < 2; ++k) dst[m][k] = *(const PG8_LAS bf16x8*)(lds + PG8_SA(b, h) + aoff + m * 2048 + k * 1024); } while (0)
; #define PG8_WAIT_V(n) asm volatile("s_waitcnt vmcnt(" #n ")" ::: "memory")
; #define PG8_WAIT_L(n) asm volatile("s_waitcnt lgkmcnt(" #n ")" ::: "memory")
;     ...
;         const bool has_next = S.next(ui + 1, nxt);
;         const char* nA = Sched::GATHER ? cA : (has_next ? (const char*)g.A + (size_t)nxt.pm * tstep : cA);
;         if constexpr (Sched::GATHER) { if (has_next) { PG8_AOFF(vAn, ui + 1); } else { _Pragma("unroll") for (int h_ = 0; h_ < 2; ++h_) _Pragma("unroll") for (int i_ = 0; i_ < 2; ++i_) vAn[h_][i_] = vA[h_][i_]; } } const char* nB = has_next ? (const char*)g.Bt + (size_t)nxt.pb * tstep : cB;
; #pragma nounroll
;         for (int t = 0; t < nt; t += 2) {
;             const bool last = (t == nt - 2);
;             const char* a1 = cA + (size_t)(t + 1) * kstep;
;             const char* a2 = last ? nA : cA + (size_t)(t + 2) * kstep; const char* b2 = last ? nB : cB + (size_t)(t + 2) * kstep;
;             const char* a3 = a2 + kstep; const char* b3 = b2 + kstep;
;             if (last && has_next) S.a_ready(nxt);
;             if constexpr (SP2) {
;             PG8_LDB(B0, 0, 0); PG8_LDB(B1, 0, 1); PG8_SCHED; PG8_LDA(At, 0, 0); PG8_STAGE_A(PG8_SA(1, 1), a1, 1, false);
;             PG8_WAIT_V(8); PG8_WAIT_L(0); PG8_BAR; PG8_MMA(0, 0, At, B0); PG8_MMA(0, 1, At, B1); PG8_BAR; PG8_SCHED;
;             PG8_LDA(At, 0, 1); PG8_STAGE(PG8_SB(0, 0), b2, voffB); PG8_STAGE(PG8_SB(0, 1), b2 + hstepB, voffB); PG8_STAGE_A(PG8_SA(0, 0), a2, 0, last);
;             PG8_WAIT_V(8); PG8_WAIT_L(0); PG8_BAR; PG8_MMA(1, 0, At, B0); PG8_MMA(1, 1, At, B1); PG8_BAR; PG8_SCHED;
.LBB0_1571:
	s_ashr_i32 s17, s16, 31
	s_lshl_b64 s[18:19], s[16:17], 18
	v_readlane_b32 s22, v255, 1
	v_readlane_b32 s23, v255, 2
	s_add_u32 s18, s22, s18
	s_addc_u32 s19, s23, s19
	s_and_b64 s[4:5], s[4:5], exec
	s_cselect_b32 s17, s19, s21
	s_cselect_b32 s51, s18, s20
	v_mov_b32_e32 v175, v167
	v_mov_b32_e32 v177, v167
	s_add_u32 s52, s20, 0x100
	v_readlane_b32 s58, v254, 0
	v_lshl_add_u64 v[178:179], s[12:13], 0, v[176:177]
	v_lshl_add_u64 v[180:181], s[12:13], 0, v[174:175]
	s_addc_u32 s53, s21, 0
	s_mov_b32 s54, -2
	s_mov_b64 s[4:5], 0
	v_readlane_b32 s59, v254, 1
	ds_read_b128 v[26:29], v194
	ds_read_b128 v[30:33], v194 offset:1024
	ds_read_b128 v[18:21], v194 offset:2048
	ds_read_b128 v[22:25], v194 offset:3072
	ds_read_b128 v[10:13], v195
	ds_read_b128 v[14:17], v195 offset:1024
	ds_read_b128 v[2:5], v195 offset:2048
	ds_read_b128 v[6:9], v195 offset:3072
	s_add_u32 s20, s58, s4
	s_addc_u32 s21, s59, s5
	s_add_u32 s22, s20, 0x25400100
	s_addc_u32 s23, s21, 0
	s_add_u32 s55, s52, s4
	s_addc_u32 s56, s53, s5
	s_cmpk_eq_i32 s4, 0x300
	s_cselect_b64 vcc, -1, 0
	s_and_b64 s[20:21], vcc, exec
	s_cselect_b32 s23, s93, s23
	s_cselect_b32 s22, s92, s22
	s_cselect_b32 s21, s17, s56
	s_cselect_b32 s20, s51, s55
	s_mov_b32 m0, s39
	v_lshl_add_u64 v[232:233], v[180:181], 0, s[4:5]
	ds_read_b128 v[182:185], v196
	ds_read_b128 v[186:189], v196 offset:1024
	ds_read_b128 v[208:211], v196 offset:2048
	ds_read_b128 v[212:215], v196 offset:3072
	ds_read_b128 v[216:219], v196 offset:4096
	ds_read_b128 v[220:223], v196 offset:5120
	ds_read_b128 v[224:227], v196 offset:6144
	ds_read_b128 v[228:231], v196 offset:7168
	global_load_lds_dwordx4 v[232:233], off
	v_lshl_add_u64 v[232:233], v[178:179], 0, s[4:5]
	s_mov_b32 m0, s40
	s_nop 0
	global_load_lds_dwordx4 v[232:233], off
	s_waitcnt vmcnt(8)
	s_waitcnt lgkmcnt(0)
	s_barrier
	s_setprio 1
	v_mfma_scale_f32_16x16x128_f8f6f4 v[158:161], v[26:33], v[182:189], 0, v197, v198 op_sel_hi:[0,0,0]
	v_mfma_scale_f32_16x16x128_f8f6f4 v[150:153], v[18:25], v[182:189], 0, v197, v198 op_sel_hi:[0,0,0]
	v_mfma_scale_f32_16x16x128_f8f6f4 v[142:145], v[26:33], v[208:215], 0, v197, v198 op_sel_hi:[0,0,0]
	v_mfma_scale_f32_16x16x128_f8f6f4 v[134:137], v[18:25], v[208:215], 0, v197, v198 op_sel_hi:[0,0,0]
	v_mfma_scale_f32_16x16x128_f8f6f4 v[126:129], v[26:33], v[216:223], 0, v197, v198 op_sel_hi:[0,0,0]
	v_mfma_scale_f32_16x16x128_f8f6f4 v[118:121], v[18:25], v[216:223], 0, v197, v198 op_sel_hi:[0,0,0]
	v_mfma_scale_f32_16x16x128_f8f6f4 v[110:113], v[26:33], v[224:231], 0, v197, v198 op_sel_hi:[0,0,0]
	v_mfma_scale_f32_16x16x128_f8f6f4 v[98:101], v[18:25], v[224:231], 0, v197, v198 op_sel_hi:[0,0,0]
	s_setprio 0
	s_setprio 1
	s_nop 0
	v_mfma_scale_f32_16x16x128_f8f6f4 v[154:157], v[10:17], v[182:189], 0, v197, v198 op_sel_hi:[0,0,0]
	v_mfma_scale_f32_16x16x128_f8f6f4 v[146:149], v[2:9], v[182:189], 0, v197, v198 op_sel_hi:[0,0,0]
	v_mfma_scale_f32_16x16x128_f8f6f4 v[138:141], v[10:17], v[208:215], 0, v197, v198 op_sel_hi:[0,0,0]
	v_mfma_scale_f32_16x16x128_f8f6f4 v[130:133], v[2:9], v[208:215], 0, v197, v198 op_sel_hi:[0,0,0]
	v_mfma_scale_f32_16x16x128_f8f6f4 v[122:125], v[10:17], v[216:223], 0, v197, v198 op_sel_hi:[0,0,0]
	v_mfma_scale_f32_16x16x128_f8f6f4 v[114:117], v[2:9], v[216:223], 0, v197, v198 op_sel_hi:[0,0,0]
	v_mfma_scale_f32_16x16x128_f8f6f4 v[106:109], v[10:17], v[224:231], 0, v197, v198 op_sel_hi:[0,0,0]
	v_mfma_scale_f32_16x16x128_f8f6f4 v[94:97], v[2:9], v[224:231], 0, v197, v198 op_sel_hi:[0,0,0]
	s_setprio 0
	s_barrier
	s_mov_b32 m0, s41
	v_lshl_add_u64 v[182:183], s[20:21], 0, v[164:165]
	s_add_u32 s56, s20, 0x20000
	ds_read_b128 v[208:211], v196 offset:16384
	ds_read_b128 v[212:215], v196 offset:17408
	ds_read_b128 v[216:219], v196 offset:18432
	ds_read_b128 v[220:223], v196 offset:19456
	ds_read_b128 v[224:227], v196 offset:20480
	ds_read_b128 v[228:231], v196 offset:21504
	ds_read_b128 v[232:235], v196 offset:22528
	ds_read_b128 v[236:239], v196 offset:23552
	global_load_lds_dwordx4 v[182:183], off
	v_lshl_add_u64 v[184:185], s[20:21], 0, v[162:163]
	s_mov_b32 m0, s42
	s_addc_u32 s57, s21, 0
	global_load_lds_dwordx4 v[184:185], off
	v_lshl_add_u64 v[186:187], s[56:57], 0, v[164:165]
	s_mov_b32 m0, s43
	v_cndmask_b32_e32 v166, v206, v202, vcc
	global_load_lds_dwordx4 v[186:187], off
	v_lshl_add_u64 v[186:187], s[56:57], 0, v[162:163]
	s_mov_b32 m0, s44
	v_lshl_add_u64 v[188:189], s[22:23], 0, v[166:167]
	global_load_lds_dwordx4 v[186:187], off
	s_mov_b32 m0, s26
	v_cndmask_b32_e32 v186, v172, v203, vcc
	global_load_lds_dwordx4 v166, s[22:23]
	s_mov_b32 m0, s27
	v_mov_b32_e32 v187, v167
	global_load_lds_dwordx4 v186, s[22:23]
	s_waitcnt vmcnt(8)
	s_waitcnt lgkmcnt(0)
	v_lshl_add_u64 v[186:187], s[22:23], 0, v[186:187]
	s_barrier
	s_setprio 1
	s_nop 0
	s_waitcnt lgkmcnt(0)
	v_mfma_scale_f32_16x16x128_f8f6f4 v[82:85], v[26:33], v[208:215], 0, v197, v198 op_sel_hi:[0,0,0]
	v_mfma_scale_f32_16x16x128_f8f6f4 v[70:73], v[18:25], v[208:215], 0, v197, v198 op_sel_hi:[0,0,0]
	v_mfma_scale_f32_16x16x128_f8f6f4 v[78:81], v[26:33], v[216:223], 0, v197, v198 op_sel_hi:[0,0,0]
	v_mfma_scale_f32_16x16x128_f8f6f4 v[66:69], v[18:25], v[216:223], 0, v197, v198 op_sel_hi:[0,0,0]
	v_mfma_scale_f32_16x16x128_f8f6f4 v[58:61], v[26:33], v[224:231], 0, v197, v198 op_sel_hi:[0,0,0]
	v_mfma_scale_f32_16x16x128_f8f6f4 v[50:53], v[18:25], v[224:231], 0, v197, v198 op_sel_hi:[0,0,0]
	v_mfma_scale_f32_16x16x128_f8f6f4 v[42:45], v[26:33], v[232:239], 0, v197, v198 op_sel_hi:[0,0,0]
	v_mfma_scale_f32_16x16x128_f8f6f4 v[34:37], v[18:25], v[232:239], 0, v197, v198 op_sel_hi:[0,0,0]
	s_setprio 0
	s_setprio 1
	s_nop 0
	v_mfma_scale_f32_16x16x128_f8f6f4 v[102:105], v[10:17], v[208:215], 0, v197, v198 op_sel_hi:[0,0,0]
	v_mfma_scale_f32_16x16x128_f8f6f4 v[90:93], v[2:9], v[208:215], 0, v197, v198 op_sel_hi:[0,0,0]
	v_mfma_scale_f32_16x16x128_f8f6f4 v[86:89], v[10:17], v[216:223], 0, v197, v198 op_sel_hi:[0,0,0]
	v_mfma_scale_f32_16x16x128_f8f6f4 v[74:77], v[2:9], v[216:223], 0, v197, v198 op_sel_hi:[0,0,0]
	v_mfma_scale_f32_16x16x128_f8f6f4 v[62:65], v[10:17], v[224:231], 0, v197, v198 op_sel_hi:[0,0,0]
	v_mfma_scale_f32_16x16x128_f8f6f4 v[54:57], v[2:9], v[224:231], 0, v197, v198 op_sel_hi:[0,0,0]
	v_mfma_scale_f32_16x16x128_f8f6f4 v[46:49], v[10:17], v[232:239], 0, v197, v198 op_sel_hi:[0,0,0]
	v_mfma_scale_f32_16x16x128_f8f6f4 v[38:41], v[2:9], v[232:239], 0, v197, v198 op_sel_hi:[0,0,0]
	s_setprio 0
	s_barrier
; #define PG8_STAGE(bufoff, gbase, voff) do { _Pragma("unroll") for (int _i = 0; _i < 2; ++_i) \
;         __builtin_amdgcn_global_load_lds((const unsigned*)((const char*)(gbase) + (voff)[_i]), (PG8_LAS unsigned*)(lds + (bufoff) + ldsw + _i * 8192), 16, 0, 0); } while (0)
; #define PG8_STAGE_A(bufoff, gbase, h, nx) do { if constexpr (Sched::GATHER) { const unsigned vv_[2] = {(nx) ? vAn[h][0] : vA[h][0], (nx) ? vAn[h][1] : vA[h][1]}; PG8_STAGE(bufoff, gbase, vv_); } \
;         else { PG8_STAGE(bufoff, (gbase) + (h) * hstep, voffA); } } while (0)
; #define PG8_LDA(dst, b, h) do { _Pragma("unroll") for (int m = 0; m < 4; ++m) _Pragma("unroll") for (int k = 0; k < 2; ++k) dst[m][k] = *(const PG8_LAS bf16x8*)(lds + PG8_SA(b, h) + aoff + m * 2048 + k * 1024); } while (0)
; #define PG8_LDB(dst, b, h) do { _Pragma("unroll") for (int n = 0; n < 2; ++n) _Pragma("unroll") for (int k = 0; k < 2; ++k) dst[n][k] = *(const PG8_LAS bf16x8*)(lds + PG8_SB(b, h) + boff + n * 2048 + k * 1024); } while (0)
; #define PG8_WAIT_V(n) asm volatile("s_waitcnt vmcnt(" #n ")" ::: "memory")
; #define PG8_WAIT_L(n) asm volatile("s_waitcnt lgkmcnt(" #n ")" ::: "memory")
; #define PG8_BAR __builtin_amdgcn_s_barrier()
; #define PG8_SCHED __builtin_amdgcn_sched_barrier(0)
;     ...
;             PG8_LDB(B0, 1, 0); PG8_LDB(B1, 1, 1); PG8_SCHED; PG8_LDA(At, 1, 0); PG8_STAGE_A(PG8_SA(0, 1), a2, 1, last);
;             PG8_WAIT_V(8); PG8_WAIT_L(0); PG8_BAR; PG8_MMA(0, 0, At, B0); PG8_MMA(0, 1, At, B1); PG8_BAR; PG8_SCHED;
;             PG8_LDA(At, 1, 1); PG8_STAGE(PG8_SB(1, 0), b3, voffB); PG8_STAGE(PG8_SB(1, 1), b3 + hstepB, voffB); PG8_STAGE_A(PG8_SA(1, 0), a3, 0, last);
;             PG8_WAIT_V(8); PG8_WAIT_L(0); PG8_BAR; PG8_MMA(1, 0, At, B0); PG8_MMA(1, 1, At, B1); PG8_BAR; PG8_SCHED;
	ds_read_b128 v[2:5], v199
	ds_read_b128 v[6:9], v199 offset:1024
	ds_read_b128 v[10:13], v199 offset:2048
	ds_read_b128 v[14:17], v199 offset:3072
	ds_read_b128 v[18:21], v200
	ds_read_b128 v[22:25], v200 offset:1024
	ds_read_b128 v[26:29], v200 offset:2048
	ds_read_b128 v[30:33], v200 offset:3072
	s_mov_b32 m0, s28
	v_cndmask_b32_e32 v166, v174, v204, vcc
	ds_read_b128 v[208:211], v196 offset:32768
	ds_read_b128 v[212:215], v196 offset:33792
	ds_read_b128 v[216:219], v196 offset:34816
	ds_read_b128 v[220:223], v196 offset:35840
	ds_read_b128 v[224:227], v196 offset:36864
	ds_read_b128 v[228:231], v196 offset:37888
	ds_read_b128 v[232:235], v196 offset:38912
	ds_read_b128 v[236:239], v196 offset:39936
	v_cndmask_b32_e32 v175, v176, v205, vcc
	global_load_lds_dwordx4 v166, s[22:23]
	s_mov_b32 m0, s29
	s_nop 0
	global_load_lds_dwordx4 v175, s[22:23]
	s_waitcnt vmcnt(8)
	s_waitcnt lgkmcnt(0)
	s_barrier
	s_setprio 1
	v_mfma_scale_f32_16x16x128_f8f6f4 v[158:161], v[2:9], v[208:215], v[158:161], v197, v198 op_sel_hi:[0,0,0]
	v_mfma_scale_f32_16x16x128_f8f6f4 v[150:153], v[10:17], v[208:215], v[150:153], v197, v198 op_sel_hi:[0,0,0]
	v_mfma_scale_f32_16x16x128_f8f6f4 v[142:145], v[2:9], v[216:223], v[142:145], v197, v198 op_sel_hi:[0,0,0]
	v_mfma_scale_f32_16x16x128_f8f6f4 v[134:137], v[10:17], v[216:223], v[134:137], v197, v198 op_sel_hi:[0,0,0]
	v_mfma_scale_f32_16x16x128_f8f6f4 v[126:129], v[2:9], v[224:231], v[126:129], v197, v198 op_sel_hi:[0,0,0]
	v_mfma_scale_f32_16x16x128_f8f6f4 v[118:121], v[10:17], v[224:231], v[118:121], v197, v198 op_sel_hi:[0,0,0]
	v_mfma_scale_f32_16x16x128_f8f6f4 v[110:113], v[2:9], v[232:239], v[110:113], v197, v198 op_sel_hi:[0,0,0]
	v_mfma_scale_f32_16x16x128_f8f6f4 v[98:101], v[10:17], v[232:239], v[98:101], v197, v198 op_sel_hi:[0,0,0]
	s_setprio 0
	s_setprio 1
	s_nop 0
	v_mfma_scale_f32_16x16x128_f8f6f4 v[154:157], v[18:25], v[208:215], v[154:157], v197, v198 op_sel_hi:[0,0,0]
	v_mfma_scale_f32_16x16x128_f8f6f4 v[146:149], v[26:33], v[208:215], v[146:149], v197, v198 op_sel_hi:[0,0,0]
	v_mfma_scale_f32_16x16x128_f8f6f4 v[138:141], v[18:25], v[216:223], v[138:141], v197, v198 op_sel_hi:[0,0,0]
	v_mfma_scale_f32_16x16x128_f8f6f4 v[130:133], v[26:33], v[216:223], v[130:133], v197, v198 op_sel_hi:[0,0,0]
	v_mfma_scale_f32_16x16x128_f8f6f4 v[122:125], v[18:25], v[224:231], v[122:125], v197, v198 op_sel_hi:[0,0,0]
	v_mfma_scale_f32_16x16x128_f8f6f4 v[114:117], v[26:33], v[224:231], v[114:117], v197, v198 op_sel_hi:[0,0,0]
	v_mfma_scale_f32_16x16x128_f8f6f4 v[106:109], v[18:25], v[232:239], v[106:109], v197, v198 op_sel_hi:[0,0,0]
	v_mfma_scale_f32_16x16x128_f8f6f4 v[94:97], v[26:33], v[232:239], v[94:97], v197, v198 op_sel_hi:[0,0,0]
	s_setprio 0
	s_barrier
	s_mov_b32 m0, s45
	v_lshl_add_u64 v[182:183], v[182:183], 0, s[10:11]
	s_add_u32 s20, s20, 0x20080
	ds_read_b128 v[208:211], v196 offset:49152
	ds_read_b128 v[212:215], v196 offset:50176
	ds_read_b128 v[216:219], v196 offset:51200
	ds_read_b128 v[220:223], v196 offset:52224
	ds_read_b128 v[224:227], v196 offset:53248
	ds_read_b128 v[228:231], v196 offset:54272
	ds_read_b128 v[232:235], v196 offset:55296
	ds_read_b128 v[236:239], v196 offset:56320
	global_load_lds_dwordx4 v[182:183], off
	v_lshl_add_u64 v[182:183], v[184:185], 0, s[10:11]
	s_mov_b32 m0, s46
	s_addc_u32 s21, s21, 0
	global_load_lds_dwordx4 v[182:183], off
	v_lshl_add_u64 v[182:183], s[20:21], 0, v[164:165]
	s_mov_b32 m0, s47
	s_nop 0
	global_load_lds_dwordx4 v[182:183], off
	v_lshl_add_u64 v[182:183], s[20:21], 0, v[162:163]
	s_add_i32 m0, s47, 0x2000
	s_nop 0
	global_load_lds_dwordx4 v[182:183], off
	v_lshl_add_u64 v[182:183], v[188:189], 0, s[10:11]
	s_mov_b32 m0, s31
	s_nop 0
	global_load_lds_dwordx4 v[182:183], off
	v_lshl_add_u64 v[182:183], v[186:187], 0, s[10:11]
	s_mov_b32 m0, s34
	s_nop 0
	global_load_lds_dwordx4 v[182:183], off
	s_waitcnt vmcnt(8)
	s_waitcnt lgkmcnt(0)
	s_barrier
	s_setprio 1
	v_mfma_scale_f32_16x16x128_f8f6f4 v[82:85], v[2:9], v[208:215], v[82:85], v197, v198 op_sel_hi:[0,0,0]
	v_mfma_scale_f32_16x16x128_f8f6f4 v[70:73], v[10:17], v[208:215], v[70:73], v197, v198 op_sel_hi:[0,0,0]
	v_mfma_scale_f32_16x16x128_f8f6f4 v[78:81], v[2:9], v[216:223], v[78:81], v197, v198 op_sel_hi:[0,0,0]
	v_mfma_scale_f32_16x16x128_f8f6f4 v[66:69], v[10:17], v[216:223], v[66:69], v197, v198 op_sel_hi:[0,0,0]
	v_mfma_scale_f32_16x16x128_f8f6f4 v[58:61], v[2:9], v[224:231], v[58:61], v197, v198 op_sel_hi:[0,0,0]
	v_mfma_scale_f32_16x16x128_f8f6f4 v[50:53], v[10:17], v[224:231], v[50:53], v197, v198 op_sel_hi:[0,0,0]
	v_mfma_scale_f32_16x16x128_f8f6f4 v[42:45], v[2:9], v[232:239], v[42:45], v197, v198 op_sel_hi:[0,0,0]
	v_mfma_scale_f32_16x16x128_f8f6f4 v[34:37], v[10:17], v[232:239], v[34:37], v197, v198 op_sel_hi:[0,0,0]
	s_setprio 0
	s_setprio 1
	s_nop 0
	v_mfma_scale_f32_16x16x128_f8f6f4 v[102:105], v[18:25], v[208:215], v[102:105], v197, v198 op_sel_hi:[0,0,0]
	v_mfma_scale_f32_16x16x128_f8f6f4 v[90:93], v[26:33], v[208:215], v[90:93], v197, v198 op_sel_hi:[0,0,0]
	v_mfma_scale_f32_16x16x128_f8f6f4 v[86:89], v[18:25], v[216:223], v[86:89], v197, v198 op_sel_hi:[0,0,0]
	v_mfma_scale_f32_16x16x128_f8f6f4 v[74:77], v[26:33], v[216:223], v[74:77], v197, v198 op_sel_hi:[0,0,0]
	v_mfma_scale_f32_16x16x128_f8f6f4 v[62:65], v[18:25], v[224:231], v[62:65], v197, v198 op_sel_hi:[0,0,0]
	v_mfma_scale_f32_16x16x128_f8f6f4 v[54:57], v[26:33], v[224:231], v[54:57], v197, v198 op_sel_hi:[0,0,0]
	v_mfma_scale_f32_16x16x128_f8f6f4 v[46:49], v[18:25], v[232:239], v[46:49], v197, v198 op_sel_hi:[0,0,0]
	v_mfma_scale_f32_16x16x128_f8f6f4 v[38:41], v[26:33], v[232:239], v[38:41], v197, v198 op_sel_hi:[0,0,0]
	s_setprio 0
	s_barrier
	s_add_i32 s54, s54, 2
	s_add_u32 s4, s4, 0x100
	s_addc_u32 s5, s5, 0
; #define PG8_STAGE(bufoff, gbase, voff) do { _Pragma("unroll") for (int _i = 0; _i < 2; ++_i) \
;         __builtin_amdgcn_global_load_lds((const unsigned*)((const char*)(gbase) + (voff)[_i]), (PG8_LAS unsigned*)(lds + (bufoff) + ldsw + _i * 8192), 16, 0, 0); } while (0)
; #define PG8_STAGE_A(bufoff, gbase, h, nx) do { if constexpr (Sched::GATHER) { const unsigned vv_[2] = {(nx) ? vAn[h][0] : vA[h][0], (nx) ? vAn[h][1] : vA[h][1]}; PG8_STAGE(bufoff, gbase, vv_); } \
;         else { PG8_STAGE(bufoff, (gbase) + (h) * hstep, voffA); } } while (0)
; #define PG8_LDA(dst, b, h) do { _Pragma("unroll") for (int m = 0; m < 4; ++m) _Pragma("unroll") for (int k = 0; k < 2; ++k) dst[m][k] = *(const PG8_LAS bf16x8*)(lds + PG8_SA(b, h) + aoff + m * 2048 + k * 1024); } while (0)
; #define PG8_LDB(dst, b, h) do { _Pragma("unroll") for (int n = 0; n < 2; ++n) _Pragma("unroll") for (int k = 0; k < 2; ++k) dst[n][k] = *(const PG8_LAS bf16x8*)(lds + PG8_SB(b, h) + boff + n * 2048 + k * 1024); } while (0)
; #define PG8_WAIT_V(n) asm volatile("s_waitcnt vmcnt(" #n ")" ::: "memory")
; #define PG8_WAIT_L(n) asm volatile("s_waitcnt lgkmcnt(" #n ")" ::: "memory")
; #define PG8_BAR __builtin_amdgcn_s_barrier()
; #define PG8_SCHED __builtin_amdgcn_sched_barrier(0)
;     ...
;             PG8_LDB(B0, 0, 0); PG8_LDB(B1, 0, 1); PG8_SCHED; PG8_LDA(At, 0, 0); PG8_STAGE_A(PG8_SA(1, 1), a1, 1, false);
;             PG8_WAIT_V(8); PG8_WAIT_L(0); PG8_BAR; PG8_MMA(0, 0, At, B0); PG8_MMA(0, 1, At, B1); PG8_BAR; PG8_SCHED;
;             PG8_LDA(At, 0, 1); PG8_STAGE(PG8_SB(0, 0), b2, voffB); PG8_STAGE(PG8_SB(0, 1), b2 + hstepB, voffB); PG8_STAGE_A(PG8_SA(0, 0), a2, 0, last);
;             PG8_WAIT_V(8); PG8_WAIT_L(0); PG8_BAR; PG8_MMA(1, 0, At, B0); PG8_MMA(1, 1, At, B1); PG8_BAR; PG8_SCHED;
.LBB0_1572:
	ds_read_b128 v[26:29], v194
	ds_read_b128 v[30:33], v194 offset:1024
	ds_read_b128 v[18:21], v194 offset:2048
	ds_read_b128 v[22:25], v194 offset:3072
	ds_read_b128 v[10:13], v195
	ds_read_b128 v[14:17], v195 offset:1024
	ds_read_b128 v[2:5], v195 offset:2048
	ds_read_b128 v[6:9], v195 offset:3072
	s_add_u32 s20, s58, s4
	s_addc_u32 s21, s59, s5
	s_add_u32 s22, s20, 0x25400100
	s_addc_u32 s23, s21, 0
	s_add_u32 s55, s52, s4
	s_addc_u32 s56, s53, s5
	s_cmpk_eq_i32 s4, 0x300
	s_cselect_b64 vcc, -1, 0
	s_and_b64 s[20:21], vcc, exec
	s_cselect_b32 s23, s93, s23
	s_cselect_b32 s22, s92, s22
	s_cselect_b32 s21, s17, s56
	s_cselect_b32 s20, s51, s55
	s_mov_b32 m0, s39
	v_lshl_add_u64 v[232:233], v[180:181], 0, s[4:5]
	ds_read_b128 v[182:185], v196
	ds_read_b128 v[186:189], v196 offset:1024
	ds_read_b128 v[208:211], v196 offset:2048
	ds_read_b128 v[212:215], v196 offset:3072
	ds_read_b128 v[216:219], v196 offset:4096
	ds_read_b128 v[220:223], v196 offset:5120
	ds_read_b128 v[224:227], v196 offset:6144
	ds_read_b128 v[228:231], v196 offset:7168
	global_load_lds_dwordx4 v[232:233], off
	v_lshl_add_u64 v[232:233], v[178:179], 0, s[4:5]
	s_mov_b32 m0, s40
	s_nop 0
	global_load_lds_dwordx4 v[232:233], off
	s_waitcnt vmcnt(8)
	s_waitcnt lgkmcnt(0)
	s_barrier
	s_setprio 1
	v_mfma_scale_f32_16x16x128_f8f6f4 v[158:161], v[26:33], v[182:189], v[158:161], v197, v198 op_sel_hi:[0,0,0]
	v_mfma_scale_f32_16x16x128_f8f6f4 v[150:153], v[18:25], v[182:189], v[150:153], v197, v198 op_sel_hi:[0,0,0]
	v_mfma_scale_f32_16x16x128_f8f6f4 v[142:145], v[26:33], v[208:215], v[142:145], v197, v198 op_sel_hi:[0,0,0]
	v_mfma_scale_f32_16x16x128_f8f6f4 v[134:137], v[18:25], v[208:215], v[134:137], v197, v198 op_sel_hi:[0,0,0]
	v_mfma_scale_f32_16x16x128_f8f6f4 v[126:129], v[26:33], v[216:223], v[126:129], v197, v198 op_sel_hi:[0,0,0]
	v_mfma_scale_f32_16x16x128_f8f6f4 v[118:121], v[18:25], v[216:223], v[118:121], v197, v198 op_sel_hi:[0,0,0]
	v_mfma_scale_f32_16x16x128_f8f6f4 v[110:113], v[26:33], v[224:231], v[110:113], v197, v198 op_sel_hi:[0,0,0]
	v_mfma_scale_f32_16x16x128_f8f6f4 v[98:101], v[18:25], v[224:231], v[98:101], v197, v198 op_sel_hi:[0,0,0]
	s_setprio 0
	s_setprio 1
	s_nop 0
	v_mfma_scale_f32_16x16x128_f8f6f4 v[154:157], v[10:17], v[182:189], v[154:157], v197, v198 op_sel_hi:[0,0,0]
	v_mfma_scale_f32_16x16x128_f8f6f4 v[146:149], v[2:9], v[182:189], v[146:149], v197, v198 op_sel_hi:[0,0,0]
	v_mfma_scale_f32_16x16x128_f8f6f4 v[138:141], v[10:17], v[208:215], v[138:141], v197, v198 op_sel_hi:[0,0,0]
	v_mfma_scale_f32_16x16x128_f8f6f4 v[130:133], v[2:9], v[208:215], v[130:133], v197, v198 op_sel_hi:[0,0,0]
	v_mfma_scale_f32_16x16x128_f8f6f4 v[122:125], v[10:17], v[216:223], v[122:125], v197, v198 op_sel_hi:[0,0,0]
	v_mfma_scale_f32_16x16x128_f8f6f4 v[114:117], v[2:9], v[216:223], v[114:117], v197, v198 op_sel_hi:[0,0,0]
	v_mfma_scale_f32_16x16x128_f8f6f4 v[106:109], v[10:17], v[224:231], v[106:109], v197, v198 op_sel_hi:[0,0,0]
	v_mfma_scale_f32_16x16x128_f8f6f4 v[94:97], v[2:9], v[224:231], v[94:97], v197, v198 op_sel_hi:[0,0,0]
	s_setprio 0
	s_barrier
	s_mov_b32 m0, s41
	v_lshl_add_u64 v[182:183], s[20:21], 0, v[164:165]
	s_add_u32 s56, s20, 0x20000
	ds_read_b128 v[208:211], v196 offset:16384
	ds_read_b128 v[212:215], v196 offset:17408
	ds_read_b128 v[216:219], v196 offset:18432
	ds_read_b128 v[220:223], v196 offset:19456
	ds_read_b128 v[224:227], v196 offset:20480
	ds_read_b128 v[228:231], v196 offset:21504
	ds_read_b128 v[232:235], v196 offset:22528
	ds_read_b128 v[236:239], v196 offset:23552
	global_load_lds_dwordx4 v[182:183], off
	v_lshl_add_u64 v[184:185], s[20:21], 0, v[162:163]
	s_mov_b32 m0, s42
	s_addc_u32 s57, s21, 0
	global_load_lds_dwordx4 v[184:185], off
	v_lshl_add_u64 v[186:187], s[56:57], 0, v[164:165]
	s_mov_b32 m0, s43
	v_cndmask_b32_e32 v166, v206, v202, vcc
	global_load_lds_dwordx4 v[186:187], off
	v_lshl_add_u64 v[186:187], s[56:57], 0, v[162:163]
	s_mov_b32 m0, s44
	v_lshl_add_u64 v[188:189], s[22:23], 0, v[166:167]
	global_load_lds_dwordx4 v[186:187], off
	s_mov_b32 m0, s26
	v_cndmask_b32_e32 v186, v172, v203, vcc
	global_load_lds_dwordx4 v166, s[22:23]
	s_mov_b32 m0, s27
	v_mov_b32_e32 v187, v167
	global_load_lds_dwordx4 v186, s[22:23]
	s_waitcnt vmcnt(8)
	s_waitcnt lgkmcnt(0)
	v_lshl_add_u64 v[186:187], s[22:23], 0, v[186:187]
	s_barrier
	s_setprio 1
	s_nop 0
	s_waitcnt lgkmcnt(0)
	v_mfma_scale_f32_16x16x128_f8f6f4 v[82:85], v[26:33], v[208:215], v[82:85], v197, v198 op_sel_hi:[0,0,0]
	v_mfma_scale_f32_16x16x128_f8f6f4 v[70:73], v[18:25], v[208:215], v[70:73], v197, v198 op_sel_hi:[0,0,0]
	v_mfma_scale_f32_16x16x128_f8f6f4 v[78:81], v[26:33], v[216:223], v[78:81], v197, v198 op_sel_hi:[0,0,0]
	v_mfma_scale_f32_16x16x128_f8f6f4 v[66:69], v[18:25], v[216:223], v[66:69], v197, v198 op_sel_hi:[0,0,0]
	v_mfma_scale_f32_16x16x128_f8f6f4 v[58:61], v[26:33], v[224:231], v[58:61], v197, v198 op_sel_hi:[0,0,0]
	v_mfma_scale_f32_16x16x128_f8f6f4 v[50:53], v[18:25], v[224:231], v[50:53], v197, v198 op_sel_hi:[0,0,0]
	v_mfma_scale_f32_16x16x128_f8f6f4 v[42:45], v[26:33], v[232:239], v[42:45], v197, v198 op_sel_hi:[0,0,0]
	v_mfma_scale_f32_16x16x128_f8f6f4 v[34:37], v[18:25], v[232:239], v[34:37], v197, v198 op_sel_hi:[0,0,0]
	s_setprio 0
	s_setprio 1
	s_nop 0
	v_mfma_scale_f32_16x16x128_f8f6f4 v[102:105], v[10:17], v[208:215], v[102:105], v197, v198 op_sel_hi:[0,0,0]
	v_mfma_scale_f32_16x16x128_f8f6f4 v[90:93], v[2:9], v[208:215], v[90:93], v197, v198 op_sel_hi:[0,0,0]
	v_mfma_scale_f32_16x16x128_f8f6f4 v[86:89], v[10:17], v[216:223], v[86:89], v197, v198 op_sel_hi:[0,0,0]
	v_mfma_scale_f32_16x16x128_f8f6f4 v[74:77], v[2:9], v[216:223], v[74:77], v197, v198 op_sel_hi:[0,0,0]
	v_mfma_scale_f32_16x16x128_f8f6f4 v[62:65], v[10:17], v[224:231], v[62:65], v197, v198 op_sel_hi:[0,0,0]
	v_mfma_scale_f32_16x16x128_f8f6f4 v[54:57], v[2:9], v[224:231], v[54:57], v197, v198 op_sel_hi:[0,0,0]
	v_mfma_scale_f32_16x16x128_f8f6f4 v[46:49], v[10:17], v[232:239], v[46:49], v197, v198 op_sel_hi:[0,0,0]
	v_mfma_scale_f32_16x16x128_f8f6f4 v[38:41], v[2:9], v[232:239], v[38:41], v197, v198 op_sel_hi:[0,0,0]
	s_setprio 0
	s_barrier
; #define PG8_STAGE(bufoff, gbase, voff) do { _Pragma("unroll") for (int _i = 0; _i < 2; ++_i) \
;         __builtin_amdgcn_global_load_lds((const unsigned*)((const char*)(gbase) + (voff)[_i]), (PG8_LAS unsigned*)(lds + (bufoff) + ldsw + _i * 8192), 16, 0, 0); } while (0)
; #define PG8_STAGE_A(bufoff, gbase, h, nx) do { if constexpr (Sched::GATHER) { const unsigned vv_[2] = {(nx) ? vAn[h][0] : vA[h][0], (nx) ? vAn[h][1] : vA[h][1]}; PG8_STAGE(bufoff, gbase, vv_); } \
;         else { PG8_STAGE(bufoff, (gbase) + (h) * hstep, voffA); } } while (0)
; #define PG8_LDA(dst, b, h) do { _Pragma("unroll") for (int m = 0; m < 4; ++m) _Pragma("unroll") for (int k = 0; k < 2; ++k) dst[m][k] = *(const PG8_LAS bf16x8*)(lds + PG8_SA(b, h) + aoff + m * 2048 + k * 1024); } while (0)
; #define PG8_LDB(dst, b, h) do { _Pragma("unroll") for (int n = 0; n < 2; ++n) _Pragma("unroll") for (int k = 0; k < 2; ++k) dst[n][k] = *(const PG8_LAS bf16x8*)(lds + PG8_SB(b, h) + boff + n * 2048 + k * 1024); } while (0)
; #define PG8_WAIT_V(n) asm volatile("s_waitcnt vmcnt(" #n ")" ::: "memory")
; #define PG8_WAIT_L(n) asm volatile("s_waitcnt lgkmcnt(" #n ")" ::: "memory")
; #define PG8_BAR __builtin_amdgcn_s_barrier()
; #define PG8_SCHED __builtin_amdgcn_sched_barrier(0)
;     ...
;             PG8_LDB(B0, 0, 0); PG8_LDB(B1, 0, 1); PG8_SCHED; PG8_LDA(At, 0, 0); PG8_STAGE_A(PG8_SA(1, 1), a1, 1, false);
;             PG8_WAIT_V(8); PG8_WAIT_L(0); PG8_BAR; PG8_MMA(0, 0, At, B0); PG8_MMA(0, 1, At, B1); PG8_BAR; PG8_SCHED;
;             PG8_LDA(At, 0, 1); PG8_STAGE(PG8_SB(0, 0), b2, voffB); PG8_STAGE(PG8_SB(0, 1), b2 + hstepB, voffB); PG8_STAGE_A(PG8_SA(0, 0), a2, 0, last);
;             PG8_WAIT_V(8); PG8_WAIT_L(0); PG8_BAR; PG8_MMA(1, 0, At, B0); PG8_MMA(1, 1, At, B1); PG8_BAR; PG8_SCHED;
;             PG8_LDB(B0, 1, 0); PG8_LDB(B1, 1, 1); PG8_SCHED; PG8_LDA(At, 1, 0); PG8_STAGE_A(PG8_SA(0, 1), a2, 1, last);
;             PG8_WAIT_V(8); PG8_WAIT_L(0); PG8_BAR; PG8_MMA(0, 0, At, B0); PG8_MMA(0, 1, At, B1); PG8_BAR; PG8_SCHED;
;             PG8_LDA(At, 1, 1); PG8_STAGE(PG8_SB(1, 0), b3, voffB); PG8_STAGE(PG8_SB(1, 1), b3 + hstepB, voffB); PG8_STAGE_A(PG8_SA(1, 0), a3, 0, last);
;             PG8_WAIT_V(8); PG8_WAIT_L(0); PG8_BAR; PG8_MMA(1, 0, At, B0); PG8_MMA(1, 1, At, B1); PG8_BAR; PG8_SCHED;
	ds_read_b128 v[2:5], v199
	ds_read_b128 v[6:9], v199 offset:1024
	ds_read_b128 v[10:13], v199 offset:2048
	ds_read_b128 v[14:17], v199 offset:3072
	ds_read_b128 v[18:21], v200
	ds_read_b128 v[22:25], v200 offset:1024
	ds_read_b128 v[26:29], v200 offset:2048
	ds_read_b128 v[30:33], v200 offset:3072
	s_mov_b32 m0, s28
	v_cndmask_b32_e32 v166, v174, v204, vcc
	ds_read_b128 v[208:211], v196 offset:32768
	ds_read_b128 v[212:215], v196 offset:33792
	ds_read_b128 v[216:219], v196 offset:34816
	ds_read_b128 v[220:223], v196 offset:35840
	ds_read_b128 v[224:227], v196 offset:36864
	ds_read_b128 v[228:231], v196 offset:37888
	ds_read_b128 v[232:235], v196 offset:38912
	ds_read_b128 v[236:239], v196 offset:39936
	v_cndmask_b32_e32 v175, v176, v205, vcc
	global_load_lds_dwordx4 v166, s[22:23]
	s_mov_b32 m0, s29
	s_nop 0
	global_load_lds_dwordx4 v175, s[22:23]
	s_waitcnt vmcnt(8)
	s_waitcnt lgkmcnt(0)
	s_barrier
	s_setprio 1
	v_mfma_scale_f32_16x16x128_f8f6f4 v[158:161], v[2:9], v[208:215], v[158:161], v197, v198 op_sel_hi:[0,0,0]
	v_mfma_scale_f32_16x16x128_f8f6f4 v[150:153], v[10:17], v[208:215], v[150:153], v197, v198 op_sel_hi:[0,0,0]
	v_mfma_scale_f32_16x16x128_f8f6f4 v[142:145], v[2:9], v[216:223], v[142:145], v197, v198 op_sel_hi:[0,0,0]
	v_mfma_scale_f32_16x16x128_f8f6f4 v[134:137], v[10:17], v[216:223], v[134:137], v197, v198 op_sel_hi:[0,0,0]
	v_mfma_scale_f32_16x16x128_f8f6f4 v[126:129], v[2:9], v[224:231], v[126:129], v197, v198 op_sel_hi:[0,0,0]
	v_mfma_scale_f32_16x16x128_f8f6f4 v[118:121], v[10:17], v[224:231], v[118:121], v197, v198 op_sel_hi:[0,0,0]
	v_mfma_scale_f32_16x16x128_f8f6f4 v[110:113], v[2:9], v[232:239], v[110:113], v197, v198 op_sel_hi:[0,0,0]
	v_mfma_scale_f32_16x16x128_f8f6f4 v[98:101], v[10:17], v[232:239], v[98:101], v197, v198 op_sel_hi:[0,0,0]
	s_setprio 0
	s_setprio 1
	s_nop 0
	v_mfma_scale_f32_16x16x128_f8f6f4 v[154:157], v[18:25], v[208:215], v[154:157], v197, v198 op_sel_hi:[0,0,0]
	v_mfma_scale_f32_16x16x128_f8f6f4 v[146:149], v[26:33], v[208:215], v[146:149], v197, v198 op_sel_hi:[0,0,0]
	v_mfma_scale_f32_16x16x128_f8f6f4 v[138:141], v[18:25], v[216:223], v[138:141], v197, v198 op_sel_hi:[0,0,0]
	v_mfma_scale_f32_16x16x128_f8f6f4 v[130:133], v[26:33], v[216:223], v[130:133], v197, v198 op_sel_hi:[0,0,0]
	v_mfma_scale_f32_16x16x128_f8f6f4 v[122:125], v[18:25], v[224:231], v[122:125], v197, v198 op_sel_hi:[0,0,0]
	v_mfma_scale_f32_16x16x128_f8f6f4 v[114:117], v[26:33], v[224:231], v[114:117], v197, v198 op_sel_hi:[0,0,0]
	v_mfma_scale_f32_16x16x128_f8f6f4 v[106:109], v[18:25], v[232:239], v[106:109], v197, v198 op_sel_hi:[0,0,0]
	v_mfma_scale_f32_16x16x128_f8f6f4 v[94:97], v[26:33], v[232:239], v[94:97], v197, v198 op_sel_hi:[0,0,0]
	s_setprio 0
	s_barrier
	s_mov_b32 m0, s45
	v_lshl_add_u64 v[182:183], v[182:183], 0, s[10:11]
	s_add_u32 s20, s20, 0x20080
	ds_read_b128 v[208:211], v196 offset:49152
	ds_read_b128 v[212:215], v196 offset:50176
	ds_read_b128 v[216:219], v196 offset:51200
	ds_read_b128 v[220:223], v196 offset:52224
	ds_read_b128 v[224:227], v196 offset:53248
	ds_read_b128 v[228:231], v196 offset:54272
	ds_read_b128 v[232:235], v196 offset:55296
	ds_read_b128 v[236:239], v196 offset:56320
	global_load_lds_dwordx4 v[182:183], off
	v_lshl_add_u64 v[182:183], v[184:185], 0, s[10:11]
	s_mov_b32 m0, s46
	s_addc_u32 s21, s21, 0
	global_load_lds_dwordx4 v[182:183], off
	v_lshl_add_u64 v[182:183], s[20:21], 0, v[164:165]
	s_mov_b32 m0, s47
	s_nop 0
	global_load_lds_dwordx4 v[182:183], off
	v_lshl_add_u64 v[182:183], s[20:21], 0, v[162:163]
	s_add_i32 m0, s47, 0x2000
	s_nop 0
	global_load_lds_dwordx4 v[182:183], off
	v_lshl_add_u64 v[182:183], v[188:189], 0, s[10:11]
	s_mov_b32 m0, s31
	s_nop 0
	global_load_lds_dwordx4 v[182:183], off
	v_lshl_add_u64 v[182:183], v[186:187], 0, s[10:11]
	s_mov_b32 m0, s34
	s_nop 0
	global_load_lds_dwordx4 v[182:183], off
	s_waitcnt vmcnt(8)
	s_waitcnt lgkmcnt(0)
	s_barrier
	s_setprio 1
	v_mfma_scale_f32_16x16x128_f8f6f4 v[82:85], v[2:9], v[208:215], v[82:85], v197, v198 op_sel_hi:[0,0,0]
	v_mfma_scale_f32_16x16x128_f8f6f4 v[70:73], v[10:17], v[208:215], v[70:73], v197, v198 op_sel_hi:[0,0,0]
	v_mfma_scale_f32_16x16x128_f8f6f4 v[78:81], v[2:9], v[216:223], v[78:81], v197, v198 op_sel_hi:[0,0,0]
	v_mfma_scale_f32_16x16x128_f8f6f4 v[66:69], v[10:17], v[216:223], v[66:69], v197, v198 op_sel_hi:[0,0,0]
	v_mfma_scale_f32_16x16x128_f8f6f4 v[58:61], v[2:9], v[224:231], v[58:61], v197, v198 op_sel_hi:[0,0,0]
	v_mfma_scale_f32_16x16x128_f8f6f4 v[50:53], v[10:17], v[224:231], v[50:53], v197, v198 op_sel_hi:[0,0,0]
	v_mfma_scale_f32_16x16x128_f8f6f4 v[42:45], v[2:9], v[232:239], v[42:45], v197, v198 op_sel_hi:[0,0,0]
	v_mfma_scale_f32_16x16x128_f8f6f4 v[34:37], v[10:17], v[232:239], v[34:37], v197, v198 op_sel_hi:[0,0,0]
	s_setprio 0
	s_setprio 1
	s_nop 0
	v_mfma_scale_f32_16x16x128_f8f6f4 v[102:105], v[18:25], v[208:215], v[102:105], v197, v198 op_sel_hi:[0,0,0]
	v_mfma_scale_f32_16x16x128_f8f6f4 v[90:93], v[26:33], v[208:215], v[90:93], v197, v198 op_sel_hi:[0,0,0]
	v_mfma_scale_f32_16x16x128_f8f6f4 v[86:89], v[18:25], v[216:223], v[86:89], v197, v198 op_sel_hi:[0,0,0]
	v_mfma_scale_f32_16x16x128_f8f6f4 v[74:77], v[26:33], v[216:223], v[74:77], v197, v198 op_sel_hi:[0,0,0]
	v_mfma_scale_f32_16x16x128_f8f6f4 v[62:65], v[18:25], v[224:231], v[62:65], v197, v198 op_sel_hi:[0,0,0]
	v_mfma_scale_f32_16x16x128_f8f6f4 v[54:57], v[26:33], v[224:231], v[54:57], v197, v198 op_sel_hi:[0,0,0]
	v_mfma_scale_f32_16x16x128_f8f6f4 v[46:49], v[18:25], v[232:239], v[46:49], v197, v198 op_sel_hi:[0,0,0]
	v_mfma_scale_f32_16x16x128_f8f6f4 v[38:41], v[26:33], v[232:239], v[38:41], v197, v198 op_sel_hi:[0,0,0]
	s_setprio 0
	s_barrier
	s_add_i32 s54, s54, 2
	s_add_u32 s4, s4, 0x100
	s_addc_u32 s5, s5, 0
	s_cmp_gt_u32 s54, 5
	s_cbranch_scc0 .LBB0_1572
	s_and_b64 vcc, exec, s[14:15]
	s_cbranch_vccz .LBB0_1575
	s_barrier

; #define PG8_STAGE(bufoff, gbase, voff) do { _Pragma("unroll") for (int _i = 0; _i < 2; ++_i) \
;         __builtin_amdgcn_global_load_lds((const unsigned*)((const char*)(gbase) + (voff)[_i]), (PG8_LAS unsigned*)(lds + (bufoff) + ldsw + _i * 8192), 16, 0, 0); } while (0)
; #define PG8_STAGE_A(bufoff, gbase, h, nx) do { if constexpr (Sched::GATHER) { const unsigned vv_[2] = {(nx) ? vAn[h][0] : vA[h][0], (nx) ? vAn[h][1] : vA[h][1]}; PG8_STAGE(bufoff, gbase, vv_); } \
;         else { PG8_STAGE(bufoff, (gbase) + (h) * hstep, voffA); } } while (0)
; #define PG8_LDA(dst, b, h) do { _Pragma("unroll") for (int m = 0; m < 4; ++m) _Pragma("unroll") for (int k = 0; k < 2; ++k) dst[m][k] = *(const PG8_LAS bf16x8*)(lds + PG8_SA(b, h) + aoff + m * 2048 + k * 1024); } while (0)
; #define PG8_WAIT_V(n) asm volatile("s_waitcnt vmcnt(" #n ")" ::: "memory")
; #define PG8_WAIT_L(n) asm volatile("s_waitcnt lgkmcnt(" #n ")" ::: "memory")
;     ...
;         const bool has_next = S.next(ui + 1, nxt);
;         const char* nA = Sched::GATHER ? cA : (has_next ? (const char*)g.A + (size_t)nxt.pm * tstep : cA);
;         if constexpr (Sched::GATHER) { if (has_next) { PG8_AOFF(vAn, ui + 1); } else { _Pragma("unroll") for (int h_ = 0; h_ < 2; ++h_) _Pragma("unroll") for (int i_ = 0; i_ < 2; ++i_) vAn[h_][i_] = vA[h_][i_]; } } const char* nB = has_next ? (const char*)g.Bt + (size_t)nxt.pb * tstep : cB;
; #pragma nounroll
;         for (int t = 0; t < nt; t += 2) {
;             const bool last = (t == nt - 2);
;             const char* a1 = cA + (size_t)(t + 1) * kstep;
;             const char* a2 = last ? nA : cA + (size_t)(t + 2) * kstep; const char* b2 = last ? nB : cB + (size_t)(t + 2) * kstep;
;             const char* a3 = a2 + kstep; const char* b3 = b2 + kstep;
;             if (last && has_next) S.a_ready(nxt);
;             if constexpr (SP2) {
;             PG8_LDB(B0, 0, 0); PG8_LDB(B1, 0, 1); PG8_SCHED; PG8_LDA(At, 0, 0); PG8_STAGE_A(PG8_SA(1, 1), a1, 1, false);
;             PG8_WAIT_V(8); PG8_WAIT_L(0); PG8_BAR; PG8_MMA(0, 0, At, B0); PG8_MMA(0, 1, At, B1); PG8_BAR; PG8_SCHED;
;             PG8_LDA(At, 0, 1); PG8_STAGE(PG8_SB(0, 0), b2, voffB); PG8_STAGE(PG8_SB(0, 1), b2 + hstepB, voffB); PG8_STAGE_A(PG8_SA(0, 0), a2, 0, last);
;             PG8_WAIT_V(8); PG8_WAIT_L(0); PG8_BAR; PG8_MMA(1, 0, At, B0); PG8_MMA(1, 1, At, B1); PG8_BAR; PG8_SCHED;
.LBB0_1625:
	s_ashr_i32 s13, s12, 31
	s_lshl_b64 s[16:17], s[12:13], 19
	v_readlane_b32 s18, v255, 9
	v_readlane_b32 s19, v255, 10
	s_add_u32 s16, s18, s16
	s_addc_u32 s17, s19, s17
	s_and_b64 s[18:19], s[2:3], exec
	s_cselect_b32 s13, s17, s23
	s_cselect_b32 s46, s16, s22
	s_ashr_i32 s15, s14, 31
	s_lshl_b64 s[18:19], s[14:15], 19
	v_readlane_b32 s26, v255, 3
	v_readlane_b32 s27, v255, 4
	s_add_u32 s18, s26, s18
	s_addc_u32 s19, s27, s19
	s_and_b64 s[26:27], s[2:3], exec
	s_cselect_b32 s15, s19, s25
	s_cselect_b32 s47, s18, s24
	s_add_u32 s22, s22, 0x40080
	s_addc_u32 s23, s23, 0
	s_add_u32 s48, s24, 0x100
	s_addc_u32 s49, s25, 0
	s_mov_b32 s50, -2
	ds_read_b128 v[26:29], v188
	ds_read_b128 v[30:33], v188 offset:1024
	ds_read_b128 v[18:21], v188 offset:2048
	ds_read_b128 v[22:25], v188 offset:3072
	ds_read_b128 v[10:13], v189
	ds_read_b128 v[14:17], v189 offset:1024
	ds_read_b128 v[2:5], v189 offset:2048
	ds_read_b128 v[6:9], v189 offset:3072
	s_add_u32 s24, s22, 0xfffc0080
	s_addc_u32 s25, s23, -1
	s_cmp_eq_u32 s50, 12
	s_cselect_b32 s27, s13, s25
	s_cselect_b32 s26, s46, s24
	s_cselect_b32 s25, s15, s49
	s_cselect_b32 s24, s47, s48
	v_lshl_add_u64 v[218:219], s[22:23], 0, v[170:171]
	s_add_i32 m0, s28, 0xc000
	ds_read_b128 v[178:181], v190
	ds_read_b128 v[182:185], v190 offset:1024
	ds_read_b128 v[194:197], v190 offset:2048
	ds_read_b128 v[198:201], v190 offset:3072
	ds_read_b128 v[202:205], v190 offset:4096
	ds_read_b128 v[206:209], v190 offset:5120
	ds_read_b128 v[210:213], v190 offset:6144
	ds_read_b128 v[214:217], v190 offset:7168
	global_load_lds_dwordx4 v[218:219], off
	v_lshl_add_u64 v[218:219], s[22:23], 0, v[172:173]
	s_add_i32 m0, s28, 0xe000
	s_nop 0
	global_load_lds_dwordx4 v[218:219], off
	s_waitcnt vmcnt(8)
	s_waitcnt lgkmcnt(0)
	s_barrier
	s_setprio 1
	v_mfma_scale_f32_16x16x128_f8f6f4 v[158:161], v[26:33], v[178:185], 0, v191, v192 op_sel_hi:[0,0,0]
	v_mfma_scale_f32_16x16x128_f8f6f4 v[154:157], v[18:25], v[178:185], 0, v191, v192 op_sel_hi:[0,0,0]
	v_mfma_scale_f32_16x16x128_f8f6f4 v[142:145], v[26:33], v[194:201], 0, v191, v192 op_sel_hi:[0,0,0]
	v_mfma_scale_f32_16x16x128_f8f6f4 v[138:141], v[18:25], v[194:201], 0, v191, v192 op_sel_hi:[0,0,0]
	v_mfma_scale_f32_16x16x128_f8f6f4 v[126:129], v[26:33], v[202:209], 0, v191, v192 op_sel_hi:[0,0,0]
	v_mfma_scale_f32_16x16x128_f8f6f4 v[122:125], v[18:25], v[202:209], 0, v191, v192 op_sel_hi:[0,0,0]
	v_mfma_scale_f32_16x16x128_f8f6f4 v[110:113], v[26:33], v[210:217], 0, v191, v192 op_sel_hi:[0,0,0]
	v_mfma_scale_f32_16x16x128_f8f6f4 v[106:109], v[18:25], v[210:217], 0, v191, v192 op_sel_hi:[0,0,0]
	s_setprio 0
	s_setprio 1
	s_nop 0
	v_mfma_scale_f32_16x16x128_f8f6f4 v[150:153], v[10:17], v[178:185], 0, v191, v192 op_sel_hi:[0,0,0]
	v_mfma_scale_f32_16x16x128_f8f6f4 v[146:149], v[2:9], v[178:185], 0, v191, v192 op_sel_hi:[0,0,0]
	v_mfma_scale_f32_16x16x128_f8f6f4 v[134:137], v[10:17], v[194:201], 0, v191, v192 op_sel_hi:[0,0,0]
	v_mfma_scale_f32_16x16x128_f8f6f4 v[130:133], v[2:9], v[194:201], 0, v191, v192 op_sel_hi:[0,0,0]
	v_mfma_scale_f32_16x16x128_f8f6f4 v[118:121], v[10:17], v[202:209], 0, v191, v192 op_sel_hi:[0,0,0]
	v_mfma_scale_f32_16x16x128_f8f6f4 v[114:117], v[2:9], v[202:209], 0, v191, v192 op_sel_hi:[0,0,0]
	v_mfma_scale_f32_16x16x128_f8f6f4 v[102:105], v[10:17], v[210:217], 0, v191, v192 op_sel_hi:[0,0,0]
	v_mfma_scale_f32_16x16x128_f8f6f4 v[98:101], v[2:9], v[210:217], 0, v191, v192 op_sel_hi:[0,0,0]
	s_setprio 0
	s_barrier
	s_add_i32 s51, s39, s21
	v_lshl_add_u64 v[178:179], s[24:25], 0, v[166:167]
	s_mov_b32 m0, s51
	ds_read_b128 v[194:197], v190 offset:16384
	ds_read_b128 v[198:201], v190 offset:17408
	ds_read_b128 v[202:205], v190 offset:18432
	ds_read_b128 v[206:209], v190 offset:19456
	ds_read_b128 v[210:213], v190 offset:20480
	ds_read_b128 v[214:217], v190 offset:21504
	ds_read_b128 v[218:221], v190 offset:22528
	ds_read_b128 v[222:225], v190 offset:23552
	global_load_lds_dwordx4 v[178:179], off
	s_add_i32 m0, s51, 0x2000
	s_add_u32 s52, s24, 0x4000
	v_lshl_add_u64 v[180:181], s[24:25], 0, v[162:163]
	s_addc_u32 s53, s25, 0
	s_add_i32 s51, s40, s21
	global_load_lds_dwordx4 v[180:181], off
	v_lshl_add_u64 v[182:183], s[52:53], 0, v[166:167]
	s_mov_b32 m0, s51
	v_lshl_add_u64 v[184:185], s[26:27], 0, v[164:165]
	global_load_lds_dwordx4 v[182:183], off
	v_lshl_add_u64 v[182:183], s[52:53], 0, v[162:163]
	s_add_i32 m0, s51, 0x2000
	s_nop 0
	global_load_lds_dwordx4 v[182:183], off
	v_lshl_add_u64 v[182:183], s[26:27], 0, v[168:169]
	s_mov_b32 m0, s28
	s_nop 0
	global_load_lds_dwordx4 v[182:183], off
	s_mov_b32 m0, s29
	s_nop 0
	global_load_lds_dwordx4 v[184:185], off
	s_waitcnt vmcnt(8)
	s_waitcnt lgkmcnt(0)
	s_barrier
	s_setprio 1
	v_mfma_scale_f32_16x16x128_f8f6f4 v[94:97], v[26:33], v[194:201], 0, v191, v192 op_sel_hi:[0,0,0]
	v_mfma_scale_f32_16x16x128_f8f6f4 v[90:93], v[18:25], v[194:201], 0, v191, v192 op_sel_hi:[0,0,0]
	v_mfma_scale_f32_16x16x128_f8f6f4 v[78:81], v[26:33], v[202:209], 0, v191, v192 op_sel_hi:[0,0,0]
	v_mfma_scale_f32_16x16x128_f8f6f4 v[74:77], v[18:25], v[202:209], 0, v191, v192 op_sel_hi:[0,0,0]
	v_mfma_scale_f32_16x16x128_f8f6f4 v[62:65], v[26:33], v[210:217], 0, v191, v192 op_sel_hi:[0,0,0]
	v_mfma_scale_f32_16x16x128_f8f6f4 v[58:61], v[18:25], v[210:217], 0, v191, v192 op_sel_hi:[0,0,0]
	v_mfma_scale_f32_16x16x128_f8f6f4 v[46:49], v[26:33], v[218:225], 0, v191, v192 op_sel_hi:[0,0,0]
	v_mfma_scale_f32_16x16x128_f8f6f4 v[42:45], v[18:25], v[218:225], 0, v191, v192 op_sel_hi:[0,0,0]
	s_setprio 0
	s_setprio 1
	s_nop 0
	v_mfma_scale_f32_16x16x128_f8f6f4 v[86:89], v[10:17], v[194:201], 0, v191, v192 op_sel_hi:[0,0,0]
	v_mfma_scale_f32_16x16x128_f8f6f4 v[82:85], v[2:9], v[194:201], 0, v191, v192 op_sel_hi:[0,0,0]
	v_mfma_scale_f32_16x16x128_f8f6f4 v[70:73], v[10:17], v[202:209], 0, v191, v192 op_sel_hi:[0,0,0]
	v_mfma_scale_f32_16x16x128_f8f6f4 v[66:69], v[2:9], v[202:209], 0, v191, v192 op_sel_hi:[0,0,0]
	v_mfma_scale_f32_16x16x128_f8f6f4 v[54:57], v[10:17], v[210:217], 0, v191, v192 op_sel_hi:[0,0,0]
	v_mfma_scale_f32_16x16x128_f8f6f4 v[50:53], v[2:9], v[210:217], 0, v191, v192 op_sel_hi:[0,0,0]
	v_mfma_scale_f32_16x16x128_f8f6f4 v[38:41], v[10:17], v[218:225], 0, v191, v192 op_sel_hi:[0,0,0]
	v_mfma_scale_f32_16x16x128_f8f6f4 v[34:37], v[2:9], v[218:225], 0, v191, v192 op_sel_hi:[0,0,0]
	s_setprio 0
	s_barrier
; #define PG8_STAGE(bufoff, gbase, voff) do { _Pragma("unroll") for (int _i = 0; _i < 2; ++_i) \
;         __builtin_amdgcn_global_load_lds((const unsigned*)((const char*)(gbase) + (voff)[_i]), (PG8_LAS unsigned*)(lds + (bufoff) + ldsw + _i * 8192), 16, 0, 0); } while (0)
; #define PG8_STAGE_A(bufoff, gbase, h, nx) do { if constexpr (Sched::GATHER) { const unsigned vv_[2] = {(nx) ? vAn[h][0] : vA[h][0], (nx) ? vAn[h][1] : vA[h][1]}; PG8_STAGE(bufoff, gbase, vv_); } \
;         else { PG8_STAGE(bufoff, (gbase) + (h) * hstep, voffA); } } while (0)
; #define PG8_LDA(dst, b, h) do { _Pragma("unroll") for (int m = 0; m < 4; ++m) _Pragma("unroll") for (int k = 0; k < 2; ++k) dst[m][k] = *(const PG8_LAS bf16x8*)(lds + PG8_SA(b, h) + aoff + m * 2048 + k * 1024); } while (0)
; #define PG8_LDB(dst, b, h) do { _Pragma("unroll") for (int n = 0; n < 2; ++n) _Pragma("unroll") for (int k = 0; k < 2; ++k) dst[n][k] = *(const PG8_LAS bf16x8*)(lds + PG8_SB(b, h) + boff + n * 2048 + k * 1024); } while (0)
; #define PG8_WAIT_V(n) asm volatile("s_waitcnt vmcnt(" #n ")" ::: "memory")
; #define PG8_WAIT_L(n) asm volatile("s_waitcnt lgkmcnt(" #n ")" ::: "memory")
; #define PG8_BAR __builtin_amdgcn_s_barrier()
; #define PG8_SCHED __builtin_amdgcn_sched_barrier(0)
;     ...
;             PG8_LDB(B0, 1, 0); PG8_LDB(B1, 1, 1); PG8_SCHED; PG8_LDA(At, 1, 0); PG8_STAGE_A(PG8_SA(0, 1), a2, 1, last);
;             PG8_WAIT_V(8); PG8_WAIT_L(0); PG8_BAR; PG8_MMA(0, 0, At, B0); PG8_MMA(0, 1, At, B1); PG8_BAR; PG8_SCHED;
;             PG8_LDA(At, 1, 1); PG8_STAGE(PG8_SB(1, 0), b3, voffB); PG8_STAGE(PG8_SB(1, 1), b3 + hstepB, voffB); PG8_STAGE_A(PG8_SA(1, 0), a3, 0, last);
;             PG8_WAIT_V(8); PG8_WAIT_L(0); PG8_BAR; PG8_MMA(1, 0, At, B0); PG8_MMA(1, 1, At, B1); PG8_BAR; PG8_SCHED;
	s_add_i32 s51, 0, 0x18000
	s_add_i32 s52, 0, 0x1c000
	v_add_u32_e32 v14, s51, v186
	v_add_u32_e32 v30, s52, v186
	ds_read_b128 v[2:5], v14
	ds_read_b128 v[6:9], v14 offset:1024
	ds_read_b128 v[10:13], v14 offset:2048
	ds_read_b128 v[14:17], v14 offset:3072
	ds_read_b128 v[18:21], v30
	ds_read_b128 v[22:25], v30 offset:1024
	ds_read_b128 v[26:29], v30 offset:2048
	ds_read_b128 v[30:33], v30 offset:3072
	s_add_u32 s26, s26, 0x40000
	s_addc_u32 s27, s27, 0
	s_mov_b32 m0, s30
	v_lshl_add_u64 v[226:227], s[26:27], 0, v[168:169]
	ds_read_b128 v[194:197], v190 offset:32768
	ds_read_b128 v[198:201], v190 offset:33792
	ds_read_b128 v[202:205], v190 offset:34816
	ds_read_b128 v[206:209], v190 offset:35840
	ds_read_b128 v[210:213], v190 offset:36864
	ds_read_b128 v[214:217], v190 offset:37888
	ds_read_b128 v[218:221], v190 offset:38912
	ds_read_b128 v[222:225], v190 offset:39936
	global_load_lds_dwordx4 v[226:227], off
	v_lshl_add_u64 v[226:227], s[26:27], 0, v[164:165]
	s_mov_b32 m0, s31
	s_nop 0
	global_load_lds_dwordx4 v[226:227], off
	s_waitcnt vmcnt(8)
	s_waitcnt lgkmcnt(0)
	s_barrier
	s_setprio 1
	v_mfma_scale_f32_16x16x128_f8f6f4 v[158:161], v[2:9], v[194:201], v[158:161], v191, v192 op_sel_hi:[0,0,0]
	v_mfma_scale_f32_16x16x128_f8f6f4 v[154:157], v[10:17], v[194:201], v[154:157], v191, v192 op_sel_hi:[0,0,0]
	v_mfma_scale_f32_16x16x128_f8f6f4 v[142:145], v[2:9], v[202:209], v[142:145], v191, v192 op_sel_hi:[0,0,0]
	v_mfma_scale_f32_16x16x128_f8f6f4 v[138:141], v[10:17], v[202:209], v[138:141], v191, v192 op_sel_hi:[0,0,0]
	v_mfma_scale_f32_16x16x128_f8f6f4 v[126:129], v[2:9], v[210:217], v[126:129], v191, v192 op_sel_hi:[0,0,0]
	v_mfma_scale_f32_16x16x128_f8f6f4 v[122:125], v[10:17], v[210:217], v[122:125], v191, v192 op_sel_hi:[0,0,0]
	v_mfma_scale_f32_16x16x128_f8f6f4 v[110:113], v[2:9], v[218:225], v[110:113], v191, v192 op_sel_hi:[0,0,0]
	v_mfma_scale_f32_16x16x128_f8f6f4 v[106:109], v[10:17], v[218:225], v[106:109], v191, v192 op_sel_hi:[0,0,0]
	s_setprio 0
	s_setprio 1
	s_nop 0
	v_mfma_scale_f32_16x16x128_f8f6f4 v[150:153], v[18:25], v[194:201], v[150:153], v191, v192 op_sel_hi:[0,0,0]
	v_mfma_scale_f32_16x16x128_f8f6f4 v[146:149], v[26:33], v[194:201], v[146:149], v191, v192 op_sel_hi:[0,0,0]
	v_mfma_scale_f32_16x16x128_f8f6f4 v[134:137], v[18:25], v[202:209], v[134:137], v191, v192 op_sel_hi:[0,0,0]
	v_mfma_scale_f32_16x16x128_f8f6f4 v[130:133], v[26:33], v[202:209], v[130:133], v191, v192 op_sel_hi:[0,0,0]
	v_mfma_scale_f32_16x16x128_f8f6f4 v[118:121], v[18:25], v[210:217], v[118:121], v191, v192 op_sel_hi:[0,0,0]
	v_mfma_scale_f32_16x16x128_f8f6f4 v[114:117], v[26:33], v[210:217], v[114:117], v191, v192 op_sel_hi:[0,0,0]
	v_mfma_scale_f32_16x16x128_f8f6f4 v[102:105], v[18:25], v[218:225], v[102:105], v191, v192 op_sel_hi:[0,0,0]
	v_mfma_scale_f32_16x16x128_f8f6f4 v[98:101], v[26:33], v[218:225], v[98:101], v191, v192 op_sel_hi:[0,0,0]
	s_setprio 0
	s_barrier
	s_add_i32 s26, s51, s21
	v_lshl_add_u64 v[178:179], v[178:179], 0, s[8:9]
	s_mov_b32 m0, s26
	ds_read_b128 v[194:197], v190 offset:49152
	ds_read_b128 v[198:201], v190 offset:50176
	ds_read_b128 v[202:205], v190 offset:51200
	ds_read_b128 v[206:209], v190 offset:52224
	ds_read_b128 v[210:213], v190 offset:53248
	ds_read_b128 v[214:217], v190 offset:54272
	ds_read_b128 v[218:221], v190 offset:55296
	ds_read_b128 v[222:225], v190 offset:56320
	global_load_lds_dwordx4 v[178:179], off
	s_add_i32 m0, s26, 0x2000
	s_add_u32 s24, s24, 0x4080
	v_lshl_add_u64 v[178:179], v[180:181], 0, s[8:9]
	s_addc_u32 s25, s25, 0
	s_add_i32 s26, s52, s21
	global_load_lds_dwordx4 v[178:179], off
	v_lshl_add_u64 v[178:179], s[24:25], 0, v[166:167]
	s_mov_b32 m0, s26
	s_nop 0
	global_load_lds_dwordx4 v[178:179], off
	v_lshl_add_u64 v[178:179], s[24:25], 0, v[162:163]
	s_add_i32 m0, s26, 0x2000
	s_nop 0
	global_load_lds_dwordx4 v[178:179], off
	v_lshl_add_u64 v[178:179], v[182:183], 0, s[8:9]
	s_mov_b32 m0, s36
	s_nop 0
	global_load_lds_dwordx4 v[178:179], off
	v_lshl_add_u64 v[178:179], v[184:185], 0, s[8:9]
	s_mov_b32 m0, s37
	s_nop 0
	global_load_lds_dwordx4 v[178:179], off
	s_waitcnt vmcnt(8)
	s_waitcnt lgkmcnt(0)
	s_barrier
	s_setprio 1
	v_mfma_scale_f32_16x16x128_f8f6f4 v[94:97], v[2:9], v[194:201], v[94:97], v191, v192 op_sel_hi:[0,0,0]
	v_mfma_scale_f32_16x16x128_f8f6f4 v[90:93], v[10:17], v[194:201], v[90:93], v191, v192 op_sel_hi:[0,0,0]
	v_mfma_scale_f32_16x16x128_f8f6f4 v[78:81], v[2:9], v[202:209], v[78:81], v191, v192 op_sel_hi:[0,0,0]
	v_mfma_scale_f32_16x16x128_f8f6f4 v[74:77], v[10:17], v[202:209], v[74:77], v191, v192 op_sel_hi:[0,0,0]
	v_mfma_scale_f32_16x16x128_f8f6f4 v[62:65], v[2:9], v[210:217], v[62:65], v191, v192 op_sel_hi:[0,0,0]
	v_mfma_scale_f32_16x16x128_f8f6f4 v[58:61], v[10:17], v[210:217], v[58:61], v191, v192 op_sel_hi:[0,0,0]
	v_mfma_scale_f32_16x16x128_f8f6f4 v[46:49], v[2:9], v[218:225], v[46:49], v191, v192 op_sel_hi:[0,0,0]
	v_mfma_scale_f32_16x16x128_f8f6f4 v[42:45], v[10:17], v[218:225], v[42:45], v191, v192 op_sel_hi:[0,0,0]
	s_setprio 0
	s_setprio 1
	s_nop 0
	v_mfma_scale_f32_16x16x128_f8f6f4 v[86:89], v[18:25], v[194:201], v[86:89], v191, v192 op_sel_hi:[0,0,0]
	v_mfma_scale_f32_16x16x128_f8f6f4 v[82:85], v[26:33], v[194:201], v[82:85], v191, v192 op_sel_hi:[0,0,0]
	v_mfma_scale_f32_16x16x128_f8f6f4 v[70:73], v[18:25], v[202:209], v[70:73], v191, v192 op_sel_hi:[0,0,0]
	v_mfma_scale_f32_16x16x128_f8f6f4 v[66:69], v[26:33], v[202:209], v[66:69], v191, v192 op_sel_hi:[0,0,0]
	v_mfma_scale_f32_16x16x128_f8f6f4 v[54:57], v[18:25], v[210:217], v[54:57], v191, v192 op_sel_hi:[0,0,0]
	v_mfma_scale_f32_16x16x128_f8f6f4 v[50:53], v[26:33], v[210:217], v[50:53], v191, v192 op_sel_hi:[0,0,0]
	v_mfma_scale_f32_16x16x128_f8f6f4 v[38:41], v[18:25], v[218:225], v[38:41], v191, v192 op_sel_hi:[0,0,0]
	v_mfma_scale_f32_16x16x128_f8f6f4 v[34:37], v[26:33], v[218:225], v[34:37], v191, v192 op_sel_hi:[0,0,0]
	s_setprio 0
	s_barrier
	s_add_i32 s50, s50, 2
	s_add_u32 s22, s22, 0x100
	s_addc_u32 s23, s23, 0
	s_add_u32 s48, s48, 0x100
	s_addc_u32 s49, s49, 0
; #define PG8_STAGE(bufoff, gbase, voff) do { _Pragma("unroll") for (int _i = 0; _i < 2; ++_i) \
;         __builtin_amdgcn_global_load_lds((const unsigned*)((const char*)(gbase) + (voff)[_i]), (PG8_LAS unsigned*)(lds + (bufoff) + ldsw + _i * 8192), 16, 0, 0); } while (0)
; #define PG8_STAGE_A(bufoff, gbase, h, nx) do { if constexpr (Sched::GATHER) { const unsigned vv_[2] = {(nx) ? vAn[h][0] : vA[h][0], (nx) ? vAn[h][1] : vA[h][1]}; PG8_STAGE(bufoff, gbase, vv_); } \
;         else { PG8_STAGE(bufoff, (gbase) + (h) * hstep, voffA); } } while (0)
; #define PG8_LDA(dst, b, h) do { _Pragma("unroll") for (int m = 0; m < 4; ++m) _Pragma("unroll") for (int k = 0; k < 2; ++k) dst[m][k] = *(const PG8_LAS bf16x8*)(lds + PG8_SA(b, h) + aoff + m * 2048 + k * 1024); } while (0)
; #define PG8_LDB(dst, b, h) do { _Pragma("unroll") for (int n = 0; n < 2; ++n) _Pragma("unroll") for (int k = 0; k < 2; ++k) dst[n][k] = *(const PG8_LAS bf16x8*)(lds + PG8_SB(b, h) + boff + n * 2048 + k * 1024); } while (0)
; #define PG8_WAIT_V(n) asm volatile("s_waitcnt vmcnt(" #n ")" ::: "memory")
; #define PG8_WAIT_L(n) asm volatile("s_waitcnt lgkmcnt(" #n ")" ::: "memory")
; #define PG8_BAR __builtin_amdgcn_s_barrier()
; #define PG8_SCHED __builtin_amdgcn_sched_barrier(0)
;     ...
;             PG8_LDB(B0, 0, 0); PG8_LDB(B1, 0, 1); PG8_SCHED; PG8_LDA(At, 0, 0); PG8_STAGE_A(PG8_SA(1, 1), a1, 1, false);
;             PG8_WAIT_V(8); PG8_WAIT_L(0); PG8_BAR; PG8_MMA(0, 0, At, B0); PG8_MMA(0, 1, At, B1); PG8_BAR; PG8_SCHED;
;             PG8_LDA(At, 0, 1); PG8_STAGE(PG8_SB(0, 0), b2, voffB); PG8_STAGE(PG8_SB(0, 1), b2 + hstepB, voffB); PG8_STAGE_A(PG8_SA(0, 0), a2, 0, last);
;             PG8_WAIT_V(8); PG8_WAIT_L(0); PG8_BAR; PG8_MMA(1, 0, At, B0); PG8_MMA(1, 1, At, B1); PG8_BAR; PG8_SCHED;
.LBB0_1626:
	ds_read_b128 v[26:29], v188
	ds_read_b128 v[30:33], v188 offset:1024
	ds_read_b128 v[18:21], v188 offset:2048
	ds_read_b128 v[22:25], v188 offset:3072
	ds_read_b128 v[10:13], v189
	ds_read_b128 v[14:17], v189 offset:1024
	ds_read_b128 v[2:5], v189 offset:2048
	ds_read_b128 v[6:9], v189 offset:3072
	s_add_u32 s24, s22, 0xfffc0080
	s_addc_u32 s25, s23, -1
	s_cmp_eq_u32 s50, 12
	s_cselect_b32 s27, s13, s25
	s_cselect_b32 s26, s46, s24
	s_cselect_b32 s25, s15, s49
	s_cselect_b32 s24, s47, s48
	v_lshl_add_u64 v[218:219], s[22:23], 0, v[170:171]
	s_add_i32 m0, s28, 0xc000
	ds_read_b128 v[178:181], v190
	ds_read_b128 v[182:185], v190 offset:1024
	ds_read_b128 v[194:197], v190 offset:2048
	ds_read_b128 v[198:201], v190 offset:3072
	ds_read_b128 v[202:205], v190 offset:4096
	ds_read_b128 v[206:209], v190 offset:5120
	ds_read_b128 v[210:213], v190 offset:6144
	ds_read_b128 v[214:217], v190 offset:7168
	global_load_lds_dwordx4 v[218:219], off
	v_lshl_add_u64 v[218:219], s[22:23], 0, v[172:173]
	s_add_i32 m0, s28, 0xe000
	s_nop 0
	global_load_lds_dwordx4 v[218:219], off
	s_waitcnt vmcnt(8)
	s_waitcnt lgkmcnt(0)
	s_barrier
	s_setprio 1
	v_mfma_scale_f32_16x16x128_f8f6f4 v[158:161], v[26:33], v[178:185], v[158:161], v191, v192 op_sel_hi:[0,0,0]
	v_mfma_scale_f32_16x16x128_f8f6f4 v[154:157], v[18:25], v[178:185], v[154:157], v191, v192 op_sel_hi:[0,0,0]
	v_mfma_scale_f32_16x16x128_f8f6f4 v[142:145], v[26:33], v[194:201], v[142:145], v191, v192 op_sel_hi:[0,0,0]
	v_mfma_scale_f32_16x16x128_f8f6f4 v[138:141], v[18:25], v[194:201], v[138:141], v191, v192 op_sel_hi:[0,0,0]
	v_mfma_scale_f32_16x16x128_f8f6f4 v[126:129], v[26:33], v[202:209], v[126:129], v191, v192 op_sel_hi:[0,0,0]
	v_mfma_scale_f32_16x16x128_f8f6f4 v[122:125], v[18:25], v[202:209], v[122:125], v191, v192 op_sel_hi:[0,0,0]
	v_mfma_scale_f32_16x16x128_f8f6f4 v[110:113], v[26:33], v[210:217], v[110:113], v191, v192 op_sel_hi:[0,0,0]
	v_mfma_scale_f32_16x16x128_f8f6f4 v[106:109], v[18:25], v[210:217], v[106:109], v191, v192 op_sel_hi:[0,0,0]
	s_setprio 0
	s_setprio 1
	s_nop 0
	v_mfma_scale_f32_16x16x128_f8f6f4 v[150:153], v[10:17], v[178:185], v[150:153], v191, v192 op_sel_hi:[0,0,0]
	v_mfma_scale_f32_16x16x128_f8f6f4 v[146:149], v[2:9], v[178:185], v[146:149], v191, v192 op_sel_hi:[0,0,0]
	v_mfma_scale_f32_16x16x128_f8f6f4 v[134:137], v[10:17], v[194:201], v[134:137], v191, v192 op_sel_hi:[0,0,0]
	v_mfma_scale_f32_16x16x128_f8f6f4 v[130:133], v[2:9], v[194:201], v[130:133], v191, v192 op_sel_hi:[0,0,0]
	v_mfma_scale_f32_16x16x128_f8f6f4 v[118:121], v[10:17], v[202:209], v[118:121], v191, v192 op_sel_hi:[0,0,0]
	v_mfma_scale_f32_16x16x128_f8f6f4 v[114:117], v[2:9], v[202:209], v[114:117], v191, v192 op_sel_hi:[0,0,0]
	v_mfma_scale_f32_16x16x128_f8f6f4 v[102:105], v[10:17], v[210:217], v[102:105], v191, v192 op_sel_hi:[0,0,0]
	v_mfma_scale_f32_16x16x128_f8f6f4 v[98:101], v[2:9], v[210:217], v[98:101], v191, v192 op_sel_hi:[0,0,0]
	s_setprio 0
	s_barrier
	s_add_i32 s51, s39, s21
	v_lshl_add_u64 v[178:179], s[24:25], 0, v[166:167]
	s_mov_b32 m0, s51
	ds_read_b128 v[194:197], v190 offset:16384
	ds_read_b128 v[198:201], v190 offset:17408
	ds_read_b128 v[202:205], v190 offset:18432
	ds_read_b128 v[206:209], v190 offset:19456
	ds_read_b128 v[210:213], v190 offset:20480
	ds_read_b128 v[214:217], v190 offset:21504
	ds_read_b128 v[218:221], v190 offset:22528
	ds_read_b128 v[222:225], v190 offset:23552
	global_load_lds_dwordx4 v[178:179], off
	s_add_i32 m0, s51, 0x2000
	s_add_u32 s52, s24, 0x4000
	v_lshl_add_u64 v[180:181], s[24:25], 0, v[162:163]
	s_addc_u32 s53, s25, 0
	s_add_i32 s51, s40, s21
	global_load_lds_dwordx4 v[180:181], off
	v_lshl_add_u64 v[182:183], s[52:53], 0, v[166:167]
	s_mov_b32 m0, s51
	v_lshl_add_u64 v[184:185], s[26:27], 0, v[164:165]
	global_load_lds_dwordx4 v[182:183], off
	v_lshl_add_u64 v[182:183], s[52:53], 0, v[162:163]
	s_add_i32 m0, s51, 0x2000
	s_nop 0
	global_load_lds_dwordx4 v[182:183], off
	v_lshl_add_u64 v[182:183], s[26:27], 0, v[168:169]
	s_mov_b32 m0, s28
	s_nop 0
	global_load_lds_dwordx4 v[182:183], off
	s_mov_b32 m0, s29
	s_nop 0
	global_load_lds_dwordx4 v[184:185], off
	s_waitcnt vmcnt(8)
	s_waitcnt lgkmcnt(0)
	s_barrier
	s_setprio 1
	v_mfma_scale_f32_16x16x128_f8f6f4 v[94:97], v[26:33], v[194:201], v[94:97], v191, v192 op_sel_hi:[0,0,0]
	v_mfma_scale_f32_16x16x128_f8f6f4 v[90:93], v[18:25], v[194:201], v[90:93], v191, v192 op_sel_hi:[0,0,0]
	v_mfma_scale_f32_16x16x128_f8f6f4 v[78:81], v[26:33], v[202:209], v[78:81], v191, v192 op_sel_hi:[0,0,0]
	v_mfma_scale_f32_16x16x128_f8f6f4 v[74:77], v[18:25], v[202:209], v[74:77], v191, v192 op_sel_hi:[0,0,0]
	v_mfma_scale_f32_16x16x128_f8f6f4 v[62:65], v[26:33], v[210:217], v[62:65], v191, v192 op_sel_hi:[0,0,0]
	v_mfma_scale_f32_16x16x128_f8f6f4 v[58:61], v[18:25], v[210:217], v[58:61], v191, v192 op_sel_hi:[0,0,0]
	v_mfma_scale_f32_16x16x128_f8f6f4 v[46:49], v[26:33], v[218:225], v[46:49], v191, v192 op_sel_hi:[0,0,0]
	v_mfma_scale_f32_16x16x128_f8f6f4 v[42:45], v[18:25], v[218:225], v[42:45], v191, v192 op_sel_hi:[0,0,0]
	s_setprio 0
	s_setprio 1
	s_nop 0
	v_mfma_scale_f32_16x16x128_f8f6f4 v[86:89], v[10:17], v[194:201], v[86:89], v191, v192 op_sel_hi:[0,0,0]
	v_mfma_scale_f32_16x16x128_f8f6f4 v[82:85], v[2:9], v[194:201], v[82:85], v191, v192 op_sel_hi:[0,0,0]
	v_mfma_scale_f32_16x16x128_f8f6f4 v[70:73], v[10:17], v[202:209], v[70:73], v191, v192 op_sel_hi:[0,0,0]
	v_mfma_scale_f32_16x16x128_f8f6f4 v[66:69], v[2:9], v[202:209], v[66:69], v191, v192 op_sel_hi:[0,0,0]
	v_mfma_scale_f32_16x16x128_f8f6f4 v[54:57], v[10:17], v[210:217], v[54:57], v191, v192 op_sel_hi:[0,0,0]
	v_mfma_scale_f32_16x16x128_f8f6f4 v[50:53], v[2:9], v[210:217], v[50:53], v191, v192 op_sel_hi:[0,0,0]
	v_mfma_scale_f32_16x16x128_f8f6f4 v[38:41], v[10:17], v[218:225], v[38:41], v191, v192 op_sel_hi:[0,0,0]
	v_mfma_scale_f32_16x16x128_f8f6f4 v[34:37], v[2:9], v[218:225], v[34:37], v191, v192 op_sel_hi:[0,0,0]
	s_setprio 0
	s_barrier
; #define PG8_STAGE(bufoff, gbase, voff) do { _Pragma("unroll") for (int _i = 0; _i < 2; ++_i) \
;         __builtin_amdgcn_global_load_lds((const unsigned*)((const char*)(gbase) + (voff)[_i]), (PG8_LAS unsigned*)(lds + (bufoff) + ldsw + _i * 8192), 16, 0, 0); } while (0)
; #define PG8_STAGE_A(bufoff, gbase, h, nx) do { if constexpr (Sched::GATHER) { const unsigned vv_[2] = {(nx) ? vAn[h][0] : vA[h][0], (nx) ? vAn[h][1] : vA[h][1]}; PG8_STAGE(bufoff, gbase, vv_); } \
;         else { PG8_STAGE(bufoff, (gbase) + (h) * hstep, voffA); } } while (0)
; #define PG8_LDA(dst, b, h) do { _Pragma("unroll") for (int m = 0; m < 4; ++m) _Pragma("unroll") for (int k = 0; k < 2; ++k) dst[m][k] = *(const PG8_LAS bf16x8*)(lds + PG8_SA(b, h) + aoff + m * 2048 + k * 1024); } while (0)
; #define PG8_LDB(dst, b, h) do { _Pragma("unroll") for (int n = 0; n < 2; ++n) _Pragma("unroll") for (int k = 0; k < 2; ++k) dst[n][k] = *(const PG8_LAS bf16x8*)(lds + PG8_SB(b, h) + boff + n * 2048 + k * 1024); } while (0)
; #define PG8_WAIT_V(n) asm volatile("s_waitcnt vmcnt(" #n ")" ::: "memory")
; #define PG8_WAIT_L(n) asm volatile("s_waitcnt lgkmcnt(" #n ")" ::: "memory")
; #define PG8_BAR __builtin_amdgcn_s_barrier()
; #define PG8_SCHED __builtin_amdgcn_sched_barrier(0)
;     ...
;             PG8_LDB(B0, 1, 0); PG8_LDB(B1, 1, 1); PG8_SCHED; PG8_LDA(At, 1, 0); PG8_STAGE_A(PG8_SA(0, 1), a2, 1, last);
;             PG8_WAIT_V(8); PG8_WAIT_L(0); PG8_BAR; PG8_MMA(0, 0, At, B0); PG8_MMA(0, 1, At, B1); PG8_BAR; PG8_SCHED;
;             PG8_LDA(At, 1, 1); PG8_STAGE(PG8_SB(1, 0), b3, voffB); PG8_STAGE(PG8_SB(1, 1), b3 + hstepB, voffB); PG8_STAGE_A(PG8_SA(1, 0), a3, 0, last);
;             PG8_WAIT_V(8); PG8_WAIT_L(0); PG8_BAR; PG8_MMA(1, 0, At, B0); PG8_MMA(1, 1, At, B1); PG8_BAR; PG8_SCHED;
;     __device__ __forceinline__ void operator()(const f32x4 (&acc)[2][2][4][2], const Unit& u, int wr, int wc, int fr, int fq) const {
;     ...
;             for (int m = 0; m < 4; ++m) { const int row = row0 + ai * HALF + m * 16; const float gt = gate[row] * YSCALE; unsigned char* rowp = O + (size_t)row * ldc + col0;
	s_add_i32 s51, 0, 0x18000
	s_add_i32 s52, 0, 0x1c000
	v_add_u32_e32 v14, s51, v186
	v_add_u32_e32 v30, s52, v186
	ds_read_b128 v[2:5], v14
	ds_read_b128 v[6:9], v14 offset:1024
	ds_read_b128 v[10:13], v14 offset:2048
	ds_read_b128 v[14:17], v14 offset:3072
	ds_read_b128 v[18:21], v30
	ds_read_b128 v[22:25], v30 offset:1024
	ds_read_b128 v[26:29], v30 offset:2048
	ds_read_b128 v[30:33], v30 offset:3072
	s_add_u32 s26, s26, 0x40000
	s_addc_u32 s27, s27, 0
	s_mov_b32 m0, s30
	v_lshl_add_u64 v[226:227], s[26:27], 0, v[168:169]
	ds_read_b128 v[194:197], v190 offset:32768
	ds_read_b128 v[198:201], v190 offset:33792
	ds_read_b128 v[202:205], v190 offset:34816
	ds_read_b128 v[206:209], v190 offset:35840
	ds_read_b128 v[210:213], v190 offset:36864
	ds_read_b128 v[214:217], v190 offset:37888
	ds_read_b128 v[218:221], v190 offset:38912
	ds_read_b128 v[222:225], v190 offset:39936
	global_load_lds_dwordx4 v[226:227], off
	v_lshl_add_u64 v[226:227], s[26:27], 0, v[164:165]
	s_mov_b32 m0, s31
	s_nop 0
	global_load_lds_dwordx4 v[226:227], off
	s_waitcnt vmcnt(8)
	s_waitcnt lgkmcnt(0)
	s_barrier
	s_setprio 1
	v_mfma_scale_f32_16x16x128_f8f6f4 v[158:161], v[2:9], v[194:201], v[158:161], v191, v192 op_sel_hi:[0,0,0]
	v_mfma_scale_f32_16x16x128_f8f6f4 v[154:157], v[10:17], v[194:201], v[154:157], v191, v192 op_sel_hi:[0,0,0]
	v_mfma_scale_f32_16x16x128_f8f6f4 v[142:145], v[2:9], v[202:209], v[142:145], v191, v192 op_sel_hi:[0,0,0]
	v_mfma_scale_f32_16x16x128_f8f6f4 v[138:141], v[10:17], v[202:209], v[138:141], v191, v192 op_sel_hi:[0,0,0]
	v_mfma_scale_f32_16x16x128_f8f6f4 v[126:129], v[2:9], v[210:217], v[126:129], v191, v192 op_sel_hi:[0,0,0]
	v_mfma_scale_f32_16x16x128_f8f6f4 v[122:125], v[10:17], v[210:217], v[122:125], v191, v192 op_sel_hi:[0,0,0]
	v_mfma_scale_f32_16x16x128_f8f6f4 v[110:113], v[2:9], v[218:225], v[110:113], v191, v192 op_sel_hi:[0,0,0]
	v_mfma_scale_f32_16x16x128_f8f6f4 v[106:109], v[10:17], v[218:225], v[106:109], v191, v192 op_sel_hi:[0,0,0]
	s_setprio 0
	s_setprio 1
	s_nop 0
	v_mfma_scale_f32_16x16x128_f8f6f4 v[150:153], v[18:25], v[194:201], v[150:153], v191, v192 op_sel_hi:[0,0,0]
	v_mfma_scale_f32_16x16x128_f8f6f4 v[146:149], v[26:33], v[194:201], v[146:149], v191, v192 op_sel_hi:[0,0,0]
	v_mfma_scale_f32_16x16x128_f8f6f4 v[134:137], v[18:25], v[202:209], v[134:137], v191, v192 op_sel_hi:[0,0,0]
	v_mfma_scale_f32_16x16x128_f8f6f4 v[130:133], v[26:33], v[202:209], v[130:133], v191, v192 op_sel_hi:[0,0,0]
	v_mfma_scale_f32_16x16x128_f8f6f4 v[118:121], v[18:25], v[210:217], v[118:121], v191, v192 op_sel_hi:[0,0,0]
	v_mfma_scale_f32_16x16x128_f8f6f4 v[114:117], v[26:33], v[210:217], v[114:117], v191, v192 op_sel_hi:[0,0,0]
	v_mfma_scale_f32_16x16x128_f8f6f4 v[102:105], v[18:25], v[218:225], v[102:105], v191, v192 op_sel_hi:[0,0,0]
	v_mfma_scale_f32_16x16x128_f8f6f4 v[98:101], v[26:33], v[218:225], v[98:101], v191, v192 op_sel_hi:[0,0,0]
	s_setprio 0
	s_barrier
	s_add_i32 s26, s51, s21
	v_lshl_add_u64 v[178:179], v[178:179], 0, s[8:9]
	s_mov_b32 m0, s26
	ds_read_b128 v[194:197], v190 offset:49152
	ds_read_b128 v[198:201], v190 offset:50176
	ds_read_b128 v[202:205], v190 offset:51200
	ds_read_b128 v[206:209], v190 offset:52224
	ds_read_b128 v[210:213], v190 offset:53248
	ds_read_b128 v[214:217], v190 offset:54272
	ds_read_b128 v[218:221], v190 offset:55296
	ds_read_b128 v[222:225], v190 offset:56320
	global_load_lds_dwordx4 v[178:179], off
	s_add_i32 m0, s26, 0x2000
	s_add_u32 s24, s24, 0x4080
	v_lshl_add_u64 v[178:179], v[180:181], 0, s[8:9]
	s_addc_u32 s25, s25, 0
	s_add_i32 s26, s52, s21
	global_load_lds_dwordx4 v[178:179], off
	v_lshl_add_u64 v[178:179], s[24:25], 0, v[166:167]
	s_mov_b32 m0, s26
	s_nop 0
	global_load_lds_dwordx4 v[178:179], off
	v_lshl_add_u64 v[178:179], s[24:25], 0, v[162:163]
	s_add_i32 m0, s26, 0x2000
	s_nop 0
	global_load_lds_dwordx4 v[178:179], off
	v_lshl_add_u64 v[178:179], v[182:183], 0, s[8:9]
	s_mov_b32 m0, s36
	s_nop 0
	global_load_lds_dwordx4 v[178:179], off
	v_lshl_add_u64 v[178:179], v[184:185], 0, s[8:9]
	s_mov_b32 m0, s37
	s_nop 0
	global_load_lds_dwordx4 v[178:179], off
	s_waitcnt vmcnt(8)
	s_cmp_eq_u32 s50, 12
	s_cbranch_scc0 .Lgate19_skip
	v_lshl_add_u32 v236, s20, 8, v1
	v_ashrrev_i32_e32 v237, 31, v236
	v_lshl_add_u64 v[236:237], v[236:237], 2, s[0:1]
	global_load_dword v228, v[236:237], off
	global_load_dword v229, v[236:237], off offset:64
	global_load_dword v230, v[236:237], off offset:128
	global_load_dword v231, v[236:237], off offset:192
	global_load_dword v232, v[236:237], off offset:512
	global_load_dword v233, v[236:237], off offset:576
	global_load_dword v234, v[236:237], off offset:640
	global_load_dword v235, v[236:237], off offset:704
.Lgate19_skip:
	s_waitcnt lgkmcnt(0)
	s_barrier
	s_setprio 1
	v_mfma_scale_f32_16x16x128_f8f6f4 v[94:97], v[2:9], v[194:201], v[94:97], v191, v192 op_sel_hi:[0,0,0]
	v_mfma_scale_f32_16x16x128_f8f6f4 v[90:93], v[10:17], v[194:201], v[90:93], v191, v192 op_sel_hi:[0,0,0]
	v_mfma_scale_f32_16x16x128_f8f6f4 v[78:81], v[2:9], v[202:209], v[78:81], v191, v192 op_sel_hi:[0,0,0]
	v_mfma_scale_f32_16x16x128_f8f6f4 v[74:77], v[10:17], v[202:209], v[74:77], v191, v192 op_sel_hi:[0,0,0]
	v_mfma_scale_f32_16x16x128_f8f6f4 v[62:65], v[2:9], v[210:217], v[62:65], v191, v192 op_sel_hi:[0,0,0]
	v_mfma_scale_f32_16x16x128_f8f6f4 v[58:61], v[10:17], v[210:217], v[58:61], v191, v192 op_sel_hi:[0,0,0]
	v_mfma_scale_f32_16x16x128_f8f6f4 v[46:49], v[2:9], v[218:225], v[46:49], v191, v192 op_sel_hi:[0,0,0]
	v_mfma_scale_f32_16x16x128_f8f6f4 v[42:45], v[10:17], v[218:225], v[42:45], v191, v192 op_sel_hi:[0,0,0]
	s_setprio 0
	s_setprio 1
	s_nop 0
	v_mfma_scale_f32_16x16x128_f8f6f4 v[86:89], v[18:25], v[194:201], v[86:89], v191, v192 op_sel_hi:[0,0,0]
	v_mfma_scale_f32_16x16x128_f8f6f4 v[82:85], v[26:33], v[194:201], v[82:85], v191, v192 op_sel_hi:[0,0,0]
	v_mfma_scale_f32_16x16x128_f8f6f4 v[70:73], v[18:25], v[202:209], v[70:73], v191, v192 op_sel_hi:[0,0,0]
	v_mfma_scale_f32_16x16x128_f8f6f4 v[66:69], v[26:33], v[202:209], v[66:69], v191, v192 op_sel_hi:[0,0,0]
	v_mfma_scale_f32_16x16x128_f8f6f4 v[54:57], v[18:25], v[210:217], v[54:57], v191, v192 op_sel_hi:[0,0,0]
	v_mfma_scale_f32_16x16x128_f8f6f4 v[50:53], v[26:33], v[210:217], v[50:53], v191, v192 op_sel_hi:[0,0,0]
	v_mfma_scale_f32_16x16x128_f8f6f4 v[38:41], v[18:25], v[218:225], v[38:41], v191, v192 op_sel_hi:[0,0,0]
	v_mfma_scale_f32_16x16x128_f8f6f4 v[34:37], v[26:33], v[218:225], v[34:37], v191, v192 op_sel_hi:[0,0,0]
	s_setprio 0
	s_barrier
	s_add_i32 s50, s50, 2
	s_add_u32 s22, s22, 0x100
	s_addc_u32 s23, s23, 0
	s_add_u32 s48, s48, 0x100
	s_addc_u32 s49, s49, 0
	s_cmp_gt_u32 s50, 13
	s_cbranch_scc0 .LBB0_1626
	s_and_b64 vcc, exec, s[10:11]
	s_cbranch_vccz .LBB0_1629
	s_barrier
